# combined: exact lgkmcnt waits + static prio waves 4-7 (attention) + combine-loop load reorder + softmax tail hoisted into P.V MFMA shadows + shortened rescale branch + merged setprio bursts in GEMM ph
# baseline (speedup 1.0000x reference)
; #define G8_STAGE_B(bufoff, gbase) do { _Pragma("unroll") for (int _i = 0; _i < 2; ++_i) \
;         __builtin_amdgcn_global_load_lds((const unsigned*)((const char*)(gbase) + voffB[_i]), (LAS unsigned*)(lds + (bufoff) + ldsw + _i * 8192), 16, 0, 0); } while (0)
; #define G8_LDA(dst, b, h) do { _Pragma("unroll") for (int m = 0; m < 4; ++m) _Pragma("unroll") for (int k = 0; k < 2; ++k) dst[m][k] = *(const LAS bf16x8*)(lds + G8_SA(b, h) + aoff + m * 2048 + k * 1024); } while (0)
; #define G8_LDB(dst, b, h) do { _Pragma("unroll") for (int n = 0; n < 2; ++n) _Pragma("unroll") for (int k = 0; k < 2; ++k) dst[n][k] = *(const LAS bf16x8*)(lds + G8_SB(b, h) + boff + n * 2048 + k * 1024); } while (0)
; #define G8_MMA(ai, bj, At, Bt) do { __builtin_amdgcn_s_setprio(1); _Pragma("unroll") for (int m = 0; m < 4; ++m) _Pragma("unroll") for (int n = 0; n < 2; ++n) _Pragma("unroll") for (int k = 0; k < 2; ++k) \
;         acc[ai][bj][m][n] = __builtin_amdgcn_mfma_f32_16x16x32_bf16(Bt[n][k], At[m][k], acc[ai][bj][m][n], 0, 0, 0); __builtin_amdgcn_s_setprio(0); } while (0)
; #define G8_WAIT_V(n) asm volatile("s_waitcnt vmcnt(" #n ")" ::: "memory")
; #define G8_WAIT_L(n) asm volatile("s_waitcnt lgkmcnt(" #n ")" ::: "memory")
; #define G8_BAR __builtin_amdgcn_s_barrier()
; #define G8_SCHED __builtin_amdgcn_sched_barrier(0)
; template <class Sched, class Epi>
; DEVI void gemm_phase(LAS unsigned char* lds, const char* Abase, const int K, const Sched& S, const Epi& E) {
;     ...
;             G8_LDB(B0, 0, 0); G8_LDB(B1, 0, 1); G8_SCHED; G8_LDA(At, 0, 0); G8_STAGE_A(G8_SA(1, 1), false, 1, k1);
;             G8_WAIT_L(0); G8_BAR; G8_MMA(0, 0, At, B0); G8_MMA(0, 1, At, B1); G8_BAR; G8_SCHED;
;             if (!skip1) G8_LDA(At, 0, 1); G8_STAGE_B(G8_SB(0, 0), b2); G8_STAGE_A(G8_SA(0, 0), last, 0, k2); G8_STAGE_B(G8_SB(0, 1), b2 + hstepB);
;             G8_WAIT_V(6); G8_WAIT_L(0); G8_BAR; if (!skip1) { G8_MMA(1, 0, At, B0); G8_MMA(1, 1, At, B1); } G8_BAR; G8_SCHED;
.LBB0_245:
	ds_read_b128 v[150:153], v218
	ds_read_b128 v[154:157], v218 offset:1024
	ds_read_b128 v[158:161], v218 offset:2048
	ds_read_b128 v[162:165], v218 offset:3072
	ds_read_b128 v[134:137], v219
	ds_read_b128 v[138:141], v219 offset:1024
	ds_read_b128 v[142:145], v219 offset:2048
	ds_read_b128 v[146:149], v219 offset:3072
	v_lshl_add_u64 v[4:5], v[206:207], 0, s[40:41]
	s_add_i32 m0, s29, 0xc000
	s_waitcnt lgkmcnt(0)
	ds_read_b128 v[178:181], v220
	ds_read_b128 v[194:197], v220 offset:1024
	ds_read_b128 v[174:177], v220 offset:2048
	ds_read_b128 v[190:193], v220 offset:3072
	ds_read_b128 v[170:173], v220 offset:4096
	ds_read_b128 v[186:189], v220 offset:5120
	ds_read_b128 v[166:169], v220 offset:6144
	ds_read_b128 v[182:185], v220 offset:7168
	global_load_lds_dwordx4 v[4:5], off
	v_lshl_add_u64 v[4:5], v[208:209], 0, s[40:41]
	s_add_i32 m0, s29, 0xe000
	s_nop 0
	global_load_lds_dwordx4 v[4:5], off
	s_waitcnt lgkmcnt(0)
	s_barrier
	s_setprio 1
	s_waitcnt lgkmcnt(0)
	v_mfma_f32_16x16x32_bf16 v[130:133], v[150:153], v[178:181], v[130:133]
	v_mfma_f32_16x16x32_bf16 v[126:129], v[158:161], v[178:181], v[126:129]
	v_mfma_f32_16x16x32_bf16 v[114:117], v[150:153], v[174:177], v[114:117]
	v_mfma_f32_16x16x32_bf16 v[110:113], v[158:161], v[174:177], v[110:113]
	v_mfma_f32_16x16x32_bf16 v[98:101], v[150:153], v[170:173], v[98:101]
	v_mfma_f32_16x16x32_bf16 v[94:97], v[158:161], v[170:173], v[94:97]
	v_mfma_f32_16x16x32_bf16 v[82:85], v[150:153], v[166:169], v[82:85]
	v_mfma_f32_16x16x32_bf16 v[78:81], v[158:161], v[166:169], v[78:81]
	v_mfma_f32_16x16x32_bf16 v[130:133], v[154:157], v[194:197], v[130:133]
	v_mfma_f32_16x16x32_bf16 v[126:129], v[162:165], v[194:197], v[126:129]
	v_mfma_f32_16x16x32_bf16 v[114:117], v[154:157], v[190:193], v[114:117]
	v_mfma_f32_16x16x32_bf16 v[110:113], v[162:165], v[190:193], v[110:113]
	v_mfma_f32_16x16x32_bf16 v[98:101], v[154:157], v[186:189], v[98:101]
	v_mfma_f32_16x16x32_bf16 v[94:97], v[162:165], v[186:189], v[94:97]
	v_mfma_f32_16x16x32_bf16 v[82:85], v[154:157], v[182:185], v[82:85]
	v_mfma_f32_16x16x32_bf16 v[78:81], v[162:165], v[182:185], v[78:81]
	v_mfma_f32_16x16x32_bf16 v[122:125], v[134:137], v[178:181], v[122:125]
	v_mfma_f32_16x16x32_bf16 v[118:121], v[142:145], v[178:181], v[118:121]
	v_mfma_f32_16x16x32_bf16 v[106:109], v[134:137], v[174:177], v[106:109]
	v_mfma_f32_16x16x32_bf16 v[102:105], v[142:145], v[174:177], v[102:105]
	v_mfma_f32_16x16x32_bf16 v[90:93], v[134:137], v[170:173], v[90:93]
	v_mfma_f32_16x16x32_bf16 v[86:89], v[142:145], v[170:173], v[86:89]
	v_mfma_f32_16x16x32_bf16 v[74:77], v[134:137], v[166:169], v[74:77]
	v_mfma_f32_16x16x32_bf16 v[70:73], v[142:145], v[166:169], v[70:73]
	v_mfma_f32_16x16x32_bf16 v[122:125], v[138:141], v[194:197], v[122:125]
	v_mfma_f32_16x16x32_bf16 v[118:121], v[146:149], v[194:197], v[118:121]
	v_mfma_f32_16x16x32_bf16 v[106:109], v[138:141], v[190:193], v[106:109]
	v_mfma_f32_16x16x32_bf16 v[102:105], v[146:149], v[190:193], v[102:105]
	v_mfma_f32_16x16x32_bf16 v[90:93], v[138:141], v[186:189], v[90:93]
	v_mfma_f32_16x16x32_bf16 v[86:89], v[146:149], v[186:189], v[86:89]
	v_mfma_f32_16x16x32_bf16 v[74:77], v[138:141], v[182:185], v[74:77]
	v_mfma_f32_16x16x32_bf16 v[70:73], v[146:149], v[182:185], v[70:73]
	s_setprio 0
	s_barrier
	v_cmp_ne_u32_e64 s[4:5], 1, v221
	s_andn2_b64 vcc, exec, s[36:37]
	s_cbranch_vccnz .LBB0_247
	ds_read_b128 v[178:181], v220 offset:16384
	ds_read_b128 v[194:197], v220 offset:17408
	ds_read_b128 v[174:177], v220 offset:18432
	ds_read_b128 v[190:193], v220 offset:19456
	ds_read_b128 v[170:173], v220 offset:20480
	ds_read_b128 v[186:189], v220 offset:21504
	ds_read_b128 v[166:169], v220 offset:22528
	ds_read_b128 v[182:185], v220 offset:23552
.LBB0_247:
	s_add_u32 s38, s40, 0x100
	s_addc_u32 s39, s41, 0
	s_add_u32 s70, s64, s40
	s_addc_u32 s71, s65, s41
	s_cmp_eq_u32 s66, 12
	s_cselect_b64 s[68:69], -1, 0
	s_and_b64 s[40:41], s[68:69], exec
	s_cselect_b32 s67, 0, s38
	s_cselect_b32 s41, s19, s71
	s_cselect_b32 s40, s21, s70
	s_and_b64 s[68:69], s[34:35], s[68:69]
	s_and_b64 s[68:69], s[68:69], exec
	s_cselect_b32 s69, s26, s30
	s_mov_b32 m0, s43
	v_lshl_add_u64 v[4:5], s[40:41], 0, v[198:199]
	s_cselect_b32 s68, s27, s31
	s_add_u32 s70, s69, s67
	global_load_lds_dwordx4 v[4:5], off
	v_lshl_add_u64 v[210:211], s[40:41], 0, v[200:201]
	s_mov_b32 m0, s44
	s_addc_u32 s71, s68, 0
	global_load_lds_dwordx4 v[210:211], off
	v_lshl_add_u64 v[212:213], s[70:71], 0, v[198:199]
	s_mov_b32 m0, s29
	v_lshl_add_u64 v[214:215], s[70:71], 0, v[200:201]
	s_add_u32 s70, s40, 0x40000
	global_load_lds_dwordx4 v[212:213], off
	s_mov_b32 m0, s45
	s_addc_u32 s71, s41, 0
	global_load_lds_dwordx4 v[214:215], off
	v_lshl_add_u64 v[222:223], s[70:71], 0, v[198:199]
	s_mov_b32 m0, s46
	s_and_b64 vcc, exec, s[4:5]
	global_load_lds_dwordx4 v[222:223], off
	v_lshl_add_u64 v[222:223], s[70:71], 0, v[200:201]
	s_mov_b32 m0, s47
	s_nop 0
	global_load_lds_dwordx4 v[222:223], off
	s_waitcnt vmcnt(6)
	s_waitcnt lgkmcnt(0)
	s_barrier
	s_cbranch_vccnz .LBB0_249
; #define G8_STAGE_B(bufoff, gbase) do { _Pragma("unroll") for (int _i = 0; _i < 2; ++_i) \
;         __builtin_amdgcn_global_load_lds((const unsigned*)((const char*)(gbase) + voffB[_i]), (LAS unsigned*)(lds + (bufoff) + ldsw + _i * 8192), 16, 0, 0); } while (0)
; #define G8_LDA(dst, b, h) do { _Pragma("unroll") for (int m = 0; m < 4; ++m) _Pragma("unroll") for (int k = 0; k < 2; ++k) dst[m][k] = *(const LAS bf16x8*)(lds + G8_SA(b, h) + aoff + m * 2048 + k * 1024); } while (0)
; #define G8_LDB(dst, b, h) do { _Pragma("unroll") for (int n = 0; n < 2; ++n) _Pragma("unroll") for (int k = 0; k < 2; ++k) dst[n][k] = *(const LAS bf16x8*)(lds + G8_SB(b, h) + boff + n * 2048 + k * 1024); } while (0)
; #define G8_MMA(ai, bj, At, Bt) do { __builtin_amdgcn_s_setprio(1); _Pragma("unroll") for (int m = 0; m < 4; ++m) _Pragma("unroll") for (int n = 0; n < 2; ++n) _Pragma("unroll") for (int k = 0; k < 2; ++k) \
;         acc[ai][bj][m][n] = __builtin_amdgcn_mfma_f32_16x16x32_bf16(Bt[n][k], At[m][k], acc[ai][bj][m][n], 0, 0, 0); __builtin_amdgcn_s_setprio(0); } while (0)
; #define G8_WAIT_V(n) asm volatile("s_waitcnt vmcnt(" #n ")" ::: "memory")
; #define G8_WAIT_L(n) asm volatile("s_waitcnt lgkmcnt(" #n ")" ::: "memory")
; #define G8_BAR __builtin_amdgcn_s_barrier()
; #define G8_SCHED __builtin_amdgcn_sched_barrier(0)
; template <class Sched, class Epi>
; DEVI void gemm_phase(LAS unsigned char* lds, const char* Abase, const int K, const Sched& S, const Epi& E) {
;     ...
;             G8_WAIT_V(6); G8_WAIT_L(0); G8_BAR; if (!skip1) { G8_MMA(1, 0, At, B0); G8_MMA(1, 1, At, B1); } G8_BAR; G8_SCHED;
;             G8_LDB(B0, 1, 0); G8_LDB(B1, 1, 1); G8_SCHED; G8_LDA(At, 1, 0); G8_STAGE_A(G8_SA(0, 1), last, 1, k2);
;             G8_WAIT_L(0); G8_BAR; G8_MMA(0, 0, At, B0); G8_MMA(0, 1, At, B1); G8_BAR; G8_SCHED;
;             if (!skip1) G8_LDA(At, 1, 1); G8_STAGE_B(G8_SB(1, 0), b3); G8_STAGE_A(G8_SA(1, 0), last, 0, k3); G8_STAGE_B(G8_SB(1, 1), b3 + hstepB);
	s_setprio 1
	s_waitcnt lgkmcnt(0)
	v_mfma_f32_16x16x32_bf16 v[66:69], v[150:153], v[178:181], v[66:69]
	v_mfma_f32_16x16x32_bf16 v[62:65], v[158:161], v[178:181], v[62:65]
	v_mfma_f32_16x16x32_bf16 v[50:53], v[150:153], v[174:177], v[50:53]
	v_mfma_f32_16x16x32_bf16 v[46:49], v[158:161], v[174:177], v[46:49]
	v_mfma_f32_16x16x32_bf16 v[34:37], v[150:153], v[170:173], v[34:37]
	v_mfma_f32_16x16x32_bf16 v[30:33], v[158:161], v[170:173], v[30:33]
	v_mfma_f32_16x16x32_bf16 v[22:25], v[150:153], v[166:169], v[22:25]
	v_mfma_f32_16x16x32_bf16 v[18:21], v[158:161], v[166:169], v[18:21]
	v_mfma_f32_16x16x32_bf16 v[66:69], v[154:157], v[194:197], v[66:69]
	v_mfma_f32_16x16x32_bf16 v[62:65], v[162:165], v[194:197], v[62:65]
	v_mfma_f32_16x16x32_bf16 v[50:53], v[154:157], v[190:193], v[50:53]
	v_mfma_f32_16x16x32_bf16 v[46:49], v[162:165], v[190:193], v[46:49]
	v_mfma_f32_16x16x32_bf16 v[34:37], v[154:157], v[186:189], v[34:37]
	v_mfma_f32_16x16x32_bf16 v[30:33], v[162:165], v[186:189], v[30:33]
	v_mfma_f32_16x16x32_bf16 v[22:25], v[154:157], v[182:185], v[22:25]
	v_mfma_f32_16x16x32_bf16 v[18:21], v[162:165], v[182:185], v[18:21]
	v_mfma_f32_16x16x32_bf16 v[58:61], v[134:137], v[178:181], v[58:61]
	v_mfma_f32_16x16x32_bf16 v[54:57], v[142:145], v[178:181], v[54:57]
	v_mfma_f32_16x16x32_bf16 v[42:45], v[134:137], v[174:177], v[42:45]
	v_mfma_f32_16x16x32_bf16 v[38:41], v[142:145], v[174:177], v[38:41]
	v_mfma_f32_16x16x32_bf16 v[26:29], v[134:137], v[170:173], v[26:29]
	v_mfma_f32_16x16x32_bf16 v[14:17], v[142:145], v[170:173], v[14:17]
	v_mfma_f32_16x16x32_bf16 v[10:13], v[134:137], v[166:169], v[10:13]
	v_mfma_f32_16x16x32_bf16 v[6:9], v[142:145], v[166:169], v[6:9]
	v_mfma_f32_16x16x32_bf16 v[58:61], v[138:141], v[194:197], v[58:61]
	v_mfma_f32_16x16x32_bf16 v[54:57], v[146:149], v[194:197], v[54:57]
	v_mfma_f32_16x16x32_bf16 v[42:45], v[138:141], v[190:193], v[42:45]
	v_mfma_f32_16x16x32_bf16 v[38:41], v[146:149], v[190:193], v[38:41]
	v_mfma_f32_16x16x32_bf16 v[26:29], v[138:141], v[186:189], v[26:29]
	v_mfma_f32_16x16x32_bf16 v[14:17], v[146:149], v[186:189], v[14:17]
	v_mfma_f32_16x16x32_bf16 v[10:13], v[138:141], v[182:185], v[10:13]
	v_mfma_f32_16x16x32_bf16 v[6:9], v[146:149], v[182:185], v[6:9]
	s_setprio 0
.LBB0_249:
	s_barrier
	v_add_u32_e32 v3, 0x18000, v217
	ds_read_b128 v[150:153], v3
	ds_read_b128 v[154:157], v3 offset:1024
	ds_read_b128 v[158:161], v3 offset:2048
	ds_read_b128 v[162:165], v3 offset:3072
	v_add_u32_e32 v3, 0x1c000, v217
	ds_read_b128 v[134:137], v3
	ds_read_b128 v[138:141], v3 offset:1024
	ds_read_b128 v[142:145], v3 offset:2048
	ds_read_b128 v[146:149], v3 offset:3072
	s_add_u32 s67, s69, s67
	s_addc_u32 s69, s68, 0
	s_add_u32 s68, s67, 0x40000
	s_addc_u32 s69, s69, 0
	s_mov_b32 m0, s48
	v_lshl_add_u64 v[222:223], s[68:69], 0, v[198:199]
	s_waitcnt lgkmcnt(0)
	ds_read_b128 v[178:181], v220 offset:32768
	ds_read_b128 v[194:197], v220 offset:33792
	ds_read_b128 v[174:177], v220 offset:34816
	ds_read_b128 v[190:193], v220 offset:35840
	ds_read_b128 v[170:173], v220 offset:36864
	ds_read_b128 v[186:189], v220 offset:37888
	ds_read_b128 v[166:169], v220 offset:38912
	ds_read_b128 v[182:185], v220 offset:39936
	global_load_lds_dwordx4 v[222:223], off
	v_lshl_add_u64 v[222:223], s[68:69], 0, v[200:201]
	s_mov_b32 m0, s49
	s_nop 0
	global_load_lds_dwordx4 v[222:223], off
	s_waitcnt lgkmcnt(0)
	s_barrier
	s_setprio 1
	s_waitcnt lgkmcnt(0)
	v_mfma_f32_16x16x32_bf16 v[130:133], v[150:153], v[178:181], v[130:133]
	v_mfma_f32_16x16x32_bf16 v[126:129], v[158:161], v[178:181], v[126:129]
	v_mfma_f32_16x16x32_bf16 v[114:117], v[150:153], v[174:177], v[114:117]
	v_mfma_f32_16x16x32_bf16 v[110:113], v[158:161], v[174:177], v[110:113]
	v_mfma_f32_16x16x32_bf16 v[98:101], v[150:153], v[170:173], v[98:101]
	v_mfma_f32_16x16x32_bf16 v[94:97], v[158:161], v[170:173], v[94:97]
	v_mfma_f32_16x16x32_bf16 v[82:85], v[150:153], v[166:169], v[82:85]
	v_mfma_f32_16x16x32_bf16 v[78:81], v[158:161], v[166:169], v[78:81]
	v_mfma_f32_16x16x32_bf16 v[130:133], v[154:157], v[194:197], v[130:133]
	v_mfma_f32_16x16x32_bf16 v[126:129], v[162:165], v[194:197], v[126:129]
	v_mfma_f32_16x16x32_bf16 v[114:117], v[154:157], v[190:193], v[114:117]
	v_mfma_f32_16x16x32_bf16 v[110:113], v[162:165], v[190:193], v[110:113]
	v_mfma_f32_16x16x32_bf16 v[98:101], v[154:157], v[186:189], v[98:101]
	v_mfma_f32_16x16x32_bf16 v[94:97], v[162:165], v[186:189], v[94:97]
	v_mfma_f32_16x16x32_bf16 v[82:85], v[154:157], v[182:185], v[82:85]
	v_mfma_f32_16x16x32_bf16 v[78:81], v[162:165], v[182:185], v[78:81]
	v_mfma_f32_16x16x32_bf16 v[122:125], v[134:137], v[178:181], v[122:125]
	v_mfma_f32_16x16x32_bf16 v[118:121], v[142:145], v[178:181], v[118:121]
	v_mfma_f32_16x16x32_bf16 v[106:109], v[134:137], v[174:177], v[106:109]
	v_mfma_f32_16x16x32_bf16 v[102:105], v[142:145], v[174:177], v[102:105]
	v_mfma_f32_16x16x32_bf16 v[90:93], v[134:137], v[170:173], v[90:93]
	v_mfma_f32_16x16x32_bf16 v[86:89], v[142:145], v[170:173], v[86:89]
	v_mfma_f32_16x16x32_bf16 v[74:77], v[134:137], v[166:169], v[74:77]
	v_mfma_f32_16x16x32_bf16 v[70:73], v[142:145], v[166:169], v[70:73]
	v_mfma_f32_16x16x32_bf16 v[122:125], v[138:141], v[194:197], v[122:125]
	v_mfma_f32_16x16x32_bf16 v[118:121], v[146:149], v[194:197], v[118:121]
	v_mfma_f32_16x16x32_bf16 v[106:109], v[138:141], v[190:193], v[106:109]
	v_mfma_f32_16x16x32_bf16 v[102:105], v[146:149], v[190:193], v[102:105]
	v_mfma_f32_16x16x32_bf16 v[90:93], v[138:141], v[186:189], v[90:93]
	v_mfma_f32_16x16x32_bf16 v[86:89], v[146:149], v[186:189], v[86:89]
	v_mfma_f32_16x16x32_bf16 v[74:77], v[138:141], v[182:185], v[74:77]
	v_mfma_f32_16x16x32_bf16 v[70:73], v[146:149], v[182:185], v[70:73]
	s_setprio 0
	s_barrier
	s_and_b64 vcc, exec, s[4:5]
	s_cbranch_vccnz .LBB0_251
	ds_read_b128 v[178:181], v220 offset:49152
	ds_read_b128 v[194:197], v220 offset:50176
	ds_read_b128 v[174:177], v220 offset:51200
	ds_read_b128 v[190:193], v220 offset:52224
	ds_read_b128 v[170:173], v220 offset:53248
	ds_read_b128 v[186:189], v220 offset:54272
	ds_read_b128 v[166:169], v220 offset:55296
	ds_read_b128 v[182:185], v220 offset:56320
; #define G8_STAGE_B(bufoff, gbase) do { _Pragma("unroll") for (int _i = 0; _i < 2; ++_i) \
;         __builtin_amdgcn_global_load_lds((const unsigned*)((const char*)(gbase) + voffB[_i]), (LAS unsigned*)(lds + (bufoff) + ldsw + _i * 8192), 16, 0, 0); } while (0)
; #define G8_LDA(dst, b, h) do { _Pragma("unroll") for (int m = 0; m < 4; ++m) _Pragma("unroll") for (int k = 0; k < 2; ++k) dst[m][k] = *(const LAS bf16x8*)(lds + G8_SA(b, h) + aoff + m * 2048 + k * 1024); } while (0)
; #define G8_MMA(ai, bj, At, Bt) do { __builtin_amdgcn_s_setprio(1); _Pragma("unroll") for (int m = 0; m < 4; ++m) _Pragma("unroll") for (int n = 0; n < 2; ++n) _Pragma("unroll") for (int k = 0; k < 2; ++k) \
;         acc[ai][bj][m][n] = __builtin_amdgcn_mfma_f32_16x16x32_bf16(Bt[n][k], At[m][k], acc[ai][bj][m][n], 0, 0, 0); __builtin_amdgcn_s_setprio(0); } while (0)
; #define G8_WAIT_V(n) asm volatile("s_waitcnt vmcnt(" #n ")" ::: "memory")
; #define G8_WAIT_L(n) asm volatile("s_waitcnt lgkmcnt(" #n ")" ::: "memory")
; #define G8_BAR __builtin_amdgcn_s_barrier()
; #define G8_SCHED __builtin_amdgcn_sched_barrier(0)
; template <class Sched, class Epi>
; DEVI void gemm_phase(LAS unsigned char* lds, const char* Abase, const int K, const Sched& S, const Epi& E) {
;     ...
;             if (!skip1) G8_LDA(At, 1, 1); G8_STAGE_B(G8_SB(1, 0), b3); G8_STAGE_A(G8_SA(1, 0), last, 0, k3); G8_STAGE_B(G8_SB(1, 1), b3 + hstepB);
;             G8_WAIT_V(6); G8_WAIT_L(0); G8_BAR; if (!skip1) { G8_MMA(1, 0, At, B0); G8_MMA(1, 1, At, B1); } G8_BAR; G8_SCHED;
.LBB0_251:
	s_mov_b32 m0, s51
	v_lshl_add_u64 v[4:5], v[4:5], 0, s[16:17]
	global_load_lds_dwordx4 v[4:5], off
	v_lshl_add_u64 v[4:5], v[210:211], 0, s[16:17]
	s_mov_b32 m0, s52
	s_add_u32 s40, s40, 0x40080
	global_load_lds_dwordx4 v[4:5], off
	v_lshl_add_u64 v[4:5], v[212:213], 0, s[16:17]
	s_mov_b32 m0, s53
	s_addc_u32 s41, s41, 0
	global_load_lds_dwordx4 v[4:5], off
	v_lshl_add_u64 v[4:5], v[214:215], 0, s[16:17]
	s_mov_b32 m0, s54
	s_and_b64 vcc, exec, s[4:5]
	global_load_lds_dwordx4 v[4:5], off
	v_lshl_add_u64 v[4:5], s[40:41], 0, v[198:199]
	s_mov_b32 m0, s55
	s_nop 0
	global_load_lds_dwordx4 v[4:5], off
	v_lshl_add_u64 v[4:5], s[40:41], 0, v[200:201]
	s_mov_b32 m0, s56
	s_nop 0
	global_load_lds_dwordx4 v[4:5], off
	s_waitcnt vmcnt(6)
	s_waitcnt lgkmcnt(0)
	s_barrier
	s_cbranch_vccnz .LBB0_253
	s_setprio 1
	s_waitcnt lgkmcnt(0)
	v_mfma_f32_16x16x32_bf16 v[66:69], v[150:153], v[178:181], v[66:69]
	v_mfma_f32_16x16x32_bf16 v[62:65], v[158:161], v[178:181], v[62:65]
	v_mfma_f32_16x16x32_bf16 v[50:53], v[150:153], v[174:177], v[50:53]
	v_mfma_f32_16x16x32_bf16 v[46:49], v[158:161], v[174:177], v[46:49]
	v_mfma_f32_16x16x32_bf16 v[34:37], v[150:153], v[170:173], v[34:37]
	v_mfma_f32_16x16x32_bf16 v[30:33], v[158:161], v[170:173], v[30:33]
	v_mfma_f32_16x16x32_bf16 v[22:25], v[150:153], v[166:169], v[22:25]
	v_mfma_f32_16x16x32_bf16 v[18:21], v[158:161], v[166:169], v[18:21]
	v_mfma_f32_16x16x32_bf16 v[66:69], v[154:157], v[194:197], v[66:69]
	v_mfma_f32_16x16x32_bf16 v[62:65], v[162:165], v[194:197], v[62:65]
	v_mfma_f32_16x16x32_bf16 v[50:53], v[154:157], v[190:193], v[50:53]
	v_mfma_f32_16x16x32_bf16 v[46:49], v[162:165], v[190:193], v[46:49]
	v_mfma_f32_16x16x32_bf16 v[34:37], v[154:157], v[186:189], v[34:37]
	v_mfma_f32_16x16x32_bf16 v[30:33], v[162:165], v[186:189], v[30:33]
	v_mfma_f32_16x16x32_bf16 v[22:25], v[154:157], v[182:185], v[22:25]
	v_mfma_f32_16x16x32_bf16 v[18:21], v[162:165], v[182:185], v[18:21]
	v_mfma_f32_16x16x32_bf16 v[58:61], v[134:137], v[178:181], v[58:61]
	v_mfma_f32_16x16x32_bf16 v[54:57], v[142:145], v[178:181], v[54:57]
	v_mfma_f32_16x16x32_bf16 v[42:45], v[134:137], v[174:177], v[42:45]
	v_mfma_f32_16x16x32_bf16 v[38:41], v[142:145], v[174:177], v[38:41]
	v_mfma_f32_16x16x32_bf16 v[26:29], v[134:137], v[170:173], v[26:29]
	v_mfma_f32_16x16x32_bf16 v[14:17], v[142:145], v[170:173], v[14:17]
	v_mfma_f32_16x16x32_bf16 v[10:13], v[134:137], v[166:169], v[10:13]
	v_mfma_f32_16x16x32_bf16 v[4:7], v[142:145], v[166:169], v[6:9]
	v_mfma_f32_16x16x32_bf16 v[58:61], v[138:141], v[194:197], v[58:61]
	v_mfma_f32_16x16x32_bf16 v[54:57], v[146:149], v[194:197], v[54:57]
	v_mfma_f32_16x16x32_bf16 v[42:45], v[138:141], v[190:193], v[42:45]
	v_mfma_f32_16x16x32_bf16 v[38:41], v[146:149], v[190:193], v[38:41]
	v_mfma_f32_16x16x32_bf16 v[26:29], v[138:141], v[186:189], v[26:29]
	v_mfma_f32_16x16x32_bf16 v[14:17], v[146:149], v[186:189], v[14:17]
	v_mfma_f32_16x16x32_bf16 v[10:13], v[138:141], v[182:185], v[10:13]
	v_mfma_f32_16x16x32_bf16 v[6:9], v[146:149], v[182:185], v[4:7]
	s_setprio 0

; #define G8_STAGE_B(bufoff, gbase) do { _Pragma("unroll") for (int _i = 0; _i < 2; ++_i) \
;         __builtin_amdgcn_global_load_lds((const unsigned*)((const char*)(gbase) + voffB[_i]), (LAS unsigned*)(lds + (bufoff) + ldsw + _i * 8192), 16, 0, 0); } while (0)
; #define G8_LDA(dst, b, h) do { _Pragma("unroll") for (int m = 0; m < 4; ++m) _Pragma("unroll") for (int k = 0; k < 2; ++k) dst[m][k] = *(const LAS bf16x8*)(lds + G8_SA(b, h) + aoff + m * 2048 + k * 1024); } while (0)
; #define G8_LDB(dst, b, h) do { _Pragma("unroll") for (int n = 0; n < 2; ++n) _Pragma("unroll") for (int k = 0; k < 2; ++k) dst[n][k] = *(const LAS bf16x8*)(lds + G8_SB(b, h) + boff + n * 2048 + k * 1024); } while (0)
; #define G8_WAIT_V(n) asm volatile("s_waitcnt vmcnt(" #n ")" ::: "memory")
; #define G8_WAIT_L(n) asm volatile("s_waitcnt lgkmcnt(" #n ")" ::: "memory")
; #define G8_BAR __builtin_amdgcn_s_barrier()
; template <class Sched, class Epi>
; DEVI void gemm_phase(LAS unsigned char* lds, const char* Abase, const int K, const Sched& S, const Epi& E) {
;     ...
;         for (int t = 0; t < ntu; t += 2) {
;             const bool last = (t == ntu - 2);
;             const size_t k1 = (size_t)(t + 1) * kstep;
;             const size_t k2 = last ? (size_t)0 : (size_t)(t + 2) * kstep, k3 = k2 + kstep;
;             const char* b2 = last ? nB : cB + (size_t)(t + 2) * kstep; const char* b3 = b2 + kstep;
;             G8_LDB(B0, 0, 0); G8_LDB(B1, 0, 1); G8_SCHED; G8_LDA(At, 0, 0); G8_STAGE_A(G8_SA(1, 1), false, 1, k1);
;             G8_WAIT_L(0); G8_BAR; G8_MMA(0, 0, At, B0); G8_MMA(0, 1, At, B1); G8_BAR; G8_SCHED;
;             if (!skip1) G8_LDA(At, 0, 1); G8_STAGE_B(G8_SB(0, 0), b2); G8_STAGE_A(G8_SA(0, 0), last, 0, k2); G8_STAGE_B(G8_SB(0, 1), b2 + hstepB);
;             G8_WAIT_V(6); G8_WAIT_L(0); G8_BAR; if (!skip1) { G8_MMA(1, 0, At, B0); G8_MMA(1, 1, At, B1); } G8_BAR; G8_SCHED;
;             G8_LDB(B0, 1, 0); G8_LDB(B1, 1, 1); G8_SCHED; G8_LDA(At, 1, 0); G8_STAGE_A(G8_SA(0, 1), last, 1, k2);
;             G8_WAIT_L(0); G8_BAR; G8_MMA(0, 0, At, B0); G8_MMA(0, 1, At, B1); G8_BAR; G8_SCHED;
;             if (!skip1) G8_LDA(At, 1, 1); G8_STAGE_B(G8_SB(1, 0), b3); G8_STAGE_A(G8_SA(1, 0), last, 0, k3); G8_STAGE_B(G8_SB(1, 1), b3 + hstepB);
;             G8_WAIT_V(6); G8_WAIT_L(0); G8_BAR; if (!skip1) { G8_MMA(1, 0, At, B0); G8_MMA(1, 1, At, B1); } G8_BAR; G8_SCHED;
.LBB0_473:
	ds_read_b128 v[148:151], v154
	ds_read_b128 v[158:161], v154 offset:1024
	ds_read_b128 v[162:165], v154 offset:2048
	ds_read_b128 v[166:169], v154 offset:3072
	ds_read_b128 v[170:173], v155
	ds_read_b128 v[174:177], v155 offset:1024
	ds_read_b128 v[178:181], v155 offset:2048
	ds_read_b128 v[182:185], v155 offset:3072
	s_add_i32 s66, s44, 2
	s_add_u32 s67, s42, 0xfff90080
	s_addc_u32 s68, s43, -1
	s_add_u32 s45, s6, s42
	s_addc_u32 s69, s7, s43
	s_add_u32 s70, s45, 0xfff90080
	s_addc_u32 s45, s69, -1
	s_add_i32 s71, s60, s48
	s_add_i32 m0, s50, 0xc000
	s_add_i32 s69, s50, 0xe000
	s_add_i32 s72, s71, 0x2000
	s_cmp_eq_u32 s27, s44
	s_cselect_b32 s44, s30, s70
	s_cselect_b32 s45, s31, s45
	s_cselect_b32 s70, 0, s68
	s_cselect_b32 s67, 0, s67
	v_lshl_add_u64 v[218:219], v[144:145], 0, s[42:43]
	ds_read_b128 v[186:189], v156
	ds_read_b128 v[190:193], v156 offset:1024
	ds_read_b128 v[194:197], v156 offset:2048
	ds_read_b128 v[198:201], v156 offset:3072
	ds_read_b128 v[202:205], v156 offset:4096
	ds_read_b128 v[206:209], v156 offset:5120
	ds_read_b128 v[210:213], v156 offset:6144
	ds_read_b128 v[214:217], v156 offset:7168
	global_load_lds_dwordx4 v[218:219], off
	v_lshl_add_u64 v[218:219], v[146:147], 0, s[42:43]
	s_mov_b32 m0, s69
	s_nop 0
	global_load_lds_dwordx4 v[218:219], off
	s_waitcnt lgkmcnt(0)
	s_barrier
	s_setprio 1
	s_waitcnt lgkmcnt(0)
	v_mfma_f32_16x16x32_bf16 v[126:129], v[148:151], v[186:189], v[126:129]
	v_mfma_f32_16x16x32_bf16 v[122:125], v[162:165], v[186:189], v[122:125]
	v_mfma_f32_16x16x32_bf16 v[110:113], v[148:151], v[194:197], v[110:113]
	v_mfma_f32_16x16x32_bf16 v[106:109], v[162:165], v[194:197], v[106:109]
	v_mfma_f32_16x16x32_bf16 v[94:97], v[148:151], v[202:205], v[94:97]
	v_mfma_f32_16x16x32_bf16 v[90:93], v[162:165], v[202:205], v[90:93]
	v_mfma_f32_16x16x32_bf16 v[78:81], v[148:151], v[210:213], v[78:81]
	v_mfma_f32_16x16x32_bf16 v[74:77], v[162:165], v[210:213], v[74:77]
	v_mfma_f32_16x16x32_bf16 v[126:129], v[158:161], v[190:193], v[126:129]
	v_mfma_f32_16x16x32_bf16 v[122:125], v[166:169], v[190:193], v[122:125]
	v_mfma_f32_16x16x32_bf16 v[110:113], v[158:161], v[198:201], v[110:113]
	v_mfma_f32_16x16x32_bf16 v[106:109], v[166:169], v[198:201], v[106:109]
	v_mfma_f32_16x16x32_bf16 v[94:97], v[158:161], v[206:209], v[94:97]
	v_mfma_f32_16x16x32_bf16 v[90:93], v[166:169], v[206:209], v[90:93]
	v_mfma_f32_16x16x32_bf16 v[78:81], v[158:161], v[214:217], v[78:81]
	v_mfma_f32_16x16x32_bf16 v[74:77], v[166:169], v[214:217], v[74:77]
	v_mfma_f32_16x16x32_bf16 v[118:121], v[170:173], v[186:189], v[118:121]
	v_mfma_f32_16x16x32_bf16 v[114:117], v[178:181], v[186:189], v[114:117]
	v_mfma_f32_16x16x32_bf16 v[102:105], v[170:173], v[194:197], v[102:105]
	v_mfma_f32_16x16x32_bf16 v[98:101], v[178:181], v[194:197], v[98:101]
	v_mfma_f32_16x16x32_bf16 v[86:89], v[170:173], v[202:205], v[86:89]
	v_mfma_f32_16x16x32_bf16 v[82:85], v[178:181], v[202:205], v[82:85]
	v_mfma_f32_16x16x32_bf16 v[70:73], v[170:173], v[210:213], v[70:73]
	v_mfma_f32_16x16x32_bf16 v[66:69], v[178:181], v[210:213], v[66:69]
	v_mfma_f32_16x16x32_bf16 v[118:121], v[174:177], v[190:193], v[118:121]
	v_mfma_f32_16x16x32_bf16 v[114:117], v[182:185], v[190:193], v[114:117]
	v_mfma_f32_16x16x32_bf16 v[102:105], v[174:177], v[198:201], v[102:105]
	v_mfma_f32_16x16x32_bf16 v[98:101], v[182:185], v[198:201], v[98:101]
	v_mfma_f32_16x16x32_bf16 v[86:89], v[174:177], v[206:209], v[86:89]
	v_mfma_f32_16x16x32_bf16 v[82:85], v[182:185], v[206:209], v[82:85]
	v_mfma_f32_16x16x32_bf16 v[70:73], v[174:177], v[214:217], v[70:73]
	v_mfma_f32_16x16x32_bf16 v[66:69], v[182:185], v[214:217], v[66:69]
	s_setprio 0
	s_barrier
	s_cselect_b32 s68, s34, s38
	s_mov_b32 m0, s71
	v_lshl_add_u64 v[218:219], s[44:45], 0, v[130:131]
	s_cselect_b32 s69, s35, s39
	s_add_u32 s68, s68, s67
	ds_read_b128 v[186:189], v156 offset:16384
	ds_read_b128 v[190:193], v156 offset:17408
	ds_read_b128 v[194:197], v156 offset:18432
	ds_read_b128 v[198:201], v156 offset:19456
	ds_read_b128 v[202:205], v156 offset:20480
	ds_read_b128 v[206:209], v156 offset:21504
	ds_read_b128 v[210:213], v156 offset:22528
	ds_read_b128 v[214:217], v156 offset:23552
	global_load_lds_dwordx4 v[218:219], off
	v_lshl_add_u64 v[220:221], s[44:45], 0, v[132:133]
	s_mov_b32 m0, s72
	s_addc_u32 s69, s69, s70
	global_load_lds_dwordx4 v[220:221], off
	v_lshl_add_u64 v[222:223], s[68:69], 0, v[134:135]
	s_mov_b32 m0, s50
	s_add_u32 s70, s44, 0x10000
	global_load_lds_dwordx4 v[222:223], off
	v_lshl_add_u64 v[224:225], s[68:69], 0, v[136:137]
	s_mov_b32 m0, s51
	s_addc_u32 s71, s45, 0
	s_add_i32 s67, s61, s48
	global_load_lds_dwordx4 v[224:225], off
	v_lshl_add_u64 v[226:227], s[70:71], 0, v[130:131]
	s_mov_b32 m0, s67
	s_nop 0
	global_load_lds_dwordx4 v[226:227], off
	v_lshl_add_u64 v[226:227], s[70:71], 0, v[132:133]
	s_add_i32 m0, s67, 0x2000
	s_nop 0
	global_load_lds_dwordx4 v[226:227], off
	s_waitcnt vmcnt(6)
	s_waitcnt lgkmcnt(0)
	s_barrier
; #define G8_STAGE_B(bufoff, gbase) do { _Pragma("unroll") for (int _i = 0; _i < 2; ++_i) \
;         __builtin_amdgcn_global_load_lds((const unsigned*)((const char*)(gbase) + voffB[_i]), (LAS unsigned*)(lds + (bufoff) + ldsw + _i * 8192), 16, 0, 0); } while (0)
; #define G8_LDA(dst, b, h) do { _Pragma("unroll") for (int m = 0; m < 4; ++m) _Pragma("unroll") for (int k = 0; k < 2; ++k) dst[m][k] = *(const LAS bf16x8*)(lds + G8_SA(b, h) + aoff + m * 2048 + k * 1024); } while (0)
; #define G8_LDB(dst, b, h) do { _Pragma("unroll") for (int n = 0; n < 2; ++n) _Pragma("unroll") for (int k = 0; k < 2; ++k) dst[n][k] = *(const LAS bf16x8*)(lds + G8_SB(b, h) + boff + n * 2048 + k * 1024); } while (0)
; #define G8_WAIT_V(n) asm volatile("s_waitcnt vmcnt(" #n ")" ::: "memory")
; #define G8_WAIT_L(n) asm volatile("s_waitcnt lgkmcnt(" #n ")" ::: "memory")
; #define G8_BAR __builtin_amdgcn_s_barrier()
; template <class Sched, class Epi>
; DEVI void gemm_phase(LAS unsigned char* lds, const char* Abase, const int K, const Sched& S, const Epi& E) {
;     ...
;         for (int t = 0; t < ntu; t += 2) {
;             const bool last = (t == ntu - 2);
;             const size_t k1 = (size_t)(t + 1) * kstep;
;             const size_t k2 = last ? (size_t)0 : (size_t)(t + 2) * kstep, k3 = k2 + kstep;
;             const char* b2 = last ? nB : cB + (size_t)(t + 2) * kstep; const char* b3 = b2 + kstep;
;             G8_LDB(B0, 0, 0); G8_LDB(B1, 0, 1); G8_SCHED; G8_LDA(At, 0, 0); G8_STAGE_A(G8_SA(1, 1), false, 1, k1);
;             G8_WAIT_L(0); G8_BAR; G8_MMA(0, 0, At, B0); G8_MMA(0, 1, At, B1); G8_BAR; G8_SCHED;
;             if (!skip1) G8_LDA(At, 0, 1); G8_STAGE_B(G8_SB(0, 0), b2); G8_STAGE_A(G8_SA(0, 0), last, 0, k2); G8_STAGE_B(G8_SB(0, 1), b2 + hstepB);
;             G8_WAIT_V(6); G8_WAIT_L(0); G8_BAR; if (!skip1) { G8_MMA(1, 0, At, B0); G8_MMA(1, 1, At, B1); } G8_BAR; G8_SCHED;
;             G8_LDB(B0, 1, 0); G8_LDB(B1, 1, 1); G8_SCHED; G8_LDA(At, 1, 0); G8_STAGE_A(G8_SA(0, 1), last, 1, k2);
;             G8_WAIT_L(0); G8_BAR; G8_MMA(0, 0, At, B0); G8_MMA(0, 1, At, B1); G8_BAR; G8_SCHED;
;             if (!skip1) G8_LDA(At, 1, 1); G8_STAGE_B(G8_SB(1, 0), b3); G8_STAGE_A(G8_SA(1, 0), last, 0, k3); G8_STAGE_B(G8_SB(1, 1), b3 + hstepB);
;             G8_WAIT_V(6); G8_WAIT_L(0); G8_BAR; if (!skip1) { G8_MMA(1, 0, At, B0); G8_MMA(1, 1, At, B1); } G8_BAR; G8_SCHED;
	s_setprio 1
	s_waitcnt lgkmcnt(0)
	v_mfma_f32_16x16x32_bf16 v[62:65], v[148:151], v[186:189], v[62:65]
	v_mfma_f32_16x16x32_bf16 v[58:61], v[162:165], v[186:189], v[58:61]
	v_mfma_f32_16x16x32_bf16 v[46:49], v[148:151], v[194:197], v[46:49]
	v_mfma_f32_16x16x32_bf16 v[42:45], v[162:165], v[194:197], v[42:45]
	v_mfma_f32_16x16x32_bf16 v[30:33], v[148:151], v[202:205], v[30:33]
	v_mfma_f32_16x16x32_bf16 v[26:29], v[162:165], v[202:205], v[26:29]
	v_mfma_f32_16x16x32_bf16 v[14:17], v[148:151], v[210:213], v[14:17]
	v_mfma_f32_16x16x32_bf16 v[10:13], v[162:165], v[210:213], v[10:13]
	v_mfma_f32_16x16x32_bf16 v[62:65], v[158:161], v[190:193], v[62:65]
	v_mfma_f32_16x16x32_bf16 v[58:61], v[166:169], v[190:193], v[58:61]
	v_mfma_f32_16x16x32_bf16 v[46:49], v[158:161], v[198:201], v[46:49]
	v_mfma_f32_16x16x32_bf16 v[42:45], v[166:169], v[198:201], v[42:45]
	v_mfma_f32_16x16x32_bf16 v[30:33], v[158:161], v[206:209], v[30:33]
	v_mfma_f32_16x16x32_bf16 v[26:29], v[166:169], v[206:209], v[26:29]
	v_mfma_f32_16x16x32_bf16 v[14:17], v[158:161], v[214:217], v[14:17]
	v_mfma_f32_16x16x32_bf16 v[10:13], v[166:169], v[214:217], v[10:13]
	v_mfma_f32_16x16x32_bf16 v[54:57], v[170:173], v[186:189], v[54:57]
	v_mfma_f32_16x16x32_bf16 v[50:53], v[178:181], v[186:189], v[50:53]
	v_mfma_f32_16x16x32_bf16 v[38:41], v[170:173], v[194:197], v[38:41]
	v_mfma_f32_16x16x32_bf16 v[34:37], v[178:181], v[194:197], v[34:37]
	v_mfma_f32_16x16x32_bf16 v[22:25], v[170:173], v[202:205], v[22:25]
	v_mfma_f32_16x16x32_bf16 v[18:21], v[178:181], v[202:205], v[18:21]
	v_mfma_f32_16x16x32_bf16 v[6:9], v[170:173], v[210:213], v[6:9]
	v_mfma_f32_16x16x32_bf16 v[2:5], v[178:181], v[210:213], v[2:5]
	v_mfma_f32_16x16x32_bf16 v[54:57], v[174:177], v[190:193], v[54:57]
	v_mfma_f32_16x16x32_bf16 v[50:53], v[182:185], v[190:193], v[50:53]
	v_mfma_f32_16x16x32_bf16 v[38:41], v[174:177], v[198:201], v[38:41]
	v_mfma_f32_16x16x32_bf16 v[34:37], v[182:185], v[198:201], v[34:37]
	v_mfma_f32_16x16x32_bf16 v[22:25], v[174:177], v[206:209], v[22:25]
	v_mfma_f32_16x16x32_bf16 v[18:21], v[182:185], v[206:209], v[18:21]
	v_mfma_f32_16x16x32_bf16 v[6:9], v[174:177], v[214:217], v[6:9]
	v_mfma_f32_16x16x32_bf16 v[2:5], v[182:185], v[214:217], v[2:5]
	s_setprio 0
	s_barrier
	s_add_i32 s67, 0, 0x18000
	v_add_u32_e32 v138, s67, v153
	s_add_i32 s70, 0, 0x1c000
	ds_read_b128 v[148:151], v138
	ds_read_b128 v[158:161], v138 offset:1024
	ds_read_b128 v[162:165], v138 offset:2048
	ds_read_b128 v[166:169], v138 offset:3072
	v_add_u32_e32 v138, s70, v153
	ds_read_b128 v[170:173], v138
	ds_read_b128 v[174:177], v138 offset:1024
	ds_read_b128 v[178:181], v138 offset:2048
	ds_read_b128 v[182:185], v138 offset:3072
	s_add_u32 s68, s68, 0x70000
	s_addc_u32 s69, s69, 0
	s_mov_b32 m0, s52
	v_lshl_add_u64 v[226:227], s[68:69], 0, v[134:135]
	ds_read_b128 v[186:189], v156 offset:32768
	ds_read_b128 v[190:193], v156 offset:33792
	ds_read_b128 v[194:197], v156 offset:34816
	ds_read_b128 v[198:201], v156 offset:35840
	ds_read_b128 v[202:205], v156 offset:36864
	ds_read_b128 v[206:209], v156 offset:37888
	ds_read_b128 v[210:213], v156 offset:38912
	ds_read_b128 v[214:217], v156 offset:39936
	global_load_lds_dwordx4 v[226:227], off
	v_lshl_add_u64 v[226:227], s[68:69], 0, v[136:137]
	s_mov_b32 m0, s53
	s_nop 0
	global_load_lds_dwordx4 v[226:227], off
	s_waitcnt lgkmcnt(0)
	s_barrier
	s_setprio 1
	s_waitcnt lgkmcnt(0)
	v_mfma_f32_16x16x32_bf16 v[126:129], v[148:151], v[186:189], v[126:129]
	v_mfma_f32_16x16x32_bf16 v[122:125], v[162:165], v[186:189], v[122:125]
	v_mfma_f32_16x16x32_bf16 v[110:113], v[148:151], v[194:197], v[110:113]
	v_mfma_f32_16x16x32_bf16 v[106:109], v[162:165], v[194:197], v[106:109]
	v_mfma_f32_16x16x32_bf16 v[94:97], v[148:151], v[202:205], v[94:97]
	v_mfma_f32_16x16x32_bf16 v[90:93], v[162:165], v[202:205], v[90:93]
	v_mfma_f32_16x16x32_bf16 v[78:81], v[148:151], v[210:213], v[78:81]
	v_mfma_f32_16x16x32_bf16 v[74:77], v[162:165], v[210:213], v[74:77]
	v_mfma_f32_16x16x32_bf16 v[126:129], v[158:161], v[190:193], v[126:129]
	v_mfma_f32_16x16x32_bf16 v[122:125], v[166:169], v[190:193], v[122:125]
	v_mfma_f32_16x16x32_bf16 v[110:113], v[158:161], v[198:201], v[110:113]
	v_mfma_f32_16x16x32_bf16 v[106:109], v[166:169], v[198:201], v[106:109]
	v_mfma_f32_16x16x32_bf16 v[94:97], v[158:161], v[206:209], v[94:97]
	v_mfma_f32_16x16x32_bf16 v[90:93], v[166:169], v[206:209], v[90:93]
	v_mfma_f32_16x16x32_bf16 v[78:81], v[158:161], v[214:217], v[78:81]
	v_mfma_f32_16x16x32_bf16 v[74:77], v[166:169], v[214:217], v[74:77]
	v_mfma_f32_16x16x32_bf16 v[118:121], v[170:173], v[186:189], v[118:121]
	v_mfma_f32_16x16x32_bf16 v[114:117], v[178:181], v[186:189], v[114:117]
	v_mfma_f32_16x16x32_bf16 v[102:105], v[170:173], v[194:197], v[102:105]
	v_mfma_f32_16x16x32_bf16 v[98:101], v[178:181], v[194:197], v[98:101]
	v_mfma_f32_16x16x32_bf16 v[86:89], v[170:173], v[202:205], v[86:89]
	v_mfma_f32_16x16x32_bf16 v[82:85], v[178:181], v[202:205], v[82:85]
	v_mfma_f32_16x16x32_bf16 v[70:73], v[170:173], v[210:213], v[70:73]
	v_mfma_f32_16x16x32_bf16 v[66:69], v[178:181], v[210:213], v[66:69]
	v_mfma_f32_16x16x32_bf16 v[118:121], v[174:177], v[190:193], v[118:121]
	v_mfma_f32_16x16x32_bf16 v[114:117], v[182:185], v[190:193], v[114:117]
	v_mfma_f32_16x16x32_bf16 v[102:105], v[174:177], v[198:201], v[102:105]
	v_mfma_f32_16x16x32_bf16 v[98:101], v[182:185], v[198:201], v[98:101]
	v_mfma_f32_16x16x32_bf16 v[86:89], v[174:177], v[206:209], v[86:89]
	v_mfma_f32_16x16x32_bf16 v[82:85], v[182:185], v[206:209], v[82:85]
	v_mfma_f32_16x16x32_bf16 v[70:73], v[174:177], v[214:217], v[70:73]
	v_mfma_f32_16x16x32_bf16 v[66:69], v[182:185], v[214:217], v[66:69]
	s_setprio 0
	s_barrier
; #define G8_STAGE_B(bufoff, gbase) do { _Pragma("unroll") for (int _i = 0; _i < 2; ++_i) \
;         __builtin_amdgcn_global_load_lds((const unsigned*)((const char*)(gbase) + voffB[_i]), (LAS unsigned*)(lds + (bufoff) + ldsw + _i * 8192), 16, 0, 0); } while (0)
; #define G8_LDA(dst, b, h) do { _Pragma("unroll") for (int m = 0; m < 4; ++m) _Pragma("unroll") for (int k = 0; k < 2; ++k) dst[m][k] = *(const LAS bf16x8*)(lds + G8_SA(b, h) + aoff + m * 2048 + k * 1024); } while (0)
; #define G8_BAR __builtin_amdgcn_s_barrier()
; template <class Sched, class Epi>
; DEVI void gemm_phase(LAS unsigned char* lds, const char* Abase, const int K, const Sched& S, const Epi& E) {
;     ...
;             G8_WAIT_L(0); G8_BAR; G8_MMA(0, 0, At, B0); G8_MMA(0, 1, At, B1); G8_BAR; G8_SCHED;
;             if (!skip1) G8_LDA(At, 0, 1); G8_STAGE_B(G8_SB(0, 0), b2); G8_STAGE_A(G8_SA(0, 0), last, 0, k2); G8_STAGE_B(G8_SB(0, 1), b2 + hstepB);
;             G8_WAIT_V(6); G8_WAIT_L(0); G8_BAR; if (!skip1) { G8_MMA(1, 0, At, B0); G8_MMA(1, 1, At, B1); } G8_BAR; G8_SCHED;
;             G8_LDB(B0, 1, 0); G8_LDB(B1, 1, 1); G8_SCHED; G8_LDA(At, 1, 0); G8_STAGE_A(G8_SA(0, 1), last, 1, k2);
;             G8_WAIT_L(0); G8_BAR; G8_MMA(0, 0, At, B0); G8_MMA(0, 1, At, B1); G8_BAR; G8_SCHED;
;             if (!skip1) G8_LDA(At, 1, 1); G8_STAGE_B(G8_SB(1, 0), b3); G8_STAGE_A(G8_SA(1, 0), last, 0, k3); G8_STAGE_B(G8_SB(1, 1), b3 + hstepB);
;             G8_WAIT_V(6); G8_WAIT_L(0); G8_BAR; if (!skip1) { G8_MMA(1, 0, At, B0); G8_MMA(1, 1, At, B1); } G8_BAR; G8_SCHED;
; DEVI void phase_gemm_proj(const Params& p, char* smem, int l) {
;     ...
;     auto E = [=](AccRef acc, const ProjSched::Unit& u, int wr, int wc, int fr, int fq) {
;         const int col16 = u.pn * 256 + wc * 64 + fq * 16;
; #pragma unroll
;         ACC_LOOP_ROWS { const int row = u.pm * 256 + ai * 128 + wr * 64 + m * 16 + fr; const float rs = u.kv ? rkv[row] : rq[row]; const int b = row >> 12, s = row & 4095;
;             u32x4 w0, w1; PACK16_BF16(w0, w1, acc, ai, m, rs);
;             bf16_t* dst;
;             if (!u.kv) dst = qbuf + (size_t)row * 768 + col16;
;             else if (col16 < 512) dst = kfull + (((size_t)(b * 8 + (col16 >> 6))) * S_ + s) * 96 + (col16 & 63);
;             else dst = vfull + (((size_t)(b * 8 + ((col16 - 512) >> 6))) * S_ + s) * 64 + (col16 & 63);
;             *(u32x4*)dst = w0; *(u32x4*)(dst + 8) = w1; }
	s_add_i32 s67, s67, s48
	v_lshl_add_u64 v[218:219], v[218:219], 0, s[24:25]
	s_mov_b32 m0, s67
	ds_read_b128 v[186:189], v156 offset:49152
	ds_read_b128 v[190:193], v156 offset:50176
	ds_read_b128 v[194:197], v156 offset:51200
	ds_read_b128 v[198:201], v156 offset:52224
	ds_read_b128 v[202:205], v156 offset:53248
	ds_read_b128 v[206:209], v156 offset:54272
	ds_read_b128 v[210:213], v156 offset:55296
	ds_read_b128 v[214:217], v156 offset:56320
	global_load_lds_dwordx4 v[218:219], off
	v_lshl_add_u64 v[218:219], v[220:221], 0, s[24:25]
	s_add_i32 m0, s67, 0x2000
	s_add_u32 s44, s44, 0x10080
	global_load_lds_dwordx4 v[218:219], off
	v_lshl_add_u64 v[218:219], v[222:223], 0, s[24:25]
	s_mov_b32 m0, s56
	s_addc_u32 s45, s45, 0
	global_load_lds_dwordx4 v[218:219], off
	v_lshl_add_u64 v[218:219], v[224:225], 0, s[24:25]
	s_mov_b32 m0, s57
	s_add_i32 s67, s70, s48
	global_load_lds_dwordx4 v[218:219], off
	v_lshl_add_u64 v[218:219], s[44:45], 0, v[130:131]
	s_mov_b32 m0, s67
	s_nop 0
	global_load_lds_dwordx4 v[218:219], off
	v_lshl_add_u64 v[218:219], s[44:45], 0, v[132:133]
	s_add_i32 m0, s67, 0x2000
	s_nop 0
	global_load_lds_dwordx4 v[218:219], off
	s_waitcnt vmcnt(6)
	s_waitcnt lgkmcnt(0)
	s_barrier
	s_setprio 1
	s_waitcnt lgkmcnt(0)
	v_mfma_f32_16x16x32_bf16 v[62:65], v[148:151], v[186:189], v[62:65]
	v_mfma_f32_16x16x32_bf16 v[58:61], v[162:165], v[186:189], v[58:61]
	v_mfma_f32_16x16x32_bf16 v[46:49], v[148:151], v[194:197], v[46:49]
	v_mfma_f32_16x16x32_bf16 v[42:45], v[162:165], v[194:197], v[42:45]
	v_mfma_f32_16x16x32_bf16 v[30:33], v[148:151], v[202:205], v[30:33]
	v_mfma_f32_16x16x32_bf16 v[26:29], v[162:165], v[202:205], v[26:29]
	v_mfma_f32_16x16x32_bf16 v[14:17], v[148:151], v[210:213], v[14:17]
	v_mfma_f32_16x16x32_bf16 v[10:13], v[162:165], v[210:213], v[10:13]
	v_mfma_f32_16x16x32_bf16 v[62:65], v[158:161], v[190:193], v[62:65]
	v_mfma_f32_16x16x32_bf16 v[58:61], v[166:169], v[190:193], v[58:61]
	v_mfma_f32_16x16x32_bf16 v[46:49], v[158:161], v[198:201], v[46:49]
	v_mfma_f32_16x16x32_bf16 v[42:45], v[166:169], v[198:201], v[42:45]
	v_mfma_f32_16x16x32_bf16 v[30:33], v[158:161], v[206:209], v[30:33]
	v_mfma_f32_16x16x32_bf16 v[26:29], v[166:169], v[206:209], v[26:29]
	v_mfma_f32_16x16x32_bf16 v[14:17], v[158:161], v[214:217], v[14:17]
	v_mfma_f32_16x16x32_bf16 v[10:13], v[166:169], v[214:217], v[10:13]
	v_mfma_f32_16x16x32_bf16 v[54:57], v[170:173], v[186:189], v[54:57]
	v_mfma_f32_16x16x32_bf16 v[50:53], v[178:181], v[186:189], v[50:53]
	v_mfma_f32_16x16x32_bf16 v[38:41], v[170:173], v[194:197], v[38:41]
	v_mfma_f32_16x16x32_bf16 v[34:37], v[178:181], v[194:197], v[34:37]
	v_mfma_f32_16x16x32_bf16 v[22:25], v[170:173], v[202:205], v[22:25]
	v_mfma_f32_16x16x32_bf16 v[18:21], v[178:181], v[202:205], v[18:21]
	v_mfma_f32_16x16x32_bf16 v[6:9], v[170:173], v[210:213], v[6:9]
	v_mfma_f32_16x16x32_bf16 v[2:5], v[178:181], v[210:213], v[2:5]
	v_mfma_f32_16x16x32_bf16 v[54:57], v[174:177], v[190:193], v[54:57]
	v_mfma_f32_16x16x32_bf16 v[50:53], v[182:185], v[190:193], v[50:53]
	v_mfma_f32_16x16x32_bf16 v[38:41], v[174:177], v[198:201], v[38:41]
	v_mfma_f32_16x16x32_bf16 v[34:37], v[182:185], v[198:201], v[34:37]
	v_mfma_f32_16x16x32_bf16 v[22:25], v[174:177], v[206:209], v[22:25]
	v_mfma_f32_16x16x32_bf16 v[18:21], v[182:185], v[206:209], v[18:21]
	v_mfma_f32_16x16x32_bf16 v[6:9], v[174:177], v[214:217], v[6:9]
	v_mfma_f32_16x16x32_bf16 v[2:5], v[182:185], v[214:217], v[2:5]
	s_setprio 0
	s_barrier
	s_add_u32 s42, s42, 0x100
	s_addc_u32 s43, s43, 0
	s_cmp_ge_u32 s66, s5
	s_mov_b32 s44, s66
	s_cbranch_scc0 .LBB0_473
	v_mov_b32_e32 v138, v1
	v_mov_b32_e32 v144, v152
	s_lshl_b32 s4, s4, 8
	s_or_b32 s27, s4, s58
	v_add_u32_e32 v138, s55, v138
	s_lshl_b32 s2, s2, 8
	v_add_u32_e32 v146, s2, v138
	s_and_b64 s[4:5], s[40:41], exec
	v_ashrrev_i32_e32 v147, 31, v146
	s_cselect_b32 s39, s9, s11
	s_cselect_b32 s38, s8, s10
	v_lshl_add_u64 v[148:149], v[146:147], 2, s[38:39]
	global_load_dword v138, v[148:149], off
	v_lshlrev_b32_e32 v145, 4, v144
	v_add_u32_e32 v144, s27, v145
	v_and_b32_e32 v158, 48, v145
	v_add_u32_e32 v145, 0xfffffe00, v144
	s_mov_b64 s[6:7], -1
	s_and_b64 vcc, exec, s[36:37]
	v_cmp_lt_i32_e64 s[4:5], s59, v144
	v_ashrrev_i32_e32 v147, 6, v144
	v_lshrrev_b32_e32 v157, 6, v145
	s_waitcnt vmcnt(0)
	v_pk_mul_f32 v[120:121], v[120:121], v[138:139] op_sel_hi:[1,0]
	v_pk_mul_f32 v[118:119], v[118:119], v[138:139] op_sel_hi:[1,0]
	v_pk_mul_f32 v[128:129], v[128:129], v[138:139] op_sel_hi:[1,0]
	v_pk_mul_f32 v[126:127], v[126:127], v[138:139] op_sel_hi:[1,0]
	v_pk_mul_f32 v[124:125], v[124:125], v[138:139] op_sel_hi:[1,0]
	v_pk_mul_f32 v[122:123], v[122:123], v[138:139] op_sel_hi:[1,0]
	v_pk_mul_f32 v[160:161], v[116:117], v[138:139] op_sel_hi:[1,0]
	v_pk_mul_f32 v[162:163], v[114:115], v[138:139] op_sel_hi:[1,0]
	v_cvt_pk_bf16_f32 v114, v126, v127
	v_cvt_pk_bf16_f32 v115, v128, v129
	v_cvt_pk_bf16_f32 v116, v122, v123
	v_cvt_pk_bf16_f32 v117, v124, v125
	v_cvt_pk_bf16_f32 v118, v118, v119
	v_cvt_pk_bf16_f32 v119, v120, v121
	s_nop 0
	v_cvt_pk_bf16_f32 v120, v162, v163
	v_cvt_pk_bf16_f32 v121, v160, v161
	s_cbranch_vccz .LBB0_480
	v_ashrrev_i32_e32 v123, 9, v146
	v_and_b32_e32 v122, 0xfff, v146
	v_and_b32_e32 v123, -8, v123
	s_and_saveexec_b64 s[6:7], s[4:5]
	s_xor_b64 s[6:7], exec, s[6:7]
	v_add_u32_e32 v124, v123, v157
	v_ashrrev_i32_e32 v125, 31, v124
	v_lshlrev_b64 v[124:125], 19, v[124:125]
	v_lshl_add_u64 v[124:125], s[22:23], 0, v[124:125]
	v_lshlrev_b32_e32 v138, 7, v122
	v_lshl_add_u64 v[122:123], v[124:125], 0, v[138:139]
	v_lshlrev_b32_e32 v138, 1, v158
	v_lshl_add_u64 v[150:151], v[122:123], 0, v[138:139]
	s_andn2_saveexec_b64 s[6:7], s[6:7]
	v_add_u32_e32 v124, v123, v147
	v_ashrrev_i32_e32 v125, 31, v124
	v_lshlrev_b64 v[124:125], 12, v[124:125]
	v_or_b32_e32 v124, v124, v122
	v_mov_b64_e32 v[122:123], s[14:15]
	v_mad_u64_u32 v[122:123], s[40:41], v124, s62, v[122:123]
	v_mad_i32_i24 v123, v125, s62, v123
	v_lshlrev_b32_e32 v138, 1, v158
	v_lshl_add_u64 v[150:151], v[122:123], 0, v[138:139]
	s_or_b64 exec, exec, s[6:7]
	s_mov_b64 s[6:7], 0

; #define SBAR() __builtin_amdgcn_sched_barrier(0)
; DEVI void pv_both(f32x16& o0, f32x16& o1, int vb, bf16x8 pa0, bf16x8 pa1, bf16x8 pa2, bf16x8 pa3) {
;     const s16x4 a0 = tr_read<v_rd_off(0, 0, 0)>(vb), b0 = tr_read<v_rd_off(0, 0, 1)>(vb), a1 = tr_read<v_rd_off(0, 1, 0)>(vb), b1 = tr_read<v_rd_off(0, 1, 1)>(vb);
;     const s16x4 a2 = tr_read<v_rd_off(0, 2, 0)>(vb), b2 = tr_read<v_rd_off(0, 2, 1)>(vb), a3 = tr_read<v_rd_off(0, 3, 0)>(vb), b3 = tr_read<v_rd_off(0, 3, 1)>(vb);
;     const s16x4 c0 = tr_read<v_rd_off(1, 0, 0)>(vb), d0 = tr_read<v_rd_off(1, 0, 1)>(vb), c1 = tr_read<v_rd_off(1, 1, 0)>(vb), d1 = tr_read<v_rd_off(1, 1, 1)>(vb);
;     const s16x4 c2 = tr_read<v_rd_off(1, 2, 0)>(vb), d2 = tr_read<v_rd_off(1, 2, 1)>(vb), c3 = tr_read<v_rd_off(1, 3, 0)>(vb), d3 = tr_read<v_rd_off(1, 3, 1)>(vb);
;     asm volatile("s_waitcnt lgkmcnt(8)" ::: "memory"); SBAR();
;     ...
;     o0 = __builtin_amdgcn_mfma_f32_32x32x16_bf16(pa0, PK(a0, b0), o0, 0, 0, 0);
;     o0 = __builtin_amdgcn_mfma_f32_32x32x16_bf16(pa1, PK(a1, b1), o0, 0, 0, 0);
;     o0 = __builtin_amdgcn_mfma_f32_32x32x16_bf16(pa2, PK(a2, b2), o0, 0, 0, 0);
; DEVI void finishSM(f32x16& p0, f32x16& p1, float alpha, float& l_reg, bf16x8& pa0, bf16x8& pa1, bf16x8& pa2, bf16x8& pa3) {
; #pragma unroll
;     for (int r = 0; r < 16; ++r) p1[r] = __builtin_amdgcn_exp2f(p1[r]);
;     f32x2 s2 = (f32x2){p0[0], p0[1]} + (f32x2){p1[0], p1[1]};
; #pragma unroll
;     for (int r = 2; r < 16; r += 2) s2 += (f32x2){p0[r], p0[r + 1]} + (f32x2){p1[r], p1[r + 1]};
;     float ps = s2[0] + s2[1];
;     { auto rr = __builtin_amdgcn_permlane32_swap(__float_as_uint(ps), __float_as_uint(ps), false, false);
;       ps = __uint_as_float(rr[0]) + __uint_as_float(rr[1]); }
;     l_reg = l_reg * alpha + ps;
;     ...
;     PK4(p0, 0, pa0); PK4(p0, 8, pa1); PK4(p1, 0, pa2); PK4(p1, 8, pa3);
;     ...
; }
; DEVI void qkt(f32x16& p0, f32x16& p1, const char* Kb, const bf16x8 (&qr)[6], int r32, int hi, const f32x16& cinit) {
; #pragma unroll
;     for (int d0 = 0; d0 < 6; ++d0) { const int cb = (d0 * 16 + hi * 8) * 2;
;         const bf16x8 k0 = *(const bf16x8*)(Kb + KSWZ(r32, cb)), k1 = *(const bf16x8*)(Kb + KSWZ(32 + r32, cb));
;         p0 = __builtin_amdgcn_mfma_f32_32x32x16_bf16(k0, qr[d0], d0 == 0 ? cinit : p0, 0, 0, 0);
;         p1 = __builtin_amdgcn_mfma_f32_32x32x16_bf16(k1, qr[d0], d0 == 0 ? cinit : p1, 0, 0, 0); }
; }
.LBB0_696:
	s_mul_i32 s6, s89, 0x6000
	s_add_i32 s6, s6, 0
	v_add_u32_e32 v86, s6, v129
	ds_read_b128 v[82:85], v86 offset:12288
	ds_read_b128 v[124:127], v86 offset:18432
	v_add_u32_e32 v174, s6, v204
	v_exp_f32_e32 v66, v66
	v_exp_f32_e32 v67, v67
	s_waitcnt lgkmcnt(1)
	v_mfma_f32_32x32x16_bf16 v[98:113], v[82:85], v[150:153], v[34:49]
	v_add_u32_e32 v82, s6, v184
	v_add_u32_e32 v83, s6, v185
	ds_read_b128 v[208:211], v82 offset:12288
	ds_read_b128 v[212:215], v82 offset:18432
	ds_read_b128 v[216:219], v83 offset:12288
	ds_read_b128 v[220:223], v83 offset:18432
	v_exp_f32_e32 v68, v68
	v_exp_f32_e32 v69, v69
	v_exp_f32_e32 v70, v70
	v_exp_f32_e32 v71, v71
	s_waitcnt lgkmcnt(4)
	v_mfma_f32_32x32x16_bf16 v[82:97], v[124:127], v[150:153], v[34:49]
	ds_read_b128 v[124:127], v174 offset:12288
	ds_read_b128 v[224:227], v174 offset:18432
	v_exp_f32_e32 v72, v72
	v_exp_f32_e32 v73, v73
	v_exp_f32_e32 v74, v74
	v_exp_f32_e32 v75, v75
	v_exp_f32_e32 v76, v76
	v_exp_f32_e32 v77, v77
	s_waitcnt lgkmcnt(5)
	v_mfma_f32_32x32x16_bf16 v[98:113], v[208:211], v[138:141], v[98:113]
	v_add_u32_e32 v174, s6, v205
	v_exp_f32_e32 v78, v78
	v_exp_f32_e32 v79, v79
	ds_read_b128 v[228:231], v174 offset:12288
	ds_read_b128 v[232:235], v174 offset:18432
	v_exp_f32_e32 v80, v80
	v_exp_f32_e32 v81, v81
	v_add_u32_e32 v174, s6, v206
	s_waitcnt lgkmcnt(6)
	v_mfma_f32_32x32x16_bf16 v[82:97], v[212:215], v[138:141], v[82:97]
	v_add_f32_e64 v212, v50, v66
	v_add_f32_e64 v213, v51, v67
	v_add_f32_e64 v214, v52, v68
	v_add_f32_e64 v215, v53, v69
	v_lshl_add_u32 v202, s89, 14, v115
	v_pk_add_f32 v[212:213], v[214:215], v[212:213]
	v_pk_add_f32 v[214:215], v[54:55], v[70:71]
	ds_read_b128 v[208:211], v174 offset:12288
	ds_read_b128 v[236:239], v174 offset:18432
	v_pk_add_f32 v[212:213], v[214:215], v[212:213]
	s_waitcnt lgkmcnt(7)
	v_mfma_f32_32x32x16_bf16 v[98:113], v[216:219], v[134:137], v[98:113]
	v_add_f32_e64 v214, v56, v72
	v_add_f32_e64 v215, v57, v73
	v_cvt_pk_bf16_f32 v50, v50, v51
	v_cvt_pk_bf16_f32 v51, v52, v53
	v_cvt_pk_bf16_f32 v52, v54, v55
	v_cvt_pk_bf16_f32 v53, v56, v57
	v_cvt_pk_bf16_f32 v54, v58, v59
	v_add_f32_e64 v212, v214, v212
	v_add_f32_e64 v213, v215, v213
	s_waitcnt lgkmcnt(6)
	v_mfma_f32_32x32x16_bf16 v[82:97], v[220:223], v[134:137], v[82:97]
	v_add_f32_e64 v214, v58, v74
	v_add_f32_e64 v215, v59, v75
	v_cvt_pk_bf16_f32 v55, v60, v61
	v_cvt_pk_bf16_f32 v56, v62, v63
	v_cvt_pk_bf16_f32 v57, v64, v65
	v_cvt_pk_bf16_f32 v58, v66, v67
	v_cvt_pk_bf16_f32 v59, v68, v69
	v_add_f32_e64 v212, v214, v212
	v_add_f32_e64 v213, v215, v213
	s_waitcnt lgkmcnt(5)
	v_mfma_f32_32x32x16_bf16 v[98:113], v[124:127], v[130:133], v[98:113]
	v_add_f32_e64 v214, v60, v76
	v_add_f32_e64 v215, v61, v77
	v_add_f32_e64 v126, v62, v78
	v_add_f32_e64 v127, v63, v79
	v_add_f32_e64 v124, v214, v212
	v_add_f32_e64 v125, v215, v213
	v_cvt_pk_bf16_f32 v60, v70, v71
	v_cvt_pk_bf16_f32 v61, v72, v73
	v_cvt_pk_bf16_f32 v62, v74, v75
	v_cvt_pk_bf16_f32 v63, v76, v77
	s_waitcnt lgkmcnt(4)
	v_mfma_f32_32x32x16_bf16 v[82:97], v[224:227], v[130:133], v[82:97]
	v_add_f32_e64 v124, v126, v124
	v_add_f32_e64 v125, v127, v125
	v_add_f32_e64 v126, v64, v80
	v_add_f32_e64 v127, v65, v81
	v_cvt_pk_bf16_f32 v64, v78, v79
	v_cvt_pk_bf16_f32 v65, v80, v81
	ds_read_b64_tr_b16 v[66:67], v202 offset:0
	ds_read_b64_tr_b16 v[68:69], v202 offset:0x400
	ds_read_b64_tr_b16 v[70:71], v202 offset:0x800
	s_waitcnt lgkmcnt(6)
	v_mfma_f32_32x32x16_bf16 v[98:113], v[228:231], v[146:149], v[98:113]
	ds_read_b64_tr_b16 v[72:73], v202 offset:0xc00
	ds_read_b64_tr_b16 v[74:75], v202 offset:0x1000
	ds_read_b64_tr_b16 v[76:77], v202 offset:0x1400
	ds_read_b64_tr_b16 v[78:79], v202 offset:0x1800
	ds_read_b64_tr_b16 v[80:81], v202 offset:0x1c00
	v_add_f32_e64 v124, v126, v124
	v_add_f32_e64 v125, v127, v125
	s_waitcnt lgkmcnt(10)
	v_mfma_f32_32x32x16_bf16 v[82:97], v[232:235], v[146:149], v[82:97]
	v_pk_add_f32 v[124:125], v[124:125], v[124:125] op_sel:[0,1] op_sel_hi:[1,0]
	s_nop 0
	v_mov_b32_e32 v125, v124
	s_nop 1
	v_permlane32_swap_b32_e32 v124, v125
	s_waitcnt lgkmcnt(9)
	v_mfma_f32_32x32x16_bf16 v[98:113], v[208:211], v[142:145], v[98:113]
	ds_read_b64_tr_b16 v[208:209], v202 offset:0x200
	ds_read_b64_tr_b16 v[210:211], v202 offset:0x600
	ds_read_b64_tr_b16 v[212:213], v202 offset:0xa00
	ds_read_b64_tr_b16 v[214:215], v202 offset:0xe00
	ds_read_b64_tr_b16 v[216:217], v202 offset:0x1200
	ds_read_b64_tr_b16 v[218:219], v202 offset:0x1600
	ds_read_b64_tr_b16 v[220:221], v202 offset:0x1a00
	s_waitcnt lgkmcnt(15)
	v_mfma_f32_32x32x16_bf16 v[82:97], v[236:239], v[142:145], v[82:97]
	ds_read_b64_tr_b16 v[222:223], v202 offset:0x1e00
	s_waitcnt lgkmcnt(14)
	v_mfma_f32_32x32x16_bf16 v[18:33], v[50:53], v[66:69], v[18:33]
	s_waitcnt lgkmcnt(12)
	v_mfma_f32_32x32x16_bf16 v[18:33], v[54:57], v[70:73], v[18:33]
	s_waitcnt lgkmcnt(10)
	v_mfma_f32_32x32x16_bf16 v[18:33], v[58:61], v[74:77], v[18:33]
	s_waitcnt lgkmcnt(8)
	v_mfma_f32_32x32x16_bf16 v[18:33], v[62:65], v[78:81], v[18:33]
	s_waitcnt lgkmcnt(6)
	v_mfma_f32_32x32x16_bf16 v[2:17], v[50:53], v[208:211], v[2:17]
	s_nop 4
	v_max_f32_e32 v249, v99, v99
	v_max_f32_e32 v250, v98, v98
	v_max_f32_e32 v249, v250, v249
	v_max3_f32 v249, v249, v100, v101
	v_max3_f32 v249, v249, v102, v103
	v_max3_f32 v251, v249, v104, v105
	v_max3_f32 v251, v251, v106, v107
	s_waitcnt lgkmcnt(4)
	v_exp_f32_e32 v50, v98
	v_exp_f32_e32 v51, v99
	v_exp_f32_e32 v52, v100
	v_exp_f32_e32 v53, v101
	v_mov_b64_e32 v[66:67], v[82:83]
	v_mov_b64_e32 v[68:69], v[84:85]
	v_mfma_f32_32x32x16_bf16 v[2:17], v[54:57], v[212:215], v[2:17]
	v_max3_f32 v251, v251, v108, v109
	v_max3_f32 v251, v251, v110, v111
	v_max3_f32 v251, v251, v112, v113
	v_max3_f32 v251, v251, v82, v83
	v_max3_f32 v251, v251, v84, v85
	v_max3_f32 v251, v251, v86, v87
	v_max3_f32 v251, v251, v88, v89
	s_waitcnt lgkmcnt(2)
	v_exp_f32_e32 v54, v102
	v_exp_f32_e32 v55, v103
	v_exp_f32_e32 v56, v104
	v_exp_f32_e32 v57, v105
	v_mov_b64_e32 v[70:71], v[86:87]
	v_mov_b64_e32 v[72:73], v[88:89]
	v_mfma_f32_32x32x16_bf16 v[2:17], v[58:61], v[216:219], v[2:17]
	v_max3_f32 v251, v251, v90, v91
	v_max3_f32 v251, v251, v92, v93
	v_max3_f32 v251, v251, v94, v95
	v_max3_f32 v251, v251, v96, v97
	v_mov_b32_e32 v252, v251
	s_nop 1
	v_permlane32_swap_b32_e32 v251, v252
	s_waitcnt lgkmcnt(0)
	v_exp_f32_e32 v58, v106
	v_exp_f32_e32 v59, v107
	v_exp_f32_e32 v60, v108
	v_exp_f32_e32 v61, v109
	v_mov_b64_e32 v[74:75], v[90:91]
	v_mov_b64_e32 v[76:77], v[92:93]
	v_mfma_f32_32x32x16_bf16 v[2:17], v[62:65], v[220:223], v[2:17]
	v_exp_f32_e32 v62, v110
	v_exp_f32_e32 v63, v111
	v_exp_f32_e32 v64, v112
	v_exp_f32_e32 v65, v113
	v_mov_b64_e32 v[78:79], v[94:95]
	v_mov_b64_e32 v[80:81], v[96:97]
	v_max_f32_e32 v252, v252, v252
	v_max_f32_e32 v251, v251, v251
	v_max_f32_e32 v126, v251, v252
	v_cmp_ge_f32_e32 vcc, s79, v126
	s_cmp_lg_u64 vcc, exec
	s_cselect_b64 s[6:7], -1, 0
	s_cbranch_scc1 .LBB0_705
	v_mov_b32_e32 v208, 1.0
	v_mov_b32_e32 v209, v203
	s_branch .LBB0_699

; #define PK4(P, BASE, OUT) do { u32x4 w = {cvt_pk_bf16(P[BASE + 0], P[BASE + 1]), cvt_pk_bf16(P[BASE + 2], P[BASE + 3]), cvt_pk_bf16(P[BASE + 4], P[BASE + 5]), cvt_pk_bf16(P[BASE + 6], P[BASE + 7])}; \
;     OUT = *reinterpret_cast<bf16x8*>(&w); } while (0)
; DEVI void finishSM(f32x16& p0, f32x16& p1, float alpha, float& l_reg, bf16x8& pa0, bf16x8& pa1, bf16x8& pa2, bf16x8& pa3) {
; #pragma unroll
;     for (int r = 0; r < 16; ++r) p1[r] = __builtin_amdgcn_exp2f(p1[r]);
;     f32x2 s2 = (f32x2){p0[0], p0[1]} + (f32x2){p1[0], p1[1]};
; #pragma unroll
;     for (int r = 2; r < 16; r += 2) s2 += (f32x2){p0[r], p0[r + 1]} + (f32x2){p1[r], p1[r + 1]};
;     float ps = s2[0] + s2[1];
;     { auto rr = __builtin_amdgcn_permlane32_swap(__float_as_uint(ps), __float_as_uint(ps), false, false);
;       ps = __uint_as_float(rr[0]) + __uint_as_float(rr[1]); }
;     l_reg = l_reg * alpha + ps;
;     ...
;     PK4(p0, 0, pa0); PK4(p0, 8, pa1); PK4(p1, 0, pa2); PK4(p1, 8, pa3);
;     ...
; }
; DEVI void qkt(f32x16& p0, f32x16& p1, const char* Kb, const bf16x8 (&qr)[6], int r32, int hi, const f32x16& cinit) {
; #pragma unroll
;     for (int d0 = 0; d0 < 6; ++d0) { const int cb = (d0 * 16 + hi * 8) * 2;
;         const bf16x8 k0 = *(const bf16x8*)(Kb + KSWZ(r32, cb)), k1 = *(const bf16x8*)(Kb + KSWZ(32 + r32, cb));
;         p0 = __builtin_amdgcn_mfma_f32_32x32x16_bf16(k0, qr[d0], d0 == 0 ? cinit : p0, 0, 0, 0);
;         p1 = __builtin_amdgcn_mfma_f32_32x32x16_bf16(k1, qr[d0], d0 == 0 ? cinit : p1, 0, 0, 0); }
; }
; DEVI void attn_unit8(const Params& p, char* smem, int unit, int l, int& cvs  , CvRun& crun) {
;     ...
;         __syncthreads();
;         if (T + 2 < NTILE) B_DMA(T + 2, s2);
;         qkt(pA0, pA1, K_lds + s1 * 24576, qr, r32, hi, cinit);
;         finishSM(pB0, pB1, alB, l_reg, pa0, pa1, pa2, pa3);
;         pv_both(o[0], o[1], vb + 8192, pa0, pa1, pa2, pa3);
.LBB0_702:
	s_mul_i32 s6, s2, 0x6000
	s_add_i32 s6, s96, s6
	v_lshl_add_u64 v[82:83], v[118:119], 0, s[12:13]
	s_mov_b32 m0, s6
	s_barrier
	global_load_lds_dwordx4 v[82:83], off
	v_lshl_add_u64 v[82:83], v[120:121], 0, s[12:13]
	s_add_i32 m0, s6, 0x2000
	v_exp_f32_e32 v66, v66
	global_load_lds_dwordx4 v[82:83], off
	s_add_i32 m0, s6, 0x4000
	s_lshl_b32 s6, s2, 14
	v_lshl_add_u64 v[82:83], v[122:123], 0, s[12:13]
	s_add_i32 s6, s97, s6
	global_load_lds_dwordx4 v[82:83], off
	s_mov_b32 m0, s6
	v_lshl_add_u64 v[82:83], v[116:117], 0, s[40:41]
	global_load_lds_dwordx4 v[116:117], off
	s_add_i32 m0, s6, 0x2000
	s_mul_i32 s6, s61, 0x6000
	global_load_lds_dwordx4 v[82:83], off
	s_add_i32 s6, s6, 0
	v_add_u32_e32 v86, s6, v129
	ds_read_b128 v[82:85], v86
	ds_read_b128 v[210:213], v86 offset:6144
	s_waitcnt lgkmcnt(1)
	v_mfma_f32_32x32x16_bf16 v[98:113], v[82:85], v[150:153], v[34:49]
	v_add_u32_e32 v126, s6, v184
	v_exp_f32_e32 v67, v67
	v_exp_f32_e32 v68, v68
	v_exp_f32_e32 v69, v69
	v_exp_f32_e32 v70, v70
	v_exp_f32_e32 v71, v71
	v_exp_f32_e32 v72, v72
	s_waitcnt lgkmcnt(0)
	v_mfma_f32_32x32x16_bf16 v[82:97], v[210:213], v[150:153], v[34:49]
	ds_read_b128 v[210:213], v126
	ds_read_b128 v[214:217], v126 offset:6144
	v_add_u32_e32 v126, s6, v185
	v_exp_f32_e32 v73, v73
	v_exp_f32_e32 v74, v74
	v_exp_f32_e32 v75, v75
	v_exp_f32_e32 v76, v76
	v_exp_f32_e32 v77, v77
	s_waitcnt lgkmcnt(1)
	v_mfma_f32_32x32x16_bf16 v[98:113], v[210:213], v[138:141], v[98:113]
	v_exp_f32_e32 v78, v78
	v_exp_f32_e32 v79, v79
	v_exp_f32_e32 v80, v80
	v_exp_f32_e32 v81, v81
	v_add_u32_e32 v174, 0x2000, v202
	s_waitcnt lgkmcnt(0)
	v_mfma_f32_32x32x16_bf16 v[82:97], v[214:217], v[138:141], v[82:97]
	ds_read_b128 v[210:213], v126
	ds_read_b128 v[214:217], v126 offset:6144
	v_add_u32_e32 v126, s6, v204
	s_waitcnt lgkmcnt(1)
	v_mfma_f32_32x32x16_bf16 v[98:113], v[210:213], v[134:137], v[98:113]
	ds_read_b128 v[210:213], v126
	ds_read_b128 v[218:221], v126 offset:6144
	v_add_u32_e32 v126, s6, v205
	s_waitcnt lgkmcnt(2)
	v_mfma_f32_32x32x16_bf16 v[82:97], v[214:217], v[134:137], v[82:97]
	ds_read_b128 v[214:217], v126
	ds_read_b128 v[222:225], v126 offset:6144
	v_add_u32_e32 v126, s6, v206
	ds_read_b128 v[226:229], v126
	ds_read_b128 v[230:233], v126 offset:6144
	v_pk_add_f32 v[126:127], v[50:51], v[66:67]
	v_cvt_pk_bf16_f32 v50, v50, v51
	v_cvt_pk_bf16_f32 v51, v52, v53
	s_waitcnt lgkmcnt(5)
	v_mfma_f32_32x32x16_bf16 v[98:113], v[210:213], v[130:133], v[98:113]
	v_add_f32_e64 v210, v52, v68
	v_add_f32_e64 v211, v53, v69
	v_cvt_pk_bf16_f32 v52, v54, v55
	v_cvt_pk_bf16_f32 v53, v56, v57
	v_add_f32_e64 v126, v210, v126
	v_add_f32_e64 v127, v211, v127
	v_add_f32_e64 v210, v54, v70
	v_add_f32_e64 v211, v55, v71
	v_cvt_pk_bf16_f32 v54, v58, v59
	s_waitcnt lgkmcnt(4)
	v_mfma_f32_32x32x16_bf16 v[82:97], v[218:221], v[130:133], v[82:97]
	v_add_f32_e64 v126, v210, v126
	v_add_f32_e64 v127, v211, v127
	v_add_f32_e64 v210, v56, v72
	v_add_f32_e64 v211, v57, v73
	v_cvt_pk_bf16_f32 v55, v60, v61
	v_cvt_pk_bf16_f32 v56, v62, v63
	v_cvt_pk_bf16_f32 v57, v64, v65
	v_add_f32_e64 v126, v210, v126
	v_add_f32_e64 v127, v211, v127
	v_pk_add_f32 v[210:211], v[58:59], v[74:75]
	v_cvt_pk_bf16_f32 v58, v66, v67
	v_cvt_pk_bf16_f32 v59, v68, v69
	s_waitcnt lgkmcnt(3)
	v_mfma_f32_32x32x16_bf16 v[98:113], v[214:217], v[146:149], v[98:113]
	v_add_f32_e64 v126, v210, v126
	v_add_f32_e64 v127, v211, v127
	v_add_f32_e64 v210, v60, v76
	v_add_f32_e64 v211, v61, v77
	v_cvt_pk_bf16_f32 v60, v70, v71
	v_cvt_pk_bf16_f32 v61, v72, v73
	v_add_f32_e64 v126, v210, v126
	v_add_f32_e64 v127, v211, v127
	v_pk_add_f32 v[210:211], v[62:63], v[78:79]
	v_cvt_pk_bf16_f32 v62, v74, v75
	v_cvt_pk_bf16_f32 v63, v76, v77
	s_waitcnt lgkmcnt(2)
; #define SBAR() __builtin_amdgcn_sched_barrier(0)
; DEVI void pv_both(f32x16& o0, f32x16& o1, int vb, bf16x8 pa0, bf16x8 pa1, bf16x8 pa2, bf16x8 pa3) {
;     const s16x4 a0 = tr_read<v_rd_off(0, 0, 0)>(vb), b0 = tr_read<v_rd_off(0, 0, 1)>(vb), a1 = tr_read<v_rd_off(0, 1, 0)>(vb), b1 = tr_read<v_rd_off(0, 1, 1)>(vb);
;     const s16x4 a2 = tr_read<v_rd_off(0, 2, 0)>(vb), b2 = tr_read<v_rd_off(0, 2, 1)>(vb), a3 = tr_read<v_rd_off(0, 3, 0)>(vb), b3 = tr_read<v_rd_off(0, 3, 1)>(vb);
;     const s16x4 c0 = tr_read<v_rd_off(1, 0, 0)>(vb), d0 = tr_read<v_rd_off(1, 0, 1)>(vb), c1 = tr_read<v_rd_off(1, 1, 0)>(vb), d1 = tr_read<v_rd_off(1, 1, 1)>(vb);
;     const s16x4 c2 = tr_read<v_rd_off(1, 2, 0)>(vb), d2 = tr_read<v_rd_off(1, 2, 1)>(vb), c3 = tr_read<v_rd_off(1, 3, 0)>(vb), d3 = tr_read<v_rd_off(1, 3, 1)>(vb);
;     asm volatile("s_waitcnt lgkmcnt(8)" ::: "memory"); SBAR();
;     ...
;     o0 = __builtin_amdgcn_mfma_f32_32x32x16_bf16(pa0, PK(a0, b0), o0, 0, 0, 0);
;     o0 = __builtin_amdgcn_mfma_f32_32x32x16_bf16(pa1, PK(a1, b1), o0, 0, 0, 0);
;     o0 = __builtin_amdgcn_mfma_f32_32x32x16_bf16(pa2, PK(a2, b2), o0, 0, 0, 0);
;     o0 = __builtin_amdgcn_mfma_f32_32x32x16_bf16(pa3, PK(a3, b3), o0, 0, 0, 0);
;     asm volatile("s_waitcnt lgkmcnt(0)" ::: "memory"); SBAR();
;     o1 = __builtin_amdgcn_mfma_f32_32x32x16_bf16(pa0, PK(c0, d0), o1, 0, 0, 0);
;     o1 = __builtin_amdgcn_mfma_f32_32x32x16_bf16(pa1, PK(c1, d1), o1, 0, 0, 0);
;     o1 = __builtin_amdgcn_mfma_f32_32x32x16_bf16(pa2, PK(c2, d2), o1, 0, 0, 0);
;     o1 = __builtin_amdgcn_mfma_f32_32x32x16_bf16(pa3, PK(c3, d3), o1, 0, 0, 0);
;     ...
; }
; template <bool FIRST> DEVI bool partialSM(f32x16& p0, f32x16& p1, float& m_reg, float& alpha) {
;     float pmax = p0[0];
; #pragma unroll
;     for (int r = 1; r < 16; ++r) pmax = fmaxf(pmax, p0[r]);
; #pragma unroll
;     for (int r = 0; r < 16; ++r) pmax = fmaxf(pmax, p1[r]);
;     { auto rr = __builtin_amdgcn_permlane32_swap(__float_as_uint(pmax), __float_as_uint(pmax), false, false);
;       pmax = fmaxf(__uint_as_float(rr[0]), __uint_as_float(rr[1])); }
;     if (FIRST) { m_reg = pmax; alpha = 1.f;
; #pragma unroll
;         for (int r = 0; r < 16; ++r) { p0[r] = __builtin_amdgcn_exp2f(p0[r] - pmax); p1[r] = p1[r] - pmax; }
;         return false;
;     } else if (__builtin_expect(__all(pmax <= ATT_THR), 1)) { alpha = 1.f;
	v_mfma_f32_32x32x16_bf16 v[82:97], v[222:225], v[146:149], v[82:97]
	v_add_f32_e64 v126, v210, v126
	v_add_f32_e64 v127, v211, v127
	v_add_f32_e64 v210, v64, v80
	v_add_f32_e64 v211, v65, v81
	v_cvt_pk_bf16_f32 v64, v78, v79
	v_cvt_pk_bf16_f32 v65, v80, v81
	ds_read_b64_tr_b16 v[66:67], v174 offset:0
	ds_read_b64_tr_b16 v[68:69], v174 offset:0x400
	ds_read_b64_tr_b16 v[70:71], v174 offset:0x800
	ds_read_b64_tr_b16 v[72:73], v174 offset:0xc00
	ds_read_b64_tr_b16 v[74:75], v174 offset:0x1000
	ds_read_b64_tr_b16 v[76:77], v174 offset:0x1400
	ds_read_b64_tr_b16 v[78:79], v174 offset:0x1800
	ds_read_b64_tr_b16 v[80:81], v174 offset:0x1c00
	v_add_f32_e64 v126, v210, v126
	v_add_f32_e64 v127, v211, v127
	ds_read_b64_tr_b16 v[210:211], v174 offset:0x200
	ds_read_b64_tr_b16 v[212:213], v174 offset:0x600
	ds_read_b64_tr_b16 v[214:215], v174 offset:0xa00
	s_waitcnt lgkmcnt(12)
	v_mfma_f32_32x32x16_bf16 v[98:113], v[226:229], v[142:145], v[98:113]
	ds_read_b64_tr_b16 v[216:217], v174 offset:0xe00
	ds_read_b64_tr_b16 v[218:219], v174 offset:0x1200
	ds_read_b64_tr_b16 v[220:221], v174 offset:0x1600
	ds_read_b64_tr_b16 v[222:223], v174 offset:0x1a00
	ds_read_b64_tr_b16 v[224:225], v174 offset:0x1e00
	v_pk_add_f32 v[126:127], v[126:127], v[126:127] op_sel:[0,1] op_sel_hi:[1,0]
	s_waitcnt lgkmcnt(15)
	v_mfma_f32_32x32x16_bf16 v[82:97], v[230:233], v[142:145], v[82:97]
	v_mov_b32_e32 v127, v126
	s_nop 1
	v_permlane32_swap_b32_e32 v126, v127
	s_waitcnt lgkmcnt(14)
	v_mfma_f32_32x32x16_bf16 v[18:33], v[50:53], v[66:69], v[18:33]
	s_waitcnt lgkmcnt(12)
	v_mfma_f32_32x32x16_bf16 v[18:33], v[54:57], v[70:73], v[18:33]
	s_waitcnt lgkmcnt(10)
	v_mfma_f32_32x32x16_bf16 v[18:33], v[58:61], v[74:77], v[18:33]
	s_waitcnt lgkmcnt(8)
	v_mfma_f32_32x32x16_bf16 v[18:33], v[62:65], v[78:81], v[18:33]
	s_waitcnt lgkmcnt(6)
	v_mfma_f32_32x32x16_bf16 v[2:17], v[50:53], v[210:213], v[2:17]
	s_nop 0
	v_max_f32_e32 v249, v99, v99
	v_max_f32_e32 v250, v98, v98
	v_max_f32_e32 v249, v250, v249
	v_max3_f32 v249, v249, v100, v101
	v_max3_f32 v249, v249, v102, v103
	v_max3_f32 v251, v249, v104, v105
	v_max3_f32 v251, v251, v106, v107
	s_waitcnt lgkmcnt(4)
	v_exp_f32_e32 v50, v98
	v_exp_f32_e32 v51, v99
	v_exp_f32_e32 v52, v100
	v_exp_f32_e32 v53, v101
	v_mov_b64_e32 v[66:67], v[82:83]
	v_mov_b64_e32 v[68:69], v[84:85]
	v_mfma_f32_32x32x16_bf16 v[2:17], v[54:57], v[214:217], v[2:17]
	v_max3_f32 v251, v251, v108, v109
	v_max3_f32 v251, v251, v110, v111
	v_max3_f32 v251, v251, v112, v113
	v_max3_f32 v251, v251, v82, v83
	v_max3_f32 v251, v251, v84, v85
	v_max3_f32 v251, v251, v86, v87
	v_max3_f32 v251, v251, v88, v89
	s_waitcnt lgkmcnt(2)
	v_exp_f32_e32 v54, v102
	v_exp_f32_e32 v55, v103
	v_exp_f32_e32 v56, v104
	v_exp_f32_e32 v57, v105
	v_mov_b64_e32 v[70:71], v[86:87]
	v_mov_b64_e32 v[72:73], v[88:89]
	v_mfma_f32_32x32x16_bf16 v[2:17], v[58:61], v[218:221], v[2:17]
	v_max3_f32 v251, v251, v90, v91
	v_max3_f32 v251, v251, v92, v93
	v_max3_f32 v251, v251, v94, v95
	v_max3_f32 v251, v251, v96, v97
	v_mov_b32_e32 v252, v251
	s_nop 1
	v_permlane32_swap_b32_e32 v251, v252
	s_waitcnt lgkmcnt(0)
	v_exp_f32_e32 v58, v106
	v_exp_f32_e32 v59, v107
	v_exp_f32_e32 v60, v108
	v_exp_f32_e32 v61, v109
	v_mov_b64_e32 v[74:75], v[90:91]
	v_mov_b64_e32 v[76:77], v[92:93]
	v_mfma_f32_32x32x16_bf16 v[2:17], v[62:65], v[222:225], v[2:17]
	v_exp_f32_e32 v62, v110
	v_exp_f32_e32 v63, v111
	v_exp_f32_e32 v64, v112
	v_exp_f32_e32 v65, v113
	v_mov_b64_e32 v[78:79], v[94:95]
	v_mov_b64_e32 v[80:81], v[96:97]
	v_max_f32_e32 v252, v252, v252
	v_max_f32_e32 v251, v251, v251
	v_max_f32_e32 v174, v251, v252
	v_cmp_ge_f32_e32 vcc, s79, v174
	s_cmp_lg_u64 vcc, exec
	s_cselect_b64 s[6:7], -1, 0
	s_cbranch_scc1 .LBB0_711
	v_mov_b32_e32 v202, 1.0
	v_mov_b32_e32 v203, v209
	s_branch .LBB0_716

; #define G8_STAGE_B(bufoff, gbase) do { _Pragma("unroll") for (int _i = 0; _i < 2; ++_i) \
;         __builtin_amdgcn_global_load_lds((const unsigned*)((const char*)(gbase) + voffB[_i]), (LAS unsigned*)(lds + (bufoff) + ldsw + _i * 8192), 16, 0, 0); } while (0)
; #define G8_LDA(dst, b, h) do { _Pragma("unroll") for (int m = 0; m < 4; ++m) _Pragma("unroll") for (int k = 0; k < 2; ++k) dst[m][k] = *(const LAS bf16x8*)(lds + G8_SA(b, h) + aoff + m * 2048 + k * 1024); } while (0)
; #define G8_LDB(dst, b, h) do { _Pragma("unroll") for (int n = 0; n < 2; ++n) _Pragma("unroll") for (int k = 0; k < 2; ++k) dst[n][k] = *(const LAS bf16x8*)(lds + G8_SB(b, h) + boff + n * 2048 + k * 1024); } while (0)
; #define G8_WAIT_V(n) asm volatile("s_waitcnt vmcnt(" #n ")" ::: "memory")
; #define G8_WAIT_L(n) asm volatile("s_waitcnt lgkmcnt(" #n ")" ::: "memory")
; #define G8_BAR __builtin_amdgcn_s_barrier()
; template <class Sched, class Epi>
; DEVI void gemm_phase(LAS unsigned char* lds, const char* Abase, const int K, const Sched& S, const Epi& E) {
;     ...
;         for (int t = 0; t < ntu; t += 2) {
;             const bool last = (t == ntu - 2);
;             const size_t k1 = (size_t)(t + 1) * kstep;
;             const size_t k2 = last ? (size_t)0 : (size_t)(t + 2) * kstep, k3 = k2 + kstep;
;             const char* b2 = last ? nB : cB + (size_t)(t + 2) * kstep; const char* b3 = b2 + kstep;
;             G8_LDB(B0, 0, 0); G8_LDB(B1, 0, 1); G8_SCHED; G8_LDA(At, 0, 0); G8_STAGE_A(G8_SA(1, 1), false, 1, k1);
;             G8_WAIT_L(0); G8_BAR; G8_MMA(0, 0, At, B0); G8_MMA(0, 1, At, B1); G8_BAR; G8_SCHED;
;             if (!skip1) G8_LDA(At, 0, 1); G8_STAGE_B(G8_SB(0, 0), b2); G8_STAGE_A(G8_SA(0, 0), last, 0, k2); G8_STAGE_B(G8_SB(0, 1), b2 + hstepB);
;             G8_WAIT_V(6); G8_WAIT_L(0); G8_BAR; if (!skip1) { G8_MMA(1, 0, At, B0); G8_MMA(1, 1, At, B1); } G8_BAR; G8_SCHED;
;             G8_LDB(B0, 1, 0); G8_LDB(B1, 1, 1); G8_SCHED; G8_LDA(At, 1, 0); G8_STAGE_A(G8_SA(0, 1), last, 1, k2);
;             G8_WAIT_L(0); G8_BAR; G8_MMA(0, 0, At, B0); G8_MMA(0, 1, At, B1); G8_BAR; G8_SCHED;
;             if (!skip1) G8_LDA(At, 1, 1); G8_STAGE_B(G8_SB(1, 0), b3); G8_STAGE_A(G8_SA(1, 0), last, 0, k3); G8_STAGE_B(G8_SB(1, 1), b3 + hstepB);
;             G8_WAIT_V(6); G8_WAIT_L(0); G8_BAR; if (!skip1) { G8_MMA(1, 0, At, B0); G8_MMA(1, 1, At, B1); } G8_BAR; G8_SCHED;
.LBB0_1015:
	ds_read_b128 v[150:153], v219
	ds_read_b128 v[154:157], v219 offset:1024
	ds_read_b128 v[158:161], v219 offset:2048
	ds_read_b128 v[162:165], v219 offset:3072
	ds_read_b128 v[134:137], v220
	ds_read_b128 v[138:141], v220 offset:1024
	ds_read_b128 v[142:145], v220 offset:2048
	ds_read_b128 v[146:149], v220 offset:3072
	v_lshl_add_u64 v[4:5], v[206:207], 0, s[36:37]
	s_add_i32 m0, s39, 0xc000
	s_waitcnt lgkmcnt(0)
	ds_read_b128 v[178:181], v221
	ds_read_b128 v[194:197], v221 offset:1024
	ds_read_b128 v[174:177], v221 offset:2048
	ds_read_b128 v[190:193], v221 offset:3072
	ds_read_b128 v[170:173], v221 offset:4096
	ds_read_b128 v[186:189], v221 offset:5120
	ds_read_b128 v[166:169], v221 offset:6144
	ds_read_b128 v[182:185], v221 offset:7168
	global_load_lds_dwordx4 v[4:5], off
	v_lshl_add_u64 v[4:5], v[208:209], 0, s[36:37]
	s_add_i32 m0, s39, 0xe000
	s_nop 0
	global_load_lds_dwordx4 v[4:5], off
	s_waitcnt lgkmcnt(0)
	s_barrier
	s_setprio 1
	s_waitcnt lgkmcnt(0)
	v_mfma_f32_16x16x32_bf16 v[130:133], v[150:153], v[178:181], v[130:133]
	v_mfma_f32_16x16x32_bf16 v[126:129], v[158:161], v[178:181], v[126:129]
	v_mfma_f32_16x16x32_bf16 v[118:121], v[150:153], v[174:177], v[118:121]
	v_mfma_f32_16x16x32_bf16 v[110:113], v[158:161], v[174:177], v[110:113]
	v_mfma_f32_16x16x32_bf16 v[98:101], v[150:153], v[170:173], v[98:101]
	v_mfma_f32_16x16x32_bf16 v[94:97], v[158:161], v[170:173], v[94:97]
	v_mfma_f32_16x16x32_bf16 v[82:85], v[150:153], v[166:169], v[82:85]
	v_mfma_f32_16x16x32_bf16 v[78:81], v[158:161], v[166:169], v[78:81]
	v_mfma_f32_16x16x32_bf16 v[130:133], v[154:157], v[194:197], v[130:133]
	v_mfma_f32_16x16x32_bf16 v[126:129], v[162:165], v[194:197], v[126:129]
	v_mfma_f32_16x16x32_bf16 v[118:121], v[154:157], v[190:193], v[118:121]
	v_mfma_f32_16x16x32_bf16 v[110:113], v[162:165], v[190:193], v[110:113]
	v_mfma_f32_16x16x32_bf16 v[98:101], v[154:157], v[186:189], v[98:101]
	v_mfma_f32_16x16x32_bf16 v[94:97], v[162:165], v[186:189], v[94:97]
	v_mfma_f32_16x16x32_bf16 v[82:85], v[154:157], v[182:185], v[82:85]
	v_mfma_f32_16x16x32_bf16 v[78:81], v[162:165], v[182:185], v[78:81]
	v_mfma_f32_16x16x32_bf16 v[122:125], v[134:137], v[178:181], v[122:125]
	v_mfma_f32_16x16x32_bf16 v[114:117], v[142:145], v[178:181], v[114:117]
	v_mfma_f32_16x16x32_bf16 v[106:109], v[134:137], v[174:177], v[106:109]
	v_mfma_f32_16x16x32_bf16 v[102:105], v[142:145], v[174:177], v[102:105]
	v_mfma_f32_16x16x32_bf16 v[90:93], v[134:137], v[170:173], v[90:93]
	v_mfma_f32_16x16x32_bf16 v[86:89], v[142:145], v[170:173], v[86:89]
	v_mfma_f32_16x16x32_bf16 v[74:77], v[134:137], v[166:169], v[74:77]
	v_mfma_f32_16x16x32_bf16 v[70:73], v[142:145], v[166:169], v[70:73]
	v_mfma_f32_16x16x32_bf16 v[122:125], v[138:141], v[194:197], v[122:125]
	v_mfma_f32_16x16x32_bf16 v[114:117], v[146:149], v[194:197], v[114:117]
	v_mfma_f32_16x16x32_bf16 v[106:109], v[138:141], v[190:193], v[106:109]
	v_mfma_f32_16x16x32_bf16 v[102:105], v[146:149], v[190:193], v[102:105]
	v_mfma_f32_16x16x32_bf16 v[90:93], v[138:141], v[186:189], v[90:93]
	v_mfma_f32_16x16x32_bf16 v[86:89], v[146:149], v[186:189], v[86:89]
	v_mfma_f32_16x16x32_bf16 v[74:77], v[138:141], v[182:185], v[74:77]
	v_mfma_f32_16x16x32_bf16 v[70:73], v[146:149], v[182:185], v[70:73]
	s_setprio 0
	s_barrier
	v_cmp_ne_u32_e64 s[4:5], 1, v222
	s_andn2_b64 vcc, exec, s[30:31]
	s_cbranch_vccnz .LBB0_1017
	ds_read_b128 v[178:181], v221 offset:16384
	ds_read_b128 v[194:197], v221 offset:17408
	ds_read_b128 v[174:177], v221 offset:18432
	ds_read_b128 v[190:193], v221 offset:19456
	ds_read_b128 v[170:173], v221 offset:20480
	ds_read_b128 v[186:189], v221 offset:21504
	ds_read_b128 v[166:169], v221 offset:22528
	ds_read_b128 v[182:185], v221 offset:23552
.LBB0_1017:
	s_add_u32 s34, s36, 0x100
	s_addc_u32 s35, s37, 0
	s_add_u32 s68, s62, s36
	s_addc_u32 s69, s63, s37
	s_cmp_eq_u32 s64, 12
	s_cselect_b64 s[66:67], -1, 0
	s_and_b64 s[36:37], s[66:67], exec
	s_cselect_b32 s65, 0, s34
	s_cselect_b32 s37, s19, s69
	s_cselect_b32 s36, s61, s68
	s_and_b64 s[66:67], s[28:29], s[66:67]
	s_and_b64 s[66:67], s[66:67], exec
	s_cselect_b32 s67, s24, s26
	s_mov_b32 m0, s40
	v_lshl_add_u64 v[4:5], s[36:37], 0, v[198:199]
	s_cselect_b32 s66, s25, s27
	s_add_u32 s68, s67, s65
	global_load_lds_dwordx4 v[4:5], off
	v_lshl_add_u64 v[210:211], s[36:37], 0, v[200:201]
	s_mov_b32 m0, s2
	s_addc_u32 s69, s66, 0
	global_load_lds_dwordx4 v[210:211], off
	v_lshl_add_u64 v[212:213], s[68:69], 0, v[198:199]
	s_mov_b32 m0, s39
	v_lshl_add_u64 v[214:215], s[68:69], 0, v[200:201]
	s_add_u32 s68, s36, 0x40000
	global_load_lds_dwordx4 v[212:213], off
	s_mov_b32 m0, s41
	s_addc_u32 s69, s37, 0
	global_load_lds_dwordx4 v[214:215], off
	v_lshl_add_u64 v[224:225], s[68:69], 0, v[198:199]
	s_mov_b32 m0, s42
	s_and_b64 vcc, exec, s[4:5]
	global_load_lds_dwordx4 v[224:225], off
	v_lshl_add_u64 v[224:225], s[68:69], 0, v[200:201]
	s_mov_b32 m0, s43
	s_nop 0
	global_load_lds_dwordx4 v[224:225], off
	s_waitcnt vmcnt(6)
	s_waitcnt lgkmcnt(0)
	s_barrier
	s_cbranch_vccnz .LBB0_1019
; #define G8_STAGE_B(bufoff, gbase) do { _Pragma("unroll") for (int _i = 0; _i < 2; ++_i) \
;         __builtin_amdgcn_global_load_lds((const unsigned*)((const char*)(gbase) + voffB[_i]), (LAS unsigned*)(lds + (bufoff) + ldsw + _i * 8192), 16, 0, 0); } while (0)
; #define G8_LDA(dst, b, h) do { _Pragma("unroll") for (int m = 0; m < 4; ++m) _Pragma("unroll") for (int k = 0; k < 2; ++k) dst[m][k] = *(const LAS bf16x8*)(lds + G8_SA(b, h) + aoff + m * 2048 + k * 1024); } while (0)
; #define G8_LDB(dst, b, h) do { _Pragma("unroll") for (int n = 0; n < 2; ++n) _Pragma("unroll") for (int k = 0; k < 2; ++k) dst[n][k] = *(const LAS bf16x8*)(lds + G8_SB(b, h) + boff + n * 2048 + k * 1024); } while (0)
; #define G8_WAIT_V(n) asm volatile("s_waitcnt vmcnt(" #n ")" ::: "memory")
; #define G8_WAIT_L(n) asm volatile("s_waitcnt lgkmcnt(" #n ")" ::: "memory")
; #define G8_BAR __builtin_amdgcn_s_barrier()
; template <class Sched, class Epi>
; DEVI void gemm_phase(LAS unsigned char* lds, const char* Abase, const int K, const Sched& S, const Epi& E) {
;     ...
;         for (int t = 0; t < ntu; t += 2) {
;             const bool last = (t == ntu - 2);
;             const size_t k1 = (size_t)(t + 1) * kstep;
;             const size_t k2 = last ? (size_t)0 : (size_t)(t + 2) * kstep, k3 = k2 + kstep;
;             const char* b2 = last ? nB : cB + (size_t)(t + 2) * kstep; const char* b3 = b2 + kstep;
;             G8_LDB(B0, 0, 0); G8_LDB(B1, 0, 1); G8_SCHED; G8_LDA(At, 0, 0); G8_STAGE_A(G8_SA(1, 1), false, 1, k1);
;             G8_WAIT_L(0); G8_BAR; G8_MMA(0, 0, At, B0); G8_MMA(0, 1, At, B1); G8_BAR; G8_SCHED;
;             if (!skip1) G8_LDA(At, 0, 1); G8_STAGE_B(G8_SB(0, 0), b2); G8_STAGE_A(G8_SA(0, 0), last, 0, k2); G8_STAGE_B(G8_SB(0, 1), b2 + hstepB);
;             G8_WAIT_V(6); G8_WAIT_L(0); G8_BAR; if (!skip1) { G8_MMA(1, 0, At, B0); G8_MMA(1, 1, At, B1); } G8_BAR; G8_SCHED;
;             G8_LDB(B0, 1, 0); G8_LDB(B1, 1, 1); G8_SCHED; G8_LDA(At, 1, 0); G8_STAGE_A(G8_SA(0, 1), last, 1, k2);
;             G8_WAIT_L(0); G8_BAR; G8_MMA(0, 0, At, B0); G8_MMA(0, 1, At, B1); G8_BAR; G8_SCHED;
;             if (!skip1) G8_LDA(At, 1, 1); G8_STAGE_B(G8_SB(1, 0), b3); G8_STAGE_A(G8_SA(1, 0), last, 0, k3); G8_STAGE_B(G8_SB(1, 1), b3 + hstepB);
;             G8_WAIT_V(6); G8_WAIT_L(0); G8_BAR; if (!skip1) { G8_MMA(1, 0, At, B0); G8_MMA(1, 1, At, B1); } G8_BAR; G8_SCHED;
	s_setprio 1
	s_waitcnt lgkmcnt(0)
	v_mfma_f32_16x16x32_bf16 v[66:69], v[150:153], v[178:181], v[66:69]
	v_mfma_f32_16x16x32_bf16 v[62:65], v[158:161], v[178:181], v[62:65]
	v_mfma_f32_16x16x32_bf16 v[50:53], v[150:153], v[174:177], v[50:53]
	v_mfma_f32_16x16x32_bf16 v[46:49], v[158:161], v[174:177], v[46:49]
	v_mfma_f32_16x16x32_bf16 v[34:37], v[150:153], v[170:173], v[34:37]
	v_mfma_f32_16x16x32_bf16 v[30:33], v[158:161], v[170:173], v[30:33]
	v_mfma_f32_16x16x32_bf16 v[18:21], v[150:153], v[166:169], v[18:21]
	v_mfma_f32_16x16x32_bf16 v[14:17], v[158:161], v[166:169], v[14:17]
	v_mfma_f32_16x16x32_bf16 v[66:69], v[154:157], v[194:197], v[66:69]
	v_mfma_f32_16x16x32_bf16 v[62:65], v[162:165], v[194:197], v[62:65]
	v_mfma_f32_16x16x32_bf16 v[50:53], v[154:157], v[190:193], v[50:53]
	v_mfma_f32_16x16x32_bf16 v[46:49], v[162:165], v[190:193], v[46:49]
	v_mfma_f32_16x16x32_bf16 v[34:37], v[154:157], v[186:189], v[34:37]
	v_mfma_f32_16x16x32_bf16 v[30:33], v[162:165], v[186:189], v[30:33]
	v_mfma_f32_16x16x32_bf16 v[18:21], v[154:157], v[182:185], v[18:21]
	v_mfma_f32_16x16x32_bf16 v[14:17], v[162:165], v[182:185], v[14:17]
	v_mfma_f32_16x16x32_bf16 v[58:61], v[134:137], v[178:181], v[58:61]
	v_mfma_f32_16x16x32_bf16 v[54:57], v[142:145], v[178:181], v[54:57]
	v_mfma_f32_16x16x32_bf16 v[42:45], v[134:137], v[174:177], v[42:45]
	v_mfma_f32_16x16x32_bf16 v[38:41], v[142:145], v[174:177], v[38:41]
	v_mfma_f32_16x16x32_bf16 v[26:29], v[134:137], v[170:173], v[26:29]
	v_mfma_f32_16x16x32_bf16 v[22:25], v[142:145], v[170:173], v[22:25]
	v_mfma_f32_16x16x32_bf16 v[10:13], v[134:137], v[166:169], v[10:13]
	v_mfma_f32_16x16x32_bf16 v[6:9], v[142:145], v[166:169], v[6:9]
	v_mfma_f32_16x16x32_bf16 v[58:61], v[138:141], v[194:197], v[58:61]
	v_mfma_f32_16x16x32_bf16 v[54:57], v[146:149], v[194:197], v[54:57]
	v_mfma_f32_16x16x32_bf16 v[42:45], v[138:141], v[190:193], v[42:45]
	v_mfma_f32_16x16x32_bf16 v[38:41], v[146:149], v[190:193], v[38:41]
	v_mfma_f32_16x16x32_bf16 v[26:29], v[138:141], v[186:189], v[26:29]
	v_mfma_f32_16x16x32_bf16 v[22:25], v[146:149], v[186:189], v[22:25]
	v_mfma_f32_16x16x32_bf16 v[10:13], v[138:141], v[182:185], v[10:13]
	v_mfma_f32_16x16x32_bf16 v[6:9], v[146:149], v[182:185], v[6:9]
	s_setprio 0
.LBB0_1019:
	s_barrier
	v_add_u32_e32 v3, 0x18000, v218
	ds_read_b128 v[150:153], v3
	ds_read_b128 v[154:157], v3 offset:1024
	ds_read_b128 v[158:161], v3 offset:2048
	ds_read_b128 v[162:165], v3 offset:3072
	v_add_u32_e32 v3, 0x1c000, v218
	ds_read_b128 v[134:137], v3
	ds_read_b128 v[138:141], v3 offset:1024
	ds_read_b128 v[142:145], v3 offset:2048
	ds_read_b128 v[146:149], v3 offset:3072
	s_add_u32 s65, s67, s65
	s_addc_u32 s67, s66, 0
	s_add_u32 s66, s65, 0x40000
	s_addc_u32 s67, s67, 0
	s_mov_b32 m0, s44
	v_lshl_add_u64 v[224:225], s[66:67], 0, v[198:199]
	s_waitcnt lgkmcnt(0)
	ds_read_b128 v[178:181], v221 offset:32768
	ds_read_b128 v[194:197], v221 offset:33792
	ds_read_b128 v[174:177], v221 offset:34816
	ds_read_b128 v[190:193], v221 offset:35840
	ds_read_b128 v[170:173], v221 offset:36864
	ds_read_b128 v[186:189], v221 offset:37888
	ds_read_b128 v[166:169], v221 offset:38912
	ds_read_b128 v[182:185], v221 offset:39936
	global_load_lds_dwordx4 v[224:225], off
	v_lshl_add_u64 v[224:225], s[66:67], 0, v[200:201]
	s_mov_b32 m0, s45
	s_nop 0
	global_load_lds_dwordx4 v[224:225], off
	s_waitcnt lgkmcnt(0)
	s_barrier
	s_setprio 1
	s_waitcnt lgkmcnt(0)
	v_mfma_f32_16x16x32_bf16 v[130:133], v[150:153], v[178:181], v[130:133]
	v_mfma_f32_16x16x32_bf16 v[126:129], v[158:161], v[178:181], v[126:129]
	v_mfma_f32_16x16x32_bf16 v[118:121], v[150:153], v[174:177], v[118:121]
	v_mfma_f32_16x16x32_bf16 v[110:113], v[158:161], v[174:177], v[110:113]
	v_mfma_f32_16x16x32_bf16 v[98:101], v[150:153], v[170:173], v[98:101]
	v_mfma_f32_16x16x32_bf16 v[94:97], v[158:161], v[170:173], v[94:97]
	v_mfma_f32_16x16x32_bf16 v[82:85], v[150:153], v[166:169], v[82:85]
	v_mfma_f32_16x16x32_bf16 v[78:81], v[158:161], v[166:169], v[78:81]
	v_mfma_f32_16x16x32_bf16 v[130:133], v[154:157], v[194:197], v[130:133]
	v_mfma_f32_16x16x32_bf16 v[126:129], v[162:165], v[194:197], v[126:129]
	v_mfma_f32_16x16x32_bf16 v[118:121], v[154:157], v[190:193], v[118:121]
	v_mfma_f32_16x16x32_bf16 v[110:113], v[162:165], v[190:193], v[110:113]
	v_mfma_f32_16x16x32_bf16 v[98:101], v[154:157], v[186:189], v[98:101]
	v_mfma_f32_16x16x32_bf16 v[94:97], v[162:165], v[186:189], v[94:97]
	v_mfma_f32_16x16x32_bf16 v[82:85], v[154:157], v[182:185], v[82:85]
	v_mfma_f32_16x16x32_bf16 v[78:81], v[162:165], v[182:185], v[78:81]
	v_mfma_f32_16x16x32_bf16 v[122:125], v[134:137], v[178:181], v[122:125]
	v_mfma_f32_16x16x32_bf16 v[114:117], v[142:145], v[178:181], v[114:117]
	v_mfma_f32_16x16x32_bf16 v[106:109], v[134:137], v[174:177], v[106:109]
	v_mfma_f32_16x16x32_bf16 v[102:105], v[142:145], v[174:177], v[102:105]
	v_mfma_f32_16x16x32_bf16 v[90:93], v[134:137], v[170:173], v[90:93]
	v_mfma_f32_16x16x32_bf16 v[86:89], v[142:145], v[170:173], v[86:89]
	v_mfma_f32_16x16x32_bf16 v[74:77], v[134:137], v[166:169], v[74:77]
	v_mfma_f32_16x16x32_bf16 v[70:73], v[142:145], v[166:169], v[70:73]
	v_mfma_f32_16x16x32_bf16 v[122:125], v[138:141], v[194:197], v[122:125]
	v_mfma_f32_16x16x32_bf16 v[114:117], v[146:149], v[194:197], v[114:117]
	v_mfma_f32_16x16x32_bf16 v[106:109], v[138:141], v[190:193], v[106:109]
	v_mfma_f32_16x16x32_bf16 v[102:105], v[146:149], v[190:193], v[102:105]
	v_mfma_f32_16x16x32_bf16 v[90:93], v[138:141], v[186:189], v[90:93]
	v_mfma_f32_16x16x32_bf16 v[86:89], v[146:149], v[186:189], v[86:89]
	v_mfma_f32_16x16x32_bf16 v[74:77], v[138:141], v[182:185], v[74:77]
	v_mfma_f32_16x16x32_bf16 v[70:73], v[146:149], v[182:185], v[70:73]
	s_setprio 0
	s_barrier
	s_and_b64 vcc, exec, s[4:5]
	s_cbranch_vccnz .LBB0_1021
	ds_read_b128 v[178:181], v221 offset:49152
	ds_read_b128 v[194:197], v221 offset:50176
	ds_read_b128 v[174:177], v221 offset:51200
	ds_read_b128 v[190:193], v221 offset:52224
	ds_read_b128 v[170:173], v221 offset:53248
	ds_read_b128 v[186:189], v221 offset:54272
	ds_read_b128 v[166:169], v221 offset:55296
	ds_read_b128 v[182:185], v221 offset:56320
; #define G8_STAGE_B(bufoff, gbase) do { _Pragma("unroll") for (int _i = 0; _i < 2; ++_i) \
;         __builtin_amdgcn_global_load_lds((const unsigned*)((const char*)(gbase) + voffB[_i]), (LAS unsigned*)(lds + (bufoff) + ldsw + _i * 8192), 16, 0, 0); } while (0)
; #define G8_LDA(dst, b, h) do { _Pragma("unroll") for (int m = 0; m < 4; ++m) _Pragma("unroll") for (int k = 0; k < 2; ++k) dst[m][k] = *(const LAS bf16x8*)(lds + G8_SA(b, h) + aoff + m * 2048 + k * 1024); } while (0)
; #define G8_LDB(dst, b, h) do { _Pragma("unroll") for (int n = 0; n < 2; ++n) _Pragma("unroll") for (int k = 0; k < 2; ++k) dst[n][k] = *(const LAS bf16x8*)(lds + G8_SB(b, h) + boff + n * 2048 + k * 1024); } while (0)
; #define G8_WAIT_V(n) asm volatile("s_waitcnt vmcnt(" #n ")" ::: "memory")
; #define G8_WAIT_L(n) asm volatile("s_waitcnt lgkmcnt(" #n ")" ::: "memory")
; #define G8_BAR __builtin_amdgcn_s_barrier()
; template <class Sched, class Epi>
; DEVI void gemm_phase(LAS unsigned char* lds, const char* Abase, const int K, const Sched& S, const Epi& E) {
;     ...
;         for (int t = 0; t < ntu; t += 2) {
;             const bool last = (t == ntu - 2);
;             const size_t k1 = (size_t)(t + 1) * kstep;
;             const size_t k2 = last ? (size_t)0 : (size_t)(t + 2) * kstep, k3 = k2 + kstep;
;             const char* b2 = last ? nB : cB + (size_t)(t + 2) * kstep; const char* b3 = b2 + kstep;
;             G8_LDB(B0, 0, 0); G8_LDB(B1, 0, 1); G8_SCHED; G8_LDA(At, 0, 0); G8_STAGE_A(G8_SA(1, 1), false, 1, k1);
;             G8_WAIT_L(0); G8_BAR; G8_MMA(0, 0, At, B0); G8_MMA(0, 1, At, B1); G8_BAR; G8_SCHED;
;             if (!skip1) G8_LDA(At, 0, 1); G8_STAGE_B(G8_SB(0, 0), b2); G8_STAGE_A(G8_SA(0, 0), last, 0, k2); G8_STAGE_B(G8_SB(0, 1), b2 + hstepB);
;             G8_WAIT_V(6); G8_WAIT_L(0); G8_BAR; if (!skip1) { G8_MMA(1, 0, At, B0); G8_MMA(1, 1, At, B1); } G8_BAR; G8_SCHED;
;             G8_LDB(B0, 1, 0); G8_LDB(B1, 1, 1); G8_SCHED; G8_LDA(At, 1, 0); G8_STAGE_A(G8_SA(0, 1), last, 1, k2);
;             G8_WAIT_L(0); G8_BAR; G8_MMA(0, 0, At, B0); G8_MMA(0, 1, At, B1); G8_BAR; G8_SCHED;
;             if (!skip1) G8_LDA(At, 1, 1); G8_STAGE_B(G8_SB(1, 0), b3); G8_STAGE_A(G8_SA(1, 0), last, 0, k3); G8_STAGE_B(G8_SB(1, 1), b3 + hstepB);
;             G8_WAIT_V(6); G8_WAIT_L(0); G8_BAR; if (!skip1) { G8_MMA(1, 0, At, B0); G8_MMA(1, 1, At, B1); } G8_BAR; G8_SCHED;
.LBB0_1021:
	s_mov_b32 m0, s50
	v_lshl_add_u64 v[4:5], v[4:5], 0, s[14:15]
	global_load_lds_dwordx4 v[4:5], off
	v_lshl_add_u64 v[4:5], v[210:211], 0, s[14:15]
	s_mov_b32 m0, s51
	s_add_u32 s36, s36, 0x40080
	global_load_lds_dwordx4 v[4:5], off
	v_lshl_add_u64 v[4:5], v[212:213], 0, s[14:15]
	s_mov_b32 m0, s52
	s_addc_u32 s37, s37, 0
	global_load_lds_dwordx4 v[4:5], off
	v_lshl_add_u64 v[4:5], v[214:215], 0, s[14:15]
	s_mov_b32 m0, s53
	s_and_b64 vcc, exec, s[4:5]
	global_load_lds_dwordx4 v[4:5], off
	v_lshl_add_u64 v[4:5], s[36:37], 0, v[198:199]
	s_mov_b32 m0, s54
	s_nop 0
	global_load_lds_dwordx4 v[4:5], off
	v_lshl_add_u64 v[4:5], s[36:37], 0, v[200:201]
	s_mov_b32 m0, s55
	s_nop 0
	global_load_lds_dwordx4 v[4:5], off
	s_waitcnt vmcnt(6)
	s_waitcnt lgkmcnt(0)
	s_barrier
	s_cbranch_vccnz .LBB0_1023
	s_setprio 1
	s_waitcnt lgkmcnt(0)
	v_mfma_f32_16x16x32_bf16 v[66:69], v[150:153], v[178:181], v[66:69]
	v_mfma_f32_16x16x32_bf16 v[62:65], v[158:161], v[178:181], v[62:65]
	v_mfma_f32_16x16x32_bf16 v[50:53], v[150:153], v[174:177], v[50:53]
	v_mfma_f32_16x16x32_bf16 v[46:49], v[158:161], v[174:177], v[46:49]
	v_mfma_f32_16x16x32_bf16 v[34:37], v[150:153], v[170:173], v[34:37]
	v_mfma_f32_16x16x32_bf16 v[30:33], v[158:161], v[170:173], v[30:33]
	v_mfma_f32_16x16x32_bf16 v[18:21], v[150:153], v[166:169], v[18:21]
	v_mfma_f32_16x16x32_bf16 v[14:17], v[158:161], v[166:169], v[14:17]
	v_mfma_f32_16x16x32_bf16 v[66:69], v[154:157], v[194:197], v[66:69]
	v_mfma_f32_16x16x32_bf16 v[62:65], v[162:165], v[194:197], v[62:65]
	v_mfma_f32_16x16x32_bf16 v[50:53], v[154:157], v[190:193], v[50:53]
	v_mfma_f32_16x16x32_bf16 v[46:49], v[162:165], v[190:193], v[46:49]
	v_mfma_f32_16x16x32_bf16 v[34:37], v[154:157], v[186:189], v[34:37]
	v_mfma_f32_16x16x32_bf16 v[30:33], v[162:165], v[186:189], v[30:33]
	v_mfma_f32_16x16x32_bf16 v[18:21], v[154:157], v[182:185], v[18:21]
	v_mfma_f32_16x16x32_bf16 v[14:17], v[162:165], v[182:185], v[14:17]
	v_mfma_f32_16x16x32_bf16 v[58:61], v[134:137], v[178:181], v[58:61]
	v_mfma_f32_16x16x32_bf16 v[54:57], v[142:145], v[178:181], v[54:57]
	v_mfma_f32_16x16x32_bf16 v[42:45], v[134:137], v[174:177], v[42:45]
	v_mfma_f32_16x16x32_bf16 v[38:41], v[142:145], v[174:177], v[38:41]
	v_mfma_f32_16x16x32_bf16 v[26:29], v[134:137], v[170:173], v[26:29]
	v_mfma_f32_16x16x32_bf16 v[22:25], v[142:145], v[170:173], v[22:25]
	v_mfma_f32_16x16x32_bf16 v[10:13], v[134:137], v[166:169], v[10:13]
	v_mfma_f32_16x16x32_bf16 v[4:7], v[142:145], v[166:169], v[6:9]
	v_mfma_f32_16x16x32_bf16 v[58:61], v[138:141], v[194:197], v[58:61]
	v_mfma_f32_16x16x32_bf16 v[54:57], v[146:149], v[194:197], v[54:57]
	v_mfma_f32_16x16x32_bf16 v[42:45], v[138:141], v[190:193], v[42:45]
	v_mfma_f32_16x16x32_bf16 v[38:41], v[146:149], v[190:193], v[38:41]
	v_mfma_f32_16x16x32_bf16 v[26:29], v[138:141], v[186:189], v[26:29]
	v_mfma_f32_16x16x32_bf16 v[22:25], v[146:149], v[186:189], v[22:25]
	v_mfma_f32_16x16x32_bf16 v[10:13], v[138:141], v[182:185], v[10:13]
	v_mfma_f32_16x16x32_bf16 v[6:9], v[146:149], v[182:185], v[4:7]
	s_setprio 0

; #define G8_STAGE_B(bufoff, gbase) do { _Pragma("unroll") for (int _i = 0; _i < 2; ++_i) \
;         __builtin_amdgcn_global_load_lds((const unsigned*)((const char*)(gbase) + voffB[_i]), (LAS unsigned*)(lds + (bufoff) + ldsw + _i * 8192), 16, 0, 0); } while (0)
; #define G8_LDA(dst, b, h) do { _Pragma("unroll") for (int m = 0; m < 4; ++m) _Pragma("unroll") for (int k = 0; k < 2; ++k) dst[m][k] = *(const LAS bf16x8*)(lds + G8_SA(b, h) + aoff + m * 2048 + k * 1024); } while (0)
; #define G8_LDB(dst, b, h) do { _Pragma("unroll") for (int n = 0; n < 2; ++n) _Pragma("unroll") for (int k = 0; k < 2; ++k) dst[n][k] = *(const LAS bf16x8*)(lds + G8_SB(b, h) + boff + n * 2048 + k * 1024); } while (0)
; #define G8_WAIT_V(n) asm volatile("s_waitcnt vmcnt(" #n ")" ::: "memory")
; #define G8_WAIT_L(n) asm volatile("s_waitcnt lgkmcnt(" #n ")" ::: "memory")
; #define G8_BAR __builtin_amdgcn_s_barrier()
; template <class Sched, class Epi>
; DEVI void gemm_phase(LAS unsigned char* lds, const char* Abase, const int K, const Sched& S, const Epi& E) {
;     ...
;         for (int t = 0; t < ntu; t += 2) {
;             const bool last = (t == ntu - 2);
;             const size_t k1 = (size_t)(t + 1) * kstep;
;             const size_t k2 = last ? (size_t)0 : (size_t)(t + 2) * kstep, k3 = k2 + kstep;
;             const char* b2 = last ? nB : cB + (size_t)(t + 2) * kstep; const char* b3 = b2 + kstep;
;             G8_LDB(B0, 0, 0); G8_LDB(B1, 0, 1); G8_SCHED; G8_LDA(At, 0, 0); G8_STAGE_A(G8_SA(1, 1), false, 1, k1);
;             G8_WAIT_L(0); G8_BAR; G8_MMA(0, 0, At, B0); G8_MMA(0, 1, At, B1); G8_BAR; G8_SCHED;
;             if (!skip1) G8_LDA(At, 0, 1); G8_STAGE_B(G8_SB(0, 0), b2); G8_STAGE_A(G8_SA(0, 0), last, 0, k2); G8_STAGE_B(G8_SB(0, 1), b2 + hstepB);
;             G8_WAIT_V(6); G8_WAIT_L(0); G8_BAR; if (!skip1) { G8_MMA(1, 0, At, B0); G8_MMA(1, 1, At, B1); } G8_BAR; G8_SCHED;
;             G8_LDB(B0, 1, 0); G8_LDB(B1, 1, 1); G8_SCHED; G8_LDA(At, 1, 0); G8_STAGE_A(G8_SA(0, 1), last, 1, k2);
;             G8_WAIT_L(0); G8_BAR; G8_MMA(0, 0, At, B0); G8_MMA(0, 1, At, B1); G8_BAR; G8_SCHED;
;             if (!skip1) G8_LDA(At, 1, 1); G8_STAGE_B(G8_SB(1, 0), b3); G8_STAGE_A(G8_SA(1, 0), last, 0, k3); G8_STAGE_B(G8_SB(1, 1), b3 + hstepB);
;             G8_WAIT_V(6); G8_WAIT_L(0); G8_BAR; if (!skip1) { G8_MMA(1, 0, At, B0); G8_MMA(1, 1, At, B1); } G8_BAR; G8_SCHED;
.LBB0_1156:
	ds_read_b128 v[150:153], v219
	ds_read_b128 v[154:157], v219 offset:1024
	ds_read_b128 v[158:161], v219 offset:2048
	ds_read_b128 v[162:165], v219 offset:3072
	ds_read_b128 v[134:137], v220
	ds_read_b128 v[138:141], v220 offset:1024
	ds_read_b128 v[142:145], v220 offset:2048
	ds_read_b128 v[146:149], v220 offset:3072
	v_lshl_add_u64 v[4:5], v[206:207], 0, s[30:31]
	s_add_i32 m0, s36, 0xc000
	s_waitcnt lgkmcnt(0)
	ds_read_b128 v[178:181], v221
	ds_read_b128 v[194:197], v221 offset:1024
	ds_read_b128 v[174:177], v221 offset:2048
	ds_read_b128 v[190:193], v221 offset:3072
	ds_read_b128 v[170:173], v221 offset:4096
	ds_read_b128 v[186:189], v221 offset:5120
	ds_read_b128 v[166:169], v221 offset:6144
	ds_read_b128 v[182:185], v221 offset:7168
	global_load_lds_dwordx4 v[4:5], off
	v_lshl_add_u64 v[4:5], v[208:209], 0, s[30:31]
	s_add_i32 m0, s36, 0xe000
	s_nop 0
	global_load_lds_dwordx4 v[4:5], off
	s_waitcnt lgkmcnt(0)
	s_barrier
	s_setprio 1
	s_waitcnt lgkmcnt(0)
	v_mfma_f32_16x16x32_bf16 v[130:133], v[150:153], v[178:181], v[130:133]
	v_mfma_f32_16x16x32_bf16 v[126:129], v[158:161], v[178:181], v[126:129]
	v_mfma_f32_16x16x32_bf16 v[122:125], v[150:153], v[174:177], v[122:125]
	v_mfma_f32_16x16x32_bf16 v[118:121], v[158:161], v[174:177], v[118:121]
	v_mfma_f32_16x16x32_bf16 v[110:113], v[150:153], v[170:173], v[110:113]
	v_mfma_f32_16x16x32_bf16 v[102:105], v[158:161], v[170:173], v[102:105]
	v_mfma_f32_16x16x32_bf16 v[94:97], v[150:153], v[166:169], v[94:97]
	v_mfma_f32_16x16x32_bf16 v[86:89], v[158:161], v[166:169], v[86:89]
	v_mfma_f32_16x16x32_bf16 v[130:133], v[154:157], v[194:197], v[130:133]
	v_mfma_f32_16x16x32_bf16 v[126:129], v[162:165], v[194:197], v[126:129]
	v_mfma_f32_16x16x32_bf16 v[122:125], v[154:157], v[190:193], v[122:125]
	v_mfma_f32_16x16x32_bf16 v[118:121], v[162:165], v[190:193], v[118:121]
	v_mfma_f32_16x16x32_bf16 v[110:113], v[154:157], v[186:189], v[110:113]
	v_mfma_f32_16x16x32_bf16 v[102:105], v[162:165], v[186:189], v[102:105]
	v_mfma_f32_16x16x32_bf16 v[94:97], v[154:157], v[182:185], v[94:97]
	v_mfma_f32_16x16x32_bf16 v[86:89], v[162:165], v[182:185], v[86:89]
	v_mfma_f32_16x16x32_bf16 v[114:117], v[134:137], v[178:181], v[114:117]
	v_mfma_f32_16x16x32_bf16 v[106:109], v[142:145], v[178:181], v[106:109]
	v_mfma_f32_16x16x32_bf16 v[98:101], v[134:137], v[174:177], v[98:101]
	v_mfma_f32_16x16x32_bf16 v[90:93], v[142:145], v[174:177], v[90:93]
	v_mfma_f32_16x16x32_bf16 v[82:85], v[134:137], v[170:173], v[82:85]
	v_mfma_f32_16x16x32_bf16 v[78:81], v[142:145], v[170:173], v[78:81]
	v_mfma_f32_16x16x32_bf16 v[74:77], v[134:137], v[166:169], v[74:77]
	v_mfma_f32_16x16x32_bf16 v[70:73], v[142:145], v[166:169], v[70:73]
	v_mfma_f32_16x16x32_bf16 v[114:117], v[138:141], v[194:197], v[114:117]
	v_mfma_f32_16x16x32_bf16 v[106:109], v[146:149], v[194:197], v[106:109]
	v_mfma_f32_16x16x32_bf16 v[98:101], v[138:141], v[190:193], v[98:101]
	v_mfma_f32_16x16x32_bf16 v[90:93], v[146:149], v[190:193], v[90:93]
	v_mfma_f32_16x16x32_bf16 v[82:85], v[138:141], v[186:189], v[82:85]
	v_mfma_f32_16x16x32_bf16 v[78:81], v[146:149], v[186:189], v[78:81]
	v_mfma_f32_16x16x32_bf16 v[74:77], v[138:141], v[182:185], v[74:77]
	v_mfma_f32_16x16x32_bf16 v[70:73], v[146:149], v[182:185], v[70:73]
	s_setprio 0
	s_barrier
	v_cmp_ne_u32_e64 s[4:5], 1, v222
	s_andn2_b64 vcc, exec, s[26:27]
	s_cbranch_vccnz .LBB0_1158
	ds_read_b128 v[178:181], v221 offset:16384
	ds_read_b128 v[194:197], v221 offset:17408
	ds_read_b128 v[174:177], v221 offset:18432
	ds_read_b128 v[190:193], v221 offset:19456
	ds_read_b128 v[170:173], v221 offset:20480
	ds_read_b128 v[186:189], v221 offset:21504
	ds_read_b128 v[166:169], v221 offset:22528
	ds_read_b128 v[182:185], v221 offset:23552
.LBB0_1158:
	s_add_u32 s28, s30, 0x100
	s_addc_u32 s29, s31, 0
	s_add_u32 s58, s44, s30
	s_addc_u32 s59, s45, s31
	s_cmpk_eq_i32 s30, 0x700
	s_cselect_b64 s[56:57], -1, 0
	s_and_b64 s[30:31], s[56:57], exec
	s_cselect_b32 s55, 0, s28
	s_cselect_b32 s31, s9, s59
	s_cselect_b32 s30, s8, s58
	s_and_b64 s[56:57], s[56:57], s[24:25]
	s_and_b64 s[56:57], s[56:57], exec
	s_cselect_b32 s57, s22, s16
	s_mov_b32 m0, s37
	v_lshl_add_u64 v[4:5], s[30:31], 0, v[198:199]
	s_cselect_b32 s56, s23, s17
	s_add_u32 s58, s57, s55
	global_load_lds_dwordx4 v[4:5], off
	v_lshl_add_u64 v[210:211], s[30:31], 0, v[200:201]
	s_mov_b32 m0, s38
	s_addc_u32 s59, s56, 0
	global_load_lds_dwordx4 v[210:211], off
	v_lshl_add_u64 v[212:213], s[58:59], 0, v[198:199]
	s_mov_b32 m0, s36
	v_lshl_add_u64 v[214:215], s[58:59], 0, v[200:201]
	s_add_u32 s58, s30, 0x40000
	global_load_lds_dwordx4 v[212:213], off
	s_mov_b32 m0, s39
	s_addc_u32 s59, s31, 0
	global_load_lds_dwordx4 v[214:215], off
	v_lshl_add_u64 v[224:225], s[58:59], 0, v[198:199]
	s_mov_b32 m0, s40
	s_and_b64 vcc, exec, s[4:5]
	global_load_lds_dwordx4 v[224:225], off
	v_lshl_add_u64 v[224:225], s[58:59], 0, v[200:201]
	s_mov_b32 m0, s41
	s_nop 0
	global_load_lds_dwordx4 v[224:225], off
	s_waitcnt vmcnt(6)
	s_waitcnt lgkmcnt(0)
	s_barrier
	s_cbranch_vccnz .LBB0_1160
; #define G8_STAGE_B(bufoff, gbase) do { _Pragma("unroll") for (int _i = 0; _i < 2; ++_i) \
;         __builtin_amdgcn_global_load_lds((const unsigned*)((const char*)(gbase) + voffB[_i]), (LAS unsigned*)(lds + (bufoff) + ldsw + _i * 8192), 16, 0, 0); } while (0)
; #define G8_LDA(dst, b, h) do { _Pragma("unroll") for (int m = 0; m < 4; ++m) _Pragma("unroll") for (int k = 0; k < 2; ++k) dst[m][k] = *(const LAS bf16x8*)(lds + G8_SA(b, h) + aoff + m * 2048 + k * 1024); } while (0)
; #define G8_LDB(dst, b, h) do { _Pragma("unroll") for (int n = 0; n < 2; ++n) _Pragma("unroll") for (int k = 0; k < 2; ++k) dst[n][k] = *(const LAS bf16x8*)(lds + G8_SB(b, h) + boff + n * 2048 + k * 1024); } while (0)
; #define G8_WAIT_V(n) asm volatile("s_waitcnt vmcnt(" #n ")" ::: "memory")
; #define G8_WAIT_L(n) asm volatile("s_waitcnt lgkmcnt(" #n ")" ::: "memory")
; #define G8_BAR __builtin_amdgcn_s_barrier()
; template <class Sched, class Epi>
; DEVI void gemm_phase(LAS unsigned char* lds, const char* Abase, const int K, const Sched& S, const Epi& E) {
;     ...
;         for (int t = 0; t < ntu; t += 2) {
;             const bool last = (t == ntu - 2);
;             const size_t k1 = (size_t)(t + 1) * kstep;
;             const size_t k2 = last ? (size_t)0 : (size_t)(t + 2) * kstep, k3 = k2 + kstep;
;             const char* b2 = last ? nB : cB + (size_t)(t + 2) * kstep; const char* b3 = b2 + kstep;
;             G8_LDB(B0, 0, 0); G8_LDB(B1, 0, 1); G8_SCHED; G8_LDA(At, 0, 0); G8_STAGE_A(G8_SA(1, 1), false, 1, k1);
;             G8_WAIT_L(0); G8_BAR; G8_MMA(0, 0, At, B0); G8_MMA(0, 1, At, B1); G8_BAR; G8_SCHED;
;             if (!skip1) G8_LDA(At, 0, 1); G8_STAGE_B(G8_SB(0, 0), b2); G8_STAGE_A(G8_SA(0, 0), last, 0, k2); G8_STAGE_B(G8_SB(0, 1), b2 + hstepB);
;             G8_WAIT_V(6); G8_WAIT_L(0); G8_BAR; if (!skip1) { G8_MMA(1, 0, At, B0); G8_MMA(1, 1, At, B1); } G8_BAR; G8_SCHED;
;             G8_LDB(B0, 1, 0); G8_LDB(B1, 1, 1); G8_SCHED; G8_LDA(At, 1, 0); G8_STAGE_A(G8_SA(0, 1), last, 1, k2);
;             G8_WAIT_L(0); G8_BAR; G8_MMA(0, 0, At, B0); G8_MMA(0, 1, At, B1); G8_BAR; G8_SCHED;
;             if (!skip1) G8_LDA(At, 1, 1); G8_STAGE_B(G8_SB(1, 0), b3); G8_STAGE_A(G8_SA(1, 0), last, 0, k3); G8_STAGE_B(G8_SB(1, 1), b3 + hstepB);
;             G8_WAIT_V(6); G8_WAIT_L(0); G8_BAR; if (!skip1) { G8_MMA(1, 0, At, B0); G8_MMA(1, 1, At, B1); } G8_BAR; G8_SCHED;
	s_setprio 1
	s_waitcnt lgkmcnt(0)
	v_mfma_f32_16x16x32_bf16 v[66:69], v[150:153], v[178:181], v[66:69]
	v_mfma_f32_16x16x32_bf16 v[62:65], v[158:161], v[178:181], v[62:65]
	v_mfma_f32_16x16x32_bf16 v[50:53], v[150:153], v[174:177], v[50:53]
	v_mfma_f32_16x16x32_bf16 v[46:49], v[158:161], v[174:177], v[46:49]
	v_mfma_f32_16x16x32_bf16 v[34:37], v[150:153], v[170:173], v[34:37]
	v_mfma_f32_16x16x32_bf16 v[30:33], v[158:161], v[170:173], v[30:33]
	v_mfma_f32_16x16x32_bf16 v[18:21], v[150:153], v[166:169], v[18:21]
	v_mfma_f32_16x16x32_bf16 v[14:17], v[158:161], v[166:169], v[14:17]
	v_mfma_f32_16x16x32_bf16 v[66:69], v[154:157], v[194:197], v[66:69]
	v_mfma_f32_16x16x32_bf16 v[62:65], v[162:165], v[194:197], v[62:65]
	v_mfma_f32_16x16x32_bf16 v[50:53], v[154:157], v[190:193], v[50:53]
	v_mfma_f32_16x16x32_bf16 v[46:49], v[162:165], v[190:193], v[46:49]
	v_mfma_f32_16x16x32_bf16 v[34:37], v[154:157], v[186:189], v[34:37]
	v_mfma_f32_16x16x32_bf16 v[30:33], v[162:165], v[186:189], v[30:33]
	v_mfma_f32_16x16x32_bf16 v[18:21], v[154:157], v[182:185], v[18:21]
	v_mfma_f32_16x16x32_bf16 v[14:17], v[162:165], v[182:185], v[14:17]
	v_mfma_f32_16x16x32_bf16 v[58:61], v[134:137], v[178:181], v[58:61]
	v_mfma_f32_16x16x32_bf16 v[54:57], v[142:145], v[178:181], v[54:57]
	v_mfma_f32_16x16x32_bf16 v[42:45], v[134:137], v[174:177], v[42:45]
	v_mfma_f32_16x16x32_bf16 v[38:41], v[142:145], v[174:177], v[38:41]
	v_mfma_f32_16x16x32_bf16 v[26:29], v[134:137], v[170:173], v[26:29]
	v_mfma_f32_16x16x32_bf16 v[22:25], v[142:145], v[170:173], v[22:25]
	v_mfma_f32_16x16x32_bf16 v[10:13], v[134:137], v[166:169], v[10:13]
	v_mfma_f32_16x16x32_bf16 v[6:9], v[142:145], v[166:169], v[6:9]
	v_mfma_f32_16x16x32_bf16 v[58:61], v[138:141], v[194:197], v[58:61]
	v_mfma_f32_16x16x32_bf16 v[54:57], v[146:149], v[194:197], v[54:57]
	v_mfma_f32_16x16x32_bf16 v[42:45], v[138:141], v[190:193], v[42:45]
	v_mfma_f32_16x16x32_bf16 v[38:41], v[146:149], v[190:193], v[38:41]
	v_mfma_f32_16x16x32_bf16 v[26:29], v[138:141], v[186:189], v[26:29]
	v_mfma_f32_16x16x32_bf16 v[22:25], v[146:149], v[186:189], v[22:25]
	v_mfma_f32_16x16x32_bf16 v[10:13], v[138:141], v[182:185], v[10:13]
	v_mfma_f32_16x16x32_bf16 v[6:9], v[146:149], v[182:185], v[6:9]
	s_setprio 0
.LBB0_1160:
	s_barrier
	v_add_u32_e32 v3, 0x18000, v218
	ds_read_b128 v[150:153], v3
	ds_read_b128 v[154:157], v3 offset:1024
	ds_read_b128 v[158:161], v3 offset:2048
	ds_read_b128 v[162:165], v3 offset:3072
	v_add_u32_e32 v3, 0x1c000, v218
	ds_read_b128 v[134:137], v3
	ds_read_b128 v[138:141], v3 offset:1024
	ds_read_b128 v[142:145], v3 offset:2048
	ds_read_b128 v[146:149], v3 offset:3072
	s_add_u32 s55, s57, s55
	s_addc_u32 s57, s56, 0
	s_add_u32 s56, s55, 0x40000
	s_addc_u32 s57, s57, 0
	s_mov_b32 m0, s42
	v_lshl_add_u64 v[224:225], s[56:57], 0, v[198:199]
	s_waitcnt lgkmcnt(0)
	ds_read_b128 v[178:181], v221 offset:32768
	ds_read_b128 v[194:197], v221 offset:33792
	ds_read_b128 v[174:177], v221 offset:34816
	ds_read_b128 v[190:193], v221 offset:35840
	ds_read_b128 v[170:173], v221 offset:36864
	ds_read_b128 v[186:189], v221 offset:37888
	ds_read_b128 v[166:169], v221 offset:38912
	ds_read_b128 v[182:185], v221 offset:39936
	global_load_lds_dwordx4 v[224:225], off
	v_lshl_add_u64 v[224:225], s[56:57], 0, v[200:201]
	s_mov_b32 m0, s43
	s_nop 0
	global_load_lds_dwordx4 v[224:225], off
	s_waitcnt lgkmcnt(0)
	s_barrier
	s_setprio 1
	s_waitcnt lgkmcnt(0)
	v_mfma_f32_16x16x32_bf16 v[130:133], v[150:153], v[178:181], v[130:133]
	v_mfma_f32_16x16x32_bf16 v[126:129], v[158:161], v[178:181], v[126:129]
	v_mfma_f32_16x16x32_bf16 v[122:125], v[150:153], v[174:177], v[122:125]
	v_mfma_f32_16x16x32_bf16 v[118:121], v[158:161], v[174:177], v[118:121]
	v_mfma_f32_16x16x32_bf16 v[110:113], v[150:153], v[170:173], v[110:113]
	v_mfma_f32_16x16x32_bf16 v[102:105], v[158:161], v[170:173], v[102:105]
	v_mfma_f32_16x16x32_bf16 v[94:97], v[150:153], v[166:169], v[94:97]
	v_mfma_f32_16x16x32_bf16 v[86:89], v[158:161], v[166:169], v[86:89]
	v_mfma_f32_16x16x32_bf16 v[130:133], v[154:157], v[194:197], v[130:133]
	v_mfma_f32_16x16x32_bf16 v[126:129], v[162:165], v[194:197], v[126:129]
	v_mfma_f32_16x16x32_bf16 v[122:125], v[154:157], v[190:193], v[122:125]
	v_mfma_f32_16x16x32_bf16 v[118:121], v[162:165], v[190:193], v[118:121]
	v_mfma_f32_16x16x32_bf16 v[110:113], v[154:157], v[186:189], v[110:113]
	v_mfma_f32_16x16x32_bf16 v[102:105], v[162:165], v[186:189], v[102:105]
	v_mfma_f32_16x16x32_bf16 v[94:97], v[154:157], v[182:185], v[94:97]
	v_mfma_f32_16x16x32_bf16 v[86:89], v[162:165], v[182:185], v[86:89]
	v_mfma_f32_16x16x32_bf16 v[114:117], v[134:137], v[178:181], v[114:117]
	v_mfma_f32_16x16x32_bf16 v[106:109], v[142:145], v[178:181], v[106:109]
	v_mfma_f32_16x16x32_bf16 v[98:101], v[134:137], v[174:177], v[98:101]
	v_mfma_f32_16x16x32_bf16 v[90:93], v[142:145], v[174:177], v[90:93]
	v_mfma_f32_16x16x32_bf16 v[82:85], v[134:137], v[170:173], v[82:85]
	v_mfma_f32_16x16x32_bf16 v[78:81], v[142:145], v[170:173], v[78:81]
	v_mfma_f32_16x16x32_bf16 v[74:77], v[134:137], v[166:169], v[74:77]
	v_mfma_f32_16x16x32_bf16 v[70:73], v[142:145], v[166:169], v[70:73]
	v_mfma_f32_16x16x32_bf16 v[114:117], v[138:141], v[194:197], v[114:117]
	v_mfma_f32_16x16x32_bf16 v[106:109], v[146:149], v[194:197], v[106:109]
	v_mfma_f32_16x16x32_bf16 v[98:101], v[138:141], v[190:193], v[98:101]
	v_mfma_f32_16x16x32_bf16 v[90:93], v[146:149], v[190:193], v[90:93]
	v_mfma_f32_16x16x32_bf16 v[82:85], v[138:141], v[186:189], v[82:85]
	v_mfma_f32_16x16x32_bf16 v[78:81], v[146:149], v[186:189], v[78:81]
	v_mfma_f32_16x16x32_bf16 v[74:77], v[138:141], v[182:185], v[74:77]
	v_mfma_f32_16x16x32_bf16 v[70:73], v[146:149], v[182:185], v[70:73]
	s_setprio 0
	s_barrier
	s_and_b64 vcc, exec, s[4:5]
	s_cbranch_vccnz .LBB0_1162
	ds_read_b128 v[178:181], v221 offset:49152
	ds_read_b128 v[194:197], v221 offset:50176
	ds_read_b128 v[174:177], v221 offset:51200
	ds_read_b128 v[190:193], v221 offset:52224
	ds_read_b128 v[170:173], v221 offset:53248
	ds_read_b128 v[186:189], v221 offset:54272
	ds_read_b128 v[166:169], v221 offset:55296
	ds_read_b128 v[182:185], v221 offset:56320
; #define G8_STAGE_B(bufoff, gbase) do { _Pragma("unroll") for (int _i = 0; _i < 2; ++_i) \
;         __builtin_amdgcn_global_load_lds((const unsigned*)((const char*)(gbase) + voffB[_i]), (LAS unsigned*)(lds + (bufoff) + ldsw + _i * 8192), 16, 0, 0); } while (0)
; #define G8_LDA(dst, b, h) do { _Pragma("unroll") for (int m = 0; m < 4; ++m) _Pragma("unroll") for (int k = 0; k < 2; ++k) dst[m][k] = *(const LAS bf16x8*)(lds + G8_SA(b, h) + aoff + m * 2048 + k * 1024); } while (0)
; #define G8_LDB(dst, b, h) do { _Pragma("unroll") for (int n = 0; n < 2; ++n) _Pragma("unroll") for (int k = 0; k < 2; ++k) dst[n][k] = *(const LAS bf16x8*)(lds + G8_SB(b, h) + boff + n * 2048 + k * 1024); } while (0)
; #define G8_WAIT_V(n) asm volatile("s_waitcnt vmcnt(" #n ")" ::: "memory")
; #define G8_WAIT_L(n) asm volatile("s_waitcnt lgkmcnt(" #n ")" ::: "memory")
; #define G8_BAR __builtin_amdgcn_s_barrier()
; template <class Sched, class Epi>
; DEVI void gemm_phase(LAS unsigned char* lds, const char* Abase, const int K, const Sched& S, const Epi& E) {
;     ...
;         for (int t = 0; t < ntu; t += 2) {
;             const bool last = (t == ntu - 2);
;             const size_t k1 = (size_t)(t + 1) * kstep;
;             const size_t k2 = last ? (size_t)0 : (size_t)(t + 2) * kstep, k3 = k2 + kstep;
;             const char* b2 = last ? nB : cB + (size_t)(t + 2) * kstep; const char* b3 = b2 + kstep;
;             G8_LDB(B0, 0, 0); G8_LDB(B1, 0, 1); G8_SCHED; G8_LDA(At, 0, 0); G8_STAGE_A(G8_SA(1, 1), false, 1, k1);
;             G8_WAIT_L(0); G8_BAR; G8_MMA(0, 0, At, B0); G8_MMA(0, 1, At, B1); G8_BAR; G8_SCHED;
;             if (!skip1) G8_LDA(At, 0, 1); G8_STAGE_B(G8_SB(0, 0), b2); G8_STAGE_A(G8_SA(0, 0), last, 0, k2); G8_STAGE_B(G8_SB(0, 1), b2 + hstepB);
;             G8_WAIT_V(6); G8_WAIT_L(0); G8_BAR; if (!skip1) { G8_MMA(1, 0, At, B0); G8_MMA(1, 1, At, B1); } G8_BAR; G8_SCHED;
;             G8_LDB(B0, 1, 0); G8_LDB(B1, 1, 1); G8_SCHED; G8_LDA(At, 1, 0); G8_STAGE_A(G8_SA(0, 1), last, 1, k2);
;             G8_WAIT_L(0); G8_BAR; G8_MMA(0, 0, At, B0); G8_MMA(0, 1, At, B1); G8_BAR; G8_SCHED;
;             if (!skip1) G8_LDA(At, 1, 1); G8_STAGE_B(G8_SB(1, 0), b3); G8_STAGE_A(G8_SA(1, 0), last, 0, k3); G8_STAGE_B(G8_SB(1, 1), b3 + hstepB);
;             G8_WAIT_V(6); G8_WAIT_L(0); G8_BAR; if (!skip1) { G8_MMA(1, 0, At, B0); G8_MMA(1, 1, At, B1); } G8_BAR; G8_SCHED;
.LBB0_1162:
	s_mov_b32 m0, s47
	v_lshl_add_u64 v[4:5], v[4:5], 0, s[12:13]
	global_load_lds_dwordx4 v[4:5], off
	v_lshl_add_u64 v[4:5], v[210:211], 0, s[12:13]
	s_mov_b32 m0, s48
	s_add_u32 s30, s30, 0x40080
	global_load_lds_dwordx4 v[4:5], off
	v_lshl_add_u64 v[4:5], v[212:213], 0, s[12:13]
	s_mov_b32 m0, s49
	s_addc_u32 s31, s31, 0
	global_load_lds_dwordx4 v[4:5], off
	v_lshl_add_u64 v[4:5], v[214:215], 0, s[12:13]
	s_mov_b32 m0, s50
	s_and_b64 vcc, exec, s[4:5]
	global_load_lds_dwordx4 v[4:5], off
	v_lshl_add_u64 v[4:5], s[30:31], 0, v[198:199]
	s_mov_b32 m0, s51
	s_nop 0
	global_load_lds_dwordx4 v[4:5], off
	v_lshl_add_u64 v[4:5], s[30:31], 0, v[200:201]
	s_mov_b32 m0, s52
	s_nop 0
	global_load_lds_dwordx4 v[4:5], off
	s_waitcnt vmcnt(6)
	s_waitcnt lgkmcnt(0)
	s_barrier
	s_cbranch_vccnz .LBB0_1164
	s_setprio 1
	s_waitcnt lgkmcnt(0)
	v_mfma_f32_16x16x32_bf16 v[66:69], v[150:153], v[178:181], v[66:69]
	v_mfma_f32_16x16x32_bf16 v[62:65], v[158:161], v[178:181], v[62:65]
	v_mfma_f32_16x16x32_bf16 v[50:53], v[150:153], v[174:177], v[50:53]
	v_mfma_f32_16x16x32_bf16 v[46:49], v[158:161], v[174:177], v[46:49]
	v_mfma_f32_16x16x32_bf16 v[34:37], v[150:153], v[170:173], v[34:37]
	v_mfma_f32_16x16x32_bf16 v[30:33], v[158:161], v[170:173], v[30:33]
	v_mfma_f32_16x16x32_bf16 v[18:21], v[150:153], v[166:169], v[18:21]
	v_mfma_f32_16x16x32_bf16 v[14:17], v[158:161], v[166:169], v[14:17]
	v_mfma_f32_16x16x32_bf16 v[66:69], v[154:157], v[194:197], v[66:69]
	v_mfma_f32_16x16x32_bf16 v[62:65], v[162:165], v[194:197], v[62:65]
	v_mfma_f32_16x16x32_bf16 v[50:53], v[154:157], v[190:193], v[50:53]
	v_mfma_f32_16x16x32_bf16 v[46:49], v[162:165], v[190:193], v[46:49]
	v_mfma_f32_16x16x32_bf16 v[34:37], v[154:157], v[186:189], v[34:37]
	v_mfma_f32_16x16x32_bf16 v[30:33], v[162:165], v[186:189], v[30:33]
	v_mfma_f32_16x16x32_bf16 v[18:21], v[154:157], v[182:185], v[18:21]
	v_mfma_f32_16x16x32_bf16 v[14:17], v[162:165], v[182:185], v[14:17]
	v_mfma_f32_16x16x32_bf16 v[58:61], v[134:137], v[178:181], v[58:61]
	v_mfma_f32_16x16x32_bf16 v[54:57], v[142:145], v[178:181], v[54:57]
	v_mfma_f32_16x16x32_bf16 v[42:45], v[134:137], v[174:177], v[42:45]
	v_mfma_f32_16x16x32_bf16 v[38:41], v[142:145], v[174:177], v[38:41]
	v_mfma_f32_16x16x32_bf16 v[26:29], v[134:137], v[170:173], v[26:29]
	v_mfma_f32_16x16x32_bf16 v[22:25], v[142:145], v[170:173], v[22:25]
	v_mfma_f32_16x16x32_bf16 v[10:13], v[134:137], v[166:169], v[10:13]
	v_mfma_f32_16x16x32_bf16 v[4:7], v[142:145], v[166:169], v[6:9]
	v_mfma_f32_16x16x32_bf16 v[58:61], v[138:141], v[194:197], v[58:61]
	v_mfma_f32_16x16x32_bf16 v[54:57], v[146:149], v[194:197], v[54:57]
	v_mfma_f32_16x16x32_bf16 v[42:45], v[138:141], v[190:193], v[42:45]
	v_mfma_f32_16x16x32_bf16 v[38:41], v[146:149], v[190:193], v[38:41]
	v_mfma_f32_16x16x32_bf16 v[26:29], v[138:141], v[186:189], v[26:29]
	v_mfma_f32_16x16x32_bf16 v[22:25], v[146:149], v[186:189], v[22:25]
	v_mfma_f32_16x16x32_bf16 v[10:13], v[138:141], v[182:185], v[10:13]
	v_mfma_f32_16x16x32_bf16 v[6:9], v[146:149], v[182:185], v[4:7]
	s_setprio 0

; #define G8_STAGE_B(bufoff, gbase) do { _Pragma("unroll") for (int _i = 0; _i < 2; ++_i) \
;         __builtin_amdgcn_global_load_lds((const unsigned*)((const char*)(gbase) + voffB[_i]), (LAS unsigned*)(lds + (bufoff) + ldsw + _i * 8192), 16, 0, 0); } while (0)
; #define G8_LDA(dst, b, h) do { _Pragma("unroll") for (int m = 0; m < 4; ++m) _Pragma("unroll") for (int k = 0; k < 2; ++k) dst[m][k] = *(const LAS bf16x8*)(lds + G8_SA(b, h) + aoff + m * 2048 + k * 1024); } while (0)
; #define G8_LDB(dst, b, h) do { _Pragma("unroll") for (int n = 0; n < 2; ++n) _Pragma("unroll") for (int k = 0; k < 2; ++k) dst[n][k] = *(const LAS bf16x8*)(lds + G8_SB(b, h) + boff + n * 2048 + k * 1024); } while (0)
; #define G8_WAIT_V(n) asm volatile("s_waitcnt vmcnt(" #n ")" ::: "memory")
; #define G8_WAIT_L(n) asm volatile("s_waitcnt lgkmcnt(" #n ")" ::: "memory")
; #define G8_BAR __builtin_amdgcn_s_barrier()
; template <class Sched, class Epi>
; DEVI void gemm_phase(LAS unsigned char* lds, const char* Abase, const int K, const Sched& S, const Epi& E) {
;     ...
;         for (int t = 0; t < ntu; t += 2) {
;             const bool last = (t == ntu - 2);
;             const size_t k1 = (size_t)(t + 1) * kstep;
;             const size_t k2 = last ? (size_t)0 : (size_t)(t + 2) * kstep, k3 = k2 + kstep;
;             const char* b2 = last ? nB : cB + (size_t)(t + 2) * kstep; const char* b3 = b2 + kstep;
;             G8_LDB(B0, 0, 0); G8_LDB(B1, 0, 1); G8_SCHED; G8_LDA(At, 0, 0); G8_STAGE_A(G8_SA(1, 1), false, 1, k1);
;             G8_WAIT_L(0); G8_BAR; G8_MMA(0, 0, At, B0); G8_MMA(0, 1, At, B1); G8_BAR; G8_SCHED;
;             if (!skip1) G8_LDA(At, 0, 1); G8_STAGE_B(G8_SB(0, 0), b2); G8_STAGE_A(G8_SA(0, 0), last, 0, k2); G8_STAGE_B(G8_SB(0, 1), b2 + hstepB);
;             G8_WAIT_V(6); G8_WAIT_L(0); G8_BAR; if (!skip1) { G8_MMA(1, 0, At, B0); G8_MMA(1, 1, At, B1); } G8_BAR; G8_SCHED;
;             G8_LDB(B0, 1, 0); G8_LDB(B1, 1, 1); G8_SCHED; G8_LDA(At, 1, 0); G8_STAGE_A(G8_SA(0, 1), last, 1, k2);
;             G8_WAIT_L(0); G8_BAR; G8_MMA(0, 0, At, B0); G8_MMA(0, 1, At, B1); G8_BAR; G8_SCHED;
;             if (!skip1) G8_LDA(At, 1, 1); G8_STAGE_B(G8_SB(1, 0), b3); G8_STAGE_A(G8_SA(1, 0), last, 0, k3); G8_STAGE_B(G8_SB(1, 1), b3 + hstepB);
;             G8_WAIT_V(6); G8_WAIT_L(0); G8_BAR; if (!skip1) { G8_MMA(1, 0, At, B0); G8_MMA(1, 1, At, B1); } G8_BAR; G8_SCHED;
.LBB0_1461:
	ds_read_b128 v[156:159], v226
	ds_read_b128 v[160:163], v226 offset:1024
	ds_read_b128 v[164:167], v226 offset:2048
	ds_read_b128 v[168:171], v226 offset:3072
	ds_read_b128 v[140:143], v227
	ds_read_b128 v[144:147], v227 offset:1024
	ds_read_b128 v[148:151], v227 offset:2048
	ds_read_b128 v[152:155], v227 offset:3072
	s_mov_b32 m0, s58
	v_lshl_add_u64 v[4:5], v[216:217], 0, s[28:29]
	s_waitcnt lgkmcnt(0)
	ds_read_b128 v[184:187], v228
	ds_read_b128 v[200:203], v228 offset:1024
	ds_read_b128 v[180:183], v228 offset:2048
	ds_read_b128 v[196:199], v228 offset:3072
	ds_read_b128 v[176:179], v228 offset:4096
	ds_read_b128 v[192:195], v228 offset:5120
	ds_read_b128 v[172:175], v228 offset:6144
	ds_read_b128 v[188:191], v228 offset:7168
	global_load_lds_dwordx4 v[4:5], off
	v_lshl_add_u64 v[4:5], v[214:215], 0, s[28:29]
	s_mov_b32 m0, s59
	s_nop 0
	global_load_lds_dwordx4 v[4:5], off
	s_waitcnt lgkmcnt(0)
	s_barrier
	s_setprio 1
	s_waitcnt lgkmcnt(0)
	v_mfma_f32_16x16x32_bf16 v[136:139], v[156:159], v[184:187], v[136:139]
	v_mfma_f32_16x16x32_bf16 v[132:135], v[164:167], v[184:187], v[132:135]
	v_mfma_f32_16x16x32_bf16 v[120:123], v[156:159], v[180:183], v[120:123]
	v_mfma_f32_16x16x32_bf16 v[116:119], v[164:167], v[180:183], v[116:119]
	v_mfma_f32_16x16x32_bf16 v[104:107], v[156:159], v[176:179], v[104:107]
	v_mfma_f32_16x16x32_bf16 v[100:103], v[164:167], v[176:179], v[100:103]
	v_mfma_f32_16x16x32_bf16 v[88:91], v[156:159], v[172:175], v[88:91]
	v_mfma_f32_16x16x32_bf16 v[84:87], v[164:167], v[172:175], v[84:87]
	v_mfma_f32_16x16x32_bf16 v[136:139], v[160:163], v[200:203], v[136:139]
	v_mfma_f32_16x16x32_bf16 v[132:135], v[168:171], v[200:203], v[132:135]
	v_mfma_f32_16x16x32_bf16 v[120:123], v[160:163], v[196:199], v[120:123]
	v_mfma_f32_16x16x32_bf16 v[116:119], v[168:171], v[196:199], v[116:119]
	v_mfma_f32_16x16x32_bf16 v[104:107], v[160:163], v[192:195], v[104:107]
	v_mfma_f32_16x16x32_bf16 v[100:103], v[168:171], v[192:195], v[100:103]
	v_mfma_f32_16x16x32_bf16 v[88:91], v[160:163], v[188:191], v[88:91]
	v_mfma_f32_16x16x32_bf16 v[84:87], v[168:171], v[188:191], v[84:87]
	v_mfma_f32_16x16x32_bf16 v[128:131], v[140:143], v[184:187], v[128:131]
	v_mfma_f32_16x16x32_bf16 v[124:127], v[148:151], v[184:187], v[124:127]
	v_mfma_f32_16x16x32_bf16 v[112:115], v[140:143], v[180:183], v[112:115]
	v_mfma_f32_16x16x32_bf16 v[108:111], v[148:151], v[180:183], v[108:111]
	v_mfma_f32_16x16x32_bf16 v[96:99], v[140:143], v[176:179], v[96:99]
	v_mfma_f32_16x16x32_bf16 v[92:95], v[148:151], v[176:179], v[92:95]
	v_mfma_f32_16x16x32_bf16 v[80:83], v[140:143], v[172:175], v[80:83]
	v_mfma_f32_16x16x32_bf16 v[76:79], v[148:151], v[172:175], v[76:79]
	v_mfma_f32_16x16x32_bf16 v[128:131], v[144:147], v[200:203], v[128:131]
	v_mfma_f32_16x16x32_bf16 v[124:127], v[152:155], v[200:203], v[124:127]
	v_mfma_f32_16x16x32_bf16 v[112:115], v[144:147], v[196:199], v[112:115]
	v_mfma_f32_16x16x32_bf16 v[108:111], v[152:155], v[196:199], v[108:111]
	v_mfma_f32_16x16x32_bf16 v[96:99], v[144:147], v[192:195], v[96:99]
	v_mfma_f32_16x16x32_bf16 v[92:95], v[152:155], v[192:195], v[92:95]
	v_mfma_f32_16x16x32_bf16 v[80:83], v[144:147], v[188:191], v[80:83]
	v_mfma_f32_16x16x32_bf16 v[76:79], v[152:155], v[188:191], v[76:79]
	s_setprio 0
	s_barrier
	s_and_b64 vcc, exec, s[4:5]
	s_cbranch_vccnz .LBB0_1463
	ds_read_b128 v[184:187], v228 offset:16384
	ds_read_b128 v[200:203], v228 offset:17408
	ds_read_b128 v[180:183], v228 offset:18432
	ds_read_b128 v[196:199], v228 offset:19456
	ds_read_b128 v[176:179], v228 offset:20480
	ds_read_b128 v[192:195], v228 offset:21504
	ds_read_b128 v[172:175], v228 offset:22528
	ds_read_b128 v[188:191], v228 offset:23552

; #define G8_STAGE_B(bufoff, gbase) do { _Pragma("unroll") for (int _i = 0; _i < 2; ++_i) \
;         __builtin_amdgcn_global_load_lds((const unsigned*)((const char*)(gbase) + voffB[_i]), (LAS unsigned*)(lds + (bufoff) + ldsw + _i * 8192), 16, 0, 0); } while (0)
; #define G8_LDA(dst, b, h) do { _Pragma("unroll") for (int m = 0; m < 4; ++m) _Pragma("unroll") for (int k = 0; k < 2; ++k) dst[m][k] = *(const LAS bf16x8*)(lds + G8_SA(b, h) + aoff + m * 2048 + k * 1024); } while (0)
; #define G8_LDB(dst, b, h) do { _Pragma("unroll") for (int n = 0; n < 2; ++n) _Pragma("unroll") for (int k = 0; k < 2; ++k) dst[n][k] = *(const LAS bf16x8*)(lds + G8_SB(b, h) + boff + n * 2048 + k * 1024); } while (0)
; #define G8_WAIT_V(n) asm volatile("s_waitcnt vmcnt(" #n ")" ::: "memory")
; #define G8_WAIT_L(n) asm volatile("s_waitcnt lgkmcnt(" #n ")" ::: "memory")
; #define G8_BAR __builtin_amdgcn_s_barrier()
; template <class Sched, class Epi>
; DEVI void gemm_phase(LAS unsigned char* lds, const char* Abase, const int K, const Sched& S, const Epi& E) {
;     ...
;         for (int t = 0; t < ntu; t += 2) {
;             const bool last = (t == ntu - 2);
;             const size_t k1 = (size_t)(t + 1) * kstep;
;             const size_t k2 = last ? (size_t)0 : (size_t)(t + 2) * kstep, k3 = k2 + kstep;
;             const char* b2 = last ? nB : cB + (size_t)(t + 2) * kstep; const char* b3 = b2 + kstep;
;             G8_LDB(B0, 0, 0); G8_LDB(B1, 0, 1); G8_SCHED; G8_LDA(At, 0, 0); G8_STAGE_A(G8_SA(1, 1), false, 1, k1);
;             G8_WAIT_L(0); G8_BAR; G8_MMA(0, 0, At, B0); G8_MMA(0, 1, At, B1); G8_BAR; G8_SCHED;
;             if (!skip1) G8_LDA(At, 0, 1); G8_STAGE_B(G8_SB(0, 0), b2); G8_STAGE_A(G8_SA(0, 0), last, 0, k2); G8_STAGE_B(G8_SB(0, 1), b2 + hstepB);
;             G8_WAIT_V(6); G8_WAIT_L(0); G8_BAR; if (!skip1) { G8_MMA(1, 0, At, B0); G8_MMA(1, 1, At, B1); } G8_BAR; G8_SCHED;
;             G8_LDB(B0, 1, 0); G8_LDB(B1, 1, 1); G8_SCHED; G8_LDA(At, 1, 0); G8_STAGE_A(G8_SA(0, 1), last, 1, k2);
;             G8_WAIT_L(0); G8_BAR; G8_MMA(0, 0, At, B0); G8_MMA(0, 1, At, B1); G8_BAR; G8_SCHED;
;             if (!skip1) G8_LDA(At, 1, 1); G8_STAGE_B(G8_SB(1, 0), b3); G8_STAGE_A(G8_SA(1, 0), last, 0, k3); G8_STAGE_B(G8_SB(1, 1), b3 + hstepB);
;             G8_WAIT_V(6); G8_WAIT_L(0); G8_BAR; if (!skip1) { G8_MMA(1, 0, At, B0); G8_MMA(1, 1, At, B1); } G8_BAR; G8_SCHED;
.LBB0_1467:
	s_add_u32 s36, s28, 0x40000
	s_mov_b32 m0, s42
	s_addc_u32 s37, s29, 0
	global_load_lds_dwordx4 v2, s[30:31]
	v_lshl_add_u64 v[222:223], s[36:37], 0, v[204:205]
	s_mov_b32 m0, s43
	s_and_b64 vcc, exec, s[4:5]
	global_load_lds_dwordx4 v[222:223], off
	v_lshl_add_u64 v[222:223], s[36:37], 0, v[206:207]
	s_mov_b32 m0, s44
	s_nop 0
	global_load_lds_dwordx4 v[222:223], off
	s_waitcnt vmcnt(6)
	s_waitcnt lgkmcnt(0)
	s_barrier
	s_cbranch_vccnz .LBB0_1469
	s_setprio 1
	s_waitcnt lgkmcnt(0)
	v_mfma_f32_16x16x32_bf16 v[72:75], v[156:159], v[184:187], v[72:75]
	v_mfma_f32_16x16x32_bf16 v[68:71], v[164:167], v[184:187], v[68:71]
	v_mfma_f32_16x16x32_bf16 v[56:59], v[156:159], v[180:183], v[56:59]
	v_mfma_f32_16x16x32_bf16 v[52:55], v[164:167], v[180:183], v[52:55]
	v_mfma_f32_16x16x32_bf16 v[40:43], v[156:159], v[176:179], v[40:43]
	v_mfma_f32_16x16x32_bf16 v[36:39], v[164:167], v[176:179], v[36:39]
	v_mfma_f32_16x16x32_bf16 v[24:27], v[156:159], v[172:175], v[24:27]
	v_mfma_f32_16x16x32_bf16 v[20:23], v[164:167], v[172:175], v[20:23]
	v_mfma_f32_16x16x32_bf16 v[72:75], v[160:163], v[200:203], v[72:75]
	v_mfma_f32_16x16x32_bf16 v[68:71], v[168:171], v[200:203], v[68:71]
	v_mfma_f32_16x16x32_bf16 v[56:59], v[160:163], v[196:199], v[56:59]
	v_mfma_f32_16x16x32_bf16 v[52:55], v[168:171], v[196:199], v[52:55]
	v_mfma_f32_16x16x32_bf16 v[40:43], v[160:163], v[192:195], v[40:43]
	v_mfma_f32_16x16x32_bf16 v[36:39], v[168:171], v[192:195], v[36:39]
	v_mfma_f32_16x16x32_bf16 v[24:27], v[160:163], v[188:191], v[24:27]
	v_mfma_f32_16x16x32_bf16 v[20:23], v[168:171], v[188:191], v[20:23]
	v_mfma_f32_16x16x32_bf16 v[64:67], v[140:143], v[184:187], v[64:67]
	v_mfma_f32_16x16x32_bf16 v[60:63], v[148:151], v[184:187], v[60:63]
	v_mfma_f32_16x16x32_bf16 v[48:51], v[140:143], v[180:183], v[48:51]
	v_mfma_f32_16x16x32_bf16 v[44:47], v[148:151], v[180:183], v[44:47]
	v_mfma_f32_16x16x32_bf16 v[32:35], v[140:143], v[176:179], v[32:35]
	v_mfma_f32_16x16x32_bf16 v[28:31], v[148:151], v[176:179], v[28:31]
	v_mfma_f32_16x16x32_bf16 v[16:19], v[140:143], v[172:175], v[16:19]
	v_mfma_f32_16x16x32_bf16 v[12:15], v[148:151], v[172:175], v[12:15]
	v_mfma_f32_16x16x32_bf16 v[64:67], v[144:147], v[200:203], v[64:67]
	v_mfma_f32_16x16x32_bf16 v[60:63], v[152:155], v[200:203], v[60:63]
	v_mfma_f32_16x16x32_bf16 v[48:51], v[144:147], v[196:199], v[48:51]
	v_mfma_f32_16x16x32_bf16 v[44:47], v[152:155], v[196:199], v[44:47]
	v_mfma_f32_16x16x32_bf16 v[32:35], v[144:147], v[192:195], v[32:35]
	v_mfma_f32_16x16x32_bf16 v[28:31], v[152:155], v[192:195], v[28:31]
	v_mfma_f32_16x16x32_bf16 v[16:19], v[144:147], v[188:191], v[16:19]
	v_mfma_f32_16x16x32_bf16 v[12:15], v[152:155], v[188:191], v[12:15]
	s_setprio 0

; #define G8_STAGE_B(bufoff, gbase) do { _Pragma("unroll") for (int _i = 0; _i < 2; ++_i) \
;         __builtin_amdgcn_global_load_lds((const unsigned*)((const char*)(gbase) + voffB[_i]), (LAS unsigned*)(lds + (bufoff) + ldsw + _i * 8192), 16, 0, 0); } while (0)
; #define G8_LDA(dst, b, h) do { _Pragma("unroll") for (int m = 0; m < 4; ++m) _Pragma("unroll") for (int k = 0; k < 2; ++k) dst[m][k] = *(const LAS bf16x8*)(lds + G8_SA(b, h) + aoff + m * 2048 + k * 1024); } while (0)
; #define G8_LDB(dst, b, h) do { _Pragma("unroll") for (int n = 0; n < 2; ++n) _Pragma("unroll") for (int k = 0; k < 2; ++k) dst[n][k] = *(const LAS bf16x8*)(lds + G8_SB(b, h) + boff + n * 2048 + k * 1024); } while (0)
; #define G8_WAIT_V(n) asm volatile("s_waitcnt vmcnt(" #n ")" ::: "memory")
; #define G8_WAIT_L(n) asm volatile("s_waitcnt lgkmcnt(" #n ")" ::: "memory")
; #define G8_BAR __builtin_amdgcn_s_barrier()
; template <class Sched, class Epi>
; DEVI void gemm_phase(LAS unsigned char* lds, const char* Abase, const int K, const Sched& S, const Epi& E) {
;     ...
;         for (int t = 0; t < ntu; t += 2) {
;             const bool last = (t == ntu - 2);
;             const size_t k1 = (size_t)(t + 1) * kstep;
;             const size_t k2 = last ? (size_t)0 : (size_t)(t + 2) * kstep, k3 = k2 + kstep;
;             const char* b2 = last ? nB : cB + (size_t)(t + 2) * kstep; const char* b3 = b2 + kstep;
;             G8_LDB(B0, 0, 0); G8_LDB(B1, 0, 1); G8_SCHED; G8_LDA(At, 0, 0); G8_STAGE_A(G8_SA(1, 1), false, 1, k1);
;             G8_WAIT_L(0); G8_BAR; G8_MMA(0, 0, At, B0); G8_MMA(0, 1, At, B1); G8_BAR; G8_SCHED;
;             if (!skip1) G8_LDA(At, 0, 1); G8_STAGE_B(G8_SB(0, 0), b2); G8_STAGE_A(G8_SA(0, 0), last, 0, k2); G8_STAGE_B(G8_SB(0, 1), b2 + hstepB);
;             G8_WAIT_V(6); G8_WAIT_L(0); G8_BAR; if (!skip1) { G8_MMA(1, 0, At, B0); G8_MMA(1, 1, At, B1); } G8_BAR; G8_SCHED;
;             G8_LDB(B0, 1, 0); G8_LDB(B1, 1, 1); G8_SCHED; G8_LDA(At, 1, 0); G8_STAGE_A(G8_SA(0, 1), last, 1, k2);
;             G8_WAIT_L(0); G8_BAR; G8_MMA(0, 0, At, B0); G8_MMA(0, 1, At, B1); G8_BAR; G8_SCHED;
;             if (!skip1) G8_LDA(At, 1, 1); G8_STAGE_B(G8_SB(1, 0), b3); G8_STAGE_A(G8_SA(1, 0), last, 0, k3); G8_STAGE_B(G8_SB(1, 1), b3 + hstepB);
;             G8_WAIT_V(6); G8_WAIT_L(0); G8_BAR; if (!skip1) { G8_MMA(1, 0, At, B0); G8_MMA(1, 1, At, B1); } G8_BAR; G8_SCHED;
.LBB0_1473:
	v_lshl_add_u64 v[222:223], s[30:31], 0, v[222:223]
	s_mov_b32 m0, s47
	s_nop 0
	global_load_lds_dwordx4 v[222:223], off
	s_waitcnt lgkmcnt(0)
	s_barrier
	s_setprio 1
	s_waitcnt lgkmcnt(0)
	v_mfma_f32_16x16x32_bf16 v[136:139], v[156:159], v[184:187], v[136:139]
	v_mfma_f32_16x16x32_bf16 v[132:135], v[164:167], v[184:187], v[132:135]
	v_mfma_f32_16x16x32_bf16 v[120:123], v[156:159], v[180:183], v[120:123]
	v_mfma_f32_16x16x32_bf16 v[116:119], v[164:167], v[180:183], v[116:119]
	v_mfma_f32_16x16x32_bf16 v[104:107], v[156:159], v[176:179], v[104:107]
	v_mfma_f32_16x16x32_bf16 v[100:103], v[164:167], v[176:179], v[100:103]
	v_mfma_f32_16x16x32_bf16 v[88:91], v[156:159], v[172:175], v[88:91]
	v_mfma_f32_16x16x32_bf16 v[84:87], v[164:167], v[172:175], v[84:87]
	v_mfma_f32_16x16x32_bf16 v[136:139], v[160:163], v[200:203], v[136:139]
	v_mfma_f32_16x16x32_bf16 v[132:135], v[168:171], v[200:203], v[132:135]
	v_mfma_f32_16x16x32_bf16 v[120:123], v[160:163], v[196:199], v[120:123]
	v_mfma_f32_16x16x32_bf16 v[116:119], v[168:171], v[196:199], v[116:119]
	v_mfma_f32_16x16x32_bf16 v[104:107], v[160:163], v[192:195], v[104:107]
	v_mfma_f32_16x16x32_bf16 v[100:103], v[168:171], v[192:195], v[100:103]
	v_mfma_f32_16x16x32_bf16 v[88:91], v[160:163], v[188:191], v[88:91]
	v_mfma_f32_16x16x32_bf16 v[84:87], v[168:171], v[188:191], v[84:87]
	v_mfma_f32_16x16x32_bf16 v[128:131], v[140:143], v[184:187], v[128:131]
	v_mfma_f32_16x16x32_bf16 v[124:127], v[148:151], v[184:187], v[124:127]
	v_mfma_f32_16x16x32_bf16 v[112:115], v[140:143], v[180:183], v[112:115]
	v_mfma_f32_16x16x32_bf16 v[108:111], v[148:151], v[180:183], v[108:111]
	v_mfma_f32_16x16x32_bf16 v[96:99], v[140:143], v[176:179], v[96:99]
	v_mfma_f32_16x16x32_bf16 v[92:95], v[148:151], v[176:179], v[92:95]
	v_mfma_f32_16x16x32_bf16 v[80:83], v[140:143], v[172:175], v[80:83]
	v_mfma_f32_16x16x32_bf16 v[76:79], v[148:151], v[172:175], v[76:79]
	v_mfma_f32_16x16x32_bf16 v[128:131], v[144:147], v[200:203], v[128:131]
	v_mfma_f32_16x16x32_bf16 v[124:127], v[152:155], v[200:203], v[124:127]
	v_mfma_f32_16x16x32_bf16 v[112:115], v[144:147], v[196:199], v[112:115]
	v_mfma_f32_16x16x32_bf16 v[108:111], v[152:155], v[196:199], v[108:111]
	v_mfma_f32_16x16x32_bf16 v[96:99], v[144:147], v[192:195], v[96:99]
	v_mfma_f32_16x16x32_bf16 v[92:95], v[152:155], v[192:195], v[92:95]
	v_mfma_f32_16x16x32_bf16 v[80:83], v[144:147], v[188:191], v[80:83]
	v_mfma_f32_16x16x32_bf16 v[76:79], v[152:155], v[188:191], v[76:79]
	s_setprio 0
	s_barrier
	s_and_b64 vcc, exec, s[4:5]
	s_cbranch_vccnz .LBB0_1475
	ds_read_b128 v[184:187], v228 offset:49152
	ds_read_b128 v[200:203], v228 offset:50176
	ds_read_b128 v[180:183], v228 offset:51200
	ds_read_b128 v[196:199], v228 offset:52224
	ds_read_b128 v[176:179], v228 offset:53248
	ds_read_b128 v[192:195], v228 offset:54272
	ds_read_b128 v[172:175], v228 offset:55296
	ds_read_b128 v[188:191], v228 offset:56320

; #define G8_STAGE_B(bufoff, gbase) do { _Pragma("unroll") for (int _i = 0; _i < 2; ++_i) \
;         __builtin_amdgcn_global_load_lds((const unsigned*)((const char*)(gbase) + voffB[_i]), (LAS unsigned*)(lds + (bufoff) + ldsw + _i * 8192), 16, 0, 0); } while (0)
; #define G8_LDA(dst, b, h) do { _Pragma("unroll") for (int m = 0; m < 4; ++m) _Pragma("unroll") for (int k = 0; k < 2; ++k) dst[m][k] = *(const LAS bf16x8*)(lds + G8_SA(b, h) + aoff + m * 2048 + k * 1024); } while (0)
; #define G8_LDB(dst, b, h) do { _Pragma("unroll") for (int n = 0; n < 2; ++n) _Pragma("unroll") for (int k = 0; k < 2; ++k) dst[n][k] = *(const LAS bf16x8*)(lds + G8_SB(b, h) + boff + n * 2048 + k * 1024); } while (0)
; #define G8_WAIT_V(n) asm volatile("s_waitcnt vmcnt(" #n ")" ::: "memory")
; #define G8_WAIT_L(n) asm volatile("s_waitcnt lgkmcnt(" #n ")" ::: "memory")
; #define G8_BAR __builtin_amdgcn_s_barrier()
; template <class Sched, class Epi>
; DEVI void gemm_phase(LAS unsigned char* lds, const char* Abase, const int K, const Sched& S, const Epi& E) {
;     ...
;         for (int t = 0; t < ntu; t += 2) {
;             const bool last = (t == ntu - 2);
;             const size_t k1 = (size_t)(t + 1) * kstep;
;             const size_t k2 = last ? (size_t)0 : (size_t)(t + 2) * kstep, k3 = k2 + kstep;
;             const char* b2 = last ? nB : cB + (size_t)(t + 2) * kstep; const char* b3 = b2 + kstep;
;             G8_LDB(B0, 0, 0); G8_LDB(B1, 0, 1); G8_SCHED; G8_LDA(At, 0, 0); G8_STAGE_A(G8_SA(1, 1), false, 1, k1);
;             G8_WAIT_L(0); G8_BAR; G8_MMA(0, 0, At, B0); G8_MMA(0, 1, At, B1); G8_BAR; G8_SCHED;
;             if (!skip1) G8_LDA(At, 0, 1); G8_STAGE_B(G8_SB(0, 0), b2); G8_STAGE_A(G8_SA(0, 0), last, 0, k2); G8_STAGE_B(G8_SB(0, 1), b2 + hstepB);
;             G8_WAIT_V(6); G8_WAIT_L(0); G8_BAR; if (!skip1) { G8_MMA(1, 0, At, B0); G8_MMA(1, 1, At, B1); } G8_BAR; G8_SCHED;
;             G8_LDB(B0, 1, 0); G8_LDB(B1, 1, 1); G8_SCHED; G8_LDA(At, 1, 0); G8_STAGE_A(G8_SA(0, 1), last, 1, k2);
;             G8_WAIT_L(0); G8_BAR; G8_MMA(0, 0, At, B0); G8_MMA(0, 1, At, B1); G8_BAR; G8_SCHED;
;             if (!skip1) G8_LDA(At, 1, 1); G8_STAGE_B(G8_SB(1, 0), b3); G8_STAGE_A(G8_SA(1, 0), last, 0, k3); G8_STAGE_B(G8_SB(1, 1), b3 + hstepB);
;             G8_WAIT_V(6); G8_WAIT_L(0); G8_BAR; if (!skip1) { G8_MMA(1, 0, At, B0); G8_MMA(1, 1, At, B1); } G8_BAR; G8_SCHED;
.LBB0_1479:
	v_lshl_add_u64 v[4:5], s[30:31], 0, v[2:3]
	s_add_u32 s28, s28, 0x40080
	s_mov_b32 m0, s53
	v_lshl_add_u64 v[4:5], v[4:5], 0, s[16:17]
	s_addc_u32 s29, s29, 0
	global_load_lds_dwordx4 v[4:5], off
	v_lshl_add_u64 v[4:5], s[28:29], 0, v[204:205]
	s_mov_b32 m0, s54
	s_and_b64 vcc, exec, s[4:5]
	global_load_lds_dwordx4 v[4:5], off
	v_lshl_add_u64 v[4:5], s[28:29], 0, v[206:207]
	s_mov_b32 m0, s55
	s_nop 0
	global_load_lds_dwordx4 v[4:5], off
	s_waitcnt vmcnt(6)
	s_waitcnt lgkmcnt(0)
	s_barrier
	s_cbranch_vccnz .LBB0_1481
	s_setprio 1
	s_waitcnt lgkmcnt(0)
	v_mfma_f32_16x16x32_bf16 v[72:75], v[156:159], v[184:187], v[72:75]
	v_mfma_f32_16x16x32_bf16 v[68:71], v[164:167], v[184:187], v[68:71]
	v_mfma_f32_16x16x32_bf16 v[56:59], v[156:159], v[180:183], v[56:59]
	v_mfma_f32_16x16x32_bf16 v[52:55], v[164:167], v[180:183], v[52:55]
	v_mfma_f32_16x16x32_bf16 v[40:43], v[156:159], v[176:179], v[40:43]
	v_mfma_f32_16x16x32_bf16 v[36:39], v[164:167], v[176:179], v[36:39]
	v_mfma_f32_16x16x32_bf16 v[24:27], v[156:159], v[172:175], v[24:27]
	v_mfma_f32_16x16x32_bf16 v[20:23], v[164:167], v[172:175], v[20:23]
	v_mfma_f32_16x16x32_bf16 v[72:75], v[160:163], v[200:203], v[72:75]
	v_mfma_f32_16x16x32_bf16 v[68:71], v[168:171], v[200:203], v[68:71]
	v_mfma_f32_16x16x32_bf16 v[56:59], v[160:163], v[196:199], v[56:59]
	v_mfma_f32_16x16x32_bf16 v[52:55], v[168:171], v[196:199], v[52:55]
	v_mfma_f32_16x16x32_bf16 v[40:43], v[160:163], v[192:195], v[40:43]
	v_mfma_f32_16x16x32_bf16 v[36:39], v[168:171], v[192:195], v[36:39]
	v_mfma_f32_16x16x32_bf16 v[24:27], v[160:163], v[188:191], v[24:27]
	v_mfma_f32_16x16x32_bf16 v[20:23], v[168:171], v[188:191], v[20:23]
	v_mfma_f32_16x16x32_bf16 v[64:67], v[140:143], v[184:187], v[64:67]
	v_mfma_f32_16x16x32_bf16 v[60:63], v[148:151], v[184:187], v[60:63]
	v_mfma_f32_16x16x32_bf16 v[48:51], v[140:143], v[180:183], v[48:51]
	v_mfma_f32_16x16x32_bf16 v[44:47], v[148:151], v[180:183], v[44:47]
	v_mfma_f32_16x16x32_bf16 v[32:35], v[140:143], v[176:179], v[32:35]
	v_mfma_f32_16x16x32_bf16 v[28:31], v[148:151], v[176:179], v[28:31]
	v_mfma_f32_16x16x32_bf16 v[16:19], v[140:143], v[172:175], v[16:19]
	v_mfma_f32_16x16x32_bf16 v[12:15], v[148:151], v[172:175], v[12:15]
	v_mfma_f32_16x16x32_bf16 v[64:67], v[144:147], v[200:203], v[64:67]
	v_mfma_f32_16x16x32_bf16 v[60:63], v[152:155], v[200:203], v[60:63]
	v_mfma_f32_16x16x32_bf16 v[48:51], v[144:147], v[196:199], v[48:51]
	v_mfma_f32_16x16x32_bf16 v[44:47], v[152:155], v[196:199], v[44:47]
	v_mfma_f32_16x16x32_bf16 v[32:35], v[144:147], v[192:195], v[32:35]
	v_mfma_f32_16x16x32_bf16 v[28:31], v[152:155], v[192:195], v[28:31]
	v_mfma_f32_16x16x32_bf16 v[16:19], v[144:147], v[188:191], v[16:19]
	v_mfma_f32_16x16x32_bf16 v[12:15], v[152:155], v[188:191], v[12:15]
	s_setprio 0

; #define G8_STAGE_B(bufoff, gbase) do { _Pragma("unroll") for (int _i = 0; _i < 2; ++_i) \
;         __builtin_amdgcn_global_load_lds((const unsigned*)((const char*)(gbase) + voffB[_i]), (LAS unsigned*)(lds + (bufoff) + ldsw + _i * 8192), 16, 0, 0); } while (0)
; #define G8_LDA(dst, b, h) do { _Pragma("unroll") for (int m = 0; m < 4; ++m) _Pragma("unroll") for (int k = 0; k < 2; ++k) dst[m][k] = *(const LAS bf16x8*)(lds + G8_SA(b, h) + aoff + m * 2048 + k * 1024); } while (0)
; #define G8_LDB(dst, b, h) do { _Pragma("unroll") for (int n = 0; n < 2; ++n) _Pragma("unroll") for (int k = 0; k < 2; ++k) dst[n][k] = *(const LAS bf16x8*)(lds + G8_SB(b, h) + boff + n * 2048 + k * 1024); } while (0)
; #define G8_WAIT_V(n) asm volatile("s_waitcnt vmcnt(" #n ")" ::: "memory")
; #define G8_WAIT_L(n) asm volatile("s_waitcnt lgkmcnt(" #n ")" ::: "memory")
; #define G8_BAR __builtin_amdgcn_s_barrier()
; template <class Sched, class Epi>
; DEVI void gemm_phase(LAS unsigned char* lds, const char* Abase, const int K, const Sched& S, const Epi& E) {
;     ...
;         for (int t = 0; t < ntu; t += 2) {
;             const bool last = (t == ntu - 2);
;             const size_t k1 = (size_t)(t + 1) * kstep;
;             const size_t k2 = last ? (size_t)0 : (size_t)(t + 2) * kstep, k3 = k2 + kstep;
;             const char* b2 = last ? nB : cB + (size_t)(t + 2) * kstep; const char* b3 = b2 + kstep;
;             G8_LDB(B0, 0, 0); G8_LDB(B1, 0, 1); G8_SCHED; G8_LDA(At, 0, 0); G8_STAGE_A(G8_SA(1, 1), false, 1, k1);
;             G8_WAIT_L(0); G8_BAR; G8_MMA(0, 0, At, B0); G8_MMA(0, 1, At, B1); G8_BAR; G8_SCHED;
;             if (!skip1) G8_LDA(At, 0, 1); G8_STAGE_B(G8_SB(0, 0), b2); G8_STAGE_A(G8_SA(0, 0), last, 0, k2); G8_STAGE_B(G8_SB(0, 1), b2 + hstepB);
;             G8_WAIT_V(6); G8_WAIT_L(0); G8_BAR; if (!skip1) { G8_MMA(1, 0, At, B0); G8_MMA(1, 1, At, B1); } G8_BAR; G8_SCHED;
;             G8_LDB(B0, 1, 0); G8_LDB(B1, 1, 1); G8_SCHED; G8_LDA(At, 1, 0); G8_STAGE_A(G8_SA(0, 1), last, 1, k2);
;             G8_WAIT_L(0); G8_BAR; G8_MMA(0, 0, At, B0); G8_MMA(0, 1, At, B1); G8_BAR; G8_SCHED;
;             if (!skip1) G8_LDA(At, 1, 1); G8_STAGE_B(G8_SB(1, 0), b3); G8_STAGE_A(G8_SA(1, 0), last, 0, k3); G8_STAGE_B(G8_SB(1, 1), b3 + hstepB);
;             G8_WAIT_V(6); G8_WAIT_L(0); G8_BAR; if (!skip1) { G8_MMA(1, 0, At, B0); G8_MMA(1, 1, At, B1); } G8_BAR; G8_SCHED;
.LBB0_1615:
	ds_read_b128 v[12:15], v230
	ds_read_b128 v[16:19], v230 offset:1024
	ds_read_b128 v[36:39], v230 offset:2048
	ds_read_b128 v[40:43], v230 offset:3072
	ds_read_b128 v[20:23], v231
	ds_read_b128 v[24:27], v231 offset:1024
	ds_read_b128 v[140:143], v231 offset:2048
	ds_read_b128 v[144:147], v231 offset:3072
	v_cmp_lt_i32_e64 s[6:7], s58, v4
	s_add_u32 s4, s38, 0x10080
	s_addc_u32 s5, s39, 0
	s_mov_b32 m0, s59
	v_lshl_add_u64 v[8:9], s[4:5], 0, v[2:3]
	ds_read_b128 v[56:59], v232
	ds_read_b128 v[68:71], v232 offset:1024
	ds_read_b128 v[52:55], v232 offset:2048
	ds_read_b128 v[164:167], v232 offset:3072
	ds_read_b128 v[152:155], v232 offset:4096
	ds_read_b128 v[160:163], v232 offset:5120
	ds_read_b128 v[148:151], v232 offset:6144
	ds_read_b128 v[156:159], v232 offset:7168
	global_load_lds_dwordx4 v[8:9], off
	v_lshl_add_u64 v[8:9], s[4:5], 0, v[220:221]
	s_mov_b32 m0, s60
	s_nop 0
	global_load_lds_dwordx4 v[8:9], off
	s_waitcnt lgkmcnt(0)
	s_barrier
	s_setprio 1
	s_waitcnt lgkmcnt(0)
	v_mfma_f32_16x16x32_bf16 v[28:31], v[12:15], v[56:59], 0
	v_mfma_f32_16x16x32_bf16 v[76:79], v[16:19], v[68:71], v[28:31]
	v_mfma_f32_16x16x32_bf16 v[28:31], v[36:39], v[56:59], 0
	v_mfma_f32_16x16x32_bf16 v[80:83], v[40:43], v[68:71], v[28:31]
	v_mfma_f32_16x16x32_bf16 v[28:31], v[12:15], v[52:55], 0
	v_mfma_f32_16x16x32_bf16 v[84:87], v[16:19], v[164:167], v[28:31]
	v_mfma_f32_16x16x32_bf16 v[28:31], v[36:39], v[52:55], 0
	v_mfma_f32_16x16x32_bf16 v[88:91], v[40:43], v[164:167], v[28:31]
	v_mfma_f32_16x16x32_bf16 v[28:31], v[12:15], v[152:155], 0
	v_mfma_f32_16x16x32_bf16 v[92:95], v[16:19], v[160:163], v[28:31]
	v_mfma_f32_16x16x32_bf16 v[28:31], v[36:39], v[152:155], 0
	v_mfma_f32_16x16x32_bf16 v[96:99], v[40:43], v[160:163], v[28:31]
	v_mfma_f32_16x16x32_bf16 v[28:31], v[12:15], v[148:151], 0
	v_mfma_f32_16x16x32_bf16 v[100:103], v[16:19], v[156:159], v[28:31]
	v_mfma_f32_16x16x32_bf16 v[28:31], v[36:39], v[148:151], 0
	v_mfma_f32_16x16x32_bf16 v[104:107], v[40:43], v[156:159], v[28:31]
	v_mfma_f32_16x16x32_bf16 v[28:31], v[20:23], v[56:59], 0
	v_mfma_f32_16x16x32_bf16 v[108:111], v[24:27], v[68:71], v[28:31]
	v_mfma_f32_16x16x32_bf16 v[28:31], v[140:143], v[56:59], 0
	v_mfma_f32_16x16x32_bf16 v[112:115], v[144:147], v[68:71], v[28:31]
	v_mfma_f32_16x16x32_bf16 v[28:31], v[20:23], v[52:55], 0
	v_mfma_f32_16x16x32_bf16 v[116:119], v[24:27], v[164:167], v[28:31]
	v_mfma_f32_16x16x32_bf16 v[28:31], v[140:143], v[52:55], 0
	v_mfma_f32_16x16x32_bf16 v[120:123], v[144:147], v[164:167], v[28:31]
	v_mfma_f32_16x16x32_bf16 v[28:31], v[20:23], v[152:155], 0
	v_mfma_f32_16x16x32_bf16 v[124:127], v[24:27], v[160:163], v[28:31]
	v_mfma_f32_16x16x32_bf16 v[28:31], v[140:143], v[152:155], 0
	v_mfma_f32_16x16x32_bf16 v[128:131], v[144:147], v[160:163], v[28:31]
	v_mfma_f32_16x16x32_bf16 v[28:31], v[20:23], v[148:151], 0
	v_mfma_f32_16x16x32_bf16 v[132:135], v[24:27], v[156:159], v[28:31]
	v_mfma_f32_16x16x32_bf16 v[28:31], v[140:143], v[148:151], 0
	v_mfma_f32_16x16x32_bf16 v[136:139], v[144:147], v[156:159], v[28:31]
	s_setprio 0
	s_barrier
	s_and_b64 vcc, exec, s[6:7]
	s_cbranch_vccz .LBB0_1617
	ds_read_b128 v[56:59], v232 offset:16384
	ds_read_b128 v[68:71], v232 offset:17408
	ds_read_b128 v[52:55], v232 offset:18432
	ds_read_b128 v[164:167], v232 offset:19456
	ds_read_b128 v[152:155], v232 offset:20480
	ds_read_b128 v[160:163], v232 offset:21504
	ds_read_b128 v[148:151], v232 offset:22528
	ds_read_b128 v[156:159], v232 offset:23552
.LBB0_1617:
	v_lshl_add_u64 v[204:205], s[40:41], 0, v[2:3]
	s_mov_b32 m0, s17
	v_lshl_add_u64 v[8:9], v[204:205], 0, s[22:23]
	v_lshl_add_u64 v[206:207], s[40:41], 0, v[220:221]
	global_load_lds_dwordx4 v[8:9], off
	v_lshl_add_u64 v[8:9], v[206:207], 0, s[22:23]
	s_mov_b32 m0, s43
	v_lshl_add_u64 v[208:209], s[38:39], 0, v[2:3]
	global_load_lds_dwordx4 v[8:9], off
	v_lshl_add_u64 v[8:9], v[208:209], 0, s[22:23]
	s_mov_b32 m0, s15
	v_lshl_add_u64 v[210:211], s[38:39], 0, v[220:221]
	s_add_u32 s4, s40, 0x10100
	global_load_lds_dwordx4 v[8:9], off
	v_lshl_add_u64 v[8:9], v[210:211], 0, s[22:23]
	s_mov_b32 m0, s44
	s_addc_u32 s5, s41, 0
	global_load_lds_dwordx4 v[8:9], off
	v_lshl_add_u64 v[8:9], s[4:5], 0, v[2:3]
	s_mov_b32 m0, s45
	v_cndmask_b32_e64 v7, 0, 1, s[6:7]
	global_load_lds_dwordx4 v[8:9], off
	v_lshl_add_u64 v[8:9], s[4:5], 0, v[220:221]
	s_mov_b32 m0, s46
	v_cmp_ne_u32_e64 s[4:5], 1, v7
	global_load_lds_dwordx4 v[8:9], off
	s_waitcnt vmcnt(6)
	s_waitcnt lgkmcnt(0)
	s_andn2_b64 vcc, exec, s[6:7]
	s_barrier
	s_cbranch_vccnz .LBB0_1619
	s_setprio 1
	s_waitcnt lgkmcnt(0)
	v_mfma_f32_16x16x32_bf16 v[28:31], v[12:15], v[56:59], 0
	v_mfma_f32_16x16x32_bf16 v[64:67], v[16:19], v[68:71], v[28:31]
	v_mfma_f32_16x16x32_bf16 v[28:31], v[36:39], v[56:59], 0
	v_mfma_f32_16x16x32_bf16 v[60:63], v[40:43], v[68:71], v[28:31]
	v_mfma_f32_16x16x32_bf16 v[28:31], v[12:15], v[52:55], 0
	v_mfma_f32_16x16x32_bf16 v[48:51], v[16:19], v[164:167], v[28:31]
	v_mfma_f32_16x16x32_bf16 v[28:31], v[36:39], v[52:55], 0
	v_mfma_f32_16x16x32_bf16 v[44:47], v[40:43], v[164:167], v[28:31]
	v_mfma_f32_16x16x32_bf16 v[28:31], v[12:15], v[152:155], 0
	v_mfma_f32_16x16x32_bf16 v[12:15], v[12:15], v[148:151], 0
	v_mfma_f32_16x16x32_bf16 v[32:35], v[16:19], v[160:163], v[28:31]
	v_mfma_f32_16x16x32_bf16 v[28:31], v[36:39], v[152:155], 0
	v_mfma_f32_16x16x32_bf16 v[16:19], v[16:19], v[156:159], v[12:15]
	v_mfma_f32_16x16x32_bf16 v[12:15], v[36:39], v[148:151], 0
	v_mfma_f32_16x16x32_bf16 v[28:31], v[40:43], v[160:163], v[28:31]
	v_mfma_f32_16x16x32_bf16 v[12:15], v[40:43], v[156:159], v[12:15]
	v_mfma_f32_16x16x32_bf16 v[36:39], v[20:23], v[56:59], 0
	v_mfma_f32_16x16x32_bf16 v[72:75], v[24:27], v[68:71], v[36:39]
	v_mfma_f32_16x16x32_bf16 v[36:39], v[140:143], v[56:59], 0
	v_mfma_f32_16x16x32_bf16 v[68:71], v[144:147], v[68:71], v[36:39]
	v_mfma_f32_16x16x32_bf16 v[36:39], v[20:23], v[52:55], 0
	v_mfma_f32_16x16x32_bf16 v[56:59], v[24:27], v[164:167], v[36:39]
	v_mfma_f32_16x16x32_bf16 v[36:39], v[140:143], v[52:55], 0
	v_mfma_f32_16x16x32_bf16 v[52:55], v[144:147], v[164:167], v[36:39]
	v_mfma_f32_16x16x32_bf16 v[36:39], v[20:23], v[152:155], 0
	v_mfma_f32_16x16x32_bf16 v[20:23], v[20:23], v[148:151], 0
	v_mfma_f32_16x16x32_bf16 v[40:43], v[24:27], v[160:163], v[36:39]
	v_mfma_f32_16x16x32_bf16 v[36:39], v[140:143], v[152:155], 0
	v_mfma_f32_16x16x32_bf16 v[24:27], v[24:27], v[156:159], v[20:23]
	v_mfma_f32_16x16x32_bf16 v[20:23], v[140:143], v[148:151], 0
	v_mfma_f32_16x16x32_bf16 v[36:39], v[144:147], v[160:163], v[36:39]
	v_mfma_f32_16x16x32_bf16 v[20:23], v[144:147], v[156:159], v[20:23]
	s_setprio 0
	s_branch .LBB0_1620

; #define G8_STAGE_B(bufoff, gbase) do { _Pragma("unroll") for (int _i = 0; _i < 2; ++_i) \
;         __builtin_amdgcn_global_load_lds((const unsigned*)((const char*)(gbase) + voffB[_i]), (LAS unsigned*)(lds + (bufoff) + ldsw + _i * 8192), 16, 0, 0); } while (0)
; #define G8_LDA(dst, b, h) do { _Pragma("unroll") for (int m = 0; m < 4; ++m) _Pragma("unroll") for (int k = 0; k < 2; ++k) dst[m][k] = *(const LAS bf16x8*)(lds + G8_SA(b, h) + aoff + m * 2048 + k * 1024); } while (0)
; #define G8_LDB(dst, b, h) do { _Pragma("unroll") for (int n = 0; n < 2; ++n) _Pragma("unroll") for (int k = 0; k < 2; ++k) dst[n][k] = *(const LAS bf16x8*)(lds + G8_SB(b, h) + boff + n * 2048 + k * 1024); } while (0)
; #define G8_WAIT_V(n) asm volatile("s_waitcnt vmcnt(" #n ")" ::: "memory")
; #define G8_WAIT_L(n) asm volatile("s_waitcnt lgkmcnt(" #n ")" ::: "memory")
; #define G8_BAR __builtin_amdgcn_s_barrier()
; template <class Sched, class Epi>
; DEVI void gemm_phase(LAS unsigned char* lds, const char* Abase, const int K, const Sched& S, const Epi& E) {
;     ...
;         for (int t = 0; t < ntu; t += 2) {
;             const bool last = (t == ntu - 2);
;             const size_t k1 = (size_t)(t + 1) * kstep;
;             const size_t k2 = last ? (size_t)0 : (size_t)(t + 2) * kstep, k3 = k2 + kstep;
;             const char* b2 = last ? nB : cB + (size_t)(t + 2) * kstep; const char* b3 = b2 + kstep;
;             G8_LDB(B0, 0, 0); G8_LDB(B1, 0, 1); G8_SCHED; G8_LDA(At, 0, 0); G8_STAGE_A(G8_SA(1, 1), false, 1, k1);
;             G8_WAIT_L(0); G8_BAR; G8_MMA(0, 0, At, B0); G8_MMA(0, 1, At, B1); G8_BAR; G8_SCHED;
;             if (!skip1) G8_LDA(At, 0, 1); G8_STAGE_B(G8_SB(0, 0), b2); G8_STAGE_A(G8_SA(0, 0), last, 0, k2); G8_STAGE_B(G8_SB(0, 1), b2 + hstepB);
;             G8_WAIT_V(6); G8_WAIT_L(0); G8_BAR; if (!skip1) { G8_MMA(1, 0, At, B0); G8_MMA(1, 1, At, B1); } G8_BAR; G8_SCHED;
;             G8_LDB(B0, 1, 0); G8_LDB(B1, 1, 1); G8_SCHED; G8_LDA(At, 1, 0); G8_STAGE_A(G8_SA(0, 1), last, 1, k2);
;             G8_WAIT_L(0); G8_BAR; G8_MMA(0, 0, At, B0); G8_MMA(0, 1, At, B1); G8_BAR; G8_SCHED;
;             if (!skip1) G8_LDA(At, 1, 1); G8_STAGE_B(G8_SB(1, 0), b3); G8_STAGE_A(G8_SA(1, 0), last, 0, k3); G8_STAGE_B(G8_SB(1, 1), b3 + hstepB);
;             G8_WAIT_V(6); G8_WAIT_L(0); G8_BAR; if (!skip1) { G8_MMA(1, 0, At, B0); G8_MMA(1, 1, At, B1); } G8_BAR; G8_SCHED;
.LBB0_1620:
	s_barrier
	v_add_u32_e32 v7, 0x18000, v229
	v_add_u32_e32 v11, 0x1c000, v229
	ds_read_b128 v[156:159], v7
	ds_read_b128 v[160:163], v7 offset:1024
	ds_read_b128 v[164:167], v7 offset:2048
	ds_read_b128 v[168:171], v7 offset:3072
	ds_read_b128 v[140:143], v11
	ds_read_b128 v[144:147], v11 offset:1024
	ds_read_b128 v[148:151], v11 offset:2048
	ds_read_b128 v[152:155], v11 offset:3072
	s_add_u32 s6, s38, 0x10100
	s_addc_u32 s7, s39, 0
	s_mov_b32 m0, s47
	v_lshl_add_u64 v[8:9], s[6:7], 0, v[2:3]
	ds_read_b128 v[184:187], v232 offset:32768
	ds_read_b128 v[200:203], v232 offset:33792
	ds_read_b128 v[180:183], v232 offset:34816
	ds_read_b128 v[196:199], v232 offset:35840
	ds_read_b128 v[176:179], v232 offset:36864
	ds_read_b128 v[192:195], v232 offset:37888
	ds_read_b128 v[172:175], v232 offset:38912
	ds_read_b128 v[188:191], v232 offset:39936
	global_load_lds_dwordx4 v[8:9], off
	v_lshl_add_u64 v[8:9], s[6:7], 0, v[220:221]
	s_mov_b32 m0, s48
	s_nop 0
	global_load_lds_dwordx4 v[8:9], off
	s_waitcnt lgkmcnt(0)
	s_barrier
	s_setprio 1
	s_waitcnt lgkmcnt(0)
	v_mfma_f32_16x16x32_bf16 v[76:79], v[156:159], v[184:187], v[76:79]
	v_mfma_f32_16x16x32_bf16 v[80:83], v[164:167], v[184:187], v[80:83]
	v_mfma_f32_16x16x32_bf16 v[84:87], v[156:159], v[180:183], v[84:87]
	v_mfma_f32_16x16x32_bf16 v[88:91], v[164:167], v[180:183], v[88:91]
	v_mfma_f32_16x16x32_bf16 v[92:95], v[156:159], v[176:179], v[92:95]
	v_mfma_f32_16x16x32_bf16 v[96:99], v[164:167], v[176:179], v[96:99]
	v_mfma_f32_16x16x32_bf16 v[100:103], v[156:159], v[172:175], v[100:103]
	v_mfma_f32_16x16x32_bf16 v[104:107], v[164:167], v[172:175], v[104:107]
	v_mfma_f32_16x16x32_bf16 v[76:79], v[160:163], v[200:203], v[76:79]
	v_mfma_f32_16x16x32_bf16 v[80:83], v[168:171], v[200:203], v[80:83]
	v_mfma_f32_16x16x32_bf16 v[84:87], v[160:163], v[196:199], v[84:87]
	v_mfma_f32_16x16x32_bf16 v[88:91], v[168:171], v[196:199], v[88:91]
	v_mfma_f32_16x16x32_bf16 v[92:95], v[160:163], v[192:195], v[92:95]
	v_mfma_f32_16x16x32_bf16 v[96:99], v[168:171], v[192:195], v[96:99]
	v_mfma_f32_16x16x32_bf16 v[100:103], v[160:163], v[188:191], v[100:103]
	v_mfma_f32_16x16x32_bf16 v[104:107], v[168:171], v[188:191], v[104:107]
	v_mfma_f32_16x16x32_bf16 v[108:111], v[140:143], v[184:187], v[108:111]
	v_mfma_f32_16x16x32_bf16 v[112:115], v[148:151], v[184:187], v[112:115]
	v_mfma_f32_16x16x32_bf16 v[116:119], v[140:143], v[180:183], v[116:119]
	v_mfma_f32_16x16x32_bf16 v[120:123], v[148:151], v[180:183], v[120:123]
	v_mfma_f32_16x16x32_bf16 v[124:127], v[140:143], v[176:179], v[124:127]
	v_mfma_f32_16x16x32_bf16 v[128:131], v[148:151], v[176:179], v[128:131]
	v_mfma_f32_16x16x32_bf16 v[132:135], v[140:143], v[172:175], v[132:135]
	v_mfma_f32_16x16x32_bf16 v[136:139], v[148:151], v[172:175], v[136:139]
	v_mfma_f32_16x16x32_bf16 v[108:111], v[144:147], v[200:203], v[108:111]
	v_mfma_f32_16x16x32_bf16 v[112:115], v[152:155], v[200:203], v[112:115]
	v_mfma_f32_16x16x32_bf16 v[116:119], v[144:147], v[196:199], v[116:119]
	v_mfma_f32_16x16x32_bf16 v[120:123], v[152:155], v[196:199], v[120:123]
	v_mfma_f32_16x16x32_bf16 v[124:127], v[144:147], v[192:195], v[124:127]
	v_mfma_f32_16x16x32_bf16 v[128:131], v[152:155], v[192:195], v[128:131]
	v_mfma_f32_16x16x32_bf16 v[132:135], v[144:147], v[188:191], v[132:135]
	v_mfma_f32_16x16x32_bf16 v[136:139], v[152:155], v[188:191], v[136:139]
	s_setprio 0
	s_barrier
	s_and_b64 vcc, exec, s[4:5]
	s_cbranch_vccnz .LBB0_1622
	ds_read_b128 v[184:187], v232 offset:49152
	ds_read_b128 v[200:203], v232 offset:50176
	ds_read_b128 v[180:183], v232 offset:51200
	ds_read_b128 v[196:199], v232 offset:52224
	ds_read_b128 v[176:179], v232 offset:53248
	ds_read_b128 v[192:195], v232 offset:54272
	ds_read_b128 v[172:175], v232 offset:55296
	ds_read_b128 v[188:191], v232 offset:56320
.LBB0_1622:
	s_mov_b32 m0, s50
	v_lshl_add_u64 v[8:9], v[204:205], 0, s[24:25]
	global_load_lds_dwordx4 v[8:9], off
	v_lshl_add_u64 v[8:9], v[206:207], 0, s[24:25]
	s_mov_b32 m0, s51
	s_add_u32 s6, s40, 0x10180
	global_load_lds_dwordx4 v[8:9], off
	v_lshl_add_u64 v[8:9], v[208:209], 0, s[24:25]
	s_mov_b32 m0, s52
	s_addc_u32 s7, s41, 0
	global_load_lds_dwordx4 v[8:9], off
	v_lshl_add_u64 v[8:9], v[210:211], 0, s[24:25]
	s_mov_b32 m0, s53
	s_and_b64 vcc, exec, s[4:5]
	global_load_lds_dwordx4 v[8:9], off
	v_lshl_add_u64 v[8:9], s[6:7], 0, v[2:3]
	s_mov_b32 m0, s54
	s_nop 0
	global_load_lds_dwordx4 v[8:9], off
	v_lshl_add_u64 v[8:9], s[6:7], 0, v[220:221]
	s_mov_b32 m0, s55
	s_nop 0
	global_load_lds_dwordx4 v[8:9], off
	s_waitcnt vmcnt(6)
	s_waitcnt lgkmcnt(0)
	s_barrier
	s_cbranch_vccnz .LBB0_1624
	s_setprio 1
	s_waitcnt lgkmcnt(0)
	v_mfma_f32_16x16x32_bf16 v[64:67], v[156:159], v[184:187], v[64:67]
	v_mfma_f32_16x16x32_bf16 v[60:63], v[164:167], v[184:187], v[60:63]
	v_mfma_f32_16x16x32_bf16 v[48:51], v[156:159], v[180:183], v[48:51]
	v_mfma_f32_16x16x32_bf16 v[44:47], v[164:167], v[180:183], v[44:47]
	v_mfma_f32_16x16x32_bf16 v[32:35], v[156:159], v[176:179], v[32:35]
	v_mfma_f32_16x16x32_bf16 v[28:31], v[164:167], v[176:179], v[28:31]
	v_mfma_f32_16x16x32_bf16 v[16:19], v[156:159], v[172:175], v[16:19]
	v_mfma_f32_16x16x32_bf16 v[12:15], v[164:167], v[172:175], v[12:15]
	v_mfma_f32_16x16x32_bf16 v[64:67], v[160:163], v[200:203], v[64:67]
	v_mfma_f32_16x16x32_bf16 v[60:63], v[168:171], v[200:203], v[60:63]
	v_mfma_f32_16x16x32_bf16 v[48:51], v[160:163], v[196:199], v[48:51]
	v_mfma_f32_16x16x32_bf16 v[44:47], v[168:171], v[196:199], v[44:47]
	v_mfma_f32_16x16x32_bf16 v[32:35], v[160:163], v[192:195], v[32:35]
	v_mfma_f32_16x16x32_bf16 v[28:31], v[168:171], v[192:195], v[28:31]
	v_mfma_f32_16x16x32_bf16 v[16:19], v[160:163], v[188:191], v[16:19]
	v_mfma_f32_16x16x32_bf16 v[12:15], v[168:171], v[188:191], v[12:15]
	v_mfma_f32_16x16x32_bf16 v[72:75], v[140:143], v[184:187], v[72:75]
	v_mfma_f32_16x16x32_bf16 v[68:71], v[148:151], v[184:187], v[68:71]
	v_mfma_f32_16x16x32_bf16 v[56:59], v[140:143], v[180:183], v[56:59]
	v_mfma_f32_16x16x32_bf16 v[52:55], v[148:151], v[180:183], v[52:55]
	v_mfma_f32_16x16x32_bf16 v[40:43], v[140:143], v[176:179], v[40:43]
	v_mfma_f32_16x16x32_bf16 v[36:39], v[148:151], v[176:179], v[36:39]
	v_mfma_f32_16x16x32_bf16 v[24:27], v[140:143], v[172:175], v[24:27]
	v_mfma_f32_16x16x32_bf16 v[20:23], v[148:151], v[172:175], v[20:23]
	v_mfma_f32_16x16x32_bf16 v[72:75], v[144:147], v[200:203], v[72:75]
	v_mfma_f32_16x16x32_bf16 v[68:71], v[152:155], v[200:203], v[68:71]
	v_mfma_f32_16x16x32_bf16 v[56:59], v[144:147], v[196:199], v[56:59]
	v_mfma_f32_16x16x32_bf16 v[52:55], v[152:155], v[196:199], v[52:55]
	v_mfma_f32_16x16x32_bf16 v[40:43], v[144:147], v[192:195], v[40:43]
	v_mfma_f32_16x16x32_bf16 v[36:39], v[152:155], v[192:195], v[36:39]
	v_mfma_f32_16x16x32_bf16 v[24:27], v[144:147], v[188:191], v[24:27]
	v_mfma_f32_16x16x32_bf16 v[20:23], v[152:155], v[188:191], v[20:23]
	s_setprio 0
; #define G8_STAGE_B(bufoff, gbase) do { _Pragma("unroll") for (int _i = 0; _i < 2; ++_i) \
;         __builtin_amdgcn_global_load_lds((const unsigned*)((const char*)(gbase) + voffB[_i]), (LAS unsigned*)(lds + (bufoff) + ldsw + _i * 8192), 16, 0, 0); } while (0)
; #define G8_LDA(dst, b, h) do { _Pragma("unroll") for (int m = 0; m < 4; ++m) _Pragma("unroll") for (int k = 0; k < 2; ++k) dst[m][k] = *(const LAS bf16x8*)(lds + G8_SA(b, h) + aoff + m * 2048 + k * 1024); } while (0)
; #define G8_LDB(dst, b, h) do { _Pragma("unroll") for (int n = 0; n < 2; ++n) _Pragma("unroll") for (int k = 0; k < 2; ++k) dst[n][k] = *(const LAS bf16x8*)(lds + G8_SB(b, h) + boff + n * 2048 + k * 1024); } while (0)
; #define G8_WAIT_V(n) asm volatile("s_waitcnt vmcnt(" #n ")" ::: "memory")
; #define G8_WAIT_L(n) asm volatile("s_waitcnt lgkmcnt(" #n ")" ::: "memory")
; #define G8_BAR __builtin_amdgcn_s_barrier()
; template <class Sched, class Epi>
; DEVI void gemm_phase(LAS unsigned char* lds, const char* Abase, const int K, const Sched& S, const Epi& E) {
;     ...
;         for (int t = 0; t < ntu; t += 2) {
;             const bool last = (t == ntu - 2);
;             const size_t k1 = (size_t)(t + 1) * kstep;
;             const size_t k2 = last ? (size_t)0 : (size_t)(t + 2) * kstep, k3 = k2 + kstep;
;             const char* b2 = last ? nB : cB + (size_t)(t + 2) * kstep; const char* b3 = b2 + kstep;
;             G8_LDB(B0, 0, 0); G8_LDB(B1, 0, 1); G8_SCHED; G8_LDA(At, 0, 0); G8_STAGE_A(G8_SA(1, 1), false, 1, k1);
;             G8_WAIT_L(0); G8_BAR; G8_MMA(0, 0, At, B0); G8_MMA(0, 1, At, B1); G8_BAR; G8_SCHED;
;             if (!skip1) G8_LDA(At, 0, 1); G8_STAGE_B(G8_SB(0, 0), b2); G8_STAGE_A(G8_SA(0, 0), last, 0, k2); G8_STAGE_B(G8_SB(0, 1), b2 + hstepB);
;             G8_WAIT_V(6); G8_WAIT_L(0); G8_BAR; if (!skip1) { G8_MMA(1, 0, At, B0); G8_MMA(1, 1, At, B1); } G8_BAR; G8_SCHED;
;             G8_LDB(B0, 1, 0); G8_LDB(B1, 1, 1); G8_SCHED; G8_LDA(At, 1, 0); G8_STAGE_A(G8_SA(0, 1), last, 1, k2);
;             G8_WAIT_L(0); G8_BAR; G8_MMA(0, 0, At, B0); G8_MMA(0, 1, At, B1); G8_BAR; G8_SCHED;
;             if (!skip1) G8_LDA(At, 1, 1); G8_STAGE_B(G8_SB(1, 0), b3); G8_STAGE_A(G8_SA(1, 0), last, 0, k3); G8_STAGE_B(G8_SB(1, 1), b3 + hstepB);
;             G8_WAIT_V(6); G8_WAIT_L(0); G8_BAR; if (!skip1) { G8_MMA(1, 0, At, B0); G8_MMA(1, 1, At, B1); } G8_BAR; G8_SCHED;
.LBB0_1624:
	s_barrier
	ds_read_b128 v[168:171], v230
	s_waitcnt lgkmcnt(0)
	ds_read_b128 v[172:175], v230 offset:1024
	ds_read_b128 v[176:179], v230 offset:2048
	ds_read_b128 v[180:183], v230 offset:3072
	ds_read_b128 v[152:155], v231
	ds_read_b128 v[156:159], v231 offset:1024
	ds_read_b128 v[160:163], v231 offset:2048
	ds_read_b128 v[164:167], v231 offset:3072
	s_add_u32 s6, s38, 0x10180
	s_addc_u32 s7, s39, 0
	s_mov_b32 m0, s59
	v_lshl_add_u64 v[8:9], s[6:7], 0, v[2:3]
	ds_read_b128 v[196:199], v232
	ds_read_b128 v[212:215], v232 offset:1024
	ds_read_b128 v[192:195], v232 offset:2048
	ds_read_b128 v[208:211], v232 offset:3072
	ds_read_b128 v[188:191], v232 offset:4096
	ds_read_b128 v[204:207], v232 offset:5120
	ds_read_b128 v[184:187], v232 offset:6144
	ds_read_b128 v[200:203], v232 offset:7168
	global_load_lds_dwordx4 v[8:9], off
	v_lshl_add_u64 v[8:9], s[6:7], 0, v[220:221]
	s_mov_b32 m0, s60
	s_nop 0
	global_load_lds_dwordx4 v[8:9], off
	s_waitcnt lgkmcnt(0)
	s_barrier
	s_setprio 1
	s_waitcnt lgkmcnt(0)
	v_mfma_f32_16x16x32_bf16 v[76:79], v[168:171], v[196:199], v[76:79]
	v_mfma_f32_16x16x32_bf16 v[80:83], v[176:179], v[196:199], v[80:83]
	v_mfma_f32_16x16x32_bf16 v[84:87], v[168:171], v[192:195], v[84:87]
	v_mfma_f32_16x16x32_bf16 v[88:91], v[176:179], v[192:195], v[88:91]
	v_mfma_f32_16x16x32_bf16 v[92:95], v[168:171], v[188:191], v[92:95]
	v_mfma_f32_16x16x32_bf16 v[96:99], v[176:179], v[188:191], v[96:99]
	v_mfma_f32_16x16x32_bf16 v[100:103], v[168:171], v[184:187], v[100:103]
	v_mfma_f32_16x16x32_bf16 v[104:107], v[176:179], v[184:187], v[104:107]
	v_mfma_f32_16x16x32_bf16 v[76:79], v[172:175], v[212:215], v[76:79]
	v_mfma_f32_16x16x32_bf16 v[80:83], v[180:183], v[212:215], v[80:83]
	v_mfma_f32_16x16x32_bf16 v[84:87], v[172:175], v[208:211], v[84:87]
	v_mfma_f32_16x16x32_bf16 v[88:91], v[180:183], v[208:211], v[88:91]
	v_mfma_f32_16x16x32_bf16 v[92:95], v[172:175], v[204:207], v[92:95]
	v_mfma_f32_16x16x32_bf16 v[96:99], v[180:183], v[204:207], v[96:99]
	v_mfma_f32_16x16x32_bf16 v[100:103], v[172:175], v[200:203], v[100:103]
	v_mfma_f32_16x16x32_bf16 v[104:107], v[180:183], v[200:203], v[104:107]
	v_mfma_f32_16x16x32_bf16 v[108:111], v[152:155], v[196:199], v[108:111]
	v_mfma_f32_16x16x32_bf16 v[140:143], v[156:159], v[212:215], v[108:111]
	v_mfma_f32_16x16x32_bf16 v[108:111], v[160:163], v[196:199], v[112:115]
	v_mfma_f32_16x16x32_bf16 v[144:147], v[164:167], v[212:215], v[108:111]
	v_mfma_f32_16x16x32_bf16 v[108:111], v[152:155], v[192:195], v[116:119]
	v_mfma_f32_16x16x32_bf16 v[116:119], v[156:159], v[208:211], v[108:111]
	v_mfma_f32_16x16x32_bf16 v[108:111], v[160:163], v[192:195], v[120:123]
	v_mfma_f32_16x16x32_bf16 v[120:123], v[164:167], v[208:211], v[108:111]
	v_mfma_f32_16x16x32_bf16 v[108:111], v[152:155], v[188:191], v[124:127]
	v_mfma_f32_16x16x32_bf16 v[148:151], v[156:159], v[204:207], v[108:111]
	v_mfma_f32_16x16x32_bf16 v[108:111], v[160:163], v[188:191], v[128:131]
	v_mfma_f32_16x16x32_bf16 v[128:131], v[164:167], v[204:207], v[108:111]
	v_mfma_f32_16x16x32_bf16 v[108:111], v[152:155], v[184:187], v[132:135]
	v_mfma_f32_16x16x32_bf16 v[132:135], v[156:159], v[200:203], v[108:111]
	v_mfma_f32_16x16x32_bf16 v[108:111], v[160:163], v[184:187], v[136:139]
	v_mfma_f32_16x16x32_bf16 v[136:139], v[164:167], v[200:203], v[108:111]
	s_setprio 0
	s_barrier
	s_and_b64 vcc, exec, s[4:5]
	s_cbranch_vccnz .LBB0_1626
	ds_read_b128 v[196:199], v232 offset:16384
	ds_read_b128 v[212:215], v232 offset:17408
	ds_read_b128 v[192:195], v232 offset:18432
	ds_read_b128 v[208:211], v232 offset:19456
	ds_read_b128 v[188:191], v232 offset:20480
	ds_read_b128 v[204:207], v232 offset:21504
	ds_read_b128 v[184:187], v232 offset:22528
	ds_read_b128 v[200:203], v232 offset:23552
.LBB0_1626:
	s_mov_b32 m0, s17
	v_lshl_add_u64 v[8:9], s[34:35], 0, v[2:3]
	global_load_lds_dwordx4 v[8:9], off
	v_lshl_add_u64 v[224:225], s[34:35], 0, v[220:221]
	s_mov_b32 m0, s43
	v_lshl_add_u64 v[222:223], s[36:37], 0, v[2:3]
	global_load_lds_dwordx4 v[224:225], off
	s_mov_b32 m0, s15
	s_add_u32 s6, s34, 0x10000
	global_load_lds_dwordx4 v[222:223], off
	v_lshl_add_u64 v[226:227], s[36:37], 0, v[220:221]
	s_mov_b32 m0, s44
	s_addc_u32 s7, s35, 0
	global_load_lds_dwordx4 v[226:227], off
	v_lshl_add_u64 v[108:109], s[6:7], 0, v[2:3]
	s_mov_b32 m0, s45
	s_and_b64 vcc, exec, s[4:5]
	global_load_lds_dwordx4 v[108:109], off
	v_lshl_add_u64 v[108:109], s[6:7], 0, v[220:221]
	s_mov_b32 m0, s46
	s_nop 0
	global_load_lds_dwordx4 v[108:109], off
	s_waitcnt vmcnt(6)
	s_waitcnt lgkmcnt(0)
	s_barrier
	s_cbranch_vccnz .LBB0_1628
	s_setprio 1
	s_waitcnt lgkmcnt(0)
	v_mfma_f32_16x16x32_bf16 v[64:67], v[168:171], v[196:199], v[64:67]
	v_mfma_f32_16x16x32_bf16 v[60:63], v[176:179], v[196:199], v[60:63]
	v_mfma_f32_16x16x32_bf16 v[48:51], v[168:171], v[192:195], v[48:51]
	v_mfma_f32_16x16x32_bf16 v[44:47], v[176:179], v[192:195], v[44:47]
	v_mfma_f32_16x16x32_bf16 v[32:35], v[168:171], v[188:191], v[32:35]
	v_mfma_f32_16x16x32_bf16 v[28:31], v[176:179], v[188:191], v[28:31]
	v_mfma_f32_16x16x32_bf16 v[16:19], v[168:171], v[184:187], v[16:19]
	v_mfma_f32_16x16x32_bf16 v[12:15], v[176:179], v[184:187], v[12:15]
	v_mfma_f32_16x16x32_bf16 v[64:67], v[172:175], v[212:215], v[64:67]
	v_mfma_f32_16x16x32_bf16 v[60:63], v[180:183], v[212:215], v[60:63]
	v_mfma_f32_16x16x32_bf16 v[48:51], v[172:175], v[208:211], v[48:51]
	v_mfma_f32_16x16x32_bf16 v[44:47], v[180:183], v[208:211], v[44:47]
	v_mfma_f32_16x16x32_bf16 v[32:35], v[172:175], v[204:207], v[32:35]
	v_mfma_f32_16x16x32_bf16 v[28:31], v[180:183], v[204:207], v[28:31]
	v_mfma_f32_16x16x32_bf16 v[16:19], v[172:175], v[200:203], v[16:19]
	v_mfma_f32_16x16x32_bf16 v[12:15], v[180:183], v[200:203], v[12:15]
	v_mfma_f32_16x16x32_bf16 v[72:75], v[152:155], v[196:199], v[72:75]
	v_mfma_f32_16x16x32_bf16 v[68:71], v[160:163], v[196:199], v[68:71]
	v_mfma_f32_16x16x32_bf16 v[56:59], v[152:155], v[192:195], v[56:59]
	v_mfma_f32_16x16x32_bf16 v[52:55], v[160:163], v[192:195], v[52:55]
	v_mfma_f32_16x16x32_bf16 v[40:43], v[152:155], v[188:191], v[40:43]
	v_mfma_f32_16x16x32_bf16 v[36:39], v[160:163], v[188:191], v[36:39]
	v_mfma_f32_16x16x32_bf16 v[24:27], v[152:155], v[184:187], v[24:27]
	v_mfma_f32_16x16x32_bf16 v[20:23], v[160:163], v[184:187], v[20:23]
	v_mfma_f32_16x16x32_bf16 v[72:75], v[156:159], v[212:215], v[72:75]
	v_mfma_f32_16x16x32_bf16 v[68:71], v[164:167], v[212:215], v[68:71]
	v_mfma_f32_16x16x32_bf16 v[56:59], v[156:159], v[208:211], v[56:59]
	v_mfma_f32_16x16x32_bf16 v[52:55], v[164:167], v[208:211], v[52:55]
	v_mfma_f32_16x16x32_bf16 v[40:43], v[156:159], v[204:207], v[40:43]
	v_mfma_f32_16x16x32_bf16 v[36:39], v[164:167], v[204:207], v[36:39]
	v_mfma_f32_16x16x32_bf16 v[24:27], v[156:159], v[200:203], v[24:27]
	v_mfma_f32_16x16x32_bf16 v[20:23], v[164:167], v[200:203], v[20:23]
	s_setprio 0
; #define G8_STAGE_B(bufoff, gbase) do { _Pragma("unroll") for (int _i = 0; _i < 2; ++_i) \
;         __builtin_amdgcn_global_load_lds((const unsigned*)((const char*)(gbase) + voffB[_i]), (LAS unsigned*)(lds + (bufoff) + ldsw + _i * 8192), 16, 0, 0); } while (0)
; #define G8_LDA(dst, b, h) do { _Pragma("unroll") for (int m = 0; m < 4; ++m) _Pragma("unroll") for (int k = 0; k < 2; ++k) dst[m][k] = *(const LAS bf16x8*)(lds + G8_SA(b, h) + aoff + m * 2048 + k * 1024); } while (0)
; #define G8_LDB(dst, b, h) do { _Pragma("unroll") for (int n = 0; n < 2; ++n) _Pragma("unroll") for (int k = 0; k < 2; ++k) dst[n][k] = *(const LAS bf16x8*)(lds + G8_SB(b, h) + boff + n * 2048 + k * 1024); } while (0)
; #define G8_WAIT_V(n) asm volatile("s_waitcnt vmcnt(" #n ")" ::: "memory")
; #define G8_WAIT_L(n) asm volatile("s_waitcnt lgkmcnt(" #n ")" ::: "memory")
; #define G8_BAR __builtin_amdgcn_s_barrier()
; template <class Sched, class Epi>
; DEVI void gemm_phase(LAS unsigned char* lds, const char* Abase, const int K, const Sched& S, const Epi& E) {
;     ...
;         for (int t = 0; t < ntu; t += 2) {
;             const bool last = (t == ntu - 2);
;             const size_t k1 = (size_t)(t + 1) * kstep;
;             const size_t k2 = last ? (size_t)0 : (size_t)(t + 2) * kstep, k3 = k2 + kstep;
;             const char* b2 = last ? nB : cB + (size_t)(t + 2) * kstep; const char* b3 = b2 + kstep;
;             G8_LDB(B0, 0, 0); G8_LDB(B1, 0, 1); G8_SCHED; G8_LDA(At, 0, 0); G8_STAGE_A(G8_SA(1, 1), false, 1, k1);
;             G8_WAIT_L(0); G8_BAR; G8_MMA(0, 0, At, B0); G8_MMA(0, 1, At, B1); G8_BAR; G8_SCHED;
;             if (!skip1) G8_LDA(At, 0, 1); G8_STAGE_B(G8_SB(0, 0), b2); G8_STAGE_A(G8_SA(0, 0), last, 0, k2); G8_STAGE_B(G8_SB(0, 1), b2 + hstepB);
;             G8_WAIT_V(6); G8_WAIT_L(0); G8_BAR; if (!skip1) { G8_MMA(1, 0, At, B0); G8_MMA(1, 1, At, B1); } G8_BAR; G8_SCHED;
;             G8_LDB(B0, 1, 0); G8_LDB(B1, 1, 1); G8_SCHED; G8_LDA(At, 1, 0); G8_STAGE_A(G8_SA(0, 1), last, 1, k2);
;             G8_WAIT_L(0); G8_BAR; G8_MMA(0, 0, At, B0); G8_MMA(0, 1, At, B1); G8_BAR; G8_SCHED;
;             if (!skip1) G8_LDA(At, 1, 1); G8_STAGE_B(G8_SB(1, 0), b3); G8_STAGE_A(G8_SA(1, 0), last, 0, k3); G8_STAGE_B(G8_SB(1, 1), b3 + hstepB);
;             G8_WAIT_V(6); G8_WAIT_L(0); G8_BAR; if (!skip1) { G8_MMA(1, 0, At, B0); G8_MMA(1, 1, At, B1); } G8_BAR; G8_SCHED;
.LBB0_1628:
	s_barrier
	ds_read_b128 v[172:175], v7
	ds_read_b128 v[176:179], v7 offset:1024
	ds_read_b128 v[180:183], v7 offset:2048
	s_waitcnt lgkmcnt(0)
	ds_read_b128 v[184:187], v7 offset:3072
	ds_read_b128 v[156:159], v11
	ds_read_b128 v[160:163], v11 offset:1024
	ds_read_b128 v[164:167], v11 offset:2048
	ds_read_b128 v[168:171], v11 offset:3072
	s_add_u32 s6, s36, 0x10000
	s_addc_u32 s7, s37, 0
	s_mov_b32 m0, s47
	v_lshl_add_u64 v[108:109], s[6:7], 0, v[2:3]
	ds_read_b128 v[200:203], v232 offset:32768
	ds_read_b128 v[216:219], v232 offset:33792
	ds_read_b128 v[196:199], v232 offset:34816
	ds_read_b128 v[212:215], v232 offset:35840
	ds_read_b128 v[192:195], v232 offset:36864
	ds_read_b128 v[208:211], v232 offset:37888
	ds_read_b128 v[188:191], v232 offset:38912
	ds_read_b128 v[204:207], v232 offset:39936
	global_load_lds_dwordx4 v[108:109], off
	v_lshl_add_u64 v[108:109], s[6:7], 0, v[220:221]
	s_mov_b32 m0, s48
	s_nop 0
	global_load_lds_dwordx4 v[108:109], off
	s_waitcnt lgkmcnt(0)
	s_barrier
	s_setprio 1
	s_waitcnt lgkmcnt(0)
	v_mfma_f32_16x16x32_bf16 v[76:79], v[172:175], v[200:203], v[76:79]
	v_mfma_f32_16x16x32_bf16 v[124:127], v[176:179], v[216:219], v[76:79]
	v_mfma_f32_16x16x32_bf16 v[76:79], v[180:183], v[200:203], v[80:83]
	v_mfma_f32_16x16x32_bf16 v[152:155], v[184:187], v[216:219], v[76:79]
	v_mfma_f32_16x16x32_bf16 v[76:79], v[172:175], v[196:199], v[84:87]
	v_mfma_f32_16x16x32_bf16 v[108:111], v[176:179], v[212:215], v[76:79]
	v_mfma_f32_16x16x32_bf16 v[76:79], v[180:183], v[196:199], v[88:91]
	v_mfma_f32_16x16x32_bf16 v[112:115], v[184:187], v[212:215], v[76:79]
	v_mfma_f32_16x16x32_bf16 v[76:79], v[172:175], v[192:195], v[92:95]
	v_mfma_f32_16x16x32_bf16 v[92:95], v[176:179], v[208:211], v[76:79]
	v_mfma_f32_16x16x32_bf16 v[76:79], v[180:183], v[192:195], v[96:99]
	v_mfma_f32_16x16x32_bf16 v[96:99], v[184:187], v[208:211], v[76:79]
	v_mfma_f32_16x16x32_bf16 v[76:79], v[172:175], v[188:191], v[100:103]
	v_mfma_f32_16x16x32_bf16 v[80:83], v[180:183], v[188:191], v[104:107]
	v_mfma_f32_16x16x32_bf16 v[76:79], v[176:179], v[204:207], v[76:79]
	v_mfma_f32_16x16x32_bf16 v[80:83], v[184:187], v[204:207], v[80:83]
	v_mfma_f32_16x16x32_bf16 v[84:87], v[156:159], v[200:203], v[140:143]
	v_mfma_f32_16x16x32_bf16 v[140:143], v[160:163], v[216:219], v[84:87]
	v_mfma_f32_16x16x32_bf16 v[84:87], v[164:167], v[200:203], v[144:147]
	v_mfma_f32_16x16x32_bf16 v[144:147], v[168:171], v[216:219], v[84:87]
	v_mfma_f32_16x16x32_bf16 v[84:87], v[156:159], v[196:199], v[116:119]
	v_mfma_f32_16x16x32_bf16 v[116:119], v[160:163], v[212:215], v[84:87]
	v_mfma_f32_16x16x32_bf16 v[84:87], v[164:167], v[196:199], v[120:123]
	v_mfma_f32_16x16x32_bf16 v[120:123], v[168:171], v[212:215], v[84:87]
	v_mfma_f32_16x16x32_bf16 v[84:87], v[156:159], v[192:195], v[148:151]
	v_mfma_f32_16x16x32_bf16 v[100:103], v[160:163], v[208:211], v[84:87]
	v_mfma_f32_16x16x32_bf16 v[84:87], v[164:167], v[192:195], v[128:131]
	v_mfma_f32_16x16x32_bf16 v[104:107], v[168:171], v[208:211], v[84:87]
	v_mfma_f32_16x16x32_bf16 v[84:87], v[156:159], v[188:191], v[132:135]
	v_mfma_f32_16x16x32_bf16 v[88:91], v[164:167], v[188:191], v[136:139]
	v_mfma_f32_16x16x32_bf16 v[84:87], v[160:163], v[204:207], v[84:87]
	v_mfma_f32_16x16x32_bf16 v[88:91], v[168:171], v[204:207], v[88:91]
	s_setprio 0
	s_barrier
	s_and_b64 vcc, exec, s[4:5]
	s_cbranch_vccnz .LBB0_1630
	ds_read_b128 v[200:203], v232 offset:49152
	ds_read_b128 v[216:219], v232 offset:50176
	ds_read_b128 v[196:199], v232 offset:51200
	ds_read_b128 v[212:215], v232 offset:52224
	ds_read_b128 v[192:195], v232 offset:53248
	ds_read_b128 v[208:211], v232 offset:54272
	ds_read_b128 v[188:191], v232 offset:55296
	ds_read_b128 v[204:207], v232 offset:56320
.LBB0_1630:
	s_mov_b32 m0, s50
	v_lshl_add_u64 v[8:9], v[8:9], 0, s[20:21]
	global_load_lds_dwordx4 v[8:9], off
	v_lshl_add_u64 v[8:9], v[224:225], 0, s[20:21]
	s_mov_b32 m0, s51
	s_add_u32 s6, s34, 0x10080
	global_load_lds_dwordx4 v[8:9], off
	v_lshl_add_u64 v[8:9], v[222:223], 0, s[20:21]
	s_mov_b32 m0, s52
	s_addc_u32 s7, s35, 0
	global_load_lds_dwordx4 v[8:9], off
	v_lshl_add_u64 v[8:9], v[226:227], 0, s[20:21]
	s_mov_b32 m0, s53
	s_and_b64 vcc, exec, s[4:5]
	global_load_lds_dwordx4 v[8:9], off
	v_lshl_add_u64 v[8:9], s[6:7], 0, v[2:3]
	s_mov_b32 m0, s54
	s_nop 0
	global_load_lds_dwordx4 v[8:9], off
	v_lshl_add_u64 v[8:9], s[6:7], 0, v[220:221]
	s_mov_b32 m0, s55
	s_nop 0
	global_load_lds_dwordx4 v[8:9], off
	s_waitcnt vmcnt(6)
	s_waitcnt lgkmcnt(0)
	s_barrier
	s_cbranch_vccnz .LBB0_1632
	s_setprio 1
	s_waitcnt lgkmcnt(0)
	v_mfma_f32_16x16x32_bf16 v[64:67], v[172:175], v[200:203], v[64:67]
	v_mfma_f32_16x16x32_bf16 v[60:63], v[180:183], v[200:203], v[60:63]
	v_mfma_f32_16x16x32_bf16 v[48:51], v[172:175], v[196:199], v[48:51]
	v_mfma_f32_16x16x32_bf16 v[44:47], v[180:183], v[196:199], v[44:47]
	v_mfma_f32_16x16x32_bf16 v[32:35], v[172:175], v[192:195], v[32:35]
	v_mfma_f32_16x16x32_bf16 v[28:31], v[180:183], v[192:195], v[28:31]
	v_mfma_f32_16x16x32_bf16 v[16:19], v[172:175], v[188:191], v[16:19]
	v_mfma_f32_16x16x32_bf16 v[12:15], v[180:183], v[188:191], v[12:15]
	v_mfma_f32_16x16x32_bf16 v[64:67], v[176:179], v[216:219], v[64:67]
	v_mfma_f32_16x16x32_bf16 v[60:63], v[184:187], v[216:219], v[60:63]
	v_mfma_f32_16x16x32_bf16 v[48:51], v[176:179], v[212:215], v[48:51]
	v_mfma_f32_16x16x32_bf16 v[44:47], v[184:187], v[212:215], v[44:47]
	v_mfma_f32_16x16x32_bf16 v[32:35], v[176:179], v[208:211], v[32:35]
	v_mfma_f32_16x16x32_bf16 v[28:31], v[184:187], v[208:211], v[28:31]
	v_mfma_f32_16x16x32_bf16 v[16:19], v[176:179], v[204:207], v[16:19]
	v_mfma_f32_16x16x32_bf16 v[12:15], v[184:187], v[204:207], v[12:15]
	v_mfma_f32_16x16x32_bf16 v[72:75], v[156:159], v[200:203], v[72:75]
	v_mfma_f32_16x16x32_bf16 v[68:71], v[164:167], v[200:203], v[68:71]
	v_mfma_f32_16x16x32_bf16 v[56:59], v[156:159], v[196:199], v[56:59]
	v_mfma_f32_16x16x32_bf16 v[52:55], v[164:167], v[196:199], v[52:55]
	v_mfma_f32_16x16x32_bf16 v[40:43], v[156:159], v[192:195], v[40:43]
	v_mfma_f32_16x16x32_bf16 v[36:39], v[164:167], v[192:195], v[36:39]
	v_mfma_f32_16x16x32_bf16 v[24:27], v[156:159], v[188:191], v[24:27]
	v_mfma_f32_16x16x32_bf16 v[20:23], v[164:167], v[188:191], v[20:23]
	v_mfma_f32_16x16x32_bf16 v[72:75], v[160:163], v[216:219], v[72:75]
	v_mfma_f32_16x16x32_bf16 v[68:71], v[168:171], v[216:219], v[68:71]
	v_mfma_f32_16x16x32_bf16 v[56:59], v[160:163], v[212:215], v[56:59]
	v_mfma_f32_16x16x32_bf16 v[52:55], v[168:171], v[212:215], v[52:55]
	v_mfma_f32_16x16x32_bf16 v[40:43], v[160:163], v[208:211], v[40:43]
	v_mfma_f32_16x16x32_bf16 v[36:39], v[168:171], v[208:211], v[36:39]
	v_mfma_f32_16x16x32_bf16 v[24:27], v[160:163], v[204:207], v[24:27]
	v_mfma_f32_16x16x32_bf16 v[20:23], v[168:171], v[204:207], v[20:23]
	s_setprio 0

; #define G8_STAGE_B(bufoff, gbase) do { _Pragma("unroll") for (int _i = 0; _i < 2; ++_i) \
;         __builtin_amdgcn_global_load_lds((const unsigned*)((const char*)(gbase) + voffB[_i]), (LAS unsigned*)(lds + (bufoff) + ldsw + _i * 8192), 16, 0, 0); } while (0)
; #define G8_LDA(dst, b, h) do { _Pragma("unroll") for (int m = 0; m < 4; ++m) _Pragma("unroll") for (int k = 0; k < 2; ++k) dst[m][k] = *(const LAS bf16x8*)(lds + G8_SA(b, h) + aoff + m * 2048 + k * 1024); } while (0)
; #define G8_LDB(dst, b, h) do { _Pragma("unroll") for (int n = 0; n < 2; ++n) _Pragma("unroll") for (int k = 0; k < 2; ++k) dst[n][k] = *(const LAS bf16x8*)(lds + G8_SB(b, h) + boff + n * 2048 + k * 1024); } while (0)
; #define G8_WAIT_V(n) asm volatile("s_waitcnt vmcnt(" #n ")" ::: "memory")
; #define G8_WAIT_L(n) asm volatile("s_waitcnt lgkmcnt(" #n ")" ::: "memory")
; #define G8_BAR __builtin_amdgcn_s_barrier()
; template <class Sched, class Epi>
; DEVI void gemm_phase(LAS unsigned char* lds, const char* Abase, const int K, const Sched& S, const Epi& E) {
;     ...
;         for (int t = 0; t < ntu; t += 2) {
;             const bool last = (t == ntu - 2);
;             const size_t k1 = (size_t)(t + 1) * kstep;
;             const size_t k2 = last ? (size_t)0 : (size_t)(t + 2) * kstep, k3 = k2 + kstep;
;             const char* b2 = last ? nB : cB + (size_t)(t + 2) * kstep; const char* b3 = b2 + kstep;
;             G8_LDB(B0, 0, 0); G8_LDB(B1, 0, 1); G8_SCHED; G8_LDA(At, 0, 0); G8_STAGE_A(G8_SA(1, 1), false, 1, k1);
;             G8_WAIT_L(0); G8_BAR; G8_MMA(0, 0, At, B0); G8_MMA(0, 1, At, B1); G8_BAR; G8_SCHED;
;             if (!skip1) G8_LDA(At, 0, 1); G8_STAGE_B(G8_SB(0, 0), b2); G8_STAGE_A(G8_SA(0, 0), last, 0, k2); G8_STAGE_B(G8_SB(0, 1), b2 + hstepB);
;             G8_WAIT_V(6); G8_WAIT_L(0); G8_BAR; if (!skip1) { G8_MMA(1, 0, At, B0); G8_MMA(1, 1, At, B1); } G8_BAR; G8_SCHED;
;             G8_LDB(B0, 1, 0); G8_LDB(B1, 1, 1); G8_SCHED; G8_LDA(At, 1, 0); G8_STAGE_A(G8_SA(0, 1), last, 1, k2);
;             G8_WAIT_L(0); G8_BAR; G8_MMA(0, 0, At, B0); G8_MMA(0, 1, At, B1); G8_BAR; G8_SCHED;
;             if (!skip1) G8_LDA(At, 1, 1); G8_STAGE_B(G8_SB(1, 0), b3); G8_STAGE_A(G8_SA(1, 0), last, 0, k3); G8_STAGE_B(G8_SB(1, 1), b3 + hstepB);
;             G8_WAIT_V(6); G8_WAIT_L(0); G8_BAR; if (!skip1) { G8_MMA(1, 0, At, B0); G8_MMA(1, 1, At, B1); } G8_BAR; G8_SCHED;
.LBB0_1809:
	ds_read_b128 v[150:153], v219
	ds_read_b128 v[154:157], v219 offset:1024
	ds_read_b128 v[158:161], v219 offset:2048
	ds_read_b128 v[162:165], v219 offset:3072
	ds_read_b128 v[134:137], v220
	ds_read_b128 v[138:141], v220 offset:1024
	ds_read_b128 v[142:145], v220 offset:2048
	ds_read_b128 v[146:149], v220 offset:3072
	v_lshl_add_u64 v[4:5], v[206:207], 0, s[38:39]
	s_add_i32 m0, s27, 0xc000
	s_waitcnt lgkmcnt(0)
	ds_read_b128 v[178:181], v221
	ds_read_b128 v[194:197], v221 offset:1024
	ds_read_b128 v[174:177], v221 offset:2048
	ds_read_b128 v[190:193], v221 offset:3072
	ds_read_b128 v[170:173], v221 offset:4096
	ds_read_b128 v[186:189], v221 offset:5120
	ds_read_b128 v[166:169], v221 offset:6144
	ds_read_b128 v[182:185], v221 offset:7168
	global_load_lds_dwordx4 v[4:5], off
	v_lshl_add_u64 v[4:5], v[208:209], 0, s[38:39]
	s_add_i32 m0, s27, 0xe000
	s_nop 0
	global_load_lds_dwordx4 v[4:5], off
	s_waitcnt lgkmcnt(0)
	s_barrier
	s_setprio 1
	s_waitcnt lgkmcnt(0)
	v_mfma_f32_16x16x32_bf16 v[130:133], v[150:153], v[178:181], v[130:133]
	v_mfma_f32_16x16x32_bf16 v[126:129], v[158:161], v[178:181], v[126:129]
	v_mfma_f32_16x16x32_bf16 v[114:117], v[150:153], v[174:177], v[114:117]
	v_mfma_f32_16x16x32_bf16 v[110:113], v[158:161], v[174:177], v[110:113]
	v_mfma_f32_16x16x32_bf16 v[98:101], v[150:153], v[170:173], v[98:101]
	v_mfma_f32_16x16x32_bf16 v[94:97], v[158:161], v[170:173], v[94:97]
	v_mfma_f32_16x16x32_bf16 v[82:85], v[150:153], v[166:169], v[82:85]
	v_mfma_f32_16x16x32_bf16 v[78:81], v[158:161], v[166:169], v[78:81]
	v_mfma_f32_16x16x32_bf16 v[130:133], v[154:157], v[194:197], v[130:133]
	v_mfma_f32_16x16x32_bf16 v[126:129], v[162:165], v[194:197], v[126:129]
	v_mfma_f32_16x16x32_bf16 v[114:117], v[154:157], v[190:193], v[114:117]
	v_mfma_f32_16x16x32_bf16 v[110:113], v[162:165], v[190:193], v[110:113]
	v_mfma_f32_16x16x32_bf16 v[98:101], v[154:157], v[186:189], v[98:101]
	v_mfma_f32_16x16x32_bf16 v[94:97], v[162:165], v[186:189], v[94:97]
	v_mfma_f32_16x16x32_bf16 v[82:85], v[154:157], v[182:185], v[82:85]
	v_mfma_f32_16x16x32_bf16 v[78:81], v[162:165], v[182:185], v[78:81]
	v_mfma_f32_16x16x32_bf16 v[122:125], v[134:137], v[178:181], v[122:125]
	v_mfma_f32_16x16x32_bf16 v[118:121], v[142:145], v[178:181], v[118:121]
	v_mfma_f32_16x16x32_bf16 v[106:109], v[134:137], v[174:177], v[106:109]
	v_mfma_f32_16x16x32_bf16 v[102:105], v[142:145], v[174:177], v[102:105]
	v_mfma_f32_16x16x32_bf16 v[90:93], v[134:137], v[170:173], v[90:93]
	v_mfma_f32_16x16x32_bf16 v[86:89], v[142:145], v[170:173], v[86:89]
	v_mfma_f32_16x16x32_bf16 v[74:77], v[134:137], v[166:169], v[74:77]
	v_mfma_f32_16x16x32_bf16 v[70:73], v[142:145], v[166:169], v[70:73]
	v_mfma_f32_16x16x32_bf16 v[122:125], v[138:141], v[194:197], v[122:125]
	v_mfma_f32_16x16x32_bf16 v[118:121], v[146:149], v[194:197], v[118:121]
	v_mfma_f32_16x16x32_bf16 v[106:109], v[138:141], v[190:193], v[106:109]
	v_mfma_f32_16x16x32_bf16 v[102:105], v[146:149], v[190:193], v[102:105]
	v_mfma_f32_16x16x32_bf16 v[90:93], v[138:141], v[186:189], v[90:93]
	v_mfma_f32_16x16x32_bf16 v[86:89], v[146:149], v[186:189], v[86:89]
	v_mfma_f32_16x16x32_bf16 v[74:77], v[138:141], v[182:185], v[74:77]
	v_mfma_f32_16x16x32_bf16 v[70:73], v[146:149], v[182:185], v[70:73]
	s_setprio 0
	s_barrier
	v_cmp_ne_u32_e64 s[4:5], 1, v222
	s_andn2_b64 vcc, exec, s[34:35]
	s_cbranch_vccnz .LBB0_1811
	ds_read_b128 v[178:181], v221 offset:16384
	ds_read_b128 v[194:197], v221 offset:17408
	ds_read_b128 v[174:177], v221 offset:18432
	ds_read_b128 v[190:193], v221 offset:19456
	ds_read_b128 v[170:173], v221 offset:20480
	ds_read_b128 v[186:189], v221 offset:21504
	ds_read_b128 v[166:169], v221 offset:22528
	ds_read_b128 v[182:185], v221 offset:23552
.LBB0_1811:
	s_add_u32 s36, s38, 0x100
	s_addc_u32 s37, s39, 0
	s_add_u32 s70, s64, s38
	s_addc_u32 s71, s65, s39
	s_cmp_eq_u32 s66, 12
	s_cselect_b64 s[68:69], -1, 0
	s_and_b64 s[38:39], s[68:69], exec
	s_cselect_b32 s67, 0, s36
	s_cselect_b32 s39, s17, s71
	s_cselect_b32 s38, s19, s70
	s_and_b64 s[68:69], s[30:31], s[68:69]
	s_and_b64 s[68:69], s[68:69], exec
	s_cselect_b32 s69, s24, s28
	s_mov_b32 m0, s43
	v_lshl_add_u64 v[4:5], s[38:39], 0, v[198:199]
	s_cselect_b32 s68, s25, s29
	s_add_u32 s70, s69, s67
	global_load_lds_dwordx4 v[4:5], off
	v_lshl_add_u64 v[210:211], s[38:39], 0, v[200:201]
	s_mov_b32 m0, s44
	s_addc_u32 s71, s68, 0
	global_load_lds_dwordx4 v[210:211], off
	v_lshl_add_u64 v[212:213], s[70:71], 0, v[198:199]
	s_mov_b32 m0, s27
	v_lshl_add_u64 v[214:215], s[70:71], 0, v[200:201]
	s_add_u32 s70, s38, 0x40000
	global_load_lds_dwordx4 v[212:213], off
	s_mov_b32 m0, s45
	s_addc_u32 s71, s39, 0
	global_load_lds_dwordx4 v[214:215], off
	v_lshl_add_u64 v[224:225], s[70:71], 0, v[198:199]
	s_mov_b32 m0, s46
	s_and_b64 vcc, exec, s[4:5]
	global_load_lds_dwordx4 v[224:225], off
	v_lshl_add_u64 v[224:225], s[70:71], 0, v[200:201]
	s_mov_b32 m0, s47
	s_nop 0
	global_load_lds_dwordx4 v[224:225], off
	s_waitcnt vmcnt(6)
	s_waitcnt lgkmcnt(0)
	s_barrier
	s_cbranch_vccnz .LBB0_1813
; #define G8_STAGE_B(bufoff, gbase) do { _Pragma("unroll") for (int _i = 0; _i < 2; ++_i) \
;         __builtin_amdgcn_global_load_lds((const unsigned*)((const char*)(gbase) + voffB[_i]), (LAS unsigned*)(lds + (bufoff) + ldsw + _i * 8192), 16, 0, 0); } while (0)
; #define G8_LDA(dst, b, h) do { _Pragma("unroll") for (int m = 0; m < 4; ++m) _Pragma("unroll") for (int k = 0; k < 2; ++k) dst[m][k] = *(const LAS bf16x8*)(lds + G8_SA(b, h) + aoff + m * 2048 + k * 1024); } while (0)
; #define G8_LDB(dst, b, h) do { _Pragma("unroll") for (int n = 0; n < 2; ++n) _Pragma("unroll") for (int k = 0; k < 2; ++k) dst[n][k] = *(const LAS bf16x8*)(lds + G8_SB(b, h) + boff + n * 2048 + k * 1024); } while (0)
; #define G8_WAIT_V(n) asm volatile("s_waitcnt vmcnt(" #n ")" ::: "memory")
; #define G8_WAIT_L(n) asm volatile("s_waitcnt lgkmcnt(" #n ")" ::: "memory")
; #define G8_BAR __builtin_amdgcn_s_barrier()
; template <class Sched, class Epi>
; DEVI void gemm_phase(LAS unsigned char* lds, const char* Abase, const int K, const Sched& S, const Epi& E) {
;     ...
;         for (int t = 0; t < ntu; t += 2) {
;             const bool last = (t == ntu - 2);
;             const size_t k1 = (size_t)(t + 1) * kstep;
;             const size_t k2 = last ? (size_t)0 : (size_t)(t + 2) * kstep, k3 = k2 + kstep;
;             const char* b2 = last ? nB : cB + (size_t)(t + 2) * kstep; const char* b3 = b2 + kstep;
;             G8_LDB(B0, 0, 0); G8_LDB(B1, 0, 1); G8_SCHED; G8_LDA(At, 0, 0); G8_STAGE_A(G8_SA(1, 1), false, 1, k1);
;             G8_WAIT_L(0); G8_BAR; G8_MMA(0, 0, At, B0); G8_MMA(0, 1, At, B1); G8_BAR; G8_SCHED;
;             if (!skip1) G8_LDA(At, 0, 1); G8_STAGE_B(G8_SB(0, 0), b2); G8_STAGE_A(G8_SA(0, 0), last, 0, k2); G8_STAGE_B(G8_SB(0, 1), b2 + hstepB);
;             G8_WAIT_V(6); G8_WAIT_L(0); G8_BAR; if (!skip1) { G8_MMA(1, 0, At, B0); G8_MMA(1, 1, At, B1); } G8_BAR; G8_SCHED;
;             G8_LDB(B0, 1, 0); G8_LDB(B1, 1, 1); G8_SCHED; G8_LDA(At, 1, 0); G8_STAGE_A(G8_SA(0, 1), last, 1, k2);
;             G8_WAIT_L(0); G8_BAR; G8_MMA(0, 0, At, B0); G8_MMA(0, 1, At, B1); G8_BAR; G8_SCHED;
;             if (!skip1) G8_LDA(At, 1, 1); G8_STAGE_B(G8_SB(1, 0), b3); G8_STAGE_A(G8_SA(1, 0), last, 0, k3); G8_STAGE_B(G8_SB(1, 1), b3 + hstepB);
;             G8_WAIT_V(6); G8_WAIT_L(0); G8_BAR; if (!skip1) { G8_MMA(1, 0, At, B0); G8_MMA(1, 1, At, B1); } G8_BAR; G8_SCHED;
	s_setprio 1
	s_waitcnt lgkmcnt(0)
	v_mfma_f32_16x16x32_bf16 v[66:69], v[150:153], v[178:181], v[66:69]
	v_mfma_f32_16x16x32_bf16 v[62:65], v[158:161], v[178:181], v[62:65]
	v_mfma_f32_16x16x32_bf16 v[50:53], v[150:153], v[174:177], v[50:53]
	v_mfma_f32_16x16x32_bf16 v[46:49], v[158:161], v[174:177], v[46:49]
	v_mfma_f32_16x16x32_bf16 v[34:37], v[150:153], v[170:173], v[34:37]
	v_mfma_f32_16x16x32_bf16 v[30:33], v[158:161], v[170:173], v[30:33]
	v_mfma_f32_16x16x32_bf16 v[18:21], v[150:153], v[166:169], v[18:21]
	v_mfma_f32_16x16x32_bf16 v[14:17], v[158:161], v[166:169], v[14:17]
	v_mfma_f32_16x16x32_bf16 v[66:69], v[154:157], v[194:197], v[66:69]
	v_mfma_f32_16x16x32_bf16 v[62:65], v[162:165], v[194:197], v[62:65]
	v_mfma_f32_16x16x32_bf16 v[50:53], v[154:157], v[190:193], v[50:53]
	v_mfma_f32_16x16x32_bf16 v[46:49], v[162:165], v[190:193], v[46:49]
	v_mfma_f32_16x16x32_bf16 v[34:37], v[154:157], v[186:189], v[34:37]
	v_mfma_f32_16x16x32_bf16 v[30:33], v[162:165], v[186:189], v[30:33]
	v_mfma_f32_16x16x32_bf16 v[18:21], v[154:157], v[182:185], v[18:21]
	v_mfma_f32_16x16x32_bf16 v[14:17], v[162:165], v[182:185], v[14:17]
	v_mfma_f32_16x16x32_bf16 v[58:61], v[134:137], v[178:181], v[58:61]
	v_mfma_f32_16x16x32_bf16 v[54:57], v[142:145], v[178:181], v[54:57]
	v_mfma_f32_16x16x32_bf16 v[42:45], v[134:137], v[174:177], v[42:45]
	v_mfma_f32_16x16x32_bf16 v[38:41], v[142:145], v[174:177], v[38:41]
	v_mfma_f32_16x16x32_bf16 v[26:29], v[134:137], v[170:173], v[26:29]
	v_mfma_f32_16x16x32_bf16 v[22:25], v[142:145], v[170:173], v[22:25]
	v_mfma_f32_16x16x32_bf16 v[10:13], v[134:137], v[166:169], v[10:13]
	v_mfma_f32_16x16x32_bf16 v[6:9], v[142:145], v[166:169], v[6:9]
	v_mfma_f32_16x16x32_bf16 v[58:61], v[138:141], v[194:197], v[58:61]
	v_mfma_f32_16x16x32_bf16 v[54:57], v[146:149], v[194:197], v[54:57]
	v_mfma_f32_16x16x32_bf16 v[42:45], v[138:141], v[190:193], v[42:45]
	v_mfma_f32_16x16x32_bf16 v[38:41], v[146:149], v[190:193], v[38:41]
	v_mfma_f32_16x16x32_bf16 v[26:29], v[138:141], v[186:189], v[26:29]
	v_mfma_f32_16x16x32_bf16 v[22:25], v[146:149], v[186:189], v[22:25]
	v_mfma_f32_16x16x32_bf16 v[10:13], v[138:141], v[182:185], v[10:13]
	v_mfma_f32_16x16x32_bf16 v[6:9], v[146:149], v[182:185], v[6:9]
	s_setprio 0
.LBB0_1813:
	s_barrier
	v_add_u32_e32 v3, 0x18000, v218
	ds_read_b128 v[150:153], v3
	ds_read_b128 v[154:157], v3 offset:1024
	ds_read_b128 v[158:161], v3 offset:2048
	ds_read_b128 v[162:165], v3 offset:3072
	v_add_u32_e32 v3, 0x1c000, v218
	ds_read_b128 v[134:137], v3
	ds_read_b128 v[138:141], v3 offset:1024
	ds_read_b128 v[142:145], v3 offset:2048
	ds_read_b128 v[146:149], v3 offset:3072
	s_add_u32 s67, s69, s67
	s_addc_u32 s69, s68, 0
	s_add_u32 s68, s67, 0x40000
	s_addc_u32 s69, s69, 0
	s_mov_b32 m0, s48
	v_lshl_add_u64 v[224:225], s[68:69], 0, v[198:199]
	s_waitcnt lgkmcnt(0)
	ds_read_b128 v[178:181], v221 offset:32768
	ds_read_b128 v[194:197], v221 offset:33792
	ds_read_b128 v[174:177], v221 offset:34816
	ds_read_b128 v[190:193], v221 offset:35840
	ds_read_b128 v[170:173], v221 offset:36864
	ds_read_b128 v[186:189], v221 offset:37888
	ds_read_b128 v[166:169], v221 offset:38912
	ds_read_b128 v[182:185], v221 offset:39936
	global_load_lds_dwordx4 v[224:225], off
	v_lshl_add_u64 v[224:225], s[68:69], 0, v[200:201]
	s_mov_b32 m0, s49
	s_nop 0
	global_load_lds_dwordx4 v[224:225], off
	s_waitcnt lgkmcnt(0)
	s_barrier
	s_setprio 1
	s_waitcnt lgkmcnt(0)
	v_mfma_f32_16x16x32_bf16 v[130:133], v[150:153], v[178:181], v[130:133]
	v_mfma_f32_16x16x32_bf16 v[126:129], v[158:161], v[178:181], v[126:129]
	v_mfma_f32_16x16x32_bf16 v[114:117], v[150:153], v[174:177], v[114:117]
	v_mfma_f32_16x16x32_bf16 v[110:113], v[158:161], v[174:177], v[110:113]
	v_mfma_f32_16x16x32_bf16 v[98:101], v[150:153], v[170:173], v[98:101]
	v_mfma_f32_16x16x32_bf16 v[94:97], v[158:161], v[170:173], v[94:97]
	v_mfma_f32_16x16x32_bf16 v[82:85], v[150:153], v[166:169], v[82:85]
	v_mfma_f32_16x16x32_bf16 v[78:81], v[158:161], v[166:169], v[78:81]
	v_mfma_f32_16x16x32_bf16 v[130:133], v[154:157], v[194:197], v[130:133]
	v_mfma_f32_16x16x32_bf16 v[126:129], v[162:165], v[194:197], v[126:129]
	v_mfma_f32_16x16x32_bf16 v[114:117], v[154:157], v[190:193], v[114:117]
	v_mfma_f32_16x16x32_bf16 v[110:113], v[162:165], v[190:193], v[110:113]
	v_mfma_f32_16x16x32_bf16 v[98:101], v[154:157], v[186:189], v[98:101]
	v_mfma_f32_16x16x32_bf16 v[94:97], v[162:165], v[186:189], v[94:97]
	v_mfma_f32_16x16x32_bf16 v[82:85], v[154:157], v[182:185], v[82:85]
	v_mfma_f32_16x16x32_bf16 v[78:81], v[162:165], v[182:185], v[78:81]
	v_mfma_f32_16x16x32_bf16 v[122:125], v[134:137], v[178:181], v[122:125]
	v_mfma_f32_16x16x32_bf16 v[118:121], v[142:145], v[178:181], v[118:121]
	v_mfma_f32_16x16x32_bf16 v[106:109], v[134:137], v[174:177], v[106:109]
	v_mfma_f32_16x16x32_bf16 v[102:105], v[142:145], v[174:177], v[102:105]
	v_mfma_f32_16x16x32_bf16 v[90:93], v[134:137], v[170:173], v[90:93]
	v_mfma_f32_16x16x32_bf16 v[86:89], v[142:145], v[170:173], v[86:89]
	v_mfma_f32_16x16x32_bf16 v[74:77], v[134:137], v[166:169], v[74:77]
	v_mfma_f32_16x16x32_bf16 v[70:73], v[142:145], v[166:169], v[70:73]
	v_mfma_f32_16x16x32_bf16 v[122:125], v[138:141], v[194:197], v[122:125]
	v_mfma_f32_16x16x32_bf16 v[118:121], v[146:149], v[194:197], v[118:121]
	v_mfma_f32_16x16x32_bf16 v[106:109], v[138:141], v[190:193], v[106:109]
	v_mfma_f32_16x16x32_bf16 v[102:105], v[146:149], v[190:193], v[102:105]
	v_mfma_f32_16x16x32_bf16 v[90:93], v[138:141], v[186:189], v[90:93]
	v_mfma_f32_16x16x32_bf16 v[86:89], v[146:149], v[186:189], v[86:89]
	v_mfma_f32_16x16x32_bf16 v[74:77], v[138:141], v[182:185], v[74:77]
	v_mfma_f32_16x16x32_bf16 v[70:73], v[146:149], v[182:185], v[70:73]
	s_setprio 0
	s_barrier
	s_and_b64 vcc, exec, s[4:5]
	s_cbranch_vccnz .LBB0_1815
	ds_read_b128 v[178:181], v221 offset:49152
	ds_read_b128 v[194:197], v221 offset:50176
	ds_read_b128 v[174:177], v221 offset:51200
	ds_read_b128 v[190:193], v221 offset:52224
	ds_read_b128 v[170:173], v221 offset:53248
	ds_read_b128 v[186:189], v221 offset:54272
	ds_read_b128 v[166:169], v221 offset:55296
	ds_read_b128 v[182:185], v221 offset:56320
; #define G8_STAGE_B(bufoff, gbase) do { _Pragma("unroll") for (int _i = 0; _i < 2; ++_i) \
;         __builtin_amdgcn_global_load_lds((const unsigned*)((const char*)(gbase) + voffB[_i]), (LAS unsigned*)(lds + (bufoff) + ldsw + _i * 8192), 16, 0, 0); } while (0)
; #define G8_LDA(dst, b, h) do { _Pragma("unroll") for (int m = 0; m < 4; ++m) _Pragma("unroll") for (int k = 0; k < 2; ++k) dst[m][k] = *(const LAS bf16x8*)(lds + G8_SA(b, h) + aoff + m * 2048 + k * 1024); } while (0)
; #define G8_LDB(dst, b, h) do { _Pragma("unroll") for (int n = 0; n < 2; ++n) _Pragma("unroll") for (int k = 0; k < 2; ++k) dst[n][k] = *(const LAS bf16x8*)(lds + G8_SB(b, h) + boff + n * 2048 + k * 1024); } while (0)
; #define G8_WAIT_V(n) asm volatile("s_waitcnt vmcnt(" #n ")" ::: "memory")
; #define G8_WAIT_L(n) asm volatile("s_waitcnt lgkmcnt(" #n ")" ::: "memory")
; #define G8_BAR __builtin_amdgcn_s_barrier()
; template <class Sched, class Epi>
; DEVI void gemm_phase(LAS unsigned char* lds, const char* Abase, const int K, const Sched& S, const Epi& E) {
;     ...
;         for (int t = 0; t < ntu; t += 2) {
;             const bool last = (t == ntu - 2);
;             const size_t k1 = (size_t)(t + 1) * kstep;
;             const size_t k2 = last ? (size_t)0 : (size_t)(t + 2) * kstep, k3 = k2 + kstep;
;             const char* b2 = last ? nB : cB + (size_t)(t + 2) * kstep; const char* b3 = b2 + kstep;
;             G8_LDB(B0, 0, 0); G8_LDB(B1, 0, 1); G8_SCHED; G8_LDA(At, 0, 0); G8_STAGE_A(G8_SA(1, 1), false, 1, k1);
;             G8_WAIT_L(0); G8_BAR; G8_MMA(0, 0, At, B0); G8_MMA(0, 1, At, B1); G8_BAR; G8_SCHED;
;             if (!skip1) G8_LDA(At, 0, 1); G8_STAGE_B(G8_SB(0, 0), b2); G8_STAGE_A(G8_SA(0, 0), last, 0, k2); G8_STAGE_B(G8_SB(0, 1), b2 + hstepB);
;             G8_WAIT_V(6); G8_WAIT_L(0); G8_BAR; if (!skip1) { G8_MMA(1, 0, At, B0); G8_MMA(1, 1, At, B1); } G8_BAR; G8_SCHED;
;             G8_LDB(B0, 1, 0); G8_LDB(B1, 1, 1); G8_SCHED; G8_LDA(At, 1, 0); G8_STAGE_A(G8_SA(0, 1), last, 1, k2);
;             G8_WAIT_L(0); G8_BAR; G8_MMA(0, 0, At, B0); G8_MMA(0, 1, At, B1); G8_BAR; G8_SCHED;
;             if (!skip1) G8_LDA(At, 1, 1); G8_STAGE_B(G8_SB(1, 0), b3); G8_STAGE_A(G8_SA(1, 0), last, 0, k3); G8_STAGE_B(G8_SB(1, 1), b3 + hstepB);
;             G8_WAIT_V(6); G8_WAIT_L(0); G8_BAR; if (!skip1) { G8_MMA(1, 0, At, B0); G8_MMA(1, 1, At, B1); } G8_BAR; G8_SCHED;
.LBB0_1815:
	s_mov_b32 m0, s51
	v_lshl_add_u64 v[4:5], v[4:5], 0, s[14:15]
	global_load_lds_dwordx4 v[4:5], off
	v_lshl_add_u64 v[4:5], v[210:211], 0, s[14:15]
	s_mov_b32 m0, s52
	s_add_u32 s38, s38, 0x40080
	global_load_lds_dwordx4 v[4:5], off
	v_lshl_add_u64 v[4:5], v[212:213], 0, s[14:15]
	s_mov_b32 m0, s53
	s_addc_u32 s39, s39, 0
	global_load_lds_dwordx4 v[4:5], off
	v_lshl_add_u64 v[4:5], v[214:215], 0, s[14:15]
	s_mov_b32 m0, s54
	s_and_b64 vcc, exec, s[4:5]
	global_load_lds_dwordx4 v[4:5], off
	v_lshl_add_u64 v[4:5], s[38:39], 0, v[198:199]
	s_mov_b32 m0, s55
	s_nop 0
	global_load_lds_dwordx4 v[4:5], off
	v_lshl_add_u64 v[4:5], s[38:39], 0, v[200:201]
	s_mov_b32 m0, s56
	s_nop 0
	global_load_lds_dwordx4 v[4:5], off
	s_waitcnt vmcnt(6)
	s_waitcnt lgkmcnt(0)
	s_barrier
	s_cbranch_vccnz .LBB0_1817
	s_setprio 1
	s_waitcnt lgkmcnt(0)
	v_mfma_f32_16x16x32_bf16 v[66:69], v[150:153], v[178:181], v[66:69]
	v_mfma_f32_16x16x32_bf16 v[62:65], v[158:161], v[178:181], v[62:65]
	v_mfma_f32_16x16x32_bf16 v[50:53], v[150:153], v[174:177], v[50:53]
	v_mfma_f32_16x16x32_bf16 v[46:49], v[158:161], v[174:177], v[46:49]
	v_mfma_f32_16x16x32_bf16 v[34:37], v[150:153], v[170:173], v[34:37]
	v_mfma_f32_16x16x32_bf16 v[30:33], v[158:161], v[170:173], v[30:33]
	v_mfma_f32_16x16x32_bf16 v[18:21], v[150:153], v[166:169], v[18:21]
	v_mfma_f32_16x16x32_bf16 v[14:17], v[158:161], v[166:169], v[14:17]
	v_mfma_f32_16x16x32_bf16 v[66:69], v[154:157], v[194:197], v[66:69]
	v_mfma_f32_16x16x32_bf16 v[62:65], v[162:165], v[194:197], v[62:65]
	v_mfma_f32_16x16x32_bf16 v[50:53], v[154:157], v[190:193], v[50:53]
	v_mfma_f32_16x16x32_bf16 v[46:49], v[162:165], v[190:193], v[46:49]
	v_mfma_f32_16x16x32_bf16 v[34:37], v[154:157], v[186:189], v[34:37]
	v_mfma_f32_16x16x32_bf16 v[30:33], v[162:165], v[186:189], v[30:33]
	v_mfma_f32_16x16x32_bf16 v[18:21], v[154:157], v[182:185], v[18:21]
	v_mfma_f32_16x16x32_bf16 v[14:17], v[162:165], v[182:185], v[14:17]
	v_mfma_f32_16x16x32_bf16 v[58:61], v[134:137], v[178:181], v[58:61]
	v_mfma_f32_16x16x32_bf16 v[54:57], v[142:145], v[178:181], v[54:57]
	v_mfma_f32_16x16x32_bf16 v[42:45], v[134:137], v[174:177], v[42:45]
	v_mfma_f32_16x16x32_bf16 v[38:41], v[142:145], v[174:177], v[38:41]
	v_mfma_f32_16x16x32_bf16 v[26:29], v[134:137], v[170:173], v[26:29]
	v_mfma_f32_16x16x32_bf16 v[22:25], v[142:145], v[170:173], v[22:25]
	v_mfma_f32_16x16x32_bf16 v[10:13], v[134:137], v[166:169], v[10:13]
	v_mfma_f32_16x16x32_bf16 v[4:7], v[142:145], v[166:169], v[6:9]
	v_mfma_f32_16x16x32_bf16 v[58:61], v[138:141], v[194:197], v[58:61]
	v_mfma_f32_16x16x32_bf16 v[54:57], v[146:149], v[194:197], v[54:57]
	v_mfma_f32_16x16x32_bf16 v[42:45], v[138:141], v[190:193], v[42:45]
	v_mfma_f32_16x16x32_bf16 v[38:41], v[146:149], v[190:193], v[38:41]
	v_mfma_f32_16x16x32_bf16 v[26:29], v[138:141], v[186:189], v[26:29]
	v_mfma_f32_16x16x32_bf16 v[22:25], v[146:149], v[186:189], v[22:25]
	v_mfma_f32_16x16x32_bf16 v[10:13], v[138:141], v[182:185], v[10:13]
	v_mfma_f32_16x16x32_bf16 v[6:9], v[146:149], v[182:185], v[4:7]
	s_setprio 0

; #define G8_STAGE_B(bufoff, gbase) do { _Pragma("unroll") for (int _i = 0; _i < 2; ++_i) \
;         __builtin_amdgcn_global_load_lds((const unsigned*)((const char*)(gbase) + voffB[_i]), (LAS unsigned*)(lds + (bufoff) + ldsw + _i * 8192), 16, 0, 0); } while (0)
; #define G8_LDA(dst, b, h) do { _Pragma("unroll") for (int m = 0; m < 4; ++m) _Pragma("unroll") for (int k = 0; k < 2; ++k) dst[m][k] = *(const LAS bf16x8*)(lds + G8_SA(b, h) + aoff + m * 2048 + k * 1024); } while (0)
; #define G8_LDB(dst, b, h) do { _Pragma("unroll") for (int n = 0; n < 2; ++n) _Pragma("unroll") for (int k = 0; k < 2; ++k) dst[n][k] = *(const LAS bf16x8*)(lds + G8_SB(b, h) + boff + n * 2048 + k * 1024); } while (0)
; #define G8_WAIT_V(n) asm volatile("s_waitcnt vmcnt(" #n ")" ::: "memory")
; #define G8_WAIT_L(n) asm volatile("s_waitcnt lgkmcnt(" #n ")" ::: "memory")
; #define G8_BAR __builtin_amdgcn_s_barrier()
; template <class Sched, class Epi>
; DEVI void gemm_phase(LAS unsigned char* lds, const char* Abase, const int K, const Sched& S, const Epi& E) {
;     ...
;         for (int t = 0; t < ntu; t += 2) {
;             const bool last = (t == ntu - 2);
;             const size_t k1 = (size_t)(t + 1) * kstep;
;             const size_t k2 = last ? (size_t)0 : (size_t)(t + 2) * kstep, k3 = k2 + kstep;
;             const char* b2 = last ? nB : cB + (size_t)(t + 2) * kstep; const char* b3 = b2 + kstep;
;             G8_LDB(B0, 0, 0); G8_LDB(B1, 0, 1); G8_SCHED; G8_LDA(At, 0, 0); G8_STAGE_A(G8_SA(1, 1), false, 1, k1);
;             G8_WAIT_L(0); G8_BAR; G8_MMA(0, 0, At, B0); G8_MMA(0, 1, At, B1); G8_BAR; G8_SCHED;
;             if (!skip1) G8_LDA(At, 0, 1); G8_STAGE_B(G8_SB(0, 0), b2); G8_STAGE_A(G8_SA(0, 0), last, 0, k2); G8_STAGE_B(G8_SB(0, 1), b2 + hstepB);
;             G8_WAIT_V(6); G8_WAIT_L(0); G8_BAR; if (!skip1) { G8_MMA(1, 0, At, B0); G8_MMA(1, 1, At, B1); } G8_BAR; G8_SCHED;
;             G8_LDB(B0, 1, 0); G8_LDB(B1, 1, 1); G8_SCHED; G8_LDA(At, 1, 0); G8_STAGE_A(G8_SA(0, 1), last, 1, k2);
;             G8_WAIT_L(0); G8_BAR; G8_MMA(0, 0, At, B0); G8_MMA(0, 1, At, B1); G8_BAR; G8_SCHED;
;             if (!skip1) G8_LDA(At, 1, 1); G8_STAGE_B(G8_SB(1, 0), b3); G8_STAGE_A(G8_SA(1, 0), last, 0, k3); G8_STAGE_B(G8_SB(1, 1), b3 + hstepB);
;             G8_WAIT_V(6); G8_WAIT_L(0); G8_BAR; if (!skip1) { G8_MMA(1, 0, At, B0); G8_MMA(1, 1, At, B1); } G8_BAR; G8_SCHED;
.LBB0_2037:
	ds_read_b128 v[148:151], v155
	ds_read_b128 v[158:161], v155 offset:1024
	ds_read_b128 v[162:165], v155 offset:2048
	ds_read_b128 v[166:169], v155 offset:3072
	ds_read_b128 v[170:173], v156
	ds_read_b128 v[174:177], v156 offset:1024
	ds_read_b128 v[178:181], v156 offset:2048
	ds_read_b128 v[182:185], v156 offset:3072
	s_add_i32 s66, s40, 2
	s_add_u32 s67, s38, 0xfff90080
	s_addc_u32 s68, s39, -1
	s_add_u32 s41, s6, s38
	s_addc_u32 s69, s7, s39
	s_add_u32 s70, s41, 0xfff90080
	s_addc_u32 s41, s69, -1
	s_add_i32 s71, s60, s48
	s_add_i32 m0, s50, 0xc000
	s_add_i32 s69, s50, 0xe000
	s_add_i32 s72, s71, 0x2000
	s_cmp_eq_u32 s23, s40
	s_cselect_b32 s40, s26, s70
	s_cselect_b32 s41, s27, s41
	s_cselect_b32 s70, 0, s68
	s_cselect_b32 s67, 0, s67
	v_lshl_add_u64 v[218:219], v[144:145], 0, s[38:39]
	ds_read_b128 v[186:189], v157
	ds_read_b128 v[190:193], v157 offset:1024
	ds_read_b128 v[194:197], v157 offset:2048
	ds_read_b128 v[198:201], v157 offset:3072
	ds_read_b128 v[202:205], v157 offset:4096
	ds_read_b128 v[206:209], v157 offset:5120
	ds_read_b128 v[210:213], v157 offset:6144
	ds_read_b128 v[214:217], v157 offset:7168
	global_load_lds_dwordx4 v[218:219], off
	v_lshl_add_u64 v[218:219], v[146:147], 0, s[38:39]
	s_mov_b32 m0, s69
	s_nop 0
	global_load_lds_dwordx4 v[218:219], off
	s_waitcnt lgkmcnt(0)
	s_barrier
	s_setprio 1
	s_waitcnt lgkmcnt(0)
	v_mfma_f32_16x16x32_bf16 v[126:129], v[148:151], v[186:189], v[126:129]
	v_mfma_f32_16x16x32_bf16 v[122:125], v[162:165], v[186:189], v[122:125]
	v_mfma_f32_16x16x32_bf16 v[110:113], v[148:151], v[194:197], v[110:113]
	v_mfma_f32_16x16x32_bf16 v[106:109], v[162:165], v[194:197], v[106:109]
	v_mfma_f32_16x16x32_bf16 v[94:97], v[148:151], v[202:205], v[94:97]
	v_mfma_f32_16x16x32_bf16 v[90:93], v[162:165], v[202:205], v[90:93]
	v_mfma_f32_16x16x32_bf16 v[78:81], v[148:151], v[210:213], v[78:81]
	v_mfma_f32_16x16x32_bf16 v[74:77], v[162:165], v[210:213], v[74:77]
	v_mfma_f32_16x16x32_bf16 v[126:129], v[158:161], v[190:193], v[126:129]
	v_mfma_f32_16x16x32_bf16 v[122:125], v[166:169], v[190:193], v[122:125]
	v_mfma_f32_16x16x32_bf16 v[110:113], v[158:161], v[198:201], v[110:113]
	v_mfma_f32_16x16x32_bf16 v[106:109], v[166:169], v[198:201], v[106:109]
	v_mfma_f32_16x16x32_bf16 v[94:97], v[158:161], v[206:209], v[94:97]
	v_mfma_f32_16x16x32_bf16 v[90:93], v[166:169], v[206:209], v[90:93]
	v_mfma_f32_16x16x32_bf16 v[78:81], v[158:161], v[214:217], v[78:81]
	v_mfma_f32_16x16x32_bf16 v[74:77], v[166:169], v[214:217], v[74:77]
	v_mfma_f32_16x16x32_bf16 v[118:121], v[170:173], v[186:189], v[118:121]
	v_mfma_f32_16x16x32_bf16 v[114:117], v[178:181], v[186:189], v[114:117]
	v_mfma_f32_16x16x32_bf16 v[102:105], v[170:173], v[194:197], v[102:105]
	v_mfma_f32_16x16x32_bf16 v[98:101], v[178:181], v[194:197], v[98:101]
	v_mfma_f32_16x16x32_bf16 v[86:89], v[170:173], v[202:205], v[86:89]
	v_mfma_f32_16x16x32_bf16 v[82:85], v[178:181], v[202:205], v[82:85]
	v_mfma_f32_16x16x32_bf16 v[70:73], v[170:173], v[210:213], v[70:73]
	v_mfma_f32_16x16x32_bf16 v[66:69], v[178:181], v[210:213], v[66:69]
	v_mfma_f32_16x16x32_bf16 v[118:121], v[174:177], v[190:193], v[118:121]
	v_mfma_f32_16x16x32_bf16 v[114:117], v[182:185], v[190:193], v[114:117]
	v_mfma_f32_16x16x32_bf16 v[102:105], v[174:177], v[198:201], v[102:105]
	v_mfma_f32_16x16x32_bf16 v[98:101], v[182:185], v[198:201], v[98:101]
	v_mfma_f32_16x16x32_bf16 v[86:89], v[174:177], v[206:209], v[86:89]
	v_mfma_f32_16x16x32_bf16 v[82:85], v[182:185], v[206:209], v[82:85]
	v_mfma_f32_16x16x32_bf16 v[70:73], v[174:177], v[214:217], v[70:73]
	v_mfma_f32_16x16x32_bf16 v[66:69], v[182:185], v[214:217], v[66:69]
	s_setprio 0
	s_barrier
	s_cselect_b32 s68, s28, s34
	s_mov_b32 m0, s71
	v_lshl_add_u64 v[218:219], s[40:41], 0, v[130:131]
	s_cselect_b32 s69, s29, s35
	s_add_u32 s68, s68, s67
	ds_read_b128 v[186:189], v157 offset:16384
	ds_read_b128 v[190:193], v157 offset:17408
	ds_read_b128 v[194:197], v157 offset:18432
	ds_read_b128 v[198:201], v157 offset:19456
	ds_read_b128 v[202:205], v157 offset:20480
	ds_read_b128 v[206:209], v157 offset:21504
	ds_read_b128 v[210:213], v157 offset:22528
	ds_read_b128 v[214:217], v157 offset:23552
	global_load_lds_dwordx4 v[218:219], off
	v_lshl_add_u64 v[220:221], s[40:41], 0, v[132:133]
	s_mov_b32 m0, s72
	s_addc_u32 s69, s69, s70
	global_load_lds_dwordx4 v[220:221], off
	v_lshl_add_u64 v[222:223], s[68:69], 0, v[134:135]
	s_mov_b32 m0, s50
	s_add_u32 s70, s40, 0x10000
	global_load_lds_dwordx4 v[222:223], off
	v_lshl_add_u64 v[224:225], s[68:69], 0, v[136:137]
	s_mov_b32 m0, s51
	s_addc_u32 s71, s41, 0
	s_add_i32 s67, s61, s48
	global_load_lds_dwordx4 v[224:225], off
	v_lshl_add_u64 v[226:227], s[70:71], 0, v[130:131]
	s_mov_b32 m0, s67
	s_nop 0
	global_load_lds_dwordx4 v[226:227], off
	v_lshl_add_u64 v[226:227], s[70:71], 0, v[132:133]
	s_add_i32 m0, s67, 0x2000
	s_nop 0
	global_load_lds_dwordx4 v[226:227], off
	s_waitcnt vmcnt(6)
	s_waitcnt lgkmcnt(0)
	s_barrier
; #define G8_STAGE_B(bufoff, gbase) do { _Pragma("unroll") for (int _i = 0; _i < 2; ++_i) \
;         __builtin_amdgcn_global_load_lds((const unsigned*)((const char*)(gbase) + voffB[_i]), (LAS unsigned*)(lds + (bufoff) + ldsw + _i * 8192), 16, 0, 0); } while (0)
; #define G8_LDA(dst, b, h) do { _Pragma("unroll") for (int m = 0; m < 4; ++m) _Pragma("unroll") for (int k = 0; k < 2; ++k) dst[m][k] = *(const LAS bf16x8*)(lds + G8_SA(b, h) + aoff + m * 2048 + k * 1024); } while (0)
; #define G8_LDB(dst, b, h) do { _Pragma("unroll") for (int n = 0; n < 2; ++n) _Pragma("unroll") for (int k = 0; k < 2; ++k) dst[n][k] = *(const LAS bf16x8*)(lds + G8_SB(b, h) + boff + n * 2048 + k * 1024); } while (0)
; #define G8_MMA(ai, bj, At, Bt) do { __builtin_amdgcn_s_setprio(1); _Pragma("unroll") for (int m = 0; m < 4; ++m) _Pragma("unroll") for (int n = 0; n < 2; ++n) _Pragma("unroll") for (int k = 0; k < 2; ++k) \
;         acc[ai][bj][m][n] = __builtin_amdgcn_mfma_f32_16x16x32_bf16(Bt[n][k], At[m][k], acc[ai][bj][m][n], 0, 0, 0); __builtin_amdgcn_s_setprio(0); } while (0)
; #define G8_WAIT_V(n) asm volatile("s_waitcnt vmcnt(" #n ")" ::: "memory")
; #define G8_WAIT_L(n) asm volatile("s_waitcnt lgkmcnt(" #n ")" ::: "memory")
; template <class Sched, class Epi>
; DEVI void gemm_phase(LAS unsigned char* lds, const char* Abase, const int K, const Sched& S, const Epi& E) {
;     ...
;             G8_LDB(B0, 0, 0); G8_LDB(B1, 0, 1); G8_SCHED; G8_LDA(At, 0, 0); G8_STAGE_A(G8_SA(1, 1), false, 1, k1);
;             G8_WAIT_L(0); G8_BAR; G8_MMA(0, 0, At, B0); G8_MMA(0, 1, At, B1); G8_BAR; G8_SCHED;
;             if (!skip1) G8_LDA(At, 0, 1); G8_STAGE_B(G8_SB(0, 0), b2); G8_STAGE_A(G8_SA(0, 0), last, 0, k2); G8_STAGE_B(G8_SB(0, 1), b2 + hstepB);
;             G8_WAIT_V(6); G8_WAIT_L(0); G8_BAR; if (!skip1) { G8_MMA(1, 0, At, B0); G8_MMA(1, 1, At, B1); } G8_BAR; G8_SCHED;
;             G8_LDB(B0, 1, 0); G8_LDB(B1, 1, 1); G8_SCHED; G8_LDA(At, 1, 0); G8_STAGE_A(G8_SA(0, 1), last, 1, k2);
;             G8_WAIT_L(0); G8_BAR; G8_MMA(0, 0, At, B0); G8_MMA(0, 1, At, B1); G8_BAR; G8_SCHED;
;             if (!skip1) G8_LDA(At, 1, 1); G8_STAGE_B(G8_SB(1, 0), b3); G8_STAGE_A(G8_SA(1, 0), last, 0, k3); G8_STAGE_B(G8_SB(1, 1), b3 + hstepB);
;             G8_WAIT_V(6); G8_WAIT_L(0); G8_BAR; if (!skip1) { G8_MMA(1, 0, At, B0); G8_MMA(1, 1, At, B1); } G8_BAR; G8_SCHED;
	s_setprio 1
	s_waitcnt lgkmcnt(0)
	v_mfma_f32_16x16x32_bf16 v[62:65], v[148:151], v[186:189], v[62:65]
	v_mfma_f32_16x16x32_bf16 v[58:61], v[162:165], v[186:189], v[58:61]
	v_mfma_f32_16x16x32_bf16 v[46:49], v[148:151], v[194:197], v[46:49]
	v_mfma_f32_16x16x32_bf16 v[42:45], v[162:165], v[194:197], v[42:45]
	v_mfma_f32_16x16x32_bf16 v[30:33], v[148:151], v[202:205], v[30:33]
	v_mfma_f32_16x16x32_bf16 v[26:29], v[162:165], v[202:205], v[26:29]
	v_mfma_f32_16x16x32_bf16 v[14:17], v[148:151], v[210:213], v[14:17]
	v_mfma_f32_16x16x32_bf16 v[10:13], v[162:165], v[210:213], v[10:13]
	v_mfma_f32_16x16x32_bf16 v[62:65], v[158:161], v[190:193], v[62:65]
	v_mfma_f32_16x16x32_bf16 v[58:61], v[166:169], v[190:193], v[58:61]
	v_mfma_f32_16x16x32_bf16 v[46:49], v[158:161], v[198:201], v[46:49]
	v_mfma_f32_16x16x32_bf16 v[42:45], v[166:169], v[198:201], v[42:45]
	v_mfma_f32_16x16x32_bf16 v[30:33], v[158:161], v[206:209], v[30:33]
	v_mfma_f32_16x16x32_bf16 v[26:29], v[166:169], v[206:209], v[26:29]
	v_mfma_f32_16x16x32_bf16 v[14:17], v[158:161], v[214:217], v[14:17]
	v_mfma_f32_16x16x32_bf16 v[10:13], v[166:169], v[214:217], v[10:13]
	v_mfma_f32_16x16x32_bf16 v[54:57], v[170:173], v[186:189], v[54:57]
	v_mfma_f32_16x16x32_bf16 v[50:53], v[178:181], v[186:189], v[50:53]
	v_mfma_f32_16x16x32_bf16 v[38:41], v[170:173], v[194:197], v[38:41]
	v_mfma_f32_16x16x32_bf16 v[34:37], v[178:181], v[194:197], v[34:37]
	v_mfma_f32_16x16x32_bf16 v[22:25], v[170:173], v[202:205], v[22:25]
	v_mfma_f32_16x16x32_bf16 v[18:21], v[178:181], v[202:205], v[18:21]
	v_mfma_f32_16x16x32_bf16 v[6:9], v[170:173], v[210:213], v[6:9]
	v_mfma_f32_16x16x32_bf16 v[2:5], v[178:181], v[210:213], v[2:5]
	v_mfma_f32_16x16x32_bf16 v[54:57], v[174:177], v[190:193], v[54:57]
	v_mfma_f32_16x16x32_bf16 v[50:53], v[182:185], v[190:193], v[50:53]
	v_mfma_f32_16x16x32_bf16 v[38:41], v[174:177], v[198:201], v[38:41]
	v_mfma_f32_16x16x32_bf16 v[34:37], v[182:185], v[198:201], v[34:37]
	v_mfma_f32_16x16x32_bf16 v[22:25], v[174:177], v[206:209], v[22:25]
	v_mfma_f32_16x16x32_bf16 v[18:21], v[182:185], v[206:209], v[18:21]
	v_mfma_f32_16x16x32_bf16 v[6:9], v[174:177], v[214:217], v[6:9]
	v_mfma_f32_16x16x32_bf16 v[2:5], v[182:185], v[214:217], v[2:5]
	s_setprio 0
	s_barrier
	s_add_i32 s67, 0, 0x18000
	v_add_u32_e32 v138, s67, v154
	s_add_i32 s70, 0, 0x1c000
	ds_read_b128 v[148:151], v138
	ds_read_b128 v[158:161], v138 offset:1024
	ds_read_b128 v[162:165], v138 offset:2048
	ds_read_b128 v[166:169], v138 offset:3072
	v_add_u32_e32 v138, s70, v154
	ds_read_b128 v[170:173], v138
	ds_read_b128 v[174:177], v138 offset:1024
	ds_read_b128 v[178:181], v138 offset:2048
	ds_read_b128 v[182:185], v138 offset:3072
	s_add_u32 s68, s68, 0x70000
	s_addc_u32 s69, s69, 0
	s_mov_b32 m0, s52
	v_lshl_add_u64 v[226:227], s[68:69], 0, v[134:135]
	ds_read_b128 v[186:189], v157 offset:32768
	ds_read_b128 v[190:193], v157 offset:33792
	ds_read_b128 v[194:197], v157 offset:34816
	ds_read_b128 v[198:201], v157 offset:35840
	ds_read_b128 v[202:205], v157 offset:36864
	ds_read_b128 v[206:209], v157 offset:37888
	ds_read_b128 v[210:213], v157 offset:38912
	ds_read_b128 v[214:217], v157 offset:39936
	global_load_lds_dwordx4 v[226:227], off
	v_lshl_add_u64 v[226:227], s[68:69], 0, v[136:137]
	s_mov_b32 m0, s53
	s_nop 0
	global_load_lds_dwordx4 v[226:227], off
	s_waitcnt lgkmcnt(0)
	s_barrier
	s_setprio 1
	s_waitcnt lgkmcnt(0)
	v_mfma_f32_16x16x32_bf16 v[126:129], v[148:151], v[186:189], v[126:129]
	v_mfma_f32_16x16x32_bf16 v[122:125], v[162:165], v[186:189], v[122:125]
	v_mfma_f32_16x16x32_bf16 v[110:113], v[148:151], v[194:197], v[110:113]
	v_mfma_f32_16x16x32_bf16 v[106:109], v[162:165], v[194:197], v[106:109]
	v_mfma_f32_16x16x32_bf16 v[94:97], v[148:151], v[202:205], v[94:97]
	v_mfma_f32_16x16x32_bf16 v[90:93], v[162:165], v[202:205], v[90:93]
	v_mfma_f32_16x16x32_bf16 v[78:81], v[148:151], v[210:213], v[78:81]
	v_mfma_f32_16x16x32_bf16 v[74:77], v[162:165], v[210:213], v[74:77]
	v_mfma_f32_16x16x32_bf16 v[126:129], v[158:161], v[190:193], v[126:129]
	v_mfma_f32_16x16x32_bf16 v[122:125], v[166:169], v[190:193], v[122:125]
	v_mfma_f32_16x16x32_bf16 v[110:113], v[158:161], v[198:201], v[110:113]
	v_mfma_f32_16x16x32_bf16 v[106:109], v[166:169], v[198:201], v[106:109]
	v_mfma_f32_16x16x32_bf16 v[94:97], v[158:161], v[206:209], v[94:97]
	v_mfma_f32_16x16x32_bf16 v[90:93], v[166:169], v[206:209], v[90:93]
	v_mfma_f32_16x16x32_bf16 v[78:81], v[158:161], v[214:217], v[78:81]
	v_mfma_f32_16x16x32_bf16 v[74:77], v[166:169], v[214:217], v[74:77]
	v_mfma_f32_16x16x32_bf16 v[118:121], v[170:173], v[186:189], v[118:121]
	v_mfma_f32_16x16x32_bf16 v[114:117], v[178:181], v[186:189], v[114:117]
	v_mfma_f32_16x16x32_bf16 v[102:105], v[170:173], v[194:197], v[102:105]
	v_mfma_f32_16x16x32_bf16 v[98:101], v[178:181], v[194:197], v[98:101]
	v_mfma_f32_16x16x32_bf16 v[86:89], v[170:173], v[202:205], v[86:89]
	v_mfma_f32_16x16x32_bf16 v[82:85], v[178:181], v[202:205], v[82:85]
	v_mfma_f32_16x16x32_bf16 v[70:73], v[170:173], v[210:213], v[70:73]
	v_mfma_f32_16x16x32_bf16 v[66:69], v[178:181], v[210:213], v[66:69]
	v_mfma_f32_16x16x32_bf16 v[118:121], v[174:177], v[190:193], v[118:121]
	v_mfma_f32_16x16x32_bf16 v[114:117], v[182:185], v[190:193], v[114:117]
	v_mfma_f32_16x16x32_bf16 v[102:105], v[174:177], v[198:201], v[102:105]
	v_mfma_f32_16x16x32_bf16 v[98:101], v[182:185], v[198:201], v[98:101]
	v_mfma_f32_16x16x32_bf16 v[86:89], v[174:177], v[206:209], v[86:89]
	v_mfma_f32_16x16x32_bf16 v[82:85], v[182:185], v[206:209], v[82:85]
	v_mfma_f32_16x16x32_bf16 v[70:73], v[174:177], v[214:217], v[70:73]
	v_mfma_f32_16x16x32_bf16 v[66:69], v[182:185], v[214:217], v[66:69]
	s_setprio 0
	s_barrier
; #define G8_STAGE_B(bufoff, gbase) do { _Pragma("unroll") for (int _i = 0; _i < 2; ++_i) \
;         __builtin_amdgcn_global_load_lds((const unsigned*)((const char*)(gbase) + voffB[_i]), (LAS unsigned*)(lds + (bufoff) + ldsw + _i * 8192), 16, 0, 0); } while (0)
; #define G8_LDA(dst, b, h) do { _Pragma("unroll") for (int m = 0; m < 4; ++m) _Pragma("unroll") for (int k = 0; k < 2; ++k) dst[m][k] = *(const LAS bf16x8*)(lds + G8_SA(b, h) + aoff + m * 2048 + k * 1024); } while (0)
; #define G8_WAIT_V(n) asm volatile("s_waitcnt vmcnt(" #n ")" ::: "memory")
; #define G8_WAIT_L(n) asm volatile("s_waitcnt lgkmcnt(" #n ")" ::: "memory")
; template <class Sched, class Epi>
; DEVI void gemm_phase(LAS unsigned char* lds, const char* Abase, const int K, const Sched& S, const Epi& E) {
;     ...
;             if (!skip1) G8_LDA(At, 0, 1); G8_STAGE_B(G8_SB(0, 0), b2); G8_STAGE_A(G8_SA(0, 0), last, 0, k2); G8_STAGE_B(G8_SB(0, 1), b2 + hstepB);
;             G8_WAIT_V(6); G8_WAIT_L(0); G8_BAR; if (!skip1) { G8_MMA(1, 0, At, B0); G8_MMA(1, 1, At, B1); } G8_BAR; G8_SCHED;
;             G8_LDB(B0, 1, 0); G8_LDB(B1, 1, 1); G8_SCHED; G8_LDA(At, 1, 0); G8_STAGE_A(G8_SA(0, 1), last, 1, k2);
;             G8_WAIT_L(0); G8_BAR; G8_MMA(0, 0, At, B0); G8_MMA(0, 1, At, B1); G8_BAR; G8_SCHED;
;             if (!skip1) G8_LDA(At, 1, 1); G8_STAGE_B(G8_SB(1, 0), b3); G8_STAGE_A(G8_SA(1, 0), last, 0, k3); G8_STAGE_B(G8_SB(1, 1), b3 + hstepB);
;             G8_WAIT_V(6); G8_WAIT_L(0); G8_BAR; if (!skip1) { G8_MMA(1, 0, At, B0); G8_MMA(1, 1, At, B1); } G8_BAR; G8_SCHED;
; DEVI void phase_gemm_proj(const Params& p, char* smem, int l) {
;     ...
;     auto E = [=](AccRef acc, const ProjSched::Unit& u, int wr, int wc, int fr, int fq) {
;         const int col16 = u.pn * 256 + wc * 64 + fq * 16;
; #pragma unroll
;         ACC_LOOP_ROWS { const int row = u.pm * 256 + ai * 128 + wr * 64 + m * 16 + fr; const float rs = u.kv ? rkv[row] : rq[row]; const int b = row >> 12, s = row & 4095;
;             u32x4 w0, w1; PACK16_BF16(w0, w1, acc, ai, m, rs);
;             bf16_t* dst;
;             if (!u.kv) dst = qbuf + (size_t)row * 768 + col16;
;             else if (col16 < 512) dst = kfull + (((size_t)(b * 8 + (col16 >> 6))) * S_ + s) * 96 + (col16 & 63);
;             else dst = vfull + (((size_t)(b * 8 + ((col16 - 512) >> 6))) * S_ + s) * 64 + (col16 & 63);
;             *(u32x4*)dst = w0; *(u32x4*)(dst + 8) = w1; }
	s_add_i32 s67, s67, s48
	v_lshl_add_u64 v[218:219], v[218:219], 0, s[20:21]
	s_mov_b32 m0, s67
	ds_read_b128 v[186:189], v157 offset:49152
	ds_read_b128 v[190:193], v157 offset:50176
	ds_read_b128 v[194:197], v157 offset:51200
	ds_read_b128 v[198:201], v157 offset:52224
	ds_read_b128 v[202:205], v157 offset:53248
	ds_read_b128 v[206:209], v157 offset:54272
	ds_read_b128 v[210:213], v157 offset:55296
	ds_read_b128 v[214:217], v157 offset:56320
	global_load_lds_dwordx4 v[218:219], off
	v_lshl_add_u64 v[218:219], v[220:221], 0, s[20:21]
	s_add_i32 m0, s67, 0x2000
	s_add_u32 s40, s40, 0x10080
	global_load_lds_dwordx4 v[218:219], off
	v_lshl_add_u64 v[218:219], v[222:223], 0, s[20:21]
	s_mov_b32 m0, s56
	s_addc_u32 s41, s41, 0
	global_load_lds_dwordx4 v[218:219], off
	v_lshl_add_u64 v[218:219], v[224:225], 0, s[20:21]
	s_mov_b32 m0, s57
	s_add_i32 s67, s70, s48
	global_load_lds_dwordx4 v[218:219], off
	v_lshl_add_u64 v[218:219], s[40:41], 0, v[130:131]
	s_mov_b32 m0, s67
	s_nop 0
	global_load_lds_dwordx4 v[218:219], off
	v_lshl_add_u64 v[218:219], s[40:41], 0, v[132:133]
	s_add_i32 m0, s67, 0x2000
	s_nop 0
	global_load_lds_dwordx4 v[218:219], off
	s_waitcnt vmcnt(6)
	s_waitcnt lgkmcnt(0)
	s_barrier
	s_setprio 1
	s_waitcnt lgkmcnt(0)
	v_mfma_f32_16x16x32_bf16 v[62:65], v[148:151], v[186:189], v[62:65]
	v_mfma_f32_16x16x32_bf16 v[58:61], v[162:165], v[186:189], v[58:61]
	v_mfma_f32_16x16x32_bf16 v[46:49], v[148:151], v[194:197], v[46:49]
	v_mfma_f32_16x16x32_bf16 v[42:45], v[162:165], v[194:197], v[42:45]
	v_mfma_f32_16x16x32_bf16 v[30:33], v[148:151], v[202:205], v[30:33]
	v_mfma_f32_16x16x32_bf16 v[26:29], v[162:165], v[202:205], v[26:29]
	v_mfma_f32_16x16x32_bf16 v[14:17], v[148:151], v[210:213], v[14:17]
	v_mfma_f32_16x16x32_bf16 v[10:13], v[162:165], v[210:213], v[10:13]
	v_mfma_f32_16x16x32_bf16 v[62:65], v[158:161], v[190:193], v[62:65]
	v_mfma_f32_16x16x32_bf16 v[58:61], v[166:169], v[190:193], v[58:61]
	v_mfma_f32_16x16x32_bf16 v[46:49], v[158:161], v[198:201], v[46:49]
	v_mfma_f32_16x16x32_bf16 v[42:45], v[166:169], v[198:201], v[42:45]
	v_mfma_f32_16x16x32_bf16 v[30:33], v[158:161], v[206:209], v[30:33]
	v_mfma_f32_16x16x32_bf16 v[26:29], v[166:169], v[206:209], v[26:29]
	v_mfma_f32_16x16x32_bf16 v[14:17], v[158:161], v[214:217], v[14:17]
	v_mfma_f32_16x16x32_bf16 v[10:13], v[166:169], v[214:217], v[10:13]
	v_mfma_f32_16x16x32_bf16 v[54:57], v[170:173], v[186:189], v[54:57]
	v_mfma_f32_16x16x32_bf16 v[50:53], v[178:181], v[186:189], v[50:53]
	v_mfma_f32_16x16x32_bf16 v[38:41], v[170:173], v[194:197], v[38:41]
	v_mfma_f32_16x16x32_bf16 v[34:37], v[178:181], v[194:197], v[34:37]
	v_mfma_f32_16x16x32_bf16 v[22:25], v[170:173], v[202:205], v[22:25]
	v_mfma_f32_16x16x32_bf16 v[18:21], v[178:181], v[202:205], v[18:21]
	v_mfma_f32_16x16x32_bf16 v[6:9], v[170:173], v[210:213], v[6:9]
	v_mfma_f32_16x16x32_bf16 v[2:5], v[178:181], v[210:213], v[2:5]
	v_mfma_f32_16x16x32_bf16 v[54:57], v[174:177], v[190:193], v[54:57]
	v_mfma_f32_16x16x32_bf16 v[50:53], v[182:185], v[190:193], v[50:53]
	v_mfma_f32_16x16x32_bf16 v[38:41], v[174:177], v[198:201], v[38:41]
	v_mfma_f32_16x16x32_bf16 v[34:37], v[182:185], v[198:201], v[34:37]
	v_mfma_f32_16x16x32_bf16 v[22:25], v[174:177], v[206:209], v[22:25]
	v_mfma_f32_16x16x32_bf16 v[18:21], v[182:185], v[206:209], v[18:21]
	v_mfma_f32_16x16x32_bf16 v[6:9], v[174:177], v[214:217], v[6:9]
	v_mfma_f32_16x16x32_bf16 v[2:5], v[182:185], v[214:217], v[2:5]
	s_setprio 0
	s_barrier
	s_add_u32 s38, s38, 0x100
	s_addc_u32 s39, s39, 0
	s_cmp_ge_u32 s66, s5
	s_mov_b32 s40, s66
	s_cbranch_scc0 .LBB0_2037
	v_mov_b32_e32 v138, v152
	v_mov_b32_e32 v144, v153
	s_lshl_b32 s4, s4, 8
	s_or_b32 s23, s4, s58
	v_add_u32_e32 v138, s55, v138
	s_lshl_b32 s2, s2, 8
	v_add_u32_e32 v146, s2, v138
	s_and_b64 s[4:5], s[36:37], exec
	v_ashrrev_i32_e32 v147, 31, v146
	s_cselect_b32 s35, s9, s11
	s_cselect_b32 s34, s8, s10
	v_lshl_add_u64 v[148:149], v[146:147], 2, s[34:35]
	global_load_dword v138, v[148:149], off
	v_lshlrev_b32_e32 v145, 4, v144
	v_add_u32_e32 v144, s23, v145
	v_and_b32_e32 v159, 48, v145
	v_add_u32_e32 v145, 0xfffffe00, v144
	s_mov_b64 s[6:7], -1
	s_and_b64 vcc, exec, s[30:31]
	v_cmp_lt_i32_e64 s[4:5], s59, v144
	v_ashrrev_i32_e32 v147, 6, v144
	v_lshrrev_b32_e32 v158, 6, v145
	s_waitcnt vmcnt(0)
	v_pk_mul_f32 v[120:121], v[120:121], v[138:139] op_sel_hi:[1,0]
	v_pk_mul_f32 v[118:119], v[118:119], v[138:139] op_sel_hi:[1,0]
	v_pk_mul_f32 v[128:129], v[128:129], v[138:139] op_sel_hi:[1,0]
	v_pk_mul_f32 v[126:127], v[126:127], v[138:139] op_sel_hi:[1,0]
	v_pk_mul_f32 v[124:125], v[124:125], v[138:139] op_sel_hi:[1,0]
	v_pk_mul_f32 v[122:123], v[122:123], v[138:139] op_sel_hi:[1,0]
	v_pk_mul_f32 v[160:161], v[116:117], v[138:139] op_sel_hi:[1,0]
	v_pk_mul_f32 v[162:163], v[114:115], v[138:139] op_sel_hi:[1,0]
	v_cvt_pk_bf16_f32 v114, v126, v127
	v_cvt_pk_bf16_f32 v115, v128, v129
	v_cvt_pk_bf16_f32 v116, v122, v123
	v_cvt_pk_bf16_f32 v117, v124, v125
	v_cvt_pk_bf16_f32 v118, v118, v119
	v_cvt_pk_bf16_f32 v119, v120, v121
	s_nop 0
	v_cvt_pk_bf16_f32 v120, v162, v163
	v_cvt_pk_bf16_f32 v121, v160, v161
	s_cbranch_vccz .LBB0_2044
	v_ashrrev_i32_e32 v123, 9, v146
	v_and_b32_e32 v122, 0xfff, v146
	v_and_b32_e32 v123, -8, v123
	s_and_saveexec_b64 s[6:7], s[4:5]
	s_xor_b64 s[6:7], exec, s[6:7]
	v_add_u32_e32 v124, v123, v158
	v_ashrrev_i32_e32 v125, 31, v124
	v_lshlrev_b64 v[124:125], 19, v[124:125]
	v_lshl_add_u64 v[124:125], s[18:19], 0, v[124:125]
	v_lshlrev_b32_e32 v138, 7, v122
	v_lshl_add_u64 v[122:123], v[124:125], 0, v[138:139]
	v_lshlrev_b32_e32 v138, 1, v159
	v_lshl_add_u64 v[150:151], v[122:123], 0, v[138:139]
	s_andn2_saveexec_b64 s[6:7], s[6:7]
	v_add_u32_e32 v124, v123, v147
	v_ashrrev_i32_e32 v125, 31, v124
	v_lshlrev_b64 v[124:125], 12, v[124:125]
	v_or_b32_e32 v124, v124, v122
	v_mov_b64_e32 v[122:123], s[14:15]
	v_mad_u64_u32 v[122:123], s[36:37], v124, s62, v[122:123]
	v_mad_i32_i24 v123, v125, s62, v123
	v_lshlrev_b32_e32 v138, 1, v159
	v_lshl_add_u64 v[150:151], v[122:123], 0, v[138:139]
	s_or_b64 exec, exec, s[6:7]
	s_mov_b64 s[6:7], 0

; DEVI void pv_both(f32x16& o0, f32x16& o1, int vb, bf16x8 pa0, bf16x8 pa1, bf16x8 pa2, bf16x8 pa3) {
;     const s16x4 a0 = tr_read<v_rd_off(0, 0, 0)>(vb), b0 = tr_read<v_rd_off(0, 0, 1)>(vb), a1 = tr_read<v_rd_off(0, 1, 0)>(vb), b1 = tr_read<v_rd_off(0, 1, 1)>(vb);
;     const s16x4 a2 = tr_read<v_rd_off(0, 2, 0)>(vb), b2 = tr_read<v_rd_off(0, 2, 1)>(vb), a3 = tr_read<v_rd_off(0, 3, 0)>(vb), b3 = tr_read<v_rd_off(0, 3, 1)>(vb);
;     const s16x4 c0 = tr_read<v_rd_off(1, 0, 0)>(vb), d0 = tr_read<v_rd_off(1, 0, 1)>(vb), c1 = tr_read<v_rd_off(1, 1, 0)>(vb), d1 = tr_read<v_rd_off(1, 1, 1)>(vb);
;     const s16x4 c2 = tr_read<v_rd_off(1, 2, 0)>(vb), d2 = tr_read<v_rd_off(1, 2, 1)>(vb), c3 = tr_read<v_rd_off(1, 3, 0)>(vb), d3 = tr_read<v_rd_off(1, 3, 1)>(vb);
;     asm volatile("s_waitcnt lgkmcnt(8)" ::: "memory"); SBAR();
;     ...
;     o0 = __builtin_amdgcn_mfma_f32_32x32x16_bf16(pa0, PK(a0, b0), o0, 0, 0, 0);
;     o0 = __builtin_amdgcn_mfma_f32_32x32x16_bf16(pa1, PK(a1, b1), o0, 0, 0, 0);
;     o0 = __builtin_amdgcn_mfma_f32_32x32x16_bf16(pa2, PK(a2, b2), o0, 0, 0, 0);
;     o0 = __builtin_amdgcn_mfma_f32_32x32x16_bf16(pa3, PK(a3, b3), o0, 0, 0, 0);
;     asm volatile("s_waitcnt lgkmcnt(0)" ::: "memory"); SBAR();
;     o1 = __builtin_amdgcn_mfma_f32_32x32x16_bf16(pa0, PK(c0, d0), o1, 0, 0, 0);
;     o1 = __builtin_amdgcn_mfma_f32_32x32x16_bf16(pa1, PK(c1, d1), o1, 0, 0, 0);
;     o1 = __builtin_amdgcn_mfma_f32_32x32x16_bf16(pa2, PK(c2, d2), o1, 0, 0, 0);
;     o1 = __builtin_amdgcn_mfma_f32_32x32x16_bf16(pa3, PK(c3, d3), o1, 0, 0, 0);
;     ...
; }
; template <bool FIRST> DEVI bool partialSM(f32x16& p0, f32x16& p1, float& m_reg, float& alpha) {
;     float pmax = p0[0];
; #pragma unroll
;     for (int r = 1; r < 16; ++r) pmax = fmaxf(pmax, p0[r]);
; #pragma unroll
;     for (int r = 0; r < 16; ++r) pmax = fmaxf(pmax, p1[r]);
;     { auto rr = __builtin_amdgcn_permlane32_swap(__float_as_uint(pmax), __float_as_uint(pmax), false, false);
;       pmax = fmaxf(__uint_as_float(rr[0]), __uint_as_float(rr[1])); }
;     if (FIRST) { m_reg = pmax; alpha = 1.f;
; #pragma unroll
;         for (int r = 0; r < 16; ++r) { p0[r] = __builtin_amdgcn_exp2f(p0[r] - pmax); p1[r] = p1[r] - pmax; }
;         return false;
;     } else if (__builtin_expect(__all(pmax <= ATT_THR), 1)) { alpha = 1.f;
; #pragma unroll
;         for (int r = 0; r < 16; ++r) p0[r] = __builtin_amdgcn_exp2f(p0[r]);
.LBB0_2260:
	s_mul_i32 s6, s71, 0x6000
	s_add_i32 s6, s6, 0
	v_add_u32_e32 v86, s6, v129
	ds_read_b128 v[82:85], v86 offset:12288
	ds_read_b128 v[124:127], v86 offset:18432
	v_add_u32_e32 v174, s6, v205
	v_exp_f32_e32 v66, v66
	v_exp_f32_e32 v67, v67
	s_waitcnt lgkmcnt(1)
	v_mfma_f32_32x32x16_bf16 v[98:113], v[82:85], v[150:153], v[34:49]
	v_add_u32_e32 v82, s6, v184
	v_add_u32_e32 v83, s6, v185
	ds_read_b128 v[210:213], v82 offset:12288
	ds_read_b128 v[214:217], v82 offset:18432
	ds_read_b128 v[218:221], v83 offset:12288
	ds_read_b128 v[222:225], v83 offset:18432
	v_exp_f32_e32 v68, v68
	v_exp_f32_e32 v69, v69
	v_exp_f32_e32 v70, v70
	v_exp_f32_e32 v71, v71
	s_waitcnt lgkmcnt(4)
	v_mfma_f32_32x32x16_bf16 v[82:97], v[124:127], v[150:153], v[34:49]
	ds_read_b128 v[124:127], v174 offset:12288
	ds_read_b128 v[226:229], v174 offset:18432
	v_exp_f32_e32 v72, v72
	v_exp_f32_e32 v73, v73
	v_exp_f32_e32 v74, v74
	v_exp_f32_e32 v75, v75
	v_exp_f32_e32 v76, v76
	v_exp_f32_e32 v77, v77
	s_waitcnt lgkmcnt(5)
	v_mfma_f32_32x32x16_bf16 v[98:113], v[210:213], v[138:141], v[98:113]
	v_add_u32_e32 v174, s6, v206
	v_exp_f32_e32 v78, v78
	v_exp_f32_e32 v79, v79
	ds_read_b128 v[230:233], v174 offset:12288
	ds_read_b128 v[234:237], v174 offset:18432
	v_exp_f32_e32 v80, v80
	v_exp_f32_e32 v81, v81
	v_add_u32_e32 v174, s6, v207
	s_waitcnt lgkmcnt(6)
	v_mfma_f32_32x32x16_bf16 v[82:97], v[214:217], v[138:141], v[82:97]
	v_add_f32_e64 v214, v50, v66
	v_add_f32_e64 v215, v51, v67
	v_add_f32_e64 v216, v52, v68
	v_add_f32_e64 v217, v53, v69
	v_lshl_add_u32 v203, s71, 14, v115
	v_pk_add_f32 v[214:215], v[216:217], v[214:215]
	v_pk_add_f32 v[216:217], v[54:55], v[70:71]
	ds_read_b128 v[210:213], v174 offset:12288
	ds_read_b128 v[238:241], v174 offset:18432
	v_pk_add_f32 v[214:215], v[216:217], v[214:215]
	s_waitcnt lgkmcnt(7)
	v_mfma_f32_32x32x16_bf16 v[98:113], v[218:221], v[134:137], v[98:113]
	v_add_f32_e64 v216, v56, v72
	v_add_f32_e64 v217, v57, v73
	v_cvt_pk_bf16_f32 v50, v50, v51
	v_cvt_pk_bf16_f32 v51, v52, v53
	v_cvt_pk_bf16_f32 v52, v54, v55
	v_cvt_pk_bf16_f32 v53, v56, v57
	v_cvt_pk_bf16_f32 v54, v58, v59
	v_add_f32_e64 v214, v216, v214
	v_add_f32_e64 v215, v217, v215
	s_waitcnt lgkmcnt(6)
	v_mfma_f32_32x32x16_bf16 v[82:97], v[222:225], v[134:137], v[82:97]
	v_add_f32_e64 v216, v58, v74
	v_add_f32_e64 v217, v59, v75
	v_cvt_pk_bf16_f32 v55, v60, v61
	v_cvt_pk_bf16_f32 v56, v62, v63
	v_cvt_pk_bf16_f32 v57, v64, v65
	v_cvt_pk_bf16_f32 v58, v66, v67
	v_cvt_pk_bf16_f32 v59, v68, v69
	v_add_f32_e64 v214, v216, v214
	v_add_f32_e64 v215, v217, v215
	s_waitcnt lgkmcnt(5)
	v_mfma_f32_32x32x16_bf16 v[98:113], v[124:127], v[130:133], v[98:113]
	v_add_f32_e64 v216, v60, v76
	v_add_f32_e64 v217, v61, v77
	v_add_f32_e64 v126, v62, v78
	v_add_f32_e64 v127, v63, v79
	v_add_f32_e64 v124, v216, v214
	v_add_f32_e64 v125, v217, v215
	v_cvt_pk_bf16_f32 v60, v70, v71
	v_cvt_pk_bf16_f32 v61, v72, v73
	v_cvt_pk_bf16_f32 v62, v74, v75
	v_cvt_pk_bf16_f32 v63, v76, v77
	s_waitcnt lgkmcnt(4)
	v_mfma_f32_32x32x16_bf16 v[82:97], v[226:229], v[130:133], v[82:97]
	v_add_f32_e64 v124, v126, v124
	v_add_f32_e64 v125, v127, v125
	v_add_f32_e64 v126, v64, v80
	v_add_f32_e64 v127, v65, v81
	v_cvt_pk_bf16_f32 v64, v78, v79
	v_cvt_pk_bf16_f32 v65, v80, v81
	ds_read_b64_tr_b16 v[66:67], v203 offset:0
	ds_read_b64_tr_b16 v[68:69], v203 offset:0x400
	ds_read_b64_tr_b16 v[70:71], v203 offset:0x800
	s_waitcnt lgkmcnt(6)
	v_mfma_f32_32x32x16_bf16 v[98:113], v[230:233], v[146:149], v[98:113]
	ds_read_b64_tr_b16 v[72:73], v203 offset:0xc00
	ds_read_b64_tr_b16 v[74:75], v203 offset:0x1000
	ds_read_b64_tr_b16 v[76:77], v203 offset:0x1400
	ds_read_b64_tr_b16 v[78:79], v203 offset:0x1800
	ds_read_b64_tr_b16 v[80:81], v203 offset:0x1c00
	v_add_f32_e64 v124, v126, v124
	v_add_f32_e64 v125, v127, v125
	s_waitcnt lgkmcnt(10)
	v_mfma_f32_32x32x16_bf16 v[82:97], v[234:237], v[146:149], v[82:97]
	v_pk_add_f32 v[124:125], v[124:125], v[124:125] op_sel:[0,1] op_sel_hi:[1,0]
	s_nop 0
	v_mov_b32_e32 v125, v124
	s_nop 1
	v_permlane32_swap_b32_e32 v124, v125
	s_waitcnt lgkmcnt(9)
	v_mfma_f32_32x32x16_bf16 v[98:113], v[210:213], v[142:145], v[98:113]
	ds_read_b64_tr_b16 v[210:211], v203 offset:0x200
	ds_read_b64_tr_b16 v[212:213], v203 offset:0x600
	ds_read_b64_tr_b16 v[214:215], v203 offset:0xa00
	ds_read_b64_tr_b16 v[216:217], v203 offset:0xe00
	ds_read_b64_tr_b16 v[218:219], v203 offset:0x1200
	ds_read_b64_tr_b16 v[220:221], v203 offset:0x1600
	ds_read_b64_tr_b16 v[222:223], v203 offset:0x1a00
	s_waitcnt lgkmcnt(15)
	v_mfma_f32_32x32x16_bf16 v[82:97], v[238:241], v[142:145], v[82:97]
	ds_read_b64_tr_b16 v[224:225], v203 offset:0x1e00
	s_waitcnt lgkmcnt(14)
	v_mfma_f32_32x32x16_bf16 v[18:33], v[50:53], v[66:69], v[18:33]
	s_waitcnt lgkmcnt(12)
	v_mfma_f32_32x32x16_bf16 v[18:33], v[54:57], v[70:73], v[18:33]
	s_waitcnt lgkmcnt(10)
	v_mfma_f32_32x32x16_bf16 v[18:33], v[58:61], v[74:77], v[18:33]
	s_waitcnt lgkmcnt(8)
	v_mfma_f32_32x32x16_bf16 v[18:33], v[62:65], v[78:81], v[18:33]
	s_waitcnt lgkmcnt(6)
	v_mfma_f32_32x32x16_bf16 v[2:17], v[50:53], v[210:213], v[2:17]
	s_nop 4
	v_max_f32_e32 v249, v99, v99
	v_max_f32_e32 v250, v98, v98
	v_max_f32_e32 v249, v250, v249
	v_max3_f32 v249, v249, v100, v101
	v_max3_f32 v249, v249, v102, v103
	v_max3_f32 v251, v249, v104, v105
	v_max3_f32 v251, v251, v106, v107
	s_waitcnt lgkmcnt(4)
	v_exp_f32_e32 v50, v98
	v_exp_f32_e32 v51, v99
	v_exp_f32_e32 v52, v100
	v_exp_f32_e32 v53, v101
	v_mov_b64_e32 v[66:67], v[82:83]
	v_mov_b64_e32 v[68:69], v[84:85]
	v_mfma_f32_32x32x16_bf16 v[2:17], v[54:57], v[214:217], v[2:17]
	v_max3_f32 v251, v251, v108, v109
	v_max3_f32 v251, v251, v110, v111
	v_max3_f32 v251, v251, v112, v113
	v_max3_f32 v251, v251, v82, v83
	v_max3_f32 v251, v251, v84, v85
	v_max3_f32 v251, v251, v86, v87
	v_max3_f32 v251, v251, v88, v89
	s_waitcnt lgkmcnt(2)
	v_exp_f32_e32 v54, v102
	v_exp_f32_e32 v55, v103
	v_exp_f32_e32 v56, v104
	v_exp_f32_e32 v57, v105
	v_mov_b64_e32 v[70:71], v[86:87]
	v_mov_b64_e32 v[72:73], v[88:89]
	v_mfma_f32_32x32x16_bf16 v[2:17], v[58:61], v[218:221], v[2:17]
	v_max3_f32 v251, v251, v90, v91
	v_max3_f32 v251, v251, v92, v93
	v_max3_f32 v251, v251, v94, v95
	v_max3_f32 v251, v251, v96, v97
	v_mov_b32_e32 v252, v251
	s_nop 1
	v_permlane32_swap_b32_e32 v251, v252
	s_waitcnt lgkmcnt(0)
	v_exp_f32_e32 v58, v106
	v_exp_f32_e32 v59, v107
	v_exp_f32_e32 v60, v108
	v_exp_f32_e32 v61, v109
	v_mov_b64_e32 v[74:75], v[90:91]
	v_mov_b64_e32 v[76:77], v[92:93]
	v_mfma_f32_32x32x16_bf16 v[2:17], v[62:65], v[222:225], v[2:17]
	v_exp_f32_e32 v62, v110
	v_exp_f32_e32 v63, v111
	v_exp_f32_e32 v64, v112
	v_exp_f32_e32 v65, v113
	v_mov_b64_e32 v[78:79], v[94:95]
	v_mov_b64_e32 v[80:81], v[96:97]
	v_max_f32_e32 v252, v252, v252
	v_max_f32_e32 v251, v251, v251
	v_max_f32_e32 v126, v251, v252
	v_cmp_ge_f32_e32 vcc, s80, v126
	s_cmp_lg_u64 vcc, exec
	s_cselect_b64 s[6:7], -1, 0
	s_cbranch_scc1 .LBB0_2269
	v_mov_b32_e32 v209, 1.0
	v_mov_b32_e32 v210, v204
	s_branch .LBB0_2263

; #define PK4(P, BASE, OUT) do { u32x4 w = {cvt_pk_bf16(P[BASE + 0], P[BASE + 1]), cvt_pk_bf16(P[BASE + 2], P[BASE + 3]), cvt_pk_bf16(P[BASE + 4], P[BASE + 5]), cvt_pk_bf16(P[BASE + 6], P[BASE + 7])}; \
;     OUT = *reinterpret_cast<bf16x8*>(&w); } while (0)
; DEVI void finishSM(f32x16& p0, f32x16& p1, float alpha, float& l_reg, bf16x8& pa0, bf16x8& pa1, bf16x8& pa2, bf16x8& pa3) {
; #pragma unroll
;     for (int r = 0; r < 16; ++r) p1[r] = __builtin_amdgcn_exp2f(p1[r]);
;     f32x2 s2 = (f32x2){p0[0], p0[1]} + (f32x2){p1[0], p1[1]};
; #pragma unroll
;     for (int r = 2; r < 16; r += 2) s2 += (f32x2){p0[r], p0[r + 1]} + (f32x2){p1[r], p1[r + 1]};
;     float ps = s2[0] + s2[1];
;     { auto rr = __builtin_amdgcn_permlane32_swap(__float_as_uint(ps), __float_as_uint(ps), false, false);
;       ps = __uint_as_float(rr[0]) + __uint_as_float(rr[1]); }
;     l_reg = l_reg * alpha + ps;
;     ...
;     PK4(p0, 0, pa0); PK4(p0, 8, pa1); PK4(p1, 0, pa2); PK4(p1, 8, pa3);
;     ...
; }
; DEVI void qkt(f32x16& p0, f32x16& p1, const char* Kb, const bf16x8 (&qr)[6], int r32, int hi, const f32x16& cinit) {
; #pragma unroll
;     for (int d0 = 0; d0 < 6; ++d0) { const int cb = (d0 * 16 + hi * 8) * 2;
;         const bf16x8 k0 = *(const bf16x8*)(Kb + KSWZ(r32, cb)), k1 = *(const bf16x8*)(Kb + KSWZ(32 + r32, cb));
;         p0 = __builtin_amdgcn_mfma_f32_32x32x16_bf16(k0, qr[d0], d0 == 0 ? cinit : p0, 0, 0, 0);
;         p1 = __builtin_amdgcn_mfma_f32_32x32x16_bf16(k1, qr[d0], d0 == 0 ? cinit : p1, 0, 0, 0); }
; DEVI void attn_unit8(const Params& p, char* smem, int unit, int l, int& cvs  , CvRun& crun) {
;     ...
;         if (T + 2 < NTILE) B_DMA(T + 2, s2);
;         qkt(pA0, pA1, K_lds + s1 * 24576, qr, r32, hi, cinit);
;         finishSM(pB0, pB1, alB, l_reg, pa0, pa1, pa2, pa3);
;         pv_both(o[0], o[1], vb + 8192, pa0, pa1, pa2, pa3);
.LBB0_2266:
	s_mul_i32 s6, s61, 0x6000
	s_add_i32 s6, s96, s6
	v_lshl_add_u64 v[82:83], v[118:119], 0, s[12:13]
	s_mov_b32 m0, s6
	s_barrier
	global_load_lds_dwordx4 v[82:83], off
	v_lshl_add_u64 v[82:83], v[120:121], 0, s[12:13]
	s_add_i32 m0, s6, 0x2000
	v_exp_f32_e32 v66, v66
	global_load_lds_dwordx4 v[82:83], off
	s_add_i32 m0, s6, 0x4000
	s_lshl_b32 s6, s61, 14
	v_lshl_add_u64 v[82:83], v[122:123], 0, s[12:13]
	s_add_i32 s6, s97, s6
	global_load_lds_dwordx4 v[82:83], off
	s_mov_b32 m0, s6
	v_lshl_add_u64 v[82:83], v[116:117], 0, s[40:41]
	global_load_lds_dwordx4 v[116:117], off
	s_add_i32 m0, s6, 0x2000
	s_mul_i32 s6, s2, 0x6000
	global_load_lds_dwordx4 v[82:83], off
	s_add_i32 s6, s6, 0
	v_add_u32_e32 v86, s6, v129
	ds_read_b128 v[82:85], v86
	ds_read_b128 v[212:215], v86 offset:6144
	s_waitcnt lgkmcnt(1)
	v_mfma_f32_32x32x16_bf16 v[98:113], v[82:85], v[150:153], v[34:49]
	v_add_u32_e32 v126, s6, v184
	v_exp_f32_e32 v67, v67
	v_exp_f32_e32 v68, v68
	v_exp_f32_e32 v69, v69
	v_exp_f32_e32 v70, v70
	v_exp_f32_e32 v71, v71
	v_exp_f32_e32 v72, v72
	s_waitcnt lgkmcnt(0)
	v_mfma_f32_32x32x16_bf16 v[82:97], v[212:215], v[150:153], v[34:49]
	ds_read_b128 v[212:215], v126
	ds_read_b128 v[216:219], v126 offset:6144
	v_add_u32_e32 v126, s6, v185
	v_exp_f32_e32 v73, v73
	v_exp_f32_e32 v74, v74
	v_exp_f32_e32 v75, v75
	v_exp_f32_e32 v76, v76
	v_exp_f32_e32 v77, v77
	s_waitcnt lgkmcnt(1)
	v_mfma_f32_32x32x16_bf16 v[98:113], v[212:215], v[138:141], v[98:113]
	v_exp_f32_e32 v78, v78
	v_exp_f32_e32 v79, v79
	v_exp_f32_e32 v80, v80
	v_exp_f32_e32 v81, v81
	v_add_u32_e32 v174, 0x2000, v203
	s_waitcnt lgkmcnt(0)
	v_mfma_f32_32x32x16_bf16 v[82:97], v[216:219], v[138:141], v[82:97]
	ds_read_b128 v[212:215], v126
	ds_read_b128 v[216:219], v126 offset:6144
	v_add_u32_e32 v126, s6, v205
	s_waitcnt lgkmcnt(1)
	v_mfma_f32_32x32x16_bf16 v[98:113], v[212:215], v[134:137], v[98:113]
	ds_read_b128 v[212:215], v126
	ds_read_b128 v[220:223], v126 offset:6144
	v_add_u32_e32 v126, s6, v206
	s_waitcnt lgkmcnt(2)
	v_mfma_f32_32x32x16_bf16 v[82:97], v[216:219], v[134:137], v[82:97]
	ds_read_b128 v[216:219], v126
	ds_read_b128 v[224:227], v126 offset:6144
	v_add_u32_e32 v126, s6, v207
	ds_read_b128 v[228:231], v126
	ds_read_b128 v[232:235], v126 offset:6144
	v_pk_add_f32 v[126:127], v[50:51], v[66:67]
	v_cvt_pk_bf16_f32 v50, v50, v51
	v_cvt_pk_bf16_f32 v51, v52, v53
	s_waitcnt lgkmcnt(5)
	v_mfma_f32_32x32x16_bf16 v[98:113], v[212:215], v[130:133], v[98:113]
	v_add_f32_e64 v212, v52, v68
	v_add_f32_e64 v213, v53, v69
	v_cvt_pk_bf16_f32 v52, v54, v55
	v_cvt_pk_bf16_f32 v53, v56, v57
	v_add_f32_e64 v126, v212, v126
	v_add_f32_e64 v127, v213, v127
	v_add_f32_e64 v212, v54, v70
	v_add_f32_e64 v213, v55, v71
	v_cvt_pk_bf16_f32 v54, v58, v59
	s_waitcnt lgkmcnt(4)
	v_mfma_f32_32x32x16_bf16 v[82:97], v[220:223], v[130:133], v[82:97]
	v_add_f32_e64 v126, v212, v126
	v_add_f32_e64 v127, v213, v127
	v_add_f32_e64 v212, v56, v72
	v_add_f32_e64 v213, v57, v73
	v_cvt_pk_bf16_f32 v55, v60, v61
	v_cvt_pk_bf16_f32 v56, v62, v63
	v_cvt_pk_bf16_f32 v57, v64, v65
	v_add_f32_e64 v126, v212, v126
	v_add_f32_e64 v127, v213, v127
	v_pk_add_f32 v[212:213], v[58:59], v[74:75]
	v_cvt_pk_bf16_f32 v58, v66, v67
	v_cvt_pk_bf16_f32 v59, v68, v69
	s_waitcnt lgkmcnt(3)
	v_mfma_f32_32x32x16_bf16 v[98:113], v[216:219], v[146:149], v[98:113]
	v_add_f32_e64 v126, v212, v126
	v_add_f32_e64 v127, v213, v127
	v_add_f32_e64 v212, v60, v76
	v_add_f32_e64 v213, v61, v77
	v_cvt_pk_bf16_f32 v60, v70, v71
	v_cvt_pk_bf16_f32 v61, v72, v73
	v_add_f32_e64 v126, v212, v126
	v_add_f32_e64 v127, v213, v127
	v_pk_add_f32 v[212:213], v[62:63], v[78:79]
	v_cvt_pk_bf16_f32 v62, v74, v75
	v_cvt_pk_bf16_f32 v63, v76, v77
	s_waitcnt lgkmcnt(2)
; DEVI void pv_both(f32x16& o0, f32x16& o1, int vb, bf16x8 pa0, bf16x8 pa1, bf16x8 pa2, bf16x8 pa3) {
;     const s16x4 a0 = tr_read<v_rd_off(0, 0, 0)>(vb), b0 = tr_read<v_rd_off(0, 0, 1)>(vb), a1 = tr_read<v_rd_off(0, 1, 0)>(vb), b1 = tr_read<v_rd_off(0, 1, 1)>(vb);
;     const s16x4 a2 = tr_read<v_rd_off(0, 2, 0)>(vb), b2 = tr_read<v_rd_off(0, 2, 1)>(vb), a3 = tr_read<v_rd_off(0, 3, 0)>(vb), b3 = tr_read<v_rd_off(0, 3, 1)>(vb);
;     const s16x4 c0 = tr_read<v_rd_off(1, 0, 0)>(vb), d0 = tr_read<v_rd_off(1, 0, 1)>(vb), c1 = tr_read<v_rd_off(1, 1, 0)>(vb), d1 = tr_read<v_rd_off(1, 1, 1)>(vb);
;     const s16x4 c2 = tr_read<v_rd_off(1, 2, 0)>(vb), d2 = tr_read<v_rd_off(1, 2, 1)>(vb), c3 = tr_read<v_rd_off(1, 3, 0)>(vb), d3 = tr_read<v_rd_off(1, 3, 1)>(vb);
;     asm volatile("s_waitcnt lgkmcnt(8)" ::: "memory"); SBAR();
;     ...
;     o0 = __builtin_amdgcn_mfma_f32_32x32x16_bf16(pa0, PK(a0, b0), o0, 0, 0, 0);
;     o0 = __builtin_amdgcn_mfma_f32_32x32x16_bf16(pa1, PK(a1, b1), o0, 0, 0, 0);
;     o0 = __builtin_amdgcn_mfma_f32_32x32x16_bf16(pa2, PK(a2, b2), o0, 0, 0, 0);
;     o0 = __builtin_amdgcn_mfma_f32_32x32x16_bf16(pa3, PK(a3, b3), o0, 0, 0, 0);
;     asm volatile("s_waitcnt lgkmcnt(0)" ::: "memory"); SBAR();
;     o1 = __builtin_amdgcn_mfma_f32_32x32x16_bf16(pa0, PK(c0, d0), o1, 0, 0, 0);
;     o1 = __builtin_amdgcn_mfma_f32_32x32x16_bf16(pa1, PK(c1, d1), o1, 0, 0, 0);
;     o1 = __builtin_amdgcn_mfma_f32_32x32x16_bf16(pa2, PK(c2, d2), o1, 0, 0, 0);
;     o1 = __builtin_amdgcn_mfma_f32_32x32x16_bf16(pa3, PK(c3, d3), o1, 0, 0, 0);
;     ...
; }
; template <bool FIRST> DEVI bool partialSM(f32x16& p0, f32x16& p1, float& m_reg, float& alpha) {
;     float pmax = p0[0];
; #pragma unroll
;     for (int r = 1; r < 16; ++r) pmax = fmaxf(pmax, p0[r]);
; #pragma unroll
;     for (int r = 0; r < 16; ++r) pmax = fmaxf(pmax, p1[r]);
;     { auto rr = __builtin_amdgcn_permlane32_swap(__float_as_uint(pmax), __float_as_uint(pmax), false, false);
;       pmax = fmaxf(__uint_as_float(rr[0]), __uint_as_float(rr[1])); }
;     if (FIRST) { m_reg = pmax; alpha = 1.f;
; #pragma unroll
;         for (int r = 0; r < 16; ++r) { p0[r] = __builtin_amdgcn_exp2f(p0[r] - pmax); p1[r] = p1[r] - pmax; }
;         return false;
;     } else if (__builtin_expect(__all(pmax <= ATT_THR), 1)) { alpha = 1.f;
; #pragma unroll
;         for (int r = 0; r < 16; ++r) p0[r] = __builtin_amdgcn_exp2f(p0[r]);
	v_mfma_f32_32x32x16_bf16 v[82:97], v[224:227], v[146:149], v[82:97]
	v_add_f32_e64 v126, v212, v126
	v_add_f32_e64 v127, v213, v127
	v_add_f32_e64 v212, v64, v80
	v_add_f32_e64 v213, v65, v81
	v_cvt_pk_bf16_f32 v64, v78, v79
	v_cvt_pk_bf16_f32 v65, v80, v81
	ds_read_b64_tr_b16 v[66:67], v174 offset:0
	ds_read_b64_tr_b16 v[68:69], v174 offset:0x400
	ds_read_b64_tr_b16 v[70:71], v174 offset:0x800
	ds_read_b64_tr_b16 v[72:73], v174 offset:0xc00
	ds_read_b64_tr_b16 v[74:75], v174 offset:0x1000
	ds_read_b64_tr_b16 v[76:77], v174 offset:0x1400
	ds_read_b64_tr_b16 v[78:79], v174 offset:0x1800
	ds_read_b64_tr_b16 v[80:81], v174 offset:0x1c00
	v_add_f32_e64 v126, v212, v126
	v_add_f32_e64 v127, v213, v127
	ds_read_b64_tr_b16 v[212:213], v174 offset:0x200
	ds_read_b64_tr_b16 v[214:215], v174 offset:0x600
	ds_read_b64_tr_b16 v[216:217], v174 offset:0xa00
	s_waitcnt lgkmcnt(12)
	v_mfma_f32_32x32x16_bf16 v[98:113], v[228:231], v[142:145], v[98:113]
	ds_read_b64_tr_b16 v[218:219], v174 offset:0xe00
	ds_read_b64_tr_b16 v[220:221], v174 offset:0x1200
	ds_read_b64_tr_b16 v[222:223], v174 offset:0x1600
	ds_read_b64_tr_b16 v[224:225], v174 offset:0x1a00
	ds_read_b64_tr_b16 v[226:227], v174 offset:0x1e00
	v_pk_add_f32 v[126:127], v[126:127], v[126:127] op_sel:[0,1] op_sel_hi:[1,0]
	s_waitcnt lgkmcnt(15)
	v_mfma_f32_32x32x16_bf16 v[82:97], v[232:235], v[142:145], v[82:97]
	v_mov_b32_e32 v127, v126
	s_nop 1
	v_permlane32_swap_b32_e32 v126, v127
	s_waitcnt lgkmcnt(14)
	v_mfma_f32_32x32x16_bf16 v[18:33], v[50:53], v[66:69], v[18:33]
	s_waitcnt lgkmcnt(12)
	v_mfma_f32_32x32x16_bf16 v[18:33], v[54:57], v[70:73], v[18:33]
	s_waitcnt lgkmcnt(10)
	v_mfma_f32_32x32x16_bf16 v[18:33], v[58:61], v[74:77], v[18:33]
	s_waitcnt lgkmcnt(8)
	v_mfma_f32_32x32x16_bf16 v[18:33], v[62:65], v[78:81], v[18:33]
	s_waitcnt lgkmcnt(6)
	v_mfma_f32_32x32x16_bf16 v[2:17], v[50:53], v[212:215], v[2:17]
	s_nop 0
	v_max_f32_e32 v249, v99, v99
	v_max_f32_e32 v250, v98, v98
	v_max_f32_e32 v249, v250, v249
	v_max3_f32 v249, v249, v100, v101
	v_max3_f32 v249, v249, v102, v103
	v_max3_f32 v251, v249, v104, v105
	v_max3_f32 v251, v251, v106, v107
	s_waitcnt lgkmcnt(4)
	v_exp_f32_e32 v50, v98
	v_exp_f32_e32 v51, v99
	v_exp_f32_e32 v52, v100
	v_exp_f32_e32 v53, v101
	v_mov_b64_e32 v[66:67], v[82:83]
	v_mov_b64_e32 v[68:69], v[84:85]
	v_mfma_f32_32x32x16_bf16 v[2:17], v[54:57], v[216:219], v[2:17]
	v_max3_f32 v251, v251, v108, v109
	v_max3_f32 v251, v251, v110, v111
	v_max3_f32 v251, v251, v112, v113
	v_max3_f32 v251, v251, v82, v83
	v_max3_f32 v251, v251, v84, v85
	v_max3_f32 v251, v251, v86, v87
	v_max3_f32 v251, v251, v88, v89
	s_waitcnt lgkmcnt(2)
	v_exp_f32_e32 v54, v102
	v_exp_f32_e32 v55, v103
	v_exp_f32_e32 v56, v104
	v_exp_f32_e32 v57, v105
	v_mov_b64_e32 v[70:71], v[86:87]
	v_mov_b64_e32 v[72:73], v[88:89]
	v_mfma_f32_32x32x16_bf16 v[2:17], v[58:61], v[220:223], v[2:17]
	v_max3_f32 v251, v251, v90, v91
	v_max3_f32 v251, v251, v92, v93
	v_max3_f32 v251, v251, v94, v95
	v_max3_f32 v251, v251, v96, v97
	v_mov_b32_e32 v252, v251
	s_nop 1
	v_permlane32_swap_b32_e32 v251, v252
	s_waitcnt lgkmcnt(0)
	v_exp_f32_e32 v58, v106
	v_exp_f32_e32 v59, v107
	v_exp_f32_e32 v60, v108
	v_exp_f32_e32 v61, v109
	v_mov_b64_e32 v[74:75], v[90:91]
	v_mov_b64_e32 v[76:77], v[92:93]
	v_mfma_f32_32x32x16_bf16 v[2:17], v[62:65], v[224:227], v[2:17]
	v_exp_f32_e32 v62, v110
	v_exp_f32_e32 v63, v111
	v_exp_f32_e32 v64, v112
	v_exp_f32_e32 v65, v113
	v_mov_b64_e32 v[78:79], v[94:95]
	v_mov_b64_e32 v[80:81], v[96:97]
	v_max_f32_e32 v252, v252, v252
	v_max_f32_e32 v251, v251, v251
	v_max_f32_e32 v174, v251, v252
	v_cmp_ge_f32_e32 vcc, s80, v174
	s_cmp_lg_u64 vcc, exec
	s_cselect_b64 s[6:7], -1, 0
	s_cbranch_scc1 .LBB0_2275
	v_mov_b32_e32 v203, 1.0
	v_mov_b32_e32 v204, v210
	s_branch .LBB0_2280

; #define G8_STAGE_B(bufoff, gbase) do { _Pragma("unroll") for (int _i = 0; _i < 2; ++_i) \
;         __builtin_amdgcn_global_load_lds((const unsigned*)((const char*)(gbase) + voffB[_i]), (LAS unsigned*)(lds + (bufoff) + ldsw + _i * 8192), 16, 0, 0); } while (0)
; #define G8_LDA(dst, b, h) do { _Pragma("unroll") for (int m = 0; m < 4; ++m) _Pragma("unroll") for (int k = 0; k < 2; ++k) dst[m][k] = *(const LAS bf16x8*)(lds + G8_SA(b, h) + aoff + m * 2048 + k * 1024); } while (0)
; #define G8_LDB(dst, b, h) do { _Pragma("unroll") for (int n = 0; n < 2; ++n) _Pragma("unroll") for (int k = 0; k < 2; ++k) dst[n][k] = *(const LAS bf16x8*)(lds + G8_SB(b, h) + boff + n * 2048 + k * 1024); } while (0)
; #define G8_MMA(ai, bj, At, Bt) do { __builtin_amdgcn_s_setprio(1); _Pragma("unroll") for (int m = 0; m < 4; ++m) _Pragma("unroll") for (int n = 0; n < 2; ++n) _Pragma("unroll") for (int k = 0; k < 2; ++k) \
;         acc[ai][bj][m][n] = __builtin_amdgcn_mfma_f32_16x16x32_bf16(Bt[n][k], At[m][k], acc[ai][bj][m][n], 0, 0, 0); __builtin_amdgcn_s_setprio(0); } while (0)
; #define G8_WAIT_V(n) asm volatile("s_waitcnt vmcnt(" #n ")" ::: "memory")
; #define G8_WAIT_L(n) asm volatile("s_waitcnt lgkmcnt(" #n ")" ::: "memory")
; #define G8_BAR __builtin_amdgcn_s_barrier()
; #define G8_SCHED __builtin_amdgcn_sched_barrier(0)
; template <class Sched, class Epi>
; DEVI void gemm_phase(LAS unsigned char* lds, const char* Abase, const int K, const Sched& S, const Epi& E) {
;     ...
;             G8_LDB(B0, 0, 0); G8_LDB(B1, 0, 1); G8_SCHED; G8_LDA(At, 0, 0); G8_STAGE_A(G8_SA(1, 1), false, 1, k1);
;             G8_WAIT_L(0); G8_BAR; G8_MMA(0, 0, At, B0); G8_MMA(0, 1, At, B1); G8_BAR; G8_SCHED;
;             if (!skip1) G8_LDA(At, 0, 1); G8_STAGE_B(G8_SB(0, 0), b2); G8_STAGE_A(G8_SA(0, 0), last, 0, k2); G8_STAGE_B(G8_SB(0, 1), b2 + hstepB);
;             G8_WAIT_V(6); G8_WAIT_L(0); G8_BAR; if (!skip1) { G8_MMA(1, 0, At, B0); G8_MMA(1, 1, At, B1); } G8_BAR; G8_SCHED;
.LBB0_2579:
	ds_read_b128 v[162:165], v230
	ds_read_b128 v[166:169], v230 offset:1024
	ds_read_b128 v[170:173], v230 offset:2048
	ds_read_b128 v[174:177], v230 offset:3072
	ds_read_b128 v[138:141], v231
	ds_read_b128 v[150:153], v231 offset:1024
	ds_read_b128 v[154:157], v231 offset:2048
	ds_read_b128 v[158:161], v231 offset:3072
	v_lshl_add_u64 v[4:5], v[218:219], 0, s[34:35]
	s_add_i32 m0, s40, 0xc000
	s_waitcnt lgkmcnt(0)
	ds_read_b128 v[190:193], v232
	ds_read_b128 v[206:209], v232 offset:1024
	ds_read_b128 v[186:189], v232 offset:2048
	ds_read_b128 v[202:205], v232 offset:3072
	ds_read_b128 v[182:185], v232 offset:4096
	ds_read_b128 v[198:201], v232 offset:5120
	ds_read_b128 v[178:181], v232 offset:6144
	ds_read_b128 v[194:197], v232 offset:7168
	global_load_lds_dwordx4 v[4:5], off
	v_lshl_add_u64 v[4:5], v[220:221], 0, s[34:35]
	s_add_i32 m0, s40, 0xe000
	s_nop 0
	global_load_lds_dwordx4 v[4:5], off
	s_waitcnt lgkmcnt(0)
	s_barrier
	s_setprio 1
	s_waitcnt lgkmcnt(0)
	v_mfma_f32_16x16x32_bf16 v[118:121], v[162:165], v[190:193], v[146:149]
	v_mfma_f32_16x16x32_bf16 v[126:129], v[170:173], v[190:193], v[142:145]
	v_mfma_f32_16x16x32_bf16 v[114:117], v[162:165], v[186:189], v[114:117]
	v_mfma_f32_16x16x32_bf16 v[110:113], v[170:173], v[186:189], v[110:113]
	v_mfma_f32_16x16x32_bf16 v[98:101], v[162:165], v[182:185], v[98:101]
	v_mfma_f32_16x16x32_bf16 v[94:97], v[170:173], v[182:185], v[94:97]
	v_mfma_f32_16x16x32_bf16 v[82:85], v[162:165], v[178:181], v[82:85]
	v_mfma_f32_16x16x32_bf16 v[78:81], v[170:173], v[178:181], v[78:81]
	v_mfma_f32_16x16x32_bf16 v[118:121], v[166:169], v[206:209], v[118:121]
	v_mfma_f32_16x16x32_bf16 v[126:129], v[174:177], v[206:209], v[126:129]
	v_mfma_f32_16x16x32_bf16 v[114:117], v[166:169], v[202:205], v[114:117]
	v_mfma_f32_16x16x32_bf16 v[110:113], v[174:177], v[202:205], v[110:113]
	v_mfma_f32_16x16x32_bf16 v[98:101], v[166:169], v[198:201], v[98:101]
	v_mfma_f32_16x16x32_bf16 v[94:97], v[174:177], v[198:201], v[94:97]
	v_mfma_f32_16x16x32_bf16 v[82:85], v[166:169], v[194:197], v[82:85]
	v_mfma_f32_16x16x32_bf16 v[78:81], v[174:177], v[194:197], v[78:81]
	v_mfma_f32_16x16x32_bf16 v[130:133], v[138:141], v[190:193], v[134:137]
	v_mfma_f32_16x16x32_bf16 v[122:125], v[154:157], v[190:193], v[122:125]
	v_mfma_f32_16x16x32_bf16 v[106:109], v[138:141], v[186:189], v[106:109]
	v_mfma_f32_16x16x32_bf16 v[102:105], v[154:157], v[186:189], v[102:105]
	v_mfma_f32_16x16x32_bf16 v[90:93], v[138:141], v[182:185], v[90:93]
	v_mfma_f32_16x16x32_bf16 v[86:89], v[154:157], v[182:185], v[86:89]
	v_mfma_f32_16x16x32_bf16 v[74:77], v[138:141], v[178:181], v[74:77]
	v_mfma_f32_16x16x32_bf16 v[70:73], v[154:157], v[178:181], v[70:73]
	v_mfma_f32_16x16x32_bf16 v[130:133], v[150:153], v[206:209], v[130:133]
	v_mfma_f32_16x16x32_bf16 v[122:125], v[158:161], v[206:209], v[122:125]
	v_mfma_f32_16x16x32_bf16 v[106:109], v[150:153], v[202:205], v[106:109]
	v_mfma_f32_16x16x32_bf16 v[102:105], v[158:161], v[202:205], v[102:105]
	v_mfma_f32_16x16x32_bf16 v[90:93], v[150:153], v[198:201], v[90:93]
	v_mfma_f32_16x16x32_bf16 v[86:89], v[158:161], v[198:201], v[86:89]
	v_mfma_f32_16x16x32_bf16 v[74:77], v[150:153], v[194:197], v[74:77]
	v_mfma_f32_16x16x32_bf16 v[70:73], v[158:161], v[194:197], v[70:73]
	s_setprio 0
	s_barrier
	v_cmp_ne_u32_e64 s[4:5], 1, v233
	s_andn2_b64 vcc, exec, s[28:29]
	s_cbranch_vccnz .LBB0_2581
	ds_read_b128 v[190:193], v232 offset:16384
	ds_read_b128 v[206:209], v232 offset:17408
	ds_read_b128 v[186:189], v232 offset:18432
	ds_read_b128 v[202:205], v232 offset:19456
	ds_read_b128 v[182:185], v232 offset:20480
	ds_read_b128 v[198:201], v232 offset:21504
	ds_read_b128 v[178:181], v232 offset:22528
	ds_read_b128 v[194:197], v232 offset:23552
.LBB0_2581:
	s_add_u32 s30, s34, 0x100
	s_addc_u32 s31, s35, 0
	s_add_u32 s68, s62, s34
	s_addc_u32 s69, s63, s35
	s_cmp_eq_u32 s64, 12
	s_cselect_b64 s[66:67], -1, 0
	s_and_b64 s[34:35], s[66:67], exec
	s_cselect_b32 s65, 0, s30
	s_cselect_b32 s35, s17, s69
	s_cselect_b32 s34, s61, s68
	s_and_b64 s[66:67], s[26:27], s[66:67]
	s_and_b64 s[66:67], s[66:67], exec
	s_cselect_b32 s67, s22, s24
	s_mov_b32 m0, s41
	v_lshl_add_u64 v[4:5], s[34:35], 0, v[210:211]
	s_cselect_b32 s66, s23, s25
	s_add_u32 s68, s67, s65
	global_load_lds_dwordx4 v[4:5], off
	v_lshl_add_u64 v[222:223], s[34:35], 0, v[212:213]
	s_mov_b32 m0, s42
	s_addc_u32 s69, s66, 0
	global_load_lds_dwordx4 v[222:223], off
	v_lshl_add_u64 v[224:225], s[68:69], 0, v[210:211]
	s_mov_b32 m0, s40
	v_lshl_add_u64 v[226:227], s[68:69], 0, v[212:213]
	s_add_u32 s68, s34, 0x40000
	global_load_lds_dwordx4 v[224:225], off
	s_mov_b32 m0, s43
	s_addc_u32 s69, s35, 0
	global_load_lds_dwordx4 v[226:227], off
	v_lshl_add_u64 v[134:135], s[68:69], 0, v[210:211]
	s_mov_b32 m0, s44
	s_and_b64 vcc, exec, s[4:5]
	global_load_lds_dwordx4 v[134:135], off
	v_lshl_add_u64 v[134:135], s[68:69], 0, v[212:213]
	s_mov_b32 m0, s45
	s_nop 0
	global_load_lds_dwordx4 v[134:135], off
	s_waitcnt vmcnt(6)
	s_waitcnt lgkmcnt(0)
	s_barrier
	s_cbranch_vccnz .LBB0_2583
; #define G8_STAGE_B(bufoff, gbase) do { _Pragma("unroll") for (int _i = 0; _i < 2; ++_i) \
;         __builtin_amdgcn_global_load_lds((const unsigned*)((const char*)(gbase) + voffB[_i]), (LAS unsigned*)(lds + (bufoff) + ldsw + _i * 8192), 16, 0, 0); } while (0)
; #define G8_LDA(dst, b, h) do { _Pragma("unroll") for (int m = 0; m < 4; ++m) _Pragma("unroll") for (int k = 0; k < 2; ++k) dst[m][k] = *(const LAS bf16x8*)(lds + G8_SA(b, h) + aoff + m * 2048 + k * 1024); } while (0)
; #define G8_LDB(dst, b, h) do { _Pragma("unroll") for (int n = 0; n < 2; ++n) _Pragma("unroll") for (int k = 0; k < 2; ++k) dst[n][k] = *(const LAS bf16x8*)(lds + G8_SB(b, h) + boff + n * 2048 + k * 1024); } while (0)
; #define G8_MMA(ai, bj, At, Bt) do { __builtin_amdgcn_s_setprio(1); _Pragma("unroll") for (int m = 0; m < 4; ++m) _Pragma("unroll") for (int n = 0; n < 2; ++n) _Pragma("unroll") for (int k = 0; k < 2; ++k) \
;         acc[ai][bj][m][n] = __builtin_amdgcn_mfma_f32_16x16x32_bf16(Bt[n][k], At[m][k], acc[ai][bj][m][n], 0, 0, 0); __builtin_amdgcn_s_setprio(0); } while (0)
; #define G8_WAIT_V(n) asm volatile("s_waitcnt vmcnt(" #n ")" ::: "memory")
; #define G8_WAIT_L(n) asm volatile("s_waitcnt lgkmcnt(" #n ")" ::: "memory")
; #define G8_BAR __builtin_amdgcn_s_barrier()
; #define G8_SCHED __builtin_amdgcn_sched_barrier(0)
; template <class Sched, class Epi>
; DEVI void gemm_phase(LAS unsigned char* lds, const char* Abase, const int K, const Sched& S, const Epi& E) {
;     ...
;             G8_WAIT_V(6); G8_WAIT_L(0); G8_BAR; if (!skip1) { G8_MMA(1, 0, At, B0); G8_MMA(1, 1, At, B1); } G8_BAR; G8_SCHED;
;             G8_LDB(B0, 1, 0); G8_LDB(B1, 1, 1); G8_SCHED; G8_LDA(At, 1, 0); G8_STAGE_A(G8_SA(0, 1), last, 1, k2);
;             G8_WAIT_L(0); G8_BAR; G8_MMA(0, 0, At, B0); G8_MMA(0, 1, At, B1); G8_BAR; G8_SCHED;
;             if (!skip1) G8_LDA(At, 1, 1); G8_STAGE_B(G8_SB(1, 0), b3); G8_STAGE_A(G8_SA(1, 0), last, 0, k3); G8_STAGE_B(G8_SB(1, 1), b3 + hstepB);
	s_setprio 1
	s_waitcnt lgkmcnt(0)
	v_mfma_f32_16x16x32_bf16 v[66:69], v[162:165], v[190:193], v[66:69]
	v_mfma_f32_16x16x32_bf16 v[62:65], v[170:173], v[190:193], v[62:65]
	v_mfma_f32_16x16x32_bf16 v[50:53], v[162:165], v[186:189], v[50:53]
	v_mfma_f32_16x16x32_bf16 v[46:49], v[170:173], v[186:189], v[46:49]
	v_mfma_f32_16x16x32_bf16 v[34:37], v[162:165], v[182:185], v[34:37]
	v_mfma_f32_16x16x32_bf16 v[30:33], v[170:173], v[182:185], v[30:33]
	v_mfma_f32_16x16x32_bf16 v[18:21], v[162:165], v[178:181], v[18:21]
	v_mfma_f32_16x16x32_bf16 v[14:17], v[170:173], v[178:181], v[14:17]
	v_mfma_f32_16x16x32_bf16 v[66:69], v[166:169], v[206:209], v[66:69]
	v_mfma_f32_16x16x32_bf16 v[62:65], v[174:177], v[206:209], v[62:65]
	v_mfma_f32_16x16x32_bf16 v[50:53], v[166:169], v[202:205], v[50:53]
	v_mfma_f32_16x16x32_bf16 v[46:49], v[174:177], v[202:205], v[46:49]
	v_mfma_f32_16x16x32_bf16 v[34:37], v[166:169], v[198:201], v[34:37]
	v_mfma_f32_16x16x32_bf16 v[30:33], v[174:177], v[198:201], v[30:33]
	v_mfma_f32_16x16x32_bf16 v[18:21], v[166:169], v[194:197], v[18:21]
	v_mfma_f32_16x16x32_bf16 v[14:17], v[174:177], v[194:197], v[14:17]
	v_mfma_f32_16x16x32_bf16 v[58:61], v[138:141], v[190:193], v[58:61]
	v_mfma_f32_16x16x32_bf16 v[54:57], v[154:157], v[190:193], v[54:57]
	v_mfma_f32_16x16x32_bf16 v[42:45], v[138:141], v[186:189], v[42:45]
	v_mfma_f32_16x16x32_bf16 v[38:41], v[154:157], v[186:189], v[38:41]
	v_mfma_f32_16x16x32_bf16 v[26:29], v[138:141], v[182:185], v[26:29]
	v_mfma_f32_16x16x32_bf16 v[22:25], v[154:157], v[182:185], v[22:25]
	v_mfma_f32_16x16x32_bf16 v[10:13], v[138:141], v[178:181], v[10:13]
	v_mfma_f32_16x16x32_bf16 v[6:9], v[154:157], v[178:181], v[6:9]
	v_mfma_f32_16x16x32_bf16 v[58:61], v[150:153], v[206:209], v[58:61]
	v_mfma_f32_16x16x32_bf16 v[54:57], v[158:161], v[206:209], v[54:57]
	v_mfma_f32_16x16x32_bf16 v[42:45], v[150:153], v[202:205], v[42:45]
	v_mfma_f32_16x16x32_bf16 v[38:41], v[158:161], v[202:205], v[38:41]
	v_mfma_f32_16x16x32_bf16 v[26:29], v[150:153], v[198:201], v[26:29]
	v_mfma_f32_16x16x32_bf16 v[22:25], v[158:161], v[198:201], v[22:25]
	v_mfma_f32_16x16x32_bf16 v[10:13], v[150:153], v[194:197], v[10:13]
	v_mfma_f32_16x16x32_bf16 v[6:9], v[158:161], v[194:197], v[6:9]
	s_setprio 0
.LBB0_2583:
	s_barrier
	v_add_u32_e32 v3, 0x18000, v229
	ds_read_b128 v[162:165], v3
	ds_read_b128 v[166:169], v3 offset:1024
	ds_read_b128 v[170:173], v3 offset:2048
	ds_read_b128 v[174:177], v3 offset:3072
	v_add_u32_e32 v3, 0x1c000, v229
	ds_read_b128 v[138:141], v3
	ds_read_b128 v[150:153], v3 offset:1024
	ds_read_b128 v[154:157], v3 offset:2048
	ds_read_b128 v[158:161], v3 offset:3072
	s_add_u32 s65, s67, s65
	s_addc_u32 s67, s66, 0
	s_add_u32 s66, s65, 0x40000
	s_addc_u32 s67, s67, 0
	s_mov_b32 m0, s46
	v_lshl_add_u64 v[134:135], s[66:67], 0, v[210:211]
	s_waitcnt lgkmcnt(0)
	ds_read_b128 v[190:193], v232 offset:32768
	ds_read_b128 v[206:209], v232 offset:33792
	ds_read_b128 v[186:189], v232 offset:34816
	ds_read_b128 v[202:205], v232 offset:35840
	ds_read_b128 v[182:185], v232 offset:36864
	ds_read_b128 v[198:201], v232 offset:37888
	ds_read_b128 v[178:181], v232 offset:38912
	ds_read_b128 v[194:197], v232 offset:39936
	global_load_lds_dwordx4 v[134:135], off
	v_lshl_add_u64 v[134:135], s[66:67], 0, v[212:213]
	s_mov_b32 m0, s47
	s_nop 0
	global_load_lds_dwordx4 v[134:135], off
	s_waitcnt lgkmcnt(0)
	s_barrier
	s_setprio 1
	s_waitcnt lgkmcnt(0)
	v_mfma_f32_16x16x32_bf16 v[118:121], v[162:165], v[190:193], v[118:121]
	v_mfma_f32_16x16x32_bf16 v[146:149], v[166:169], v[206:209], v[118:121]
	v_mfma_f32_16x16x32_bf16 v[118:121], v[170:173], v[190:193], v[126:129]
	v_mfma_f32_16x16x32_bf16 v[114:117], v[162:165], v[186:189], v[114:117]
	v_mfma_f32_16x16x32_bf16 v[110:113], v[170:173], v[186:189], v[110:113]
	v_mfma_f32_16x16x32_bf16 v[98:101], v[162:165], v[182:185], v[98:101]
	v_mfma_f32_16x16x32_bf16 v[94:97], v[170:173], v[182:185], v[94:97]
	v_mfma_f32_16x16x32_bf16 v[82:85], v[162:165], v[178:181], v[82:85]
	v_mfma_f32_16x16x32_bf16 v[78:81], v[170:173], v[178:181], v[78:81]
	v_mfma_f32_16x16x32_bf16 v[142:145], v[174:177], v[206:209], v[118:121]
	v_mfma_f32_16x16x32_bf16 v[114:117], v[166:169], v[202:205], v[114:117]
	v_mfma_f32_16x16x32_bf16 v[110:113], v[174:177], v[202:205], v[110:113]
	v_mfma_f32_16x16x32_bf16 v[98:101], v[166:169], v[198:201], v[98:101]
	v_mfma_f32_16x16x32_bf16 v[94:97], v[174:177], v[198:201], v[94:97]
	v_mfma_f32_16x16x32_bf16 v[82:85], v[166:169], v[194:197], v[82:85]
	v_mfma_f32_16x16x32_bf16 v[78:81], v[174:177], v[194:197], v[78:81]
	v_mfma_f32_16x16x32_bf16 v[118:121], v[138:141], v[190:193], v[130:133]
	v_mfma_f32_16x16x32_bf16 v[134:137], v[150:153], v[206:209], v[118:121]
	v_mfma_f32_16x16x32_bf16 v[118:121], v[154:157], v[190:193], v[122:125]
	v_mfma_f32_16x16x32_bf16 v[106:109], v[138:141], v[186:189], v[106:109]
	v_mfma_f32_16x16x32_bf16 v[102:105], v[154:157], v[186:189], v[102:105]
	v_mfma_f32_16x16x32_bf16 v[90:93], v[138:141], v[182:185], v[90:93]
	v_mfma_f32_16x16x32_bf16 v[86:89], v[154:157], v[182:185], v[86:89]
	v_mfma_f32_16x16x32_bf16 v[74:77], v[138:141], v[178:181], v[74:77]
	v_mfma_f32_16x16x32_bf16 v[70:73], v[154:157], v[178:181], v[70:73]
	v_mfma_f32_16x16x32_bf16 v[122:125], v[158:161], v[206:209], v[118:121]
	v_mfma_f32_16x16x32_bf16 v[106:109], v[150:153], v[202:205], v[106:109]
	v_mfma_f32_16x16x32_bf16 v[102:105], v[158:161], v[202:205], v[102:105]
	v_mfma_f32_16x16x32_bf16 v[90:93], v[150:153], v[198:201], v[90:93]
	v_mfma_f32_16x16x32_bf16 v[86:89], v[158:161], v[198:201], v[86:89]
	v_mfma_f32_16x16x32_bf16 v[74:77], v[150:153], v[194:197], v[74:77]
	v_mfma_f32_16x16x32_bf16 v[70:73], v[158:161], v[194:197], v[70:73]
	s_setprio 0
	s_barrier
	s_and_b64 vcc, exec, s[4:5]
	s_cbranch_vccnz .LBB0_2585
	ds_read_b128 v[190:193], v232 offset:49152
	ds_read_b128 v[206:209], v232 offset:50176
	ds_read_b128 v[186:189], v232 offset:51200
	ds_read_b128 v[202:205], v232 offset:52224
	ds_read_b128 v[182:185], v232 offset:53248
	ds_read_b128 v[198:201], v232 offset:54272
	ds_read_b128 v[178:181], v232 offset:55296
	ds_read_b128 v[194:197], v232 offset:56320
; #define G8_STAGE_B(bufoff, gbase) do { _Pragma("unroll") for (int _i = 0; _i < 2; ++_i) \
;         __builtin_amdgcn_global_load_lds((const unsigned*)((const char*)(gbase) + voffB[_i]), (LAS unsigned*)(lds + (bufoff) + ldsw + _i * 8192), 16, 0, 0); } while (0)
; #define G8_LDA(dst, b, h) do { _Pragma("unroll") for (int m = 0; m < 4; ++m) _Pragma("unroll") for (int k = 0; k < 2; ++k) dst[m][k] = *(const LAS bf16x8*)(lds + G8_SA(b, h) + aoff + m * 2048 + k * 1024); } while (0)
; #define G8_MMA(ai, bj, At, Bt) do { __builtin_amdgcn_s_setprio(1); _Pragma("unroll") for (int m = 0; m < 4; ++m) _Pragma("unroll") for (int n = 0; n < 2; ++n) _Pragma("unroll") for (int k = 0; k < 2; ++k) \
;         acc[ai][bj][m][n] = __builtin_amdgcn_mfma_f32_16x16x32_bf16(Bt[n][k], At[m][k], acc[ai][bj][m][n], 0, 0, 0); __builtin_amdgcn_s_setprio(0); } while (0)
; #define G8_WAIT_V(n) asm volatile("s_waitcnt vmcnt(" #n ")" ::: "memory")
; #define G8_WAIT_L(n) asm volatile("s_waitcnt lgkmcnt(" #n ")" ::: "memory")
; #define G8_BAR __builtin_amdgcn_s_barrier()
; #define G8_SCHED __builtin_amdgcn_sched_barrier(0)
; template <class Sched, class Epi>
; DEVI void gemm_phase(LAS unsigned char* lds, const char* Abase, const int K, const Sched& S, const Epi& E) {
;     ...
;             if (!skip1) G8_LDA(At, 1, 1); G8_STAGE_B(G8_SB(1, 0), b3); G8_STAGE_A(G8_SA(1, 0), last, 0, k3); G8_STAGE_B(G8_SB(1, 1), b3 + hstepB);
;             G8_WAIT_V(6); G8_WAIT_L(0); G8_BAR; if (!skip1) { G8_MMA(1, 0, At, B0); G8_MMA(1, 1, At, B1); } G8_BAR; G8_SCHED;
.LBB0_2585:
	s_mov_b32 m0, s51
	v_lshl_add_u64 v[4:5], v[4:5], 0, s[12:13]
	global_load_lds_dwordx4 v[4:5], off
	v_lshl_add_u64 v[4:5], v[222:223], 0, s[12:13]
	s_mov_b32 m0, s52
	s_add_u32 s34, s34, 0x40080
	global_load_lds_dwordx4 v[4:5], off
	v_lshl_add_u64 v[4:5], v[224:225], 0, s[12:13]
	s_mov_b32 m0, s53
	s_addc_u32 s35, s35, 0
	global_load_lds_dwordx4 v[4:5], off
	v_lshl_add_u64 v[4:5], v[226:227], 0, s[12:13]
	s_mov_b32 m0, s54
	s_and_b64 vcc, exec, s[4:5]
	global_load_lds_dwordx4 v[4:5], off
	v_lshl_add_u64 v[4:5], s[34:35], 0, v[210:211]
	s_mov_b32 m0, s55
	s_nop 0
	global_load_lds_dwordx4 v[4:5], off
	v_lshl_add_u64 v[4:5], s[34:35], 0, v[212:213]
	s_mov_b32 m0, s56
	s_nop 0
	global_load_lds_dwordx4 v[4:5], off
	s_waitcnt vmcnt(6)
	s_waitcnt lgkmcnt(0)
	s_barrier
	s_cbranch_vccnz .LBB0_2587
	s_setprio 1
	s_waitcnt lgkmcnt(0)
	v_mfma_f32_16x16x32_bf16 v[66:69], v[162:165], v[190:193], v[66:69]
	v_mfma_f32_16x16x32_bf16 v[62:65], v[170:173], v[190:193], v[62:65]
	v_mfma_f32_16x16x32_bf16 v[50:53], v[162:165], v[186:189], v[50:53]
	v_mfma_f32_16x16x32_bf16 v[46:49], v[170:173], v[186:189], v[46:49]
	v_mfma_f32_16x16x32_bf16 v[34:37], v[162:165], v[182:185], v[34:37]
	v_mfma_f32_16x16x32_bf16 v[30:33], v[170:173], v[182:185], v[30:33]
	v_mfma_f32_16x16x32_bf16 v[18:21], v[162:165], v[178:181], v[18:21]
	v_mfma_f32_16x16x32_bf16 v[14:17], v[170:173], v[178:181], v[14:17]
	v_mfma_f32_16x16x32_bf16 v[66:69], v[166:169], v[206:209], v[66:69]
	v_mfma_f32_16x16x32_bf16 v[62:65], v[174:177], v[206:209], v[62:65]
	v_mfma_f32_16x16x32_bf16 v[50:53], v[166:169], v[202:205], v[50:53]
	v_mfma_f32_16x16x32_bf16 v[46:49], v[174:177], v[202:205], v[46:49]
	v_mfma_f32_16x16x32_bf16 v[34:37], v[166:169], v[198:201], v[34:37]
	v_mfma_f32_16x16x32_bf16 v[30:33], v[174:177], v[198:201], v[30:33]
	v_mfma_f32_16x16x32_bf16 v[18:21], v[166:169], v[194:197], v[18:21]
	v_mfma_f32_16x16x32_bf16 v[14:17], v[174:177], v[194:197], v[14:17]
	v_mfma_f32_16x16x32_bf16 v[58:61], v[138:141], v[190:193], v[58:61]
	v_mfma_f32_16x16x32_bf16 v[54:57], v[154:157], v[190:193], v[54:57]
	v_mfma_f32_16x16x32_bf16 v[42:45], v[138:141], v[186:189], v[42:45]
	v_mfma_f32_16x16x32_bf16 v[38:41], v[154:157], v[186:189], v[38:41]
	v_mfma_f32_16x16x32_bf16 v[26:29], v[138:141], v[182:185], v[26:29]
	v_mfma_f32_16x16x32_bf16 v[22:25], v[154:157], v[182:185], v[22:25]
	v_mfma_f32_16x16x32_bf16 v[10:13], v[138:141], v[178:181], v[10:13]
	v_mfma_f32_16x16x32_bf16 v[4:7], v[154:157], v[178:181], v[6:9]
	v_mfma_f32_16x16x32_bf16 v[58:61], v[150:153], v[206:209], v[58:61]
	v_mfma_f32_16x16x32_bf16 v[54:57], v[158:161], v[206:209], v[54:57]
	v_mfma_f32_16x16x32_bf16 v[42:45], v[150:153], v[202:205], v[42:45]
	v_mfma_f32_16x16x32_bf16 v[38:41], v[158:161], v[202:205], v[38:41]
	v_mfma_f32_16x16x32_bf16 v[26:29], v[150:153], v[198:201], v[26:29]
	v_mfma_f32_16x16x32_bf16 v[22:25], v[158:161], v[198:201], v[22:25]
	v_mfma_f32_16x16x32_bf16 v[10:13], v[150:153], v[194:197], v[10:13]
	v_mfma_f32_16x16x32_bf16 v[6:9], v[158:161], v[194:197], v[4:7]
	s_setprio 0

; #define G8_STAGE_B(bufoff, gbase) do { _Pragma("unroll") for (int _i = 0; _i < 2; ++_i) \
;         __builtin_amdgcn_global_load_lds((const unsigned*)((const char*)(gbase) + voffB[_i]), (LAS unsigned*)(lds + (bufoff) + ldsw + _i * 8192), 16, 0, 0); } while (0)
; #define G8_LDA(dst, b, h) do { _Pragma("unroll") for (int m = 0; m < 4; ++m) _Pragma("unroll") for (int k = 0; k < 2; ++k) dst[m][k] = *(const LAS bf16x8*)(lds + G8_SA(b, h) + aoff + m * 2048 + k * 1024); } while (0)
; #define G8_LDB(dst, b, h) do { _Pragma("unroll") for (int n = 0; n < 2; ++n) _Pragma("unroll") for (int k = 0; k < 2; ++k) dst[n][k] = *(const LAS bf16x8*)(lds + G8_SB(b, h) + boff + n * 2048 + k * 1024); } while (0)
; #define G8_MMA(ai, bj, At, Bt) do { __builtin_amdgcn_s_setprio(1); _Pragma("unroll") for (int m = 0; m < 4; ++m) _Pragma("unroll") for (int n = 0; n < 2; ++n) _Pragma("unroll") for (int k = 0; k < 2; ++k) \
;         acc[ai][bj][m][n] = __builtin_amdgcn_mfma_f32_16x16x32_bf16(Bt[n][k], At[m][k], acc[ai][bj][m][n], 0, 0, 0); __builtin_amdgcn_s_setprio(0); } while (0)
; #define G8_WAIT_V(n) asm volatile("s_waitcnt vmcnt(" #n ")" ::: "memory")
; #define G8_WAIT_L(n) asm volatile("s_waitcnt lgkmcnt(" #n ")" ::: "memory")
; #define G8_BAR __builtin_amdgcn_s_barrier()
; #define G8_SCHED __builtin_amdgcn_sched_barrier(0)
; template <class Sched, class Epi>
; DEVI void gemm_phase(LAS unsigned char* lds, const char* Abase, const int K, const Sched& S, const Epi& E) {
;     ...
;             G8_LDB(B0, 0, 0); G8_LDB(B1, 0, 1); G8_SCHED; G8_LDA(At, 0, 0); G8_STAGE_A(G8_SA(1, 1), false, 1, k1);
;             G8_WAIT_L(0); G8_BAR; G8_MMA(0, 0, At, B0); G8_MMA(0, 1, At, B1); G8_BAR; G8_SCHED;
;             if (!skip1) G8_LDA(At, 0, 1); G8_STAGE_B(G8_SB(0, 0), b2); G8_STAGE_A(G8_SA(0, 0), last, 0, k2); G8_STAGE_B(G8_SB(0, 1), b2 + hstepB);
;             G8_WAIT_V(6); G8_WAIT_L(0); G8_BAR; if (!skip1) { G8_MMA(1, 0, At, B0); G8_MMA(1, 1, At, B1); } G8_BAR; G8_SCHED;
.LBB0_2720:
	ds_read_b128 v[150:153], v218
	ds_read_b128 v[154:157], v218 offset:1024
	ds_read_b128 v[158:161], v218 offset:2048
	ds_read_b128 v[162:165], v218 offset:3072
	ds_read_b128 v[134:137], v219
	ds_read_b128 v[138:141], v219 offset:1024
	ds_read_b128 v[142:145], v219 offset:2048
	ds_read_b128 v[146:149], v219 offset:3072
	v_lshl_add_u64 v[4:5], v[206:207], 0, s[30:31]
	s_add_i32 m0, s35, 0xc000
	s_waitcnt lgkmcnt(0)
	ds_read_b128 v[178:181], v220
	ds_read_b128 v[194:197], v220 offset:1024
	ds_read_b128 v[174:177], v220 offset:2048
	ds_read_b128 v[190:193], v220 offset:3072
	ds_read_b128 v[170:173], v220 offset:4096
	ds_read_b128 v[186:189], v220 offset:5120
	ds_read_b128 v[166:169], v220 offset:6144
	ds_read_b128 v[182:185], v220 offset:7168
	global_load_lds_dwordx4 v[4:5], off
	v_lshl_add_u64 v[4:5], v[208:209], 0, s[30:31]
	s_add_i32 m0, s35, 0xe000
	s_nop 0
	global_load_lds_dwordx4 v[4:5], off
	s_waitcnt lgkmcnt(0)
	s_barrier
	s_setprio 1
	s_waitcnt lgkmcnt(0)
	v_mfma_f32_16x16x32_bf16 v[130:133], v[150:153], v[178:181], v[130:133]
	v_mfma_f32_16x16x32_bf16 v[126:129], v[158:161], v[178:181], v[126:129]
	v_mfma_f32_16x16x32_bf16 v[122:125], v[150:153], v[174:177], v[122:125]
	v_mfma_f32_16x16x32_bf16 v[118:121], v[158:161], v[174:177], v[118:121]
	v_mfma_f32_16x16x32_bf16 v[110:113], v[150:153], v[170:173], v[110:113]
	v_mfma_f32_16x16x32_bf16 v[102:105], v[158:161], v[170:173], v[102:105]
	v_mfma_f32_16x16x32_bf16 v[94:97], v[150:153], v[166:169], v[94:97]
	v_mfma_f32_16x16x32_bf16 v[86:89], v[158:161], v[166:169], v[86:89]
	v_mfma_f32_16x16x32_bf16 v[130:133], v[154:157], v[194:197], v[130:133]
	v_mfma_f32_16x16x32_bf16 v[126:129], v[162:165], v[194:197], v[126:129]
	v_mfma_f32_16x16x32_bf16 v[122:125], v[154:157], v[190:193], v[122:125]
	v_mfma_f32_16x16x32_bf16 v[118:121], v[162:165], v[190:193], v[118:121]
	v_mfma_f32_16x16x32_bf16 v[110:113], v[154:157], v[186:189], v[110:113]
	v_mfma_f32_16x16x32_bf16 v[102:105], v[162:165], v[186:189], v[102:105]
	v_mfma_f32_16x16x32_bf16 v[94:97], v[154:157], v[182:185], v[94:97]
	v_mfma_f32_16x16x32_bf16 v[86:89], v[162:165], v[182:185], v[86:89]
	v_mfma_f32_16x16x32_bf16 v[114:117], v[134:137], v[178:181], v[114:117]
	v_mfma_f32_16x16x32_bf16 v[106:109], v[142:145], v[178:181], v[106:109]
	v_mfma_f32_16x16x32_bf16 v[98:101], v[134:137], v[174:177], v[98:101]
	v_mfma_f32_16x16x32_bf16 v[90:93], v[142:145], v[174:177], v[90:93]
	v_mfma_f32_16x16x32_bf16 v[82:85], v[134:137], v[170:173], v[82:85]
	v_mfma_f32_16x16x32_bf16 v[78:81], v[142:145], v[170:173], v[78:81]
	v_mfma_f32_16x16x32_bf16 v[74:77], v[134:137], v[166:169], v[74:77]
	v_mfma_f32_16x16x32_bf16 v[70:73], v[142:145], v[166:169], v[70:73]
	v_mfma_f32_16x16x32_bf16 v[114:117], v[138:141], v[194:197], v[114:117]
	v_mfma_f32_16x16x32_bf16 v[106:109], v[146:149], v[194:197], v[106:109]
	v_mfma_f32_16x16x32_bf16 v[98:101], v[138:141], v[190:193], v[98:101]
	v_mfma_f32_16x16x32_bf16 v[90:93], v[146:149], v[190:193], v[90:93]
	v_mfma_f32_16x16x32_bf16 v[82:85], v[138:141], v[186:189], v[82:85]
	v_mfma_f32_16x16x32_bf16 v[78:81], v[146:149], v[186:189], v[78:81]
	v_mfma_f32_16x16x32_bf16 v[74:77], v[138:141], v[182:185], v[74:77]
	v_mfma_f32_16x16x32_bf16 v[70:73], v[146:149], v[182:185], v[70:73]
	s_setprio 0
	s_barrier
	v_cmp_ne_u32_e64 s[4:5], 1, v221
	s_andn2_b64 vcc, exec, s[26:27]
	s_cbranch_vccnz .LBB0_2722
	ds_read_b128 v[178:181], v220 offset:16384
	ds_read_b128 v[194:197], v220 offset:17408
	ds_read_b128 v[174:177], v220 offset:18432
	ds_read_b128 v[190:193], v220 offset:19456
	ds_read_b128 v[170:173], v220 offset:20480
	ds_read_b128 v[186:189], v220 offset:21504
	ds_read_b128 v[166:169], v220 offset:22528
	ds_read_b128 v[182:185], v220 offset:23552
.LBB0_2722:
	s_add_u32 s28, s30, 0x100
	s_addc_u32 s29, s31, 0
	s_add_u32 s58, s51, s30
	s_addc_u32 s59, s52, s31
	s_cmpk_eq_i32 s30, 0x700
	s_cselect_b64 s[56:57], -1, 0
	s_and_b64 s[30:31], s[56:57], exec
	s_cselect_b32 s55, 0, s28
	s_cselect_b32 s31, s11, s59
	s_cselect_b32 s30, s10, s58
	s_and_b64 s[56:57], s[56:57], s[24:25]
	s_and_b64 s[56:57], s[56:57], exec
	s_cselect_b32 s57, s22, s16
	s_mov_b32 m0, s36
	v_lshl_add_u64 v[4:5], s[30:31], 0, v[198:199]
	s_cselect_b32 s56, s23, s17
	s_add_u32 s58, s57, s55
	global_load_lds_dwordx4 v[4:5], off
	v_lshl_add_u64 v[210:211], s[30:31], 0, v[200:201]
	s_mov_b32 m0, s37
	s_addc_u32 s59, s56, 0
	global_load_lds_dwordx4 v[210:211], off
	v_lshl_add_u64 v[212:213], s[58:59], 0, v[198:199]
	s_mov_b32 m0, s35
	v_lshl_add_u64 v[214:215], s[58:59], 0, v[200:201]
	s_add_u32 s58, s30, 0x40000
	global_load_lds_dwordx4 v[212:213], off
	s_mov_b32 m0, s39
	s_addc_u32 s59, s31, 0
	global_load_lds_dwordx4 v[214:215], off
	v_lshl_add_u64 v[222:223], s[58:59], 0, v[198:199]
	s_mov_b32 m0, s40
	s_and_b64 vcc, exec, s[4:5]
	global_load_lds_dwordx4 v[222:223], off
	v_lshl_add_u64 v[222:223], s[58:59], 0, v[200:201]
	s_mov_b32 m0, s41
	s_nop 0
	global_load_lds_dwordx4 v[222:223], off
	s_waitcnt vmcnt(6)
	s_waitcnt lgkmcnt(0)
	s_barrier
	s_cbranch_vccnz .LBB0_2724
; #define G8_STAGE_B(bufoff, gbase) do { _Pragma("unroll") for (int _i = 0; _i < 2; ++_i) \
;         __builtin_amdgcn_global_load_lds((const unsigned*)((const char*)(gbase) + voffB[_i]), (LAS unsigned*)(lds + (bufoff) + ldsw + _i * 8192), 16, 0, 0); } while (0)
; #define G8_LDA(dst, b, h) do { _Pragma("unroll") for (int m = 0; m < 4; ++m) _Pragma("unroll") for (int k = 0; k < 2; ++k) dst[m][k] = *(const LAS bf16x8*)(lds + G8_SA(b, h) + aoff + m * 2048 + k * 1024); } while (0)
; #define G8_LDB(dst, b, h) do { _Pragma("unroll") for (int n = 0; n < 2; ++n) _Pragma("unroll") for (int k = 0; k < 2; ++k) dst[n][k] = *(const LAS bf16x8*)(lds + G8_SB(b, h) + boff + n * 2048 + k * 1024); } while (0)
; #define G8_MMA(ai, bj, At, Bt) do { __builtin_amdgcn_s_setprio(1); _Pragma("unroll") for (int m = 0; m < 4; ++m) _Pragma("unroll") for (int n = 0; n < 2; ++n) _Pragma("unroll") for (int k = 0; k < 2; ++k) \
;         acc[ai][bj][m][n] = __builtin_amdgcn_mfma_f32_16x16x32_bf16(Bt[n][k], At[m][k], acc[ai][bj][m][n], 0, 0, 0); __builtin_amdgcn_s_setprio(0); } while (0)
; #define G8_WAIT_V(n) asm volatile("s_waitcnt vmcnt(" #n ")" ::: "memory")
; #define G8_WAIT_L(n) asm volatile("s_waitcnt lgkmcnt(" #n ")" ::: "memory")
; #define G8_BAR __builtin_amdgcn_s_barrier()
; #define G8_SCHED __builtin_amdgcn_sched_barrier(0)
; template <class Sched, class Epi>
; DEVI void gemm_phase(LAS unsigned char* lds, const char* Abase, const int K, const Sched& S, const Epi& E) {
;     ...
;             G8_WAIT_V(6); G8_WAIT_L(0); G8_BAR; if (!skip1) { G8_MMA(1, 0, At, B0); G8_MMA(1, 1, At, B1); } G8_BAR; G8_SCHED;
;             G8_LDB(B0, 1, 0); G8_LDB(B1, 1, 1); G8_SCHED; G8_LDA(At, 1, 0); G8_STAGE_A(G8_SA(0, 1), last, 1, k2);
;             G8_WAIT_L(0); G8_BAR; G8_MMA(0, 0, At, B0); G8_MMA(0, 1, At, B1); G8_BAR; G8_SCHED;
;             if (!skip1) G8_LDA(At, 1, 1); G8_STAGE_B(G8_SB(1, 0), b3); G8_STAGE_A(G8_SA(1, 0), last, 0, k3); G8_STAGE_B(G8_SB(1, 1), b3 + hstepB);
	s_setprio 1
	s_waitcnt lgkmcnt(0)
	v_mfma_f32_16x16x32_bf16 v[66:69], v[150:153], v[178:181], v[66:69]
	v_mfma_f32_16x16x32_bf16 v[62:65], v[158:161], v[178:181], v[62:65]
	v_mfma_f32_16x16x32_bf16 v[50:53], v[150:153], v[174:177], v[50:53]
	v_mfma_f32_16x16x32_bf16 v[46:49], v[158:161], v[174:177], v[46:49]
	v_mfma_f32_16x16x32_bf16 v[34:37], v[150:153], v[170:173], v[34:37]
	v_mfma_f32_16x16x32_bf16 v[30:33], v[158:161], v[170:173], v[30:33]
	v_mfma_f32_16x16x32_bf16 v[18:21], v[150:153], v[166:169], v[18:21]
	v_mfma_f32_16x16x32_bf16 v[14:17], v[158:161], v[166:169], v[14:17]
	v_mfma_f32_16x16x32_bf16 v[66:69], v[154:157], v[194:197], v[66:69]
	v_mfma_f32_16x16x32_bf16 v[62:65], v[162:165], v[194:197], v[62:65]
	v_mfma_f32_16x16x32_bf16 v[50:53], v[154:157], v[190:193], v[50:53]
	v_mfma_f32_16x16x32_bf16 v[46:49], v[162:165], v[190:193], v[46:49]
	v_mfma_f32_16x16x32_bf16 v[34:37], v[154:157], v[186:189], v[34:37]
	v_mfma_f32_16x16x32_bf16 v[30:33], v[162:165], v[186:189], v[30:33]
	v_mfma_f32_16x16x32_bf16 v[18:21], v[154:157], v[182:185], v[18:21]
	v_mfma_f32_16x16x32_bf16 v[14:17], v[162:165], v[182:185], v[14:17]
	v_mfma_f32_16x16x32_bf16 v[58:61], v[134:137], v[178:181], v[58:61]
	v_mfma_f32_16x16x32_bf16 v[54:57], v[142:145], v[178:181], v[54:57]
	v_mfma_f32_16x16x32_bf16 v[42:45], v[134:137], v[174:177], v[42:45]
	v_mfma_f32_16x16x32_bf16 v[38:41], v[142:145], v[174:177], v[38:41]
	v_mfma_f32_16x16x32_bf16 v[26:29], v[134:137], v[170:173], v[26:29]
	v_mfma_f32_16x16x32_bf16 v[22:25], v[142:145], v[170:173], v[22:25]
	v_mfma_f32_16x16x32_bf16 v[10:13], v[134:137], v[166:169], v[10:13]
	v_mfma_f32_16x16x32_bf16 v[6:9], v[142:145], v[166:169], v[6:9]
	v_mfma_f32_16x16x32_bf16 v[58:61], v[138:141], v[194:197], v[58:61]
	v_mfma_f32_16x16x32_bf16 v[54:57], v[146:149], v[194:197], v[54:57]
	v_mfma_f32_16x16x32_bf16 v[42:45], v[138:141], v[190:193], v[42:45]
	v_mfma_f32_16x16x32_bf16 v[38:41], v[146:149], v[190:193], v[38:41]
	v_mfma_f32_16x16x32_bf16 v[26:29], v[138:141], v[186:189], v[26:29]
	v_mfma_f32_16x16x32_bf16 v[22:25], v[146:149], v[186:189], v[22:25]
	v_mfma_f32_16x16x32_bf16 v[10:13], v[138:141], v[182:185], v[10:13]
	v_mfma_f32_16x16x32_bf16 v[6:9], v[146:149], v[182:185], v[6:9]
	s_setprio 0
.LBB0_2724:
	s_barrier
	v_add_u32_e32 v3, 0x18000, v217
	ds_read_b128 v[150:153], v3
	ds_read_b128 v[154:157], v3 offset:1024
	ds_read_b128 v[158:161], v3 offset:2048
	ds_read_b128 v[162:165], v3 offset:3072
	v_add_u32_e32 v3, 0x1c000, v217
	ds_read_b128 v[134:137], v3
	ds_read_b128 v[138:141], v3 offset:1024
	ds_read_b128 v[142:145], v3 offset:2048
	ds_read_b128 v[146:149], v3 offset:3072
	s_add_u32 s55, s57, s55
	s_addc_u32 s57, s56, 0
	s_add_u32 s56, s55, 0x40000
	s_addc_u32 s57, s57, 0
	s_mov_b32 m0, s42
	v_lshl_add_u64 v[222:223], s[56:57], 0, v[198:199]
	s_waitcnt lgkmcnt(0)
	ds_read_b128 v[178:181], v220 offset:32768
	ds_read_b128 v[194:197], v220 offset:33792
	ds_read_b128 v[174:177], v220 offset:34816
	ds_read_b128 v[190:193], v220 offset:35840
	ds_read_b128 v[170:173], v220 offset:36864
	ds_read_b128 v[186:189], v220 offset:37888
	ds_read_b128 v[166:169], v220 offset:38912
	ds_read_b128 v[182:185], v220 offset:39936
	global_load_lds_dwordx4 v[222:223], off
	v_lshl_add_u64 v[222:223], s[56:57], 0, v[200:201]
	s_mov_b32 m0, s43
	s_nop 0
	global_load_lds_dwordx4 v[222:223], off
	s_waitcnt lgkmcnt(0)
	s_barrier
	s_setprio 1
	s_waitcnt lgkmcnt(0)
	v_mfma_f32_16x16x32_bf16 v[130:133], v[150:153], v[178:181], v[130:133]
	v_mfma_f32_16x16x32_bf16 v[126:129], v[158:161], v[178:181], v[126:129]
	v_mfma_f32_16x16x32_bf16 v[122:125], v[150:153], v[174:177], v[122:125]
	v_mfma_f32_16x16x32_bf16 v[118:121], v[158:161], v[174:177], v[118:121]
	v_mfma_f32_16x16x32_bf16 v[110:113], v[150:153], v[170:173], v[110:113]
	v_mfma_f32_16x16x32_bf16 v[102:105], v[158:161], v[170:173], v[102:105]
	v_mfma_f32_16x16x32_bf16 v[94:97], v[150:153], v[166:169], v[94:97]
	v_mfma_f32_16x16x32_bf16 v[86:89], v[158:161], v[166:169], v[86:89]
	v_mfma_f32_16x16x32_bf16 v[130:133], v[154:157], v[194:197], v[130:133]
	v_mfma_f32_16x16x32_bf16 v[126:129], v[162:165], v[194:197], v[126:129]
	v_mfma_f32_16x16x32_bf16 v[122:125], v[154:157], v[190:193], v[122:125]
	v_mfma_f32_16x16x32_bf16 v[118:121], v[162:165], v[190:193], v[118:121]
	v_mfma_f32_16x16x32_bf16 v[110:113], v[154:157], v[186:189], v[110:113]
	v_mfma_f32_16x16x32_bf16 v[102:105], v[162:165], v[186:189], v[102:105]
	v_mfma_f32_16x16x32_bf16 v[94:97], v[154:157], v[182:185], v[94:97]
	v_mfma_f32_16x16x32_bf16 v[86:89], v[162:165], v[182:185], v[86:89]
	v_mfma_f32_16x16x32_bf16 v[114:117], v[134:137], v[178:181], v[114:117]
	v_mfma_f32_16x16x32_bf16 v[106:109], v[142:145], v[178:181], v[106:109]
	v_mfma_f32_16x16x32_bf16 v[98:101], v[134:137], v[174:177], v[98:101]
	v_mfma_f32_16x16x32_bf16 v[90:93], v[142:145], v[174:177], v[90:93]
	v_mfma_f32_16x16x32_bf16 v[82:85], v[134:137], v[170:173], v[82:85]
	v_mfma_f32_16x16x32_bf16 v[78:81], v[142:145], v[170:173], v[78:81]
	v_mfma_f32_16x16x32_bf16 v[74:77], v[134:137], v[166:169], v[74:77]
	v_mfma_f32_16x16x32_bf16 v[70:73], v[142:145], v[166:169], v[70:73]
	v_mfma_f32_16x16x32_bf16 v[114:117], v[138:141], v[194:197], v[114:117]
	v_mfma_f32_16x16x32_bf16 v[106:109], v[146:149], v[194:197], v[106:109]
	v_mfma_f32_16x16x32_bf16 v[98:101], v[138:141], v[190:193], v[98:101]
	v_mfma_f32_16x16x32_bf16 v[90:93], v[146:149], v[190:193], v[90:93]
	v_mfma_f32_16x16x32_bf16 v[82:85], v[138:141], v[186:189], v[82:85]
	v_mfma_f32_16x16x32_bf16 v[78:81], v[146:149], v[186:189], v[78:81]
	v_mfma_f32_16x16x32_bf16 v[74:77], v[138:141], v[182:185], v[74:77]
	v_mfma_f32_16x16x32_bf16 v[70:73], v[146:149], v[182:185], v[70:73]
	s_setprio 0
	s_barrier
	s_and_b64 vcc, exec, s[4:5]
	s_cbranch_vccnz .LBB0_2726
	ds_read_b128 v[178:181], v220 offset:49152
	ds_read_b128 v[194:197], v220 offset:50176
	ds_read_b128 v[174:177], v220 offset:51200
	ds_read_b128 v[190:193], v220 offset:52224
	ds_read_b128 v[170:173], v220 offset:53248
	ds_read_b128 v[186:189], v220 offset:54272
	ds_read_b128 v[166:169], v220 offset:55296
	ds_read_b128 v[182:185], v220 offset:56320
; #define G8_STAGE_B(bufoff, gbase) do { _Pragma("unroll") for (int _i = 0; _i < 2; ++_i) \
;         __builtin_amdgcn_global_load_lds((const unsigned*)((const char*)(gbase) + voffB[_i]), (LAS unsigned*)(lds + (bufoff) + ldsw + _i * 8192), 16, 0, 0); } while (0)
; #define G8_LDA(dst, b, h) do { _Pragma("unroll") for (int m = 0; m < 4; ++m) _Pragma("unroll") for (int k = 0; k < 2; ++k) dst[m][k] = *(const LAS bf16x8*)(lds + G8_SA(b, h) + aoff + m * 2048 + k * 1024); } while (0)
; #define G8_MMA(ai, bj, At, Bt) do { __builtin_amdgcn_s_setprio(1); _Pragma("unroll") for (int m = 0; m < 4; ++m) _Pragma("unroll") for (int n = 0; n < 2; ++n) _Pragma("unroll") for (int k = 0; k < 2; ++k) \
;         acc[ai][bj][m][n] = __builtin_amdgcn_mfma_f32_16x16x32_bf16(Bt[n][k], At[m][k], acc[ai][bj][m][n], 0, 0, 0); __builtin_amdgcn_s_setprio(0); } while (0)
; #define G8_WAIT_V(n) asm volatile("s_waitcnt vmcnt(" #n ")" ::: "memory")
; #define G8_WAIT_L(n) asm volatile("s_waitcnt lgkmcnt(" #n ")" ::: "memory")
; #define G8_BAR __builtin_amdgcn_s_barrier()
; #define G8_SCHED __builtin_amdgcn_sched_barrier(0)
; template <class Sched, class Epi>
; DEVI void gemm_phase(LAS unsigned char* lds, const char* Abase, const int K, const Sched& S, const Epi& E) {
;     ...
;             if (!skip1) G8_LDA(At, 1, 1); G8_STAGE_B(G8_SB(1, 0), b3); G8_STAGE_A(G8_SA(1, 0), last, 0, k3); G8_STAGE_B(G8_SB(1, 1), b3 + hstepB);
;             G8_WAIT_V(6); G8_WAIT_L(0); G8_BAR; if (!skip1) { G8_MMA(1, 0, At, B0); G8_MMA(1, 1, At, B1); } G8_BAR; G8_SCHED;
.LBB0_2726:
	s_mov_b32 m0, s45
	v_lshl_add_u64 v[4:5], v[4:5], 0, s[12:13]
	global_load_lds_dwordx4 v[4:5], off
	v_lshl_add_u64 v[4:5], v[210:211], 0, s[12:13]
	s_mov_b32 m0, s46
	s_add_u32 s30, s30, 0x40080
	global_load_lds_dwordx4 v[4:5], off
	v_lshl_add_u64 v[4:5], v[212:213], 0, s[12:13]
	s_mov_b32 m0, s47
	s_addc_u32 s31, s31, 0
	global_load_lds_dwordx4 v[4:5], off
	v_lshl_add_u64 v[4:5], v[214:215], 0, s[12:13]
	s_mov_b32 m0, s48
	s_and_b64 vcc, exec, s[4:5]
	global_load_lds_dwordx4 v[4:5], off
	v_lshl_add_u64 v[4:5], s[30:31], 0, v[198:199]
	s_mov_b32 m0, s49
	s_nop 0
	global_load_lds_dwordx4 v[4:5], off
	v_lshl_add_u64 v[4:5], s[30:31], 0, v[200:201]
	s_mov_b32 m0, s50
	s_nop 0
	global_load_lds_dwordx4 v[4:5], off
	s_waitcnt vmcnt(6)
	s_waitcnt lgkmcnt(0)
	s_barrier
	s_cbranch_vccnz .LBB0_2728
	s_setprio 1
	s_waitcnt lgkmcnt(0)
	v_mfma_f32_16x16x32_bf16 v[66:69], v[150:153], v[178:181], v[66:69]
	v_mfma_f32_16x16x32_bf16 v[62:65], v[158:161], v[178:181], v[62:65]
	v_mfma_f32_16x16x32_bf16 v[50:53], v[150:153], v[174:177], v[50:53]
	v_mfma_f32_16x16x32_bf16 v[46:49], v[158:161], v[174:177], v[46:49]
	v_mfma_f32_16x16x32_bf16 v[34:37], v[150:153], v[170:173], v[34:37]
	v_mfma_f32_16x16x32_bf16 v[30:33], v[158:161], v[170:173], v[30:33]
	v_mfma_f32_16x16x32_bf16 v[18:21], v[150:153], v[166:169], v[18:21]
	v_mfma_f32_16x16x32_bf16 v[14:17], v[158:161], v[166:169], v[14:17]
	v_mfma_f32_16x16x32_bf16 v[66:69], v[154:157], v[194:197], v[66:69]
	v_mfma_f32_16x16x32_bf16 v[62:65], v[162:165], v[194:197], v[62:65]
	v_mfma_f32_16x16x32_bf16 v[50:53], v[154:157], v[190:193], v[50:53]
	v_mfma_f32_16x16x32_bf16 v[46:49], v[162:165], v[190:193], v[46:49]
	v_mfma_f32_16x16x32_bf16 v[34:37], v[154:157], v[186:189], v[34:37]
	v_mfma_f32_16x16x32_bf16 v[30:33], v[162:165], v[186:189], v[30:33]
	v_mfma_f32_16x16x32_bf16 v[18:21], v[154:157], v[182:185], v[18:21]
	v_mfma_f32_16x16x32_bf16 v[14:17], v[162:165], v[182:185], v[14:17]
	v_mfma_f32_16x16x32_bf16 v[58:61], v[134:137], v[178:181], v[58:61]
	v_mfma_f32_16x16x32_bf16 v[54:57], v[142:145], v[178:181], v[54:57]
	v_mfma_f32_16x16x32_bf16 v[42:45], v[134:137], v[174:177], v[42:45]
	v_mfma_f32_16x16x32_bf16 v[38:41], v[142:145], v[174:177], v[38:41]
	v_mfma_f32_16x16x32_bf16 v[26:29], v[134:137], v[170:173], v[26:29]
	v_mfma_f32_16x16x32_bf16 v[22:25], v[142:145], v[170:173], v[22:25]
	v_mfma_f32_16x16x32_bf16 v[10:13], v[134:137], v[166:169], v[10:13]
	v_mfma_f32_16x16x32_bf16 v[4:7], v[142:145], v[166:169], v[6:9]
	v_mfma_f32_16x16x32_bf16 v[58:61], v[138:141], v[194:197], v[58:61]
	v_mfma_f32_16x16x32_bf16 v[54:57], v[146:149], v[194:197], v[54:57]
	v_mfma_f32_16x16x32_bf16 v[42:45], v[138:141], v[190:193], v[42:45]
	v_mfma_f32_16x16x32_bf16 v[38:41], v[146:149], v[190:193], v[38:41]
	v_mfma_f32_16x16x32_bf16 v[26:29], v[138:141], v[186:189], v[26:29]
	v_mfma_f32_16x16x32_bf16 v[22:25], v[146:149], v[186:189], v[22:25]
	v_mfma_f32_16x16x32_bf16 v[10:13], v[138:141], v[182:185], v[10:13]
	v_mfma_f32_16x16x32_bf16 v[6:9], v[146:149], v[182:185], v[4:7]
	s_setprio 0

; #define G8_STAGE_B(bufoff, gbase) do { _Pragma("unroll") for (int _i = 0; _i < 2; ++_i) \
;         __builtin_amdgcn_global_load_lds((const unsigned*)((const char*)(gbase) + voffB[_i]), (LAS unsigned*)(lds + (bufoff) + ldsw + _i * 8192), 16, 0, 0); } while (0)
; #define G8_LDA(dst, b, h) do { _Pragma("unroll") for (int m = 0; m < 4; ++m) _Pragma("unroll") for (int k = 0; k < 2; ++k) dst[m][k] = *(const LAS bf16x8*)(lds + G8_SA(b, h) + aoff + m * 2048 + k * 1024); } while (0)
; #define G8_LDB(dst, b, h) do { _Pragma("unroll") for (int n = 0; n < 2; ++n) _Pragma("unroll") for (int k = 0; k < 2; ++k) dst[n][k] = *(const LAS bf16x8*)(lds + G8_SB(b, h) + boff + n * 2048 + k * 1024); } while (0)
; #define G8_MMA(ai, bj, At, Bt) do { __builtin_amdgcn_s_setprio(1); _Pragma("unroll") for (int m = 0; m < 4; ++m) _Pragma("unroll") for (int n = 0; n < 2; ++n) _Pragma("unroll") for (int k = 0; k < 2; ++k) \
;         acc[ai][bj][m][n] = __builtin_amdgcn_mfma_f32_16x16x32_bf16(Bt[n][k], At[m][k], acc[ai][bj][m][n], 0, 0, 0); __builtin_amdgcn_s_setprio(0); } while (0)
; #define G8_WAIT_V(n) asm volatile("s_waitcnt vmcnt(" #n ")" ::: "memory")
; #define G8_WAIT_L(n) asm volatile("s_waitcnt lgkmcnt(" #n ")" ::: "memory")
; #define G8_BAR __builtin_amdgcn_s_barrier()
; #define G8_SCHED __builtin_amdgcn_sched_barrier(0)
; template <class Sched, class Epi>
; DEVI void gemm_phase(LAS unsigned char* lds, const char* Abase, const int K, const Sched& S, const Epi& E) {
;     ...
;             G8_LDB(B0, 0, 0); G8_LDB(B1, 0, 1); G8_SCHED; G8_LDA(At, 0, 0); G8_STAGE_A(G8_SA(1, 1), false, 1, k1);
;             G8_WAIT_L(0); G8_BAR; G8_MMA(0, 0, At, B0); G8_MMA(0, 1, At, B1); G8_BAR; G8_SCHED;
;             if (!skip1) G8_LDA(At, 0, 1); G8_STAGE_B(G8_SB(0, 0), b2); G8_STAGE_A(G8_SA(0, 0), last, 0, k2); G8_STAGE_B(G8_SB(0, 1), b2 + hstepB);
;             G8_WAIT_V(6); G8_WAIT_L(0); G8_BAR; if (!skip1) { G8_MMA(1, 0, At, B0); G8_MMA(1, 1, At, B1); } G8_BAR; G8_SCHED;
.LBB0_3025:
	ds_read_b128 v[156:159], v225
	ds_read_b128 v[160:163], v225 offset:1024
	ds_read_b128 v[164:167], v225 offset:2048
	ds_read_b128 v[168:171], v225 offset:3072
	ds_read_b128 v[140:143], v226
	ds_read_b128 v[144:147], v226 offset:1024
	ds_read_b128 v[148:151], v226 offset:2048
	ds_read_b128 v[152:155], v226 offset:3072
	s_mov_b32 m0, s57
	v_lshl_add_u64 v[4:5], v[216:217], 0, s[28:29]
	s_waitcnt lgkmcnt(0)
	ds_read_b128 v[184:187], v227
	ds_read_b128 v[200:203], v227 offset:1024
	ds_read_b128 v[180:183], v227 offset:2048
	ds_read_b128 v[196:199], v227 offset:3072
	ds_read_b128 v[176:179], v227 offset:4096
	ds_read_b128 v[192:195], v227 offset:5120
	ds_read_b128 v[172:175], v227 offset:6144
	ds_read_b128 v[188:191], v227 offset:7168
	global_load_lds_dwordx4 v[4:5], off
	v_lshl_add_u64 v[4:5], v[214:215], 0, s[28:29]
	s_mov_b32 m0, s58
	s_nop 0
	global_load_lds_dwordx4 v[4:5], off
	s_waitcnt lgkmcnt(0)
	s_barrier
	s_setprio 1
	s_waitcnt lgkmcnt(0)
	v_mfma_f32_16x16x32_bf16 v[136:139], v[156:159], v[184:187], v[136:139]
	v_mfma_f32_16x16x32_bf16 v[132:135], v[164:167], v[184:187], v[132:135]
	v_mfma_f32_16x16x32_bf16 v[120:123], v[156:159], v[180:183], v[120:123]
	v_mfma_f32_16x16x32_bf16 v[116:119], v[164:167], v[180:183], v[116:119]
	v_mfma_f32_16x16x32_bf16 v[104:107], v[156:159], v[176:179], v[104:107]
	v_mfma_f32_16x16x32_bf16 v[100:103], v[164:167], v[176:179], v[100:103]
	v_mfma_f32_16x16x32_bf16 v[88:91], v[156:159], v[172:175], v[88:91]
	v_mfma_f32_16x16x32_bf16 v[84:87], v[164:167], v[172:175], v[84:87]
	v_mfma_f32_16x16x32_bf16 v[136:139], v[160:163], v[200:203], v[136:139]
	v_mfma_f32_16x16x32_bf16 v[132:135], v[168:171], v[200:203], v[132:135]
	v_mfma_f32_16x16x32_bf16 v[120:123], v[160:163], v[196:199], v[120:123]
	v_mfma_f32_16x16x32_bf16 v[116:119], v[168:171], v[196:199], v[116:119]
	v_mfma_f32_16x16x32_bf16 v[104:107], v[160:163], v[192:195], v[104:107]
	v_mfma_f32_16x16x32_bf16 v[100:103], v[168:171], v[192:195], v[100:103]
	v_mfma_f32_16x16x32_bf16 v[88:91], v[160:163], v[188:191], v[88:91]
	v_mfma_f32_16x16x32_bf16 v[84:87], v[168:171], v[188:191], v[84:87]
	v_mfma_f32_16x16x32_bf16 v[128:131], v[140:143], v[184:187], v[128:131]
	v_mfma_f32_16x16x32_bf16 v[124:127], v[148:151], v[184:187], v[124:127]
	v_mfma_f32_16x16x32_bf16 v[112:115], v[140:143], v[180:183], v[112:115]
	v_mfma_f32_16x16x32_bf16 v[108:111], v[148:151], v[180:183], v[108:111]
	v_mfma_f32_16x16x32_bf16 v[96:99], v[140:143], v[176:179], v[96:99]
	v_mfma_f32_16x16x32_bf16 v[92:95], v[148:151], v[176:179], v[92:95]
	v_mfma_f32_16x16x32_bf16 v[80:83], v[140:143], v[172:175], v[80:83]
	v_mfma_f32_16x16x32_bf16 v[76:79], v[148:151], v[172:175], v[76:79]
	v_mfma_f32_16x16x32_bf16 v[128:131], v[144:147], v[200:203], v[128:131]
	v_mfma_f32_16x16x32_bf16 v[124:127], v[152:155], v[200:203], v[124:127]
	v_mfma_f32_16x16x32_bf16 v[112:115], v[144:147], v[196:199], v[112:115]
	v_mfma_f32_16x16x32_bf16 v[108:111], v[152:155], v[196:199], v[108:111]
	v_mfma_f32_16x16x32_bf16 v[96:99], v[144:147], v[192:195], v[96:99]
	v_mfma_f32_16x16x32_bf16 v[92:95], v[152:155], v[192:195], v[92:95]
	v_mfma_f32_16x16x32_bf16 v[80:83], v[144:147], v[188:191], v[80:83]
	v_mfma_f32_16x16x32_bf16 v[76:79], v[152:155], v[188:191], v[76:79]
	s_setprio 0
	s_barrier
	s_and_b64 vcc, exec, s[4:5]
	s_cbranch_vccnz .LBB0_3027
	ds_read_b128 v[184:187], v227 offset:16384
	ds_read_b128 v[200:203], v227 offset:17408
	ds_read_b128 v[180:183], v227 offset:18432
	ds_read_b128 v[196:199], v227 offset:19456
	ds_read_b128 v[176:179], v227 offset:20480
	ds_read_b128 v[192:195], v227 offset:21504
	ds_read_b128 v[172:175], v227 offset:22528
	ds_read_b128 v[188:191], v227 offset:23552

; #define G8_STAGE_B(bufoff, gbase) do { _Pragma("unroll") for (int _i = 0; _i < 2; ++_i) \
;         __builtin_amdgcn_global_load_lds((const unsigned*)((const char*)(gbase) + voffB[_i]), (LAS unsigned*)(lds + (bufoff) + ldsw + _i * 8192), 16, 0, 0); } while (0)
; #define G8_LDA(dst, b, h) do { _Pragma("unroll") for (int m = 0; m < 4; ++m) _Pragma("unroll") for (int k = 0; k < 2; ++k) dst[m][k] = *(const LAS bf16x8*)(lds + G8_SA(b, h) + aoff + m * 2048 + k * 1024); } while (0)
; #define G8_LDB(dst, b, h) do { _Pragma("unroll") for (int n = 0; n < 2; ++n) _Pragma("unroll") for (int k = 0; k < 2; ++k) dst[n][k] = *(const LAS bf16x8*)(lds + G8_SB(b, h) + boff + n * 2048 + k * 1024); } while (0)
; #define G8_MMA(ai, bj, At, Bt) do { __builtin_amdgcn_s_setprio(1); _Pragma("unroll") for (int m = 0; m < 4; ++m) _Pragma("unroll") for (int n = 0; n < 2; ++n) _Pragma("unroll") for (int k = 0; k < 2; ++k) \
;         acc[ai][bj][m][n] = __builtin_amdgcn_mfma_f32_16x16x32_bf16(Bt[n][k], At[m][k], acc[ai][bj][m][n], 0, 0, 0); __builtin_amdgcn_s_setprio(0); } while (0)
; #define G8_WAIT_L(n) asm volatile("s_waitcnt lgkmcnt(" #n ")" ::: "memory")
; #define G8_BAR __builtin_amdgcn_s_barrier()
; #define G8_SCHED __builtin_amdgcn_sched_barrier(0)
; template <class Sched, class Epi>
; DEVI void gemm_phase(LAS unsigned char* lds, const char* Abase, const int K, const Sched& S, const Epi& E) {
;     ...
;             G8_LDB(B0, 1, 0); G8_LDB(B1, 1, 1); G8_SCHED; G8_LDA(At, 1, 0); G8_STAGE_A(G8_SA(0, 1), last, 1, k2);
;             G8_WAIT_L(0); G8_BAR; G8_MMA(0, 0, At, B0); G8_MMA(0, 1, At, B1); G8_BAR; G8_SCHED;
;             if (!skip1) G8_LDA(At, 1, 1); G8_STAGE_B(G8_SB(1, 0), b3); G8_STAGE_A(G8_SA(1, 0), last, 0, k3); G8_STAGE_B(G8_SB(1, 1), b3 + hstepB);
.LBB0_3037:
	v_lshl_add_u64 v[222:223], s[30:31], 0, v[222:223]
	s_mov_b32 m0, s46
	s_nop 0
	global_load_lds_dwordx4 v[222:223], off
	s_waitcnt lgkmcnt(0)
	s_barrier
	s_setprio 1
	s_waitcnt lgkmcnt(0)
	v_mfma_f32_16x16x32_bf16 v[136:139], v[156:159], v[184:187], v[136:139]
	v_mfma_f32_16x16x32_bf16 v[132:135], v[164:167], v[184:187], v[132:135]
	v_mfma_f32_16x16x32_bf16 v[120:123], v[156:159], v[180:183], v[120:123]
	v_mfma_f32_16x16x32_bf16 v[116:119], v[164:167], v[180:183], v[116:119]
	v_mfma_f32_16x16x32_bf16 v[104:107], v[156:159], v[176:179], v[104:107]
	v_mfma_f32_16x16x32_bf16 v[100:103], v[164:167], v[176:179], v[100:103]
	v_mfma_f32_16x16x32_bf16 v[88:91], v[156:159], v[172:175], v[88:91]
	v_mfma_f32_16x16x32_bf16 v[84:87], v[164:167], v[172:175], v[84:87]
	v_mfma_f32_16x16x32_bf16 v[136:139], v[160:163], v[200:203], v[136:139]
	v_mfma_f32_16x16x32_bf16 v[132:135], v[168:171], v[200:203], v[132:135]
	v_mfma_f32_16x16x32_bf16 v[120:123], v[160:163], v[196:199], v[120:123]
	v_mfma_f32_16x16x32_bf16 v[116:119], v[168:171], v[196:199], v[116:119]
	v_mfma_f32_16x16x32_bf16 v[104:107], v[160:163], v[192:195], v[104:107]
	v_mfma_f32_16x16x32_bf16 v[100:103], v[168:171], v[192:195], v[100:103]
	v_mfma_f32_16x16x32_bf16 v[88:91], v[160:163], v[188:191], v[88:91]
	v_mfma_f32_16x16x32_bf16 v[84:87], v[168:171], v[188:191], v[84:87]
	v_mfma_f32_16x16x32_bf16 v[128:131], v[140:143], v[184:187], v[128:131]
	v_mfma_f32_16x16x32_bf16 v[124:127], v[148:151], v[184:187], v[124:127]
	v_mfma_f32_16x16x32_bf16 v[112:115], v[140:143], v[180:183], v[112:115]
	v_mfma_f32_16x16x32_bf16 v[108:111], v[148:151], v[180:183], v[108:111]
	v_mfma_f32_16x16x32_bf16 v[96:99], v[140:143], v[176:179], v[96:99]
	v_mfma_f32_16x16x32_bf16 v[92:95], v[148:151], v[176:179], v[92:95]
	v_mfma_f32_16x16x32_bf16 v[80:83], v[140:143], v[172:175], v[80:83]
	v_mfma_f32_16x16x32_bf16 v[76:79], v[148:151], v[172:175], v[76:79]
	v_mfma_f32_16x16x32_bf16 v[128:131], v[144:147], v[200:203], v[128:131]
	v_mfma_f32_16x16x32_bf16 v[124:127], v[152:155], v[200:203], v[124:127]
	v_mfma_f32_16x16x32_bf16 v[112:115], v[144:147], v[196:199], v[112:115]
	v_mfma_f32_16x16x32_bf16 v[108:111], v[152:155], v[196:199], v[108:111]
	v_mfma_f32_16x16x32_bf16 v[96:99], v[144:147], v[192:195], v[96:99]
	v_mfma_f32_16x16x32_bf16 v[92:95], v[152:155], v[192:195], v[92:95]
	v_mfma_f32_16x16x32_bf16 v[80:83], v[144:147], v[188:191], v[80:83]
	v_mfma_f32_16x16x32_bf16 v[76:79], v[152:155], v[188:191], v[76:79]
	s_setprio 0
	s_barrier
	s_and_b64 vcc, exec, s[4:5]
	s_cbranch_vccnz .LBB0_3039
	ds_read_b128 v[184:187], v227 offset:49152
	ds_read_b128 v[200:203], v227 offset:50176
	ds_read_b128 v[180:183], v227 offset:51200
	ds_read_b128 v[196:199], v227 offset:52224
	ds_read_b128 v[176:179], v227 offset:53248
	ds_read_b128 v[192:195], v227 offset:54272
	ds_read_b128 v[172:175], v227 offset:55296
	ds_read_b128 v[188:191], v227 offset:56320

; #define G8_STAGE_B(bufoff, gbase) do { _Pragma("unroll") for (int _i = 0; _i < 2; ++_i) \
;         __builtin_amdgcn_global_load_lds((const unsigned*)((const char*)(gbase) + voffB[_i]), (LAS unsigned*)(lds + (bufoff) + ldsw + _i * 8192), 16, 0, 0); } while (0)
; #define G8_LDA(dst, b, h) do { _Pragma("unroll") for (int m = 0; m < 4; ++m) _Pragma("unroll") for (int k = 0; k < 2; ++k) dst[m][k] = *(const LAS bf16x8*)(lds + G8_SA(b, h) + aoff + m * 2048 + k * 1024); } while (0)
; #define G8_MMA(ai, bj, At, Bt) do { __builtin_amdgcn_s_setprio(1); _Pragma("unroll") for (int m = 0; m < 4; ++m) _Pragma("unroll") for (int n = 0; n < 2; ++n) _Pragma("unroll") for (int k = 0; k < 2; ++k) \
;         acc[ai][bj][m][n] = __builtin_amdgcn_mfma_f32_16x16x32_bf16(Bt[n][k], At[m][k], acc[ai][bj][m][n], 0, 0, 0); __builtin_amdgcn_s_setprio(0); } while (0)
; #define G8_WAIT_V(n) asm volatile("s_waitcnt vmcnt(" #n ")" ::: "memory")
; #define G8_WAIT_L(n) asm volatile("s_waitcnt lgkmcnt(" #n ")" ::: "memory")
; #define G8_BAR __builtin_amdgcn_s_barrier()
; #define G8_SCHED __builtin_amdgcn_sched_barrier(0)
; template <class Sched, class Epi>
; DEVI void gemm_phase(LAS unsigned char* lds, const char* Abase, const int K, const Sched& S, const Epi& E) {
;     ...
;             if (!skip1) G8_LDA(At, 1, 1); G8_STAGE_B(G8_SB(1, 0), b3); G8_STAGE_A(G8_SA(1, 0), last, 0, k3); G8_STAGE_B(G8_SB(1, 1), b3 + hstepB);
;             G8_WAIT_V(6); G8_WAIT_L(0); G8_BAR; if (!skip1) { G8_MMA(1, 0, At, B0); G8_MMA(1, 1, At, B1); } G8_BAR; G8_SCHED;
.LBB0_3043:
	v_lshl_add_u64 v[4:5], s[30:31], 0, v[2:3]
	s_add_u32 s28, s28, 0x40080
	s_mov_b32 m0, s52
	v_lshl_add_u64 v[4:5], v[4:5], 0, s[16:17]
	s_addc_u32 s29, s29, 0
	global_load_lds_dwordx4 v[4:5], off
	v_lshl_add_u64 v[4:5], s[28:29], 0, v[204:205]
	s_mov_b32 m0, s53
	s_and_b64 vcc, exec, s[4:5]
	global_load_lds_dwordx4 v[4:5], off
	v_lshl_add_u64 v[4:5], s[28:29], 0, v[206:207]
	s_mov_b32 m0, s54
	s_nop 0
	global_load_lds_dwordx4 v[4:5], off
	s_waitcnt vmcnt(6)
	s_waitcnt lgkmcnt(0)
	s_barrier
	s_cbranch_vccnz .LBB0_3045
	s_setprio 1
	s_waitcnt lgkmcnt(0)
	v_mfma_f32_16x16x32_bf16 v[72:75], v[156:159], v[184:187], v[72:75]
	v_mfma_f32_16x16x32_bf16 v[68:71], v[164:167], v[184:187], v[68:71]
	v_mfma_f32_16x16x32_bf16 v[56:59], v[156:159], v[180:183], v[56:59]
	v_mfma_f32_16x16x32_bf16 v[52:55], v[164:167], v[180:183], v[52:55]
	v_mfma_f32_16x16x32_bf16 v[40:43], v[156:159], v[176:179], v[40:43]
	v_mfma_f32_16x16x32_bf16 v[36:39], v[164:167], v[176:179], v[36:39]
	v_mfma_f32_16x16x32_bf16 v[24:27], v[156:159], v[172:175], v[24:27]
	v_mfma_f32_16x16x32_bf16 v[20:23], v[164:167], v[172:175], v[20:23]
	v_mfma_f32_16x16x32_bf16 v[72:75], v[160:163], v[200:203], v[72:75]
	v_mfma_f32_16x16x32_bf16 v[68:71], v[168:171], v[200:203], v[68:71]
	v_mfma_f32_16x16x32_bf16 v[56:59], v[160:163], v[196:199], v[56:59]
	v_mfma_f32_16x16x32_bf16 v[52:55], v[168:171], v[196:199], v[52:55]
	v_mfma_f32_16x16x32_bf16 v[40:43], v[160:163], v[192:195], v[40:43]
	v_mfma_f32_16x16x32_bf16 v[36:39], v[168:171], v[192:195], v[36:39]
	v_mfma_f32_16x16x32_bf16 v[24:27], v[160:163], v[188:191], v[24:27]
	v_mfma_f32_16x16x32_bf16 v[20:23], v[168:171], v[188:191], v[20:23]
	v_mfma_f32_16x16x32_bf16 v[64:67], v[140:143], v[184:187], v[64:67]
	v_mfma_f32_16x16x32_bf16 v[60:63], v[148:151], v[184:187], v[60:63]
	v_mfma_f32_16x16x32_bf16 v[48:51], v[140:143], v[180:183], v[48:51]
	v_mfma_f32_16x16x32_bf16 v[44:47], v[148:151], v[180:183], v[44:47]
	v_mfma_f32_16x16x32_bf16 v[32:35], v[140:143], v[176:179], v[32:35]
	v_mfma_f32_16x16x32_bf16 v[28:31], v[148:151], v[176:179], v[28:31]
	v_mfma_f32_16x16x32_bf16 v[16:19], v[140:143], v[172:175], v[16:19]
	v_mfma_f32_16x16x32_bf16 v[12:15], v[148:151], v[172:175], v[12:15]
	v_mfma_f32_16x16x32_bf16 v[64:67], v[144:147], v[200:203], v[64:67]
	v_mfma_f32_16x16x32_bf16 v[60:63], v[152:155], v[200:203], v[60:63]
	v_mfma_f32_16x16x32_bf16 v[48:51], v[144:147], v[196:199], v[48:51]
	v_mfma_f32_16x16x32_bf16 v[44:47], v[152:155], v[196:199], v[44:47]
	v_mfma_f32_16x16x32_bf16 v[32:35], v[144:147], v[192:195], v[32:35]
	v_mfma_f32_16x16x32_bf16 v[28:31], v[152:155], v[192:195], v[28:31]
	v_mfma_f32_16x16x32_bf16 v[16:19], v[144:147], v[188:191], v[16:19]
	v_mfma_f32_16x16x32_bf16 v[12:15], v[152:155], v[188:191], v[12:15]
	s_setprio 0

; #define G8_STAGE_B(bufoff, gbase) do { _Pragma("unroll") for (int _i = 0; _i < 2; ++_i) \
;         __builtin_amdgcn_global_load_lds((const unsigned*)((const char*)(gbase) + voffB[_i]), (LAS unsigned*)(lds + (bufoff) + ldsw + _i * 8192), 16, 0, 0); } while (0)
; #define G8_LDA(dst, b, h) do { _Pragma("unroll") for (int m = 0; m < 4; ++m) _Pragma("unroll") for (int k = 0; k < 2; ++k) dst[m][k] = *(const LAS bf16x8*)(lds + G8_SA(b, h) + aoff + m * 2048 + k * 1024); } while (0)
; #define G8_LDB(dst, b, h) do { _Pragma("unroll") for (int n = 0; n < 2; ++n) _Pragma("unroll") for (int k = 0; k < 2; ++k) dst[n][k] = *(const LAS bf16x8*)(lds + G8_SB(b, h) + boff + n * 2048 + k * 1024); } while (0)
; #define G8_MMA(ai, bj, At, Bt) do { __builtin_amdgcn_s_setprio(1); _Pragma("unroll") for (int m = 0; m < 4; ++m) _Pragma("unroll") for (int n = 0; n < 2; ++n) _Pragma("unroll") for (int k = 0; k < 2; ++k) \
;         acc[ai][bj][m][n] = __builtin_amdgcn_mfma_f32_16x16x32_bf16(Bt[n][k], At[m][k], acc[ai][bj][m][n], 0, 0, 0); __builtin_amdgcn_s_setprio(0); } while (0)
; #define G8_WAIT_V(n) asm volatile("s_waitcnt vmcnt(" #n ")" ::: "memory")
; #define G8_WAIT_L(n) asm volatile("s_waitcnt lgkmcnt(" #n ")" ::: "memory")
; #define G8_BAR __builtin_amdgcn_s_barrier()
; #define G8_SCHED __builtin_amdgcn_sched_barrier(0)
; template <class Sched, class Epi>
; DEVI void gemm_phase(LAS unsigned char* lds, const char* Abase, const int K, const Sched& S, const Epi& E) {
;     ...
;             G8_LDB(B0, 0, 0); G8_LDB(B1, 0, 1); G8_SCHED; G8_LDA(At, 0, 0); G8_STAGE_A(G8_SA(1, 1), false, 1, k1);
;             G8_WAIT_L(0); G8_BAR; G8_MMA(0, 0, At, B0); G8_MMA(0, 1, At, B1); G8_BAR; G8_SCHED;
;             if (!skip1) G8_LDA(At, 0, 1); G8_STAGE_B(G8_SB(0, 0), b2); G8_STAGE_A(G8_SA(0, 0), last, 0, k2); G8_STAGE_B(G8_SB(0, 1), b2 + hstepB);
;             G8_WAIT_V(6); G8_WAIT_L(0); G8_BAR; if (!skip1) { G8_MMA(1, 0, At, B0); G8_MMA(1, 1, At, B1); } G8_BAR; G8_SCHED;
.LBB0_3179:
	ds_read_b128 v[12:15], v229
	ds_read_b128 v[16:19], v229 offset:1024
	ds_read_b128 v[36:39], v229 offset:2048
	ds_read_b128 v[40:43], v229 offset:3072
	ds_read_b128 v[20:23], v230
	ds_read_b128 v[24:27], v230 offset:1024
	ds_read_b128 v[140:143], v230 offset:2048
	ds_read_b128 v[144:147], v230 offset:3072
	v_cmp_lt_i32_e64 s[6:7], s57, v4
	s_add_u32 s4, s38, 0x10080
	s_addc_u32 s5, s39, 0
	s_mov_b32 m0, s58
	v_lshl_add_u64 v[8:9], s[4:5], 0, v[2:3]
	ds_read_b128 v[56:59], v231
	ds_read_b128 v[68:71], v231 offset:1024
	ds_read_b128 v[52:55], v231 offset:2048
	ds_read_b128 v[164:167], v231 offset:3072
	ds_read_b128 v[152:155], v231 offset:4096
	ds_read_b128 v[160:163], v231 offset:5120
	ds_read_b128 v[148:151], v231 offset:6144
	ds_read_b128 v[156:159], v231 offset:7168
	global_load_lds_dwordx4 v[8:9], off
	v_lshl_add_u64 v[8:9], s[4:5], 0, v[220:221]
	s_mov_b32 m0, s59
	s_nop 0
	global_load_lds_dwordx4 v[8:9], off
	s_waitcnt lgkmcnt(0)
	s_barrier
	s_setprio 1
	s_waitcnt lgkmcnt(0)
	v_mfma_f32_16x16x32_bf16 v[28:31], v[12:15], v[56:59], 0
	v_mfma_f32_16x16x32_bf16 v[76:79], v[16:19], v[68:71], v[28:31]
	v_mfma_f32_16x16x32_bf16 v[28:31], v[36:39], v[56:59], 0
	v_mfma_f32_16x16x32_bf16 v[80:83], v[40:43], v[68:71], v[28:31]
	v_mfma_f32_16x16x32_bf16 v[28:31], v[12:15], v[52:55], 0
	v_mfma_f32_16x16x32_bf16 v[84:87], v[16:19], v[164:167], v[28:31]
	v_mfma_f32_16x16x32_bf16 v[28:31], v[36:39], v[52:55], 0
	v_mfma_f32_16x16x32_bf16 v[88:91], v[40:43], v[164:167], v[28:31]
	v_mfma_f32_16x16x32_bf16 v[28:31], v[12:15], v[152:155], 0
	v_mfma_f32_16x16x32_bf16 v[92:95], v[16:19], v[160:163], v[28:31]
	v_mfma_f32_16x16x32_bf16 v[28:31], v[36:39], v[152:155], 0
	v_mfma_f32_16x16x32_bf16 v[96:99], v[40:43], v[160:163], v[28:31]
	v_mfma_f32_16x16x32_bf16 v[28:31], v[12:15], v[148:151], 0
	v_mfma_f32_16x16x32_bf16 v[100:103], v[16:19], v[156:159], v[28:31]
	v_mfma_f32_16x16x32_bf16 v[28:31], v[36:39], v[148:151], 0
	v_mfma_f32_16x16x32_bf16 v[104:107], v[40:43], v[156:159], v[28:31]
	v_mfma_f32_16x16x32_bf16 v[28:31], v[20:23], v[56:59], 0
	v_mfma_f32_16x16x32_bf16 v[108:111], v[24:27], v[68:71], v[28:31]
	v_mfma_f32_16x16x32_bf16 v[28:31], v[140:143], v[56:59], 0
	v_mfma_f32_16x16x32_bf16 v[112:115], v[144:147], v[68:71], v[28:31]
	v_mfma_f32_16x16x32_bf16 v[28:31], v[20:23], v[52:55], 0
	v_mfma_f32_16x16x32_bf16 v[116:119], v[24:27], v[164:167], v[28:31]
	v_mfma_f32_16x16x32_bf16 v[28:31], v[140:143], v[52:55], 0
	v_mfma_f32_16x16x32_bf16 v[120:123], v[144:147], v[164:167], v[28:31]
	v_mfma_f32_16x16x32_bf16 v[28:31], v[20:23], v[152:155], 0
	v_mfma_f32_16x16x32_bf16 v[124:127], v[24:27], v[160:163], v[28:31]
	v_mfma_f32_16x16x32_bf16 v[28:31], v[140:143], v[152:155], 0
	v_mfma_f32_16x16x32_bf16 v[128:131], v[144:147], v[160:163], v[28:31]
	v_mfma_f32_16x16x32_bf16 v[28:31], v[20:23], v[148:151], 0
	v_mfma_f32_16x16x32_bf16 v[132:135], v[24:27], v[156:159], v[28:31]
	v_mfma_f32_16x16x32_bf16 v[28:31], v[140:143], v[148:151], 0
	v_mfma_f32_16x16x32_bf16 v[136:139], v[144:147], v[156:159], v[28:31]
	s_setprio 0
	s_barrier
	s_and_b64 vcc, exec, s[6:7]
	s_cbranch_vccz .LBB0_3181
	ds_read_b128 v[56:59], v231 offset:16384
	ds_read_b128 v[68:71], v231 offset:17408
	ds_read_b128 v[52:55], v231 offset:18432
	ds_read_b128 v[164:167], v231 offset:19456
	ds_read_b128 v[152:155], v231 offset:20480
	ds_read_b128 v[160:163], v231 offset:21504
	ds_read_b128 v[148:151], v231 offset:22528
	ds_read_b128 v[156:159], v231 offset:23552
.LBB0_3181:
	v_lshl_add_u64 v[204:205], s[40:41], 0, v[2:3]
	s_mov_b32 m0, s17
	v_lshl_add_u64 v[8:9], v[204:205], 0, s[22:23]
	v_lshl_add_u64 v[206:207], s[40:41], 0, v[220:221]
	global_load_lds_dwordx4 v[8:9], off
	v_lshl_add_u64 v[8:9], v[206:207], 0, s[22:23]
	s_mov_b32 m0, s42
	v_lshl_add_u64 v[208:209], s[38:39], 0, v[2:3]
	global_load_lds_dwordx4 v[8:9], off
	v_lshl_add_u64 v[8:9], v[208:209], 0, s[22:23]
	s_mov_b32 m0, s15
	v_lshl_add_u64 v[210:211], s[38:39], 0, v[220:221]
	s_add_u32 s4, s40, 0x10100
	global_load_lds_dwordx4 v[8:9], off
	v_lshl_add_u64 v[8:9], v[210:211], 0, s[22:23]
	s_mov_b32 m0, s43
	s_addc_u32 s5, s41, 0
	global_load_lds_dwordx4 v[8:9], off
	v_lshl_add_u64 v[8:9], s[4:5], 0, v[2:3]
	s_mov_b32 m0, s44
	v_cndmask_b32_e64 v7, 0, 1, s[6:7]
	global_load_lds_dwordx4 v[8:9], off
	v_lshl_add_u64 v[8:9], s[4:5], 0, v[220:221]
	s_mov_b32 m0, s45
	v_cmp_ne_u32_e64 s[4:5], 1, v7
	global_load_lds_dwordx4 v[8:9], off
	s_waitcnt vmcnt(6)
	s_waitcnt lgkmcnt(0)
	s_andn2_b64 vcc, exec, s[6:7]
	s_barrier
	s_cbranch_vccnz .LBB0_3183
	s_setprio 1
	s_waitcnt lgkmcnt(0)
	v_mfma_f32_16x16x32_bf16 v[28:31], v[12:15], v[56:59], 0
	v_mfma_f32_16x16x32_bf16 v[64:67], v[16:19], v[68:71], v[28:31]
	v_mfma_f32_16x16x32_bf16 v[28:31], v[36:39], v[56:59], 0
	v_mfma_f32_16x16x32_bf16 v[60:63], v[40:43], v[68:71], v[28:31]
	v_mfma_f32_16x16x32_bf16 v[28:31], v[12:15], v[52:55], 0
	v_mfma_f32_16x16x32_bf16 v[48:51], v[16:19], v[164:167], v[28:31]
	v_mfma_f32_16x16x32_bf16 v[28:31], v[36:39], v[52:55], 0
	v_mfma_f32_16x16x32_bf16 v[44:47], v[40:43], v[164:167], v[28:31]
	v_mfma_f32_16x16x32_bf16 v[28:31], v[12:15], v[152:155], 0
	v_mfma_f32_16x16x32_bf16 v[12:15], v[12:15], v[148:151], 0
	v_mfma_f32_16x16x32_bf16 v[32:35], v[16:19], v[160:163], v[28:31]
	v_mfma_f32_16x16x32_bf16 v[28:31], v[36:39], v[152:155], 0
	v_mfma_f32_16x16x32_bf16 v[16:19], v[16:19], v[156:159], v[12:15]
	v_mfma_f32_16x16x32_bf16 v[12:15], v[36:39], v[148:151], 0
	v_mfma_f32_16x16x32_bf16 v[28:31], v[40:43], v[160:163], v[28:31]
	v_mfma_f32_16x16x32_bf16 v[12:15], v[40:43], v[156:159], v[12:15]
	v_mfma_f32_16x16x32_bf16 v[36:39], v[20:23], v[56:59], 0
	v_mfma_f32_16x16x32_bf16 v[72:75], v[24:27], v[68:71], v[36:39]
	v_mfma_f32_16x16x32_bf16 v[36:39], v[140:143], v[56:59], 0
	v_mfma_f32_16x16x32_bf16 v[68:71], v[144:147], v[68:71], v[36:39]
	v_mfma_f32_16x16x32_bf16 v[36:39], v[20:23], v[52:55], 0
	v_mfma_f32_16x16x32_bf16 v[56:59], v[24:27], v[164:167], v[36:39]
	v_mfma_f32_16x16x32_bf16 v[36:39], v[140:143], v[52:55], 0
	v_mfma_f32_16x16x32_bf16 v[52:55], v[144:147], v[164:167], v[36:39]
	v_mfma_f32_16x16x32_bf16 v[36:39], v[20:23], v[152:155], 0
	v_mfma_f32_16x16x32_bf16 v[20:23], v[20:23], v[148:151], 0
	v_mfma_f32_16x16x32_bf16 v[40:43], v[24:27], v[160:163], v[36:39]
	v_mfma_f32_16x16x32_bf16 v[36:39], v[140:143], v[152:155], 0
	v_mfma_f32_16x16x32_bf16 v[24:27], v[24:27], v[156:159], v[20:23]
	v_mfma_f32_16x16x32_bf16 v[20:23], v[140:143], v[148:151], 0
	v_mfma_f32_16x16x32_bf16 v[36:39], v[144:147], v[160:163], v[36:39]
	v_mfma_f32_16x16x32_bf16 v[20:23], v[144:147], v[156:159], v[20:23]
	s_setprio 0
	s_branch .LBB0_3184

; #define G8_STAGE_B(bufoff, gbase) do { _Pragma("unroll") for (int _i = 0; _i < 2; ++_i) \
;         __builtin_amdgcn_global_load_lds((const unsigned*)((const char*)(gbase) + voffB[_i]), (LAS unsigned*)(lds + (bufoff) + ldsw + _i * 8192), 16, 0, 0); } while (0)
; #define G8_LDA(dst, b, h) do { _Pragma("unroll") for (int m = 0; m < 4; ++m) _Pragma("unroll") for (int k = 0; k < 2; ++k) dst[m][k] = *(const LAS bf16x8*)(lds + G8_SA(b, h) + aoff + m * 2048 + k * 1024); } while (0)
; #define G8_LDB(dst, b, h) do { _Pragma("unroll") for (int n = 0; n < 2; ++n) _Pragma("unroll") for (int k = 0; k < 2; ++k) dst[n][k] = *(const LAS bf16x8*)(lds + G8_SB(b, h) + boff + n * 2048 + k * 1024); } while (0)
; #define G8_MMA(ai, bj, At, Bt) do { __builtin_amdgcn_s_setprio(1); _Pragma("unroll") for (int m = 0; m < 4; ++m) _Pragma("unroll") for (int n = 0; n < 2; ++n) _Pragma("unroll") for (int k = 0; k < 2; ++k) \
;         acc[ai][bj][m][n] = __builtin_amdgcn_mfma_f32_16x16x32_bf16(Bt[n][k], At[m][k], acc[ai][bj][m][n], 0, 0, 0); __builtin_amdgcn_s_setprio(0); } while (0)
; #define G8_WAIT_V(n) asm volatile("s_waitcnt vmcnt(" #n ")" ::: "memory")
; #define G8_WAIT_L(n) asm volatile("s_waitcnt lgkmcnt(" #n ")" ::: "memory")
; #define G8_BAR __builtin_amdgcn_s_barrier()
; #define G8_SCHED __builtin_amdgcn_sched_barrier(0)
; template <class Sched, class Epi>
; DEVI void gemm_phase(LAS unsigned char* lds, const char* Abase, const int K, const Sched& S, const Epi& E) {
;     ...
;             G8_LDB(B0, 1, 0); G8_LDB(B1, 1, 1); G8_SCHED; G8_LDA(At, 1, 0); G8_STAGE_A(G8_SA(0, 1), last, 1, k2);
;             G8_WAIT_L(0); G8_BAR; G8_MMA(0, 0, At, B0); G8_MMA(0, 1, At, B1); G8_BAR; G8_SCHED;
;             if (!skip1) G8_LDA(At, 1, 1); G8_STAGE_B(G8_SB(1, 0), b3); G8_STAGE_A(G8_SA(1, 0), last, 0, k3); G8_STAGE_B(G8_SB(1, 1), b3 + hstepB);
;             G8_WAIT_V(6); G8_WAIT_L(0); G8_BAR; if (!skip1) { G8_MMA(1, 0, At, B0); G8_MMA(1, 1, At, B1); } G8_BAR; G8_SCHED;
.LBB0_3184:
	s_barrier
	v_add_u32_e32 v7, 0x18000, v228
	v_add_u32_e32 v11, 0x1c000, v228
	ds_read_b128 v[156:159], v7
	ds_read_b128 v[160:163], v7 offset:1024
	ds_read_b128 v[164:167], v7 offset:2048
	ds_read_b128 v[168:171], v7 offset:3072
	ds_read_b128 v[140:143], v11
	ds_read_b128 v[144:147], v11 offset:1024
	ds_read_b128 v[148:151], v11 offset:2048
	ds_read_b128 v[152:155], v11 offset:3072
	s_add_u32 s6, s38, 0x10100
	s_addc_u32 s7, s39, 0
	s_mov_b32 m0, s46
	v_lshl_add_u64 v[8:9], s[6:7], 0, v[2:3]
	ds_read_b128 v[184:187], v231 offset:32768
	ds_read_b128 v[200:203], v231 offset:33792
	ds_read_b128 v[180:183], v231 offset:34816
	ds_read_b128 v[196:199], v231 offset:35840
	ds_read_b128 v[176:179], v231 offset:36864
	ds_read_b128 v[192:195], v231 offset:37888
	ds_read_b128 v[172:175], v231 offset:38912
	ds_read_b128 v[188:191], v231 offset:39936
	global_load_lds_dwordx4 v[8:9], off
	v_lshl_add_u64 v[8:9], s[6:7], 0, v[220:221]
	s_mov_b32 m0, s47
	s_nop 0
	global_load_lds_dwordx4 v[8:9], off
	s_waitcnt lgkmcnt(0)
	s_barrier
	s_setprio 1
	s_waitcnt lgkmcnt(0)
	v_mfma_f32_16x16x32_bf16 v[76:79], v[156:159], v[184:187], v[76:79]
	v_mfma_f32_16x16x32_bf16 v[80:83], v[164:167], v[184:187], v[80:83]
	v_mfma_f32_16x16x32_bf16 v[84:87], v[156:159], v[180:183], v[84:87]
	v_mfma_f32_16x16x32_bf16 v[88:91], v[164:167], v[180:183], v[88:91]
	v_mfma_f32_16x16x32_bf16 v[92:95], v[156:159], v[176:179], v[92:95]
	v_mfma_f32_16x16x32_bf16 v[96:99], v[164:167], v[176:179], v[96:99]
	v_mfma_f32_16x16x32_bf16 v[100:103], v[156:159], v[172:175], v[100:103]
	v_mfma_f32_16x16x32_bf16 v[104:107], v[164:167], v[172:175], v[104:107]
	v_mfma_f32_16x16x32_bf16 v[76:79], v[160:163], v[200:203], v[76:79]
	v_mfma_f32_16x16x32_bf16 v[80:83], v[168:171], v[200:203], v[80:83]
	v_mfma_f32_16x16x32_bf16 v[84:87], v[160:163], v[196:199], v[84:87]
	v_mfma_f32_16x16x32_bf16 v[88:91], v[168:171], v[196:199], v[88:91]
	v_mfma_f32_16x16x32_bf16 v[92:95], v[160:163], v[192:195], v[92:95]
	v_mfma_f32_16x16x32_bf16 v[96:99], v[168:171], v[192:195], v[96:99]
	v_mfma_f32_16x16x32_bf16 v[100:103], v[160:163], v[188:191], v[100:103]
	v_mfma_f32_16x16x32_bf16 v[104:107], v[168:171], v[188:191], v[104:107]
	v_mfma_f32_16x16x32_bf16 v[108:111], v[140:143], v[184:187], v[108:111]
	v_mfma_f32_16x16x32_bf16 v[112:115], v[148:151], v[184:187], v[112:115]
	v_mfma_f32_16x16x32_bf16 v[116:119], v[140:143], v[180:183], v[116:119]
	v_mfma_f32_16x16x32_bf16 v[120:123], v[148:151], v[180:183], v[120:123]
	v_mfma_f32_16x16x32_bf16 v[124:127], v[140:143], v[176:179], v[124:127]
	v_mfma_f32_16x16x32_bf16 v[128:131], v[148:151], v[176:179], v[128:131]
	v_mfma_f32_16x16x32_bf16 v[132:135], v[140:143], v[172:175], v[132:135]
	v_mfma_f32_16x16x32_bf16 v[136:139], v[148:151], v[172:175], v[136:139]
	v_mfma_f32_16x16x32_bf16 v[108:111], v[144:147], v[200:203], v[108:111]
	v_mfma_f32_16x16x32_bf16 v[112:115], v[152:155], v[200:203], v[112:115]
	v_mfma_f32_16x16x32_bf16 v[116:119], v[144:147], v[196:199], v[116:119]
	v_mfma_f32_16x16x32_bf16 v[120:123], v[152:155], v[196:199], v[120:123]
	v_mfma_f32_16x16x32_bf16 v[124:127], v[144:147], v[192:195], v[124:127]
	v_mfma_f32_16x16x32_bf16 v[128:131], v[152:155], v[192:195], v[128:131]
	v_mfma_f32_16x16x32_bf16 v[132:135], v[144:147], v[188:191], v[132:135]
	v_mfma_f32_16x16x32_bf16 v[136:139], v[152:155], v[188:191], v[136:139]
	s_setprio 0
	s_barrier
	s_and_b64 vcc, exec, s[4:5]
	s_cbranch_vccnz .LBB0_3186
	ds_read_b128 v[184:187], v231 offset:49152
	ds_read_b128 v[200:203], v231 offset:50176
	ds_read_b128 v[180:183], v231 offset:51200
	ds_read_b128 v[196:199], v231 offset:52224
	ds_read_b128 v[176:179], v231 offset:53248
	ds_read_b128 v[192:195], v231 offset:54272
	ds_read_b128 v[172:175], v231 offset:55296
	ds_read_b128 v[188:191], v231 offset:56320
.LBB0_3186:
	s_mov_b32 m0, s49
	v_lshl_add_u64 v[8:9], v[204:205], 0, s[24:25]
	global_load_lds_dwordx4 v[8:9], off
	v_lshl_add_u64 v[8:9], v[206:207], 0, s[24:25]
	s_mov_b32 m0, s50
	s_add_u32 s6, s40, 0x10180
	global_load_lds_dwordx4 v[8:9], off
	v_lshl_add_u64 v[8:9], v[208:209], 0, s[24:25]
	s_mov_b32 m0, s51
	s_addc_u32 s7, s41, 0
	global_load_lds_dwordx4 v[8:9], off
	v_lshl_add_u64 v[8:9], v[210:211], 0, s[24:25]
	s_mov_b32 m0, s52
	s_and_b64 vcc, exec, s[4:5]
	global_load_lds_dwordx4 v[8:9], off
	v_lshl_add_u64 v[8:9], s[6:7], 0, v[2:3]
	s_mov_b32 m0, s53
	s_nop 0
	global_load_lds_dwordx4 v[8:9], off
	v_lshl_add_u64 v[8:9], s[6:7], 0, v[220:221]
	s_mov_b32 m0, s54
	s_nop 0
	global_load_lds_dwordx4 v[8:9], off
	s_waitcnt vmcnt(6)
	s_waitcnt lgkmcnt(0)
	s_barrier
	s_cbranch_vccnz .LBB0_3188
	s_setprio 1
	s_waitcnt lgkmcnt(0)
	v_mfma_f32_16x16x32_bf16 v[64:67], v[156:159], v[184:187], v[64:67]
	v_mfma_f32_16x16x32_bf16 v[60:63], v[164:167], v[184:187], v[60:63]
	v_mfma_f32_16x16x32_bf16 v[48:51], v[156:159], v[180:183], v[48:51]
	v_mfma_f32_16x16x32_bf16 v[44:47], v[164:167], v[180:183], v[44:47]
	v_mfma_f32_16x16x32_bf16 v[32:35], v[156:159], v[176:179], v[32:35]
	v_mfma_f32_16x16x32_bf16 v[28:31], v[164:167], v[176:179], v[28:31]
	v_mfma_f32_16x16x32_bf16 v[16:19], v[156:159], v[172:175], v[16:19]
	v_mfma_f32_16x16x32_bf16 v[12:15], v[164:167], v[172:175], v[12:15]
	v_mfma_f32_16x16x32_bf16 v[64:67], v[160:163], v[200:203], v[64:67]
	v_mfma_f32_16x16x32_bf16 v[60:63], v[168:171], v[200:203], v[60:63]
	v_mfma_f32_16x16x32_bf16 v[48:51], v[160:163], v[196:199], v[48:51]
	v_mfma_f32_16x16x32_bf16 v[44:47], v[168:171], v[196:199], v[44:47]
	v_mfma_f32_16x16x32_bf16 v[32:35], v[160:163], v[192:195], v[32:35]
	v_mfma_f32_16x16x32_bf16 v[28:31], v[168:171], v[192:195], v[28:31]
	v_mfma_f32_16x16x32_bf16 v[16:19], v[160:163], v[188:191], v[16:19]
	v_mfma_f32_16x16x32_bf16 v[12:15], v[168:171], v[188:191], v[12:15]
	v_mfma_f32_16x16x32_bf16 v[72:75], v[140:143], v[184:187], v[72:75]
	v_mfma_f32_16x16x32_bf16 v[68:71], v[148:151], v[184:187], v[68:71]
	v_mfma_f32_16x16x32_bf16 v[56:59], v[140:143], v[180:183], v[56:59]
	v_mfma_f32_16x16x32_bf16 v[52:55], v[148:151], v[180:183], v[52:55]
	v_mfma_f32_16x16x32_bf16 v[40:43], v[140:143], v[176:179], v[40:43]
	v_mfma_f32_16x16x32_bf16 v[36:39], v[148:151], v[176:179], v[36:39]
	v_mfma_f32_16x16x32_bf16 v[24:27], v[140:143], v[172:175], v[24:27]
	v_mfma_f32_16x16x32_bf16 v[20:23], v[148:151], v[172:175], v[20:23]
	v_mfma_f32_16x16x32_bf16 v[72:75], v[144:147], v[200:203], v[72:75]
	v_mfma_f32_16x16x32_bf16 v[68:71], v[152:155], v[200:203], v[68:71]
	v_mfma_f32_16x16x32_bf16 v[56:59], v[144:147], v[196:199], v[56:59]
	v_mfma_f32_16x16x32_bf16 v[52:55], v[152:155], v[196:199], v[52:55]
	v_mfma_f32_16x16x32_bf16 v[40:43], v[144:147], v[192:195], v[40:43]
	v_mfma_f32_16x16x32_bf16 v[36:39], v[152:155], v[192:195], v[36:39]
	v_mfma_f32_16x16x32_bf16 v[24:27], v[144:147], v[188:191], v[24:27]
	v_mfma_f32_16x16x32_bf16 v[20:23], v[152:155], v[188:191], v[20:23]
	s_setprio 0
; #define G8_STAGE_B(bufoff, gbase) do { _Pragma("unroll") for (int _i = 0; _i < 2; ++_i) \
;         __builtin_amdgcn_global_load_lds((const unsigned*)((const char*)(gbase) + voffB[_i]), (LAS unsigned*)(lds + (bufoff) + ldsw + _i * 8192), 16, 0, 0); } while (0)
; #define G8_LDA(dst, b, h) do { _Pragma("unroll") for (int m = 0; m < 4; ++m) _Pragma("unroll") for (int k = 0; k < 2; ++k) dst[m][k] = *(const LAS bf16x8*)(lds + G8_SA(b, h) + aoff + m * 2048 + k * 1024); } while (0)
; #define G8_LDB(dst, b, h) do { _Pragma("unroll") for (int n = 0; n < 2; ++n) _Pragma("unroll") for (int k = 0; k < 2; ++k) dst[n][k] = *(const LAS bf16x8*)(lds + G8_SB(b, h) + boff + n * 2048 + k * 1024); } while (0)
; #define G8_MMA(ai, bj, At, Bt) do { __builtin_amdgcn_s_setprio(1); _Pragma("unroll") for (int m = 0; m < 4; ++m) _Pragma("unroll") for (int n = 0; n < 2; ++n) _Pragma("unroll") for (int k = 0; k < 2; ++k) \
;         acc[ai][bj][m][n] = __builtin_amdgcn_mfma_f32_16x16x32_bf16(Bt[n][k], At[m][k], acc[ai][bj][m][n], 0, 0, 0); __builtin_amdgcn_s_setprio(0); } while (0)
; #define G8_WAIT_V(n) asm volatile("s_waitcnt vmcnt(" #n ")" ::: "memory")
; #define G8_WAIT_L(n) asm volatile("s_waitcnt lgkmcnt(" #n ")" ::: "memory")
; #define G8_BAR __builtin_amdgcn_s_barrier()
; #define G8_SCHED __builtin_amdgcn_sched_barrier(0)
; template <class Sched, class Epi>
; DEVI void gemm_phase(LAS unsigned char* lds, const char* Abase, const int K, const Sched& S, const Epi& E) {
;     ...
;             G8_LDB(B0, 0, 0); G8_LDB(B1, 0, 1); G8_SCHED; G8_LDA(At, 0, 0); G8_STAGE_A(G8_SA(1, 1), false, 1, k1);
;             G8_WAIT_L(0); G8_BAR; G8_MMA(0, 0, At, B0); G8_MMA(0, 1, At, B1); G8_BAR; G8_SCHED;
;             if (!skip1) G8_LDA(At, 0, 1); G8_STAGE_B(G8_SB(0, 0), b2); G8_STAGE_A(G8_SA(0, 0), last, 0, k2); G8_STAGE_B(G8_SB(0, 1), b2 + hstepB);
;             G8_WAIT_V(6); G8_WAIT_L(0); G8_BAR; if (!skip1) { G8_MMA(1, 0, At, B0); G8_MMA(1, 1, At, B1); } G8_BAR; G8_SCHED;
.LBB0_3188:
	s_barrier
	ds_read_b128 v[168:171], v229
	s_waitcnt lgkmcnt(0)
	ds_read_b128 v[172:175], v229 offset:1024
	ds_read_b128 v[176:179], v229 offset:2048
	ds_read_b128 v[180:183], v229 offset:3072
	ds_read_b128 v[152:155], v230
	ds_read_b128 v[156:159], v230 offset:1024
	ds_read_b128 v[160:163], v230 offset:2048
	ds_read_b128 v[164:167], v230 offset:3072
	s_add_u32 s6, s38, 0x10180
	s_addc_u32 s7, s39, 0
	s_mov_b32 m0, s58
	v_lshl_add_u64 v[8:9], s[6:7], 0, v[2:3]
	ds_read_b128 v[196:199], v231
	ds_read_b128 v[212:215], v231 offset:1024
	ds_read_b128 v[192:195], v231 offset:2048
	ds_read_b128 v[208:211], v231 offset:3072
	ds_read_b128 v[188:191], v231 offset:4096
	ds_read_b128 v[204:207], v231 offset:5120
	ds_read_b128 v[184:187], v231 offset:6144
	ds_read_b128 v[200:203], v231 offset:7168
	global_load_lds_dwordx4 v[8:9], off
	v_lshl_add_u64 v[8:9], s[6:7], 0, v[220:221]
	s_mov_b32 m0, s59
	s_nop 0
	global_load_lds_dwordx4 v[8:9], off
	s_waitcnt lgkmcnt(0)
	s_barrier
	s_setprio 1
	s_waitcnt lgkmcnt(0)
	v_mfma_f32_16x16x32_bf16 v[76:79], v[168:171], v[196:199], v[76:79]
	v_mfma_f32_16x16x32_bf16 v[80:83], v[176:179], v[196:199], v[80:83]
	v_mfma_f32_16x16x32_bf16 v[84:87], v[168:171], v[192:195], v[84:87]
	v_mfma_f32_16x16x32_bf16 v[88:91], v[176:179], v[192:195], v[88:91]
	v_mfma_f32_16x16x32_bf16 v[92:95], v[168:171], v[188:191], v[92:95]
	v_mfma_f32_16x16x32_bf16 v[96:99], v[176:179], v[188:191], v[96:99]
	v_mfma_f32_16x16x32_bf16 v[100:103], v[168:171], v[184:187], v[100:103]
	v_mfma_f32_16x16x32_bf16 v[104:107], v[176:179], v[184:187], v[104:107]
	v_mfma_f32_16x16x32_bf16 v[76:79], v[172:175], v[212:215], v[76:79]
	v_mfma_f32_16x16x32_bf16 v[80:83], v[180:183], v[212:215], v[80:83]
	v_mfma_f32_16x16x32_bf16 v[84:87], v[172:175], v[208:211], v[84:87]
	v_mfma_f32_16x16x32_bf16 v[88:91], v[180:183], v[208:211], v[88:91]
	v_mfma_f32_16x16x32_bf16 v[92:95], v[172:175], v[204:207], v[92:95]
	v_mfma_f32_16x16x32_bf16 v[96:99], v[180:183], v[204:207], v[96:99]
	v_mfma_f32_16x16x32_bf16 v[100:103], v[172:175], v[200:203], v[100:103]
	v_mfma_f32_16x16x32_bf16 v[104:107], v[180:183], v[200:203], v[104:107]
	v_mfma_f32_16x16x32_bf16 v[108:111], v[152:155], v[196:199], v[108:111]
	v_mfma_f32_16x16x32_bf16 v[140:143], v[156:159], v[212:215], v[108:111]
	v_mfma_f32_16x16x32_bf16 v[108:111], v[160:163], v[196:199], v[112:115]
	v_mfma_f32_16x16x32_bf16 v[144:147], v[164:167], v[212:215], v[108:111]
	v_mfma_f32_16x16x32_bf16 v[108:111], v[152:155], v[192:195], v[116:119]
	v_mfma_f32_16x16x32_bf16 v[116:119], v[156:159], v[208:211], v[108:111]
	v_mfma_f32_16x16x32_bf16 v[108:111], v[160:163], v[192:195], v[120:123]
	v_mfma_f32_16x16x32_bf16 v[120:123], v[164:167], v[208:211], v[108:111]
	v_mfma_f32_16x16x32_bf16 v[108:111], v[152:155], v[188:191], v[124:127]
	v_mfma_f32_16x16x32_bf16 v[148:151], v[156:159], v[204:207], v[108:111]
	v_mfma_f32_16x16x32_bf16 v[108:111], v[160:163], v[188:191], v[128:131]
	v_mfma_f32_16x16x32_bf16 v[128:131], v[164:167], v[204:207], v[108:111]
	v_mfma_f32_16x16x32_bf16 v[108:111], v[152:155], v[184:187], v[132:135]
	v_mfma_f32_16x16x32_bf16 v[132:135], v[156:159], v[200:203], v[108:111]
	v_mfma_f32_16x16x32_bf16 v[108:111], v[160:163], v[184:187], v[136:139]
	v_mfma_f32_16x16x32_bf16 v[136:139], v[164:167], v[200:203], v[108:111]
	s_setprio 0
	s_barrier
	s_and_b64 vcc, exec, s[4:5]
	s_cbranch_vccnz .LBB0_3190
	ds_read_b128 v[196:199], v231 offset:16384
	ds_read_b128 v[212:215], v231 offset:17408
	ds_read_b128 v[192:195], v231 offset:18432
	ds_read_b128 v[208:211], v231 offset:19456
	ds_read_b128 v[188:191], v231 offset:20480
	ds_read_b128 v[204:207], v231 offset:21504
	ds_read_b128 v[184:187], v231 offset:22528
	ds_read_b128 v[200:203], v231 offset:23552
.LBB0_3190:
	s_mov_b32 m0, s17
	v_lshl_add_u64 v[8:9], s[34:35], 0, v[2:3]
	global_load_lds_dwordx4 v[8:9], off
	v_lshl_add_u64 v[224:225], s[34:35], 0, v[220:221]
	s_mov_b32 m0, s42
	v_lshl_add_u64 v[222:223], s[36:37], 0, v[2:3]
	global_load_lds_dwordx4 v[224:225], off
	s_mov_b32 m0, s15
	s_add_u32 s6, s34, 0x10000
	global_load_lds_dwordx4 v[222:223], off
	v_lshl_add_u64 v[226:227], s[36:37], 0, v[220:221]
	s_mov_b32 m0, s43
	s_addc_u32 s7, s35, 0
	global_load_lds_dwordx4 v[226:227], off
	v_lshl_add_u64 v[108:109], s[6:7], 0, v[2:3]
	s_mov_b32 m0, s44
	s_and_b64 vcc, exec, s[4:5]
	global_load_lds_dwordx4 v[108:109], off
	v_lshl_add_u64 v[108:109], s[6:7], 0, v[220:221]
	s_mov_b32 m0, s45
	s_nop 0
	global_load_lds_dwordx4 v[108:109], off
	s_waitcnt vmcnt(6)
	s_waitcnt lgkmcnt(0)
	s_barrier
	s_cbranch_vccnz .LBB0_3192
	s_setprio 1
	s_waitcnt lgkmcnt(0)
	v_mfma_f32_16x16x32_bf16 v[64:67], v[168:171], v[196:199], v[64:67]
	v_mfma_f32_16x16x32_bf16 v[60:63], v[176:179], v[196:199], v[60:63]
	v_mfma_f32_16x16x32_bf16 v[48:51], v[168:171], v[192:195], v[48:51]
	v_mfma_f32_16x16x32_bf16 v[44:47], v[176:179], v[192:195], v[44:47]
	v_mfma_f32_16x16x32_bf16 v[32:35], v[168:171], v[188:191], v[32:35]
	v_mfma_f32_16x16x32_bf16 v[28:31], v[176:179], v[188:191], v[28:31]
	v_mfma_f32_16x16x32_bf16 v[16:19], v[168:171], v[184:187], v[16:19]
	v_mfma_f32_16x16x32_bf16 v[12:15], v[176:179], v[184:187], v[12:15]
	v_mfma_f32_16x16x32_bf16 v[64:67], v[172:175], v[212:215], v[64:67]
	v_mfma_f32_16x16x32_bf16 v[60:63], v[180:183], v[212:215], v[60:63]
	v_mfma_f32_16x16x32_bf16 v[48:51], v[172:175], v[208:211], v[48:51]
	v_mfma_f32_16x16x32_bf16 v[44:47], v[180:183], v[208:211], v[44:47]
	v_mfma_f32_16x16x32_bf16 v[32:35], v[172:175], v[204:207], v[32:35]
	v_mfma_f32_16x16x32_bf16 v[28:31], v[180:183], v[204:207], v[28:31]
	v_mfma_f32_16x16x32_bf16 v[16:19], v[172:175], v[200:203], v[16:19]
	v_mfma_f32_16x16x32_bf16 v[12:15], v[180:183], v[200:203], v[12:15]
	v_mfma_f32_16x16x32_bf16 v[72:75], v[152:155], v[196:199], v[72:75]
	v_mfma_f32_16x16x32_bf16 v[68:71], v[160:163], v[196:199], v[68:71]
	v_mfma_f32_16x16x32_bf16 v[56:59], v[152:155], v[192:195], v[56:59]
	v_mfma_f32_16x16x32_bf16 v[52:55], v[160:163], v[192:195], v[52:55]
	v_mfma_f32_16x16x32_bf16 v[40:43], v[152:155], v[188:191], v[40:43]
	v_mfma_f32_16x16x32_bf16 v[36:39], v[160:163], v[188:191], v[36:39]
	v_mfma_f32_16x16x32_bf16 v[24:27], v[152:155], v[184:187], v[24:27]
	v_mfma_f32_16x16x32_bf16 v[20:23], v[160:163], v[184:187], v[20:23]
	v_mfma_f32_16x16x32_bf16 v[72:75], v[156:159], v[212:215], v[72:75]
	v_mfma_f32_16x16x32_bf16 v[68:71], v[164:167], v[212:215], v[68:71]
	v_mfma_f32_16x16x32_bf16 v[56:59], v[156:159], v[208:211], v[56:59]
	v_mfma_f32_16x16x32_bf16 v[52:55], v[164:167], v[208:211], v[52:55]
	v_mfma_f32_16x16x32_bf16 v[40:43], v[156:159], v[204:207], v[40:43]
	v_mfma_f32_16x16x32_bf16 v[36:39], v[164:167], v[204:207], v[36:39]
	v_mfma_f32_16x16x32_bf16 v[24:27], v[156:159], v[200:203], v[24:27]
	v_mfma_f32_16x16x32_bf16 v[20:23], v[164:167], v[200:203], v[20:23]
	s_setprio 0
; #define G8_STAGE_B(bufoff, gbase) do { _Pragma("unroll") for (int _i = 0; _i < 2; ++_i) \
;         __builtin_amdgcn_global_load_lds((const unsigned*)((const char*)(gbase) + voffB[_i]), (LAS unsigned*)(lds + (bufoff) + ldsw + _i * 8192), 16, 0, 0); } while (0)
; #define G8_LDA(dst, b, h) do { _Pragma("unroll") for (int m = 0; m < 4; ++m) _Pragma("unroll") for (int k = 0; k < 2; ++k) dst[m][k] = *(const LAS bf16x8*)(lds + G8_SA(b, h) + aoff + m * 2048 + k * 1024); } while (0)
; #define G8_LDB(dst, b, h) do { _Pragma("unroll") for (int n = 0; n < 2; ++n) _Pragma("unroll") for (int k = 0; k < 2; ++k) dst[n][k] = *(const LAS bf16x8*)(lds + G8_SB(b, h) + boff + n * 2048 + k * 1024); } while (0)
; #define G8_MMA(ai, bj, At, Bt) do { __builtin_amdgcn_s_setprio(1); _Pragma("unroll") for (int m = 0; m < 4; ++m) _Pragma("unroll") for (int n = 0; n < 2; ++n) _Pragma("unroll") for (int k = 0; k < 2; ++k) \
;         acc[ai][bj][m][n] = __builtin_amdgcn_mfma_f32_16x16x32_bf16(Bt[n][k], At[m][k], acc[ai][bj][m][n], 0, 0, 0); __builtin_amdgcn_s_setprio(0); } while (0)
; #define G8_WAIT_V(n) asm volatile("s_waitcnt vmcnt(" #n ")" ::: "memory")
; #define G8_WAIT_L(n) asm volatile("s_waitcnt lgkmcnt(" #n ")" ::: "memory")
; #define G8_BAR __builtin_amdgcn_s_barrier()
; #define G8_SCHED __builtin_amdgcn_sched_barrier(0)
; template <class Sched, class Epi>
; DEVI void gemm_phase(LAS unsigned char* lds, const char* Abase, const int K, const Sched& S, const Epi& E) {
;     ...
;             G8_LDB(B0, 1, 0); G8_LDB(B1, 1, 1); G8_SCHED; G8_LDA(At, 1, 0); G8_STAGE_A(G8_SA(0, 1), last, 1, k2);
;             G8_WAIT_L(0); G8_BAR; G8_MMA(0, 0, At, B0); G8_MMA(0, 1, At, B1); G8_BAR; G8_SCHED;
;             if (!skip1) G8_LDA(At, 1, 1); G8_STAGE_B(G8_SB(1, 0), b3); G8_STAGE_A(G8_SA(1, 0), last, 0, k3); G8_STAGE_B(G8_SB(1, 1), b3 + hstepB);
;             G8_WAIT_V(6); G8_WAIT_L(0); G8_BAR; if (!skip1) { G8_MMA(1, 0, At, B0); G8_MMA(1, 1, At, B1); } G8_BAR; G8_SCHED;
.LBB0_3192:
	s_barrier
	ds_read_b128 v[172:175], v7
	ds_read_b128 v[176:179], v7 offset:1024
	ds_read_b128 v[180:183], v7 offset:2048
	s_waitcnt lgkmcnt(0)
	ds_read_b128 v[184:187], v7 offset:3072
	ds_read_b128 v[156:159], v11
	ds_read_b128 v[160:163], v11 offset:1024
	ds_read_b128 v[164:167], v11 offset:2048
	ds_read_b128 v[168:171], v11 offset:3072
	s_add_u32 s6, s36, 0x10000
	s_addc_u32 s7, s37, 0
	s_mov_b32 m0, s46
	v_lshl_add_u64 v[108:109], s[6:7], 0, v[2:3]
	ds_read_b128 v[200:203], v231 offset:32768
	ds_read_b128 v[216:219], v231 offset:33792
	ds_read_b128 v[196:199], v231 offset:34816
	ds_read_b128 v[212:215], v231 offset:35840
	ds_read_b128 v[192:195], v231 offset:36864
	ds_read_b128 v[208:211], v231 offset:37888
	ds_read_b128 v[188:191], v231 offset:38912
	ds_read_b128 v[204:207], v231 offset:39936
	global_load_lds_dwordx4 v[108:109], off
	v_lshl_add_u64 v[108:109], s[6:7], 0, v[220:221]
	s_mov_b32 m0, s47
	s_nop 0
	global_load_lds_dwordx4 v[108:109], off
	s_waitcnt lgkmcnt(0)
	s_barrier
	s_setprio 1
	s_waitcnt lgkmcnt(0)
	v_mfma_f32_16x16x32_bf16 v[76:79], v[172:175], v[200:203], v[76:79]
	v_mfma_f32_16x16x32_bf16 v[124:127], v[176:179], v[216:219], v[76:79]
	v_mfma_f32_16x16x32_bf16 v[76:79], v[180:183], v[200:203], v[80:83]
	v_mfma_f32_16x16x32_bf16 v[152:155], v[184:187], v[216:219], v[76:79]
	v_mfma_f32_16x16x32_bf16 v[76:79], v[172:175], v[196:199], v[84:87]
	v_mfma_f32_16x16x32_bf16 v[108:111], v[176:179], v[212:215], v[76:79]
	v_mfma_f32_16x16x32_bf16 v[76:79], v[180:183], v[196:199], v[88:91]
	v_mfma_f32_16x16x32_bf16 v[112:115], v[184:187], v[212:215], v[76:79]
	v_mfma_f32_16x16x32_bf16 v[76:79], v[172:175], v[192:195], v[92:95]
	v_mfma_f32_16x16x32_bf16 v[92:95], v[176:179], v[208:211], v[76:79]
	v_mfma_f32_16x16x32_bf16 v[76:79], v[180:183], v[192:195], v[96:99]
	v_mfma_f32_16x16x32_bf16 v[96:99], v[184:187], v[208:211], v[76:79]
	v_mfma_f32_16x16x32_bf16 v[76:79], v[172:175], v[188:191], v[100:103]
	v_mfma_f32_16x16x32_bf16 v[80:83], v[180:183], v[188:191], v[104:107]
	v_mfma_f32_16x16x32_bf16 v[76:79], v[176:179], v[204:207], v[76:79]
	v_mfma_f32_16x16x32_bf16 v[80:83], v[184:187], v[204:207], v[80:83]
	v_mfma_f32_16x16x32_bf16 v[84:87], v[156:159], v[200:203], v[140:143]
	v_mfma_f32_16x16x32_bf16 v[140:143], v[160:163], v[216:219], v[84:87]
	v_mfma_f32_16x16x32_bf16 v[84:87], v[164:167], v[200:203], v[144:147]
	v_mfma_f32_16x16x32_bf16 v[144:147], v[168:171], v[216:219], v[84:87]
	v_mfma_f32_16x16x32_bf16 v[84:87], v[156:159], v[196:199], v[116:119]
	v_mfma_f32_16x16x32_bf16 v[116:119], v[160:163], v[212:215], v[84:87]
	v_mfma_f32_16x16x32_bf16 v[84:87], v[164:167], v[196:199], v[120:123]
	v_mfma_f32_16x16x32_bf16 v[120:123], v[168:171], v[212:215], v[84:87]
	v_mfma_f32_16x16x32_bf16 v[84:87], v[156:159], v[192:195], v[148:151]
	v_mfma_f32_16x16x32_bf16 v[100:103], v[160:163], v[208:211], v[84:87]
	v_mfma_f32_16x16x32_bf16 v[84:87], v[164:167], v[192:195], v[128:131]
	v_mfma_f32_16x16x32_bf16 v[104:107], v[168:171], v[208:211], v[84:87]
	v_mfma_f32_16x16x32_bf16 v[84:87], v[156:159], v[188:191], v[132:135]
	v_mfma_f32_16x16x32_bf16 v[88:91], v[164:167], v[188:191], v[136:139]
	v_mfma_f32_16x16x32_bf16 v[84:87], v[160:163], v[204:207], v[84:87]
	v_mfma_f32_16x16x32_bf16 v[88:91], v[168:171], v[204:207], v[88:91]
	s_setprio 0
	s_barrier
	s_and_b64 vcc, exec, s[4:5]
	s_cbranch_vccnz .LBB0_3194
	ds_read_b128 v[200:203], v231 offset:49152
	ds_read_b128 v[216:219], v231 offset:50176
	ds_read_b128 v[196:199], v231 offset:51200
	ds_read_b128 v[212:215], v231 offset:52224
	ds_read_b128 v[192:195], v231 offset:53248
	ds_read_b128 v[208:211], v231 offset:54272
	ds_read_b128 v[188:191], v231 offset:55296
	ds_read_b128 v[204:207], v231 offset:56320
.LBB0_3194:
	s_mov_b32 m0, s49
	v_lshl_add_u64 v[8:9], v[8:9], 0, s[20:21]
	global_load_lds_dwordx4 v[8:9], off
	v_lshl_add_u64 v[8:9], v[224:225], 0, s[20:21]
	s_mov_b32 m0, s50
	s_add_u32 s6, s34, 0x10080
	global_load_lds_dwordx4 v[8:9], off
	v_lshl_add_u64 v[8:9], v[222:223], 0, s[20:21]
	s_mov_b32 m0, s51
	s_addc_u32 s7, s35, 0
	global_load_lds_dwordx4 v[8:9], off
	v_lshl_add_u64 v[8:9], v[226:227], 0, s[20:21]
	s_mov_b32 m0, s52
	s_and_b64 vcc, exec, s[4:5]
	global_load_lds_dwordx4 v[8:9], off
	v_lshl_add_u64 v[8:9], s[6:7], 0, v[2:3]
	s_mov_b32 m0, s53
	s_nop 0
	global_load_lds_dwordx4 v[8:9], off
	v_lshl_add_u64 v[8:9], s[6:7], 0, v[220:221]
	s_mov_b32 m0, s54
	s_nop 0
	global_load_lds_dwordx4 v[8:9], off
	s_waitcnt vmcnt(6)
	s_waitcnt lgkmcnt(0)
	s_barrier
	s_cbranch_vccnz .LBB0_3196
	s_setprio 1
	s_waitcnt lgkmcnt(0)
	v_mfma_f32_16x16x32_bf16 v[64:67], v[172:175], v[200:203], v[64:67]
	v_mfma_f32_16x16x32_bf16 v[60:63], v[180:183], v[200:203], v[60:63]
	v_mfma_f32_16x16x32_bf16 v[48:51], v[172:175], v[196:199], v[48:51]
	v_mfma_f32_16x16x32_bf16 v[44:47], v[180:183], v[196:199], v[44:47]
	v_mfma_f32_16x16x32_bf16 v[32:35], v[172:175], v[192:195], v[32:35]
	v_mfma_f32_16x16x32_bf16 v[28:31], v[180:183], v[192:195], v[28:31]
	v_mfma_f32_16x16x32_bf16 v[16:19], v[172:175], v[188:191], v[16:19]
	v_mfma_f32_16x16x32_bf16 v[12:15], v[180:183], v[188:191], v[12:15]
	v_mfma_f32_16x16x32_bf16 v[64:67], v[176:179], v[216:219], v[64:67]
	v_mfma_f32_16x16x32_bf16 v[60:63], v[184:187], v[216:219], v[60:63]
	v_mfma_f32_16x16x32_bf16 v[48:51], v[176:179], v[212:215], v[48:51]
	v_mfma_f32_16x16x32_bf16 v[44:47], v[184:187], v[212:215], v[44:47]
	v_mfma_f32_16x16x32_bf16 v[32:35], v[176:179], v[208:211], v[32:35]
	v_mfma_f32_16x16x32_bf16 v[28:31], v[184:187], v[208:211], v[28:31]
	v_mfma_f32_16x16x32_bf16 v[16:19], v[176:179], v[204:207], v[16:19]
	v_mfma_f32_16x16x32_bf16 v[12:15], v[184:187], v[204:207], v[12:15]
	v_mfma_f32_16x16x32_bf16 v[72:75], v[156:159], v[200:203], v[72:75]
	v_mfma_f32_16x16x32_bf16 v[68:71], v[164:167], v[200:203], v[68:71]
	v_mfma_f32_16x16x32_bf16 v[56:59], v[156:159], v[196:199], v[56:59]
	v_mfma_f32_16x16x32_bf16 v[52:55], v[164:167], v[196:199], v[52:55]
	v_mfma_f32_16x16x32_bf16 v[40:43], v[156:159], v[192:195], v[40:43]
	v_mfma_f32_16x16x32_bf16 v[36:39], v[164:167], v[192:195], v[36:39]
	v_mfma_f32_16x16x32_bf16 v[24:27], v[156:159], v[188:191], v[24:27]
	v_mfma_f32_16x16x32_bf16 v[20:23], v[164:167], v[188:191], v[20:23]
	v_mfma_f32_16x16x32_bf16 v[72:75], v[160:163], v[216:219], v[72:75]
	v_mfma_f32_16x16x32_bf16 v[68:71], v[168:171], v[216:219], v[68:71]
	v_mfma_f32_16x16x32_bf16 v[56:59], v[160:163], v[212:215], v[56:59]
	v_mfma_f32_16x16x32_bf16 v[52:55], v[168:171], v[212:215], v[52:55]
	v_mfma_f32_16x16x32_bf16 v[40:43], v[160:163], v[208:211], v[40:43]
	v_mfma_f32_16x16x32_bf16 v[36:39], v[168:171], v[208:211], v[36:39]
	v_mfma_f32_16x16x32_bf16 v[24:27], v[160:163], v[204:207], v[24:27]
	v_mfma_f32_16x16x32_bf16 v[20:23], v[168:171], v[204:207], v[20:23]
	s_setprio 0
